# adds: 127 more complex-product lane merges (operand writes after the second FMA no longer block the merge)
# baseline (speedup 1.0000x reference)
; __device__ __forceinline__ void lds_barrier() { asm volatile("s_waitcnt lgkmcnt(0)" ::: "memory"); __builtin_amdgcn_s_barrier(); asm volatile("" ::: "memory"); }
; template <int R, class XT, class TWT>
; __device__ __forceinline__ void dif_task(XT X, TWT tw, int s, int task) {
;     const int lgM = 13 - s, lgq = lgM - R, q = 1 << lgq;
;     const int j0 = task & (q - 1), blk = task >> lgq, base = (blk << lgM) + j0;
;     const int pb = PADI(base), qp = (q >= 32) ? q + (q >> 4) : q;
;     f32x2v v[1 << R];
; #pragma unroll
;     for (int k = 0; k < (1 << R); ++k) v[k] = X[pb + k * qp];
; #pragma unroll
;     for (int r = 0; r < R; ++r) {
;         const int pb = R - 1 - r;
; #pragma unroll
;         for (int k = 0; k < (1 << R); ++k) if (!((k >> pb) & 1)) {
;             const int klo = k & ((1 << pb) - 1);
;             const f32x2v w = tw[(j0 + (klo << lgq)) << (s + r)];
;             const f32x2v a = v[k], b = v[k + (1 << pb)], d = a - b;
;             v[k] = a + b; v[k + (1 << pb)] = (f32x2v){d.x * w.x - d.y * w.y, d.x * w.y + d.y * w.x};
;         }
;     }
; #pragma unroll
;     for (int k = 0; k < (1 << R); ++k) X[pb + k * qp] = v[k];
; }
; __device__ __forceinline__ void phase_spectra(Frame& F0, int l) {
;     ...
;         { float vv[16];
; #pragma unroll
;             for (int r = 0; r < 16; ++r) { const int e = F.tid + 512 * r, seg = e >> lgN, n = e & (N - 1); const int oc = col0 + seg;
;                 float v = 0.f;
;                 if (n < L) v = FT[(size_t)oc * L + n]; else if (n > L) v = FT[(size_t)(512 + oc) * L + (N - n)];
;                 vv[r] = v; }
; #pragma unroll
;             for (int r = 0; r < 16; ++r) X[PADI(F.tid + 512 * r)] = (f32x2v){vv[r], 0.f}; }
;         lds_barrier();
;         fft_fwd_upper(X, tw, 13 - lgN, F.tid);
.LBB0_421:
	s_or_b64 exec, exec, s[2:3]
	v_mov_b32_e32 v3, v181
	v_mov_b32_e32 v5, v181
	v_mov_b32_e32 v7, v181
	v_mov_b32_e32 v9, v181
	v_mov_b32_e32 v11, v181
	v_mov_b32_e32 v13, v181
	v_mov_b32_e32 v15, v181
	v_mov_b32_e32 v17, v181
	v_mov_b32_e32 v19, v181
	v_mov_b32_e32 v21, v181
	v_mov_b32_e32 v23, v181
	v_mov_b32_e32 v25, v181
	v_mov_b32_e32 v27, v181
	v_mov_b32_e32 v29, v181
	v_mov_b32_e32 v31, v181
	s_waitcnt vmcnt(0)
	ds_write_b64 v60, v[2:3]
	ds_write_b64 v61, v[4:5] offset:4096
	ds_write_b64 v62, v[6:7] offset:8192
	ds_write_b64 v63, v[8:9] offset:12288
	ds_write_b64 v64, v[10:11] offset:16384
	ds_write_b64 v65, v[12:13] offset:20480
	ds_write_b64 v66, v[14:15] offset:24576
	ds_write_b64 v67, v[16:17] offset:28672
	ds_write_b64 v68, v[18:19] offset:32768
	ds_write_b64 v69, v[20:21] offset:36864
	ds_write_b64 v70, v[22:23] offset:40960
	ds_write_b64 v71, v[24:25] offset:45056
	ds_write_b64 v72, v[26:27] offset:49152
	ds_write_b64 v73, v[28:29] offset:53248
	ds_write_b64 v74, v[30:31] offset:57344
	ds_write_b64 v75, v[180:181] offset:61440
	s_waitcnt lgkmcnt(0)
	s_barrier
	s_andn2_b64 vcc, exec, s[22:23]
	s_cbranch_vccnz .LBB0_487
	ds_read_b64 v[6:7], v1
	ds_read_b64 v[8:9], v1 offset:4352
	ds_read_b64 v[10:11], v1 offset:8704
	ds_read_b64 v[12:13], v1 offset:13056
	ds_read_b64 v[14:15], v1 offset:17408
	ds_read_b64 v[16:17], v1 offset:21760
	ds_read_b64 v[18:19], v1 offset:26112
	ds_read_b64 v[20:21], v1 offset:30464
	ds_read_b64 v[22:23], v1 offset:34816
	ds_read_b64 v[24:25], v1 offset:39168
	ds_read_b64 v[26:27], v1 offset:43520
	ds_read_b64 v[28:29], v1 offset:47872
	ds_read_b64 v[30:31], v1 offset:52224
	ds_read_b64 v[32:33], v1 offset:56576
	ds_read_b64 v[34:35], v1 offset:60928
	ds_read_b64 v[94:95], v1 offset:65280
	ds_read2st64_b64 v[2:5], v36 offset1:16
	ds_read_b64 v[96:97], v79
	ds_read_b64 v[98:99], v80
	ds_read_b64 v[100:101], v81
	ds_read_b64 v[102:103], v37
	ds_read_b64 v[104:105], v38
	ds_read_b64 v[106:107], v39
	ds_read_b64 v[108:109], v40
	s_waitcnt lgkmcnt(14)
	v_pk_add_f32 v[110:111], v[6:7], v[22:23] neg_lo:[0,1] neg_hi:[0,1]
	v_pk_add_f32 v[6:7], v[6:7], v[22:23]
	s_waitcnt lgkmcnt(7)
	v_pk_mul_f32 v[112:113], v[110:111], v[2:3] op_sel:[1,1] op_sel_hi:[1,0]
	s_mov_b64 s[2:3], 0x20c00000
	v_pk_fma_f32 v[114:115], v[110:111], v[2:3], v[112:113] op_sel_hi:[0,1,1] neg_lo:[0,0,1]
	v_pk_add_f32 v[110:111], v[14:15], v[30:31] neg_lo:[0,1] neg_hi:[0,1]
	v_pk_add_f32 v[14:15], v[14:15], v[30:31]
	v_pk_mul_f32 v[112:113], v[110:111], v[2:3] op_sel:[1,0] op_sel_hi:[0,0]
	v_pk_fma_f32 v[116:117], v[110:111], v[2:3], v[112:113] op_sel:[0,1,0] neg_hi:[0,0,1]
	v_pk_add_f32 v[22:23], v[6:7], v[14:15]
	v_pk_add_f32 v[2:3], v[114:115], v[116:117] neg_lo:[0,1] neg_hi:[0,1]
	v_pk_add_f32 v[6:7], v[6:7], v[14:15] neg_lo:[0,1] neg_hi:[0,1]
	s_waitcnt lgkmcnt(6)
	v_pk_mul_f32 v[110:111], v[96:97], v[2:3] op_sel:[1,1] op_sel_hi:[0,1]
	v_pk_fma_f32 v[112:113], v[96:97], v[2:3], v[110:111] op_sel_hi:[1,0,1] neg_lo:[0,0,1]
	v_pk_mul_f32 v[14:15], v[6:7], v[96:97] op_sel:[1,1] op_sel_hi:[1,0]
	v_pk_add_f32 v[2:3], v[10:11], v[26:27] neg_lo:[0,1] neg_hi:[0,1]
	v_pk_add_f32 v[10:11], v[10:11], v[26:27]
	v_pk_mul_f32 v[110:111], v[2:3], v[4:5] op_sel:[1,1] op_sel_hi:[1,0]
	s_mov_b64 s[0:1], 13
	v_pk_fma_f32 v[118:119], v[2:3], v[4:5], v[110:111] op_sel_hi:[0,1,1] neg_lo:[0,0,1]
	v_pk_add_f32 v[2:3], v[18:19], v[34:35] neg_lo:[0,1] neg_hi:[0,1]
	v_pk_add_f32 v[18:19], v[18:19], v[34:35]
	v_pk_mul_f32 v[110:111], v[2:3], v[4:5] op_sel:[1,0] op_sel_hi:[0,0]
	v_pk_fma_f32 v[120:121], v[2:3], v[4:5], v[110:111] op_sel:[0,1,0] neg_hi:[0,0,1]
	v_pk_add_f32 v[26:27], v[10:11], v[18:19]
	v_pk_add_f32 v[2:3], v[118:119], v[120:121] neg_lo:[0,1] neg_hi:[0,1]
	v_pk_add_f32 v[30:31], v[22:23], v[26:27]
	v_pk_mul_f32 v[4:5], v[96:97], v[2:3] op_sel_hi:[0,1]
	v_pk_fma_f32 v[110:111], v[96:97], v[2:3], v[4:5] op_sel:[1,0,1] op_sel_hi:[1,1,0] neg_hi:[0,0,1]
	v_pk_add_f32 v[22:23], v[22:23], v[26:27] neg_lo:[0,1] neg_hi:[0,1]
	v_pk_add_f32 v[2:3], v[112:113], v[110:111] neg_lo:[0,1] neg_hi:[0,1]
	s_waitcnt lgkmcnt(4)
	v_pk_mul_f32 v[26:27], v[22:23], v[100:101] op_sel:[1,1] op_sel_hi:[1,0]
	v_pk_mul_f32 v[4:5], v[100:101], v[2:3] op_sel:[1,1] op_sel_hi:[0,1]
	v_pk_fma_f32 v[122:123], v[100:101], v[2:3], v[4:5] op_sel_hi:[1,0,1] neg_lo:[0,0,1]
	s_nop 0
	v_pk_add_f32 v[2:3], v[8:9], v[24:25] neg_lo:[0,1] neg_hi:[0,1]
	v_pk_add_f32 v[8:9], v[8:9], v[24:25]
	s_waitcnt lgkmcnt(3)
	v_pk_mul_f32 v[4:5], v[2:3], v[102:103] op_sel:[1,1] op_sel_hi:[1,0]
	s_nop 0
	v_pk_fma_f32 v[124:125], v[2:3], v[102:103], v[4:5] op_sel_hi:[0,1,1] neg_lo:[0,0,1]
	v_pk_add_f32 v[2:3], v[16:17], v[32:33] neg_lo:[0,1] neg_hi:[0,1]
	v_pk_add_f32 v[16:17], v[16:17], v[32:33]
	v_pk_mul_f32 v[4:5], v[2:3], v[102:103] op_sel:[1,0] op_sel_hi:[0,0]
	v_pk_fma_f32 v[126:127], v[2:3], v[102:103], v[4:5] op_sel:[0,1,0] neg_hi:[0,0,1]
	v_pk_add_f32 v[24:25], v[8:9], v[16:17]
	v_pk_add_f32 v[2:3], v[124:125], v[126:127] neg_lo:[0,1] neg_hi:[0,1]
	v_pk_add_f32 v[8:9], v[8:9], v[16:17] neg_lo:[0,1] neg_hi:[0,1]
	v_pk_mul_f32 v[4:5], v[98:99], v[2:3] op_sel:[1,1] op_sel_hi:[0,1]
	v_pk_fma_f32 v[102:103], v[98:99], v[2:3], v[4:5] op_sel_hi:[1,0,1] neg_lo:[0,0,1]
	s_nop 0
	v_pk_add_f32 v[2:3], v[12:13], v[28:29] neg_lo:[0,1] neg_hi:[0,1]
	v_pk_add_f32 v[12:13], v[12:13], v[28:29]
	s_waitcnt lgkmcnt(2)
; template <int R, class XT, class TWT>
; __device__ __forceinline__ void dif_task(XT X, TWT tw, int s, int task) {
;     const int lgM = 13 - s, lgq = lgM - R, q = 1 << lgq;
;     const int j0 = task & (q - 1), blk = task >> lgq, base = (blk << lgM) + j0;
;     const int pb = PADI(base), qp = (q >= 32) ? q + (q >> 4) : q;
;     f32x2v v[1 << R];
; #pragma unroll
;     for (int k = 0; k < (1 << R); ++k) v[k] = X[pb + k * qp];
; #pragma unroll
;     for (int r = 0; r < R; ++r) {
;         const int pb = R - 1 - r;
; #pragma unroll
;         for (int k = 0; k < (1 << R); ++k) if (!((k >> pb) & 1)) {
;             const int klo = k & ((1 << pb) - 1);
;             const f32x2v w = tw[(j0 + (klo << lgq)) << (s + r)];
;             const f32x2v a = v[k], b = v[k + (1 << pb)], d = a - b;
;             v[k] = a + b; v[k + (1 << pb)] = (f32x2v){d.x * w.x - d.y * w.y, d.x * w.y + d.y * w.x};
;         }
;     }
; #pragma unroll
;     for (int k = 0; k < (1 << R); ++k) X[pb + k * qp] = v[k];
; }
	v_pk_mul_f32 v[4:5], v[2:3], v[104:105] op_sel:[1,1] op_sel_hi:[1,0]
	s_nop 0
	v_pk_fma_f32 v[128:129], v[2:3], v[104:105], v[4:5] op_sel_hi:[0,1,1] neg_lo:[0,0,1]
	v_pk_add_f32 v[2:3], v[20:21], v[94:95] neg_lo:[0,1] neg_hi:[0,1]
	v_pk_add_f32 v[20:21], v[20:21], v[94:95]
	v_pk_mul_f32 v[4:5], v[2:3], v[104:105] op_sel:[1,0] op_sel_hi:[0,0]
	v_pk_fma_f32 v[130:131], v[2:3], v[104:105], v[4:5] op_sel:[0,1,0] neg_hi:[0,0,1]
	v_pk_add_f32 v[28:29], v[12:13], v[20:21]
	v_pk_add_f32 v[2:3], v[128:129], v[130:131] neg_lo:[0,1] neg_hi:[0,1]
	v_pk_add_f32 v[32:33], v[24:25], v[28:29]
	s_waitcnt lgkmcnt(1)
	v_pk_mul_f32 v[4:5], v[106:107], v[2:3] op_sel_hi:[0,1]
	v_pk_fma_f32 v[104:105], v[106:107], v[2:3], v[4:5] op_sel:[1,0,1] op_sel_hi:[1,1,0] neg_hi:[0,0,1]
	v_pk_add_f32 v[34:35], v[30:31], v[32:33]
	v_pk_add_f32 v[2:3], v[102:103], v[104:105] neg_lo:[0,1] neg_hi:[0,1]
	v_pk_add_f32 v[30:31], v[30:31], v[32:33] neg_lo:[0,1] neg_hi:[0,1]
	v_pk_mul_f32 v[4:5], v[100:101], v[2:3] op_sel_hi:[0,1]
	v_pk_fma_f32 v[132:133], v[100:101], v[2:3], v[4:5] op_sel:[1,0,1] op_sel_hi:[1,1,0] neg_hi:[0,0,1]
	s_waitcnt lgkmcnt(0)
	v_xor_b32_e32 v4, 0x80000000, v108
	v_cndmask_b32_e64 v5, v4, v109, s[36:37]
	v_cndmask_b32_e64 v4, v109, v108, s[36:37]
	v_pk_mul_f32 v[32:33], v[30:31], v[4:5] op_sel:[1,1] op_sel_hi:[1,0]
	s_nop 0
	v_pk_fma_f32 v[94:95], v[30:31], v[4:5], v[32:33] op_sel_hi:[0,1,1] neg_lo:[0,0,1]
	v_pk_fma_f32 v[30:31], v[22:23], v[100:101], v[26:27] op_sel_hi:[0,1,1] neg_lo:[0,0,1]
	v_pk_add_f32 v[22:23], v[24:25], v[28:29] neg_lo:[0,1] neg_hi:[0,1]
	v_pk_add_f32 v[2:3], v[122:123], v[132:133] neg_lo:[0,1] neg_hi:[0,1]
	v_pk_mul_f32 v[24:25], v[22:23], v[100:101] op_sel_hi:[1,0]
	s_nop 0
	v_pk_fma_f32 v[26:27], v[22:23], v[100:101], v[24:25] op_sel:[0,1,1] op_sel_hi:[1,1,0] neg_hi:[0,0,1]
	s_nop 0
	v_pk_add_f32 v[24:25], v[30:31], v[26:27] neg_lo:[0,1] neg_hi:[0,1]
	v_pk_add_f32 v[22:23], v[30:31], v[26:27]
	v_pk_mul_f32 v[26:27], v[4:5], v[24:25] op_sel:[1,1] op_sel_hi:[0,1]
	v_pk_fma_f32 v[28:29], v[4:5], v[24:25], v[26:27] op_sel_hi:[1,0,1] neg_lo:[0,0,1]
	s_nop 0
	v_pk_fma_f32 v[24:25], v[6:7], v[96:97], v[14:15] op_sel_hi:[0,1,1] neg_lo:[0,0,1]
	v_pk_add_f32 v[6:7], v[10:11], v[18:19] neg_lo:[0,1] neg_hi:[0,1]
	s_nop 0
	v_pk_mul_f32 v[10:11], v[6:7], v[96:97] op_sel_hi:[1,0]
	s_nop 0
	v_pk_fma_f32 v[14:15], v[6:7], v[96:97], v[10:11] op_sel:[0,1,1] op_sel_hi:[1,1,0] neg_hi:[0,0,1]
	v_pk_mul_f32 v[10:11], v[8:9], v[98:99] op_sel:[1,1] op_sel_hi:[1,0]
	s_nop 0
	v_pk_fma_f32 v[16:17], v[8:9], v[98:99], v[10:11] op_sel_hi:[0,1,1] neg_lo:[0,0,1]
	v_pk_add_f32 v[8:9], v[12:13], v[20:21] neg_lo:[0,1] neg_hi:[0,1]
	v_pk_add_f32 v[6:7], v[24:25], v[14:15]
	v_pk_mul_f32 v[10:11], v[8:9], v[106:107] op_sel_hi:[1,0]
	v_pk_add_f32 v[20:21], v[124:125], v[126:127]
	v_pk_fma_f32 v[12:13], v[8:9], v[106:107], v[10:11] op_sel:[0,1,1] op_sel_hi:[1,1,0] neg_hi:[0,0,1]
	s_nop 0
	v_pk_add_f32 v[8:9], v[16:17], v[12:13]
	s_nop 0
	v_pk_add_f32 v[10:11], v[6:7], v[8:9]
	v_pk_add_f32 v[6:7], v[6:7], v[8:9] neg_lo:[0,1] neg_hi:[0,1]
	s_nop 0
	v_pk_mul_f32 v[8:9], v[4:5], v[6:7] op_sel:[1,1] op_sel_hi:[0,1]
	v_pk_fma_f32 v[18:19], v[4:5], v[6:7], v[8:9] op_sel_hi:[1,0,1] neg_lo:[0,0,1]
	s_nop 0
	v_pk_add_f32 v[6:7], v[24:25], v[14:15] neg_lo:[0,1] neg_hi:[0,1]
	v_pk_add_f32 v[24:25], v[128:129], v[130:131]
	v_pk_mul_f32 v[8:9], v[100:101], v[6:7] op_sel:[1,1] op_sel_hi:[0,1]
	v_pk_fma_f32 v[14:15], v[100:101], v[6:7], v[8:9] op_sel_hi:[1,0,1] neg_lo:[0,0,1]
	v_pk_add_f32 v[26:27], v[20:21], v[24:25]
	v_pk_add_f32 v[6:7], v[16:17], v[12:13] neg_lo:[0,1] neg_hi:[0,1]
	s_nop 0
	v_pk_mul_f32 v[8:9], v[100:101], v[6:7] op_sel_hi:[0,1]
	v_pk_fma_f32 v[12:13], v[100:101], v[6:7], v[8:9] op_sel:[1,0,1] op_sel_hi:[1,1,0] neg_hi:[0,0,1]
	s_nop 0
	v_pk_add_f32 v[8:9], v[14:15], v[12:13] neg_lo:[0,1] neg_hi:[0,1]
	v_pk_add_f32 v[6:7], v[14:15], v[12:13]
	v_pk_mul_f32 v[12:13], v[4:5], v[8:9] op_sel:[1,1] op_sel_hi:[0,1]
	v_pk_fma_f32 v[14:15], v[4:5], v[8:9], v[12:13] op_sel_hi:[1,0,1] neg_lo:[0,0,1]
	v_pk_add_f32 v[12:13], v[118:119], v[120:121]
	v_pk_add_f32 v[8:9], v[114:115], v[116:117]
	s_nop 0
	v_pk_add_f32 v[16:17], v[8:9], v[12:13]
	v_pk_add_f32 v[8:9], v[8:9], v[12:13] neg_lo:[0,1] neg_hi:[0,1]
	v_pk_add_f32 v[30:31], v[16:17], v[26:27]
	v_pk_add_f32 v[16:17], v[16:17], v[26:27] neg_lo:[0,1] neg_hi:[0,1]
	v_pk_mul_f32 v[12:13], v[100:101], v[8:9] op_sel:[1,1] op_sel_hi:[0,1]
	v_pk_mul_f32 v[26:27], v[16:17], v[4:5] op_sel:[1,1] op_sel_hi:[1,0]
	s_nop 0
	v_pk_fma_f32 v[32:33], v[16:17], v[4:5], v[26:27] op_sel_hi:[0,1,1] neg_lo:[0,0,1]
	v_pk_fma_f32 v[16:17], v[100:101], v[8:9], v[12:13] op_sel_hi:[1,0,1] neg_lo:[0,0,1]
	s_nop 0
	v_pk_add_f32 v[8:9], v[20:21], v[24:25] neg_lo:[0,1] neg_hi:[0,1]
	s_nop 0
	v_pk_mul_f32 v[12:13], v[100:101], v[8:9] op_sel_hi:[0,1]
	v_pk_fma_f32 v[20:21], v[100:101], v[8:9], v[12:13] op_sel:[1,0,1] op_sel_hi:[1,1,0] neg_hi:[0,0,1]
	s_nop 0
	v_pk_add_f32 v[12:13], v[16:17], v[20:21] neg_lo:[0,1] neg_hi:[0,1]
	v_pk_add_f32 v[8:9], v[16:17], v[20:21]
	v_pk_mul_f32 v[16:17], v[4:5], v[12:13] op_sel:[1,1] op_sel_hi:[0,1]
	v_pk_fma_f32 v[20:21], v[4:5], v[12:13], v[16:17] op_sel_hi:[1,0,1] neg_lo:[0,0,1]
	v_pk_add_f32 v[16:17], v[102:103], v[104:105]
	v_pk_add_f32 v[12:13], v[112:113], v[110:111]
	s_nop 0
	v_pk_add_f32 v[24:25], v[12:13], v[16:17]
	v_pk_add_f32 v[12:13], v[12:13], v[16:17] neg_lo:[0,1] neg_hi:[0,1]
	s_nop 0
	v_pk_mul_f32 v[16:17], v[4:5], v[12:13] op_sel:[1,1] op_sel_hi:[0,1]
	v_pk_fma_f32 v[26:27], v[4:5], v[12:13], v[16:17] op_sel_hi:[1,0,1] neg_lo:[0,0,1]
	v_pk_mul_f32 v[16:17], v[4:5], v[2:3] op_sel:[1,1] op_sel_hi:[0,1]
	v_pk_fma_f32 v[96:97], v[4:5], v[2:3], v[16:17] neg_lo:[0,0,1] neg_hi:[0,0,1]
	v_pk_fma_f32 v[2:3], v[4:5], v[2:3], v[16:17] op_sel_hi:[1,0,1]
	v_pk_add_f32 v[12:13], v[122:123], v[132:133]
	v_mov_b32_e32 v97, v3
	ds_write_b64 v1, v[34:35]
	ds_write_b64 v1, v[94:95] offset:4352
	ds_write_b64 v1, v[22:23] offset:8704
	ds_write_b64 v1, v[28:29] offset:13056
	ds_write_b64 v1, v[10:11] offset:17408
	ds_write_b64 v1, v[18:19] offset:21760
	ds_write_b64 v1, v[6:7] offset:26112
	ds_write_b64 v1, v[14:15] offset:30464
	ds_write_b64 v1, v[30:31] offset:34816
	ds_write_b64 v1, v[32:33] offset:39168
	ds_write_b64 v1, v[8:9] offset:43520
	ds_write_b64 v1, v[20:21] offset:47872
	ds_write_b64 v1, v[24:25] offset:52224
	ds_write_b64 v1, v[26:27] offset:56576
	ds_write_b64 v1, v[12:13] offset:60928
	ds_write_b64 v1, v[96:97] offset:65280
	s_waitcnt lgkmcnt(0)
	s_barrier
	s_branch .LBB0_488

; template <int R, class XT, class TWT>
; __device__ __forceinline__ void dif_task(XT X, TWT tw, int s, int task) {
;     const int lgM = 13 - s, lgq = lgM - R, q = 1 << lgq;
;     const int j0 = task & (q - 1), blk = task >> lgq, base = (blk << lgM) + j0;
;     const int pb = PADI(base), qp = (q >= 32) ? q + (q >> 4) : q;
;     f32x2v v[1 << R];
; #pragma unroll
;     for (int k = 0; k < (1 << R); ++k) v[k] = X[pb + k * qp];
; #pragma unroll
;     for (int r = 0; r < R; ++r) {
;         const int pb = R - 1 - r;
; #pragma unroll
;         for (int k = 0; k < (1 << R); ++k) if (!((k >> pb) & 1)) {
;             const int klo = k & ((1 << pb) - 1);
;             const f32x2v w = tw[(j0 + (klo << lgq)) << (s + r)];
;             const f32x2v a = v[k], b = v[k + (1 << pb)], d = a - b;
;             v[k] = a + b; v[k + (1 << pb)] = (f32x2v){d.x * w.x - d.y * w.y, d.x * w.y + d.y * w.x};
;         }
;     }
; #pragma unroll
;     for (int k = 0; k < (1 << R); ++k) X[pb + k * qp] = v[k];
; }
.LBB0_488:
	ds_read2_b64 v[2:5], v76 offset1:34
	ds_read2_b64 v[6:9], v76 offset0:68 offset1:102
	ds_read2_b64 v[10:13], v76 offset0:136 offset1:170
	ds_read2_b64 v[14:17], v76 offset0:204 offset1:238
	v_add_u32_e32 v134, 0x800, v76
	ds_read2_b64 v[18:21], v134 offset0:16 offset1:50
	ds_read2_b64 v[22:25], v134 offset0:84 offset1:118
	ds_read2_b64 v[26:29], v134 offset0:152 offset1:186
	ds_read2_b64 v[30:33], v134 offset0:220 offset1:254
	ds_read2st64_b64 v[94:97], v82 offset1:16
	ds_read_b64 v[34:35], v85
	ds_read_b64 v[98:99], v86
	ds_read_b64 v[100:101], v87
	ds_read_b64 v[102:103], v83
	ds_read_b64 v[104:105], v84
	ds_read_b64 v[106:107], v41
	ds_read_b64 v[108:109], v42
	s_waitcnt lgkmcnt(11)
	v_pk_add_f32 v[110:111], v[2:3], v[18:19] neg_lo:[0,1] neg_hi:[0,1]
	v_pk_add_f32 v[2:3], v[2:3], v[18:19]
	s_waitcnt lgkmcnt(7)
	v_pk_mul_f32 v[112:113], v[110:111], v[94:95] op_sel:[1,1] op_sel_hi:[1,0]
	s_add_u32 s4, s6, s2
	v_pk_fma_f32 v[114:115], v[110:111], v[94:95], v[112:113] op_sel_hi:[0,1,1] neg_lo:[0,0,1]
	v_pk_add_f32 v[110:111], v[10:11], v[26:27] neg_lo:[0,1] neg_hi:[0,1]
	v_pk_add_f32 v[10:11], v[10:11], v[26:27]
	v_pk_mul_f32 v[112:113], v[110:111], v[94:95] op_sel:[1,0] op_sel_hi:[0,0]
	v_pk_fma_f32 v[116:117], v[110:111], v[94:95], v[112:113] op_sel:[0,1,0] neg_hi:[0,0,1]
	v_pk_add_f32 v[18:19], v[2:3], v[10:11]
	v_pk_add_f32 v[94:95], v[114:115], v[116:117] neg_lo:[0,1] neg_hi:[0,1]
	v_pk_add_f32 v[2:3], v[2:3], v[10:11] neg_lo:[0,1] neg_hi:[0,1]
	s_waitcnt lgkmcnt(6)
	v_pk_mul_f32 v[110:111], v[34:35], v[94:95] op_sel:[1,1] op_sel_hi:[0,1]
	v_pk_fma_f32 v[112:113], v[34:35], v[94:95], v[110:111] op_sel_hi:[1,0,1] neg_lo:[0,0,1]
	v_pk_mul_f32 v[10:11], v[2:3], v[34:35] op_sel:[1,1] op_sel_hi:[1,0]
	v_pk_add_f32 v[94:95], v[6:7], v[22:23] neg_lo:[0,1] neg_hi:[0,1]
	v_pk_add_f32 v[6:7], v[6:7], v[22:23]
	v_pk_mul_f32 v[110:111], v[94:95], v[96:97] op_sel:[1,1] op_sel_hi:[1,0]
	s_addc_u32 s5, s7, s3
	v_pk_fma_f32 v[118:119], v[94:95], v[96:97], v[110:111] op_sel_hi:[0,1,1] neg_lo:[0,0,1]
	v_pk_add_f32 v[94:95], v[14:15], v[30:31] neg_lo:[0,1] neg_hi:[0,1]
	v_pk_add_f32 v[14:15], v[14:15], v[30:31]
	v_pk_mul_f32 v[110:111], v[94:95], v[96:97] op_sel:[1,0] op_sel_hi:[0,0]
	v_pk_fma_f32 v[120:121], v[94:95], v[96:97], v[110:111] op_sel:[0,1,0] neg_hi:[0,0,1]
	v_pk_add_f32 v[22:23], v[6:7], v[14:15]
	v_pk_add_f32 v[94:95], v[118:119], v[120:121] neg_lo:[0,1] neg_hi:[0,1]
	v_pk_add_f32 v[26:27], v[18:19], v[22:23]
	v_pk_mul_f32 v[96:97], v[34:35], v[94:95] op_sel_hi:[0,1]
	v_pk_fma_f32 v[110:111], v[34:35], v[94:95], v[96:97] op_sel:[1,0,1] op_sel_hi:[1,1,0] neg_hi:[0,0,1]
	v_pk_add_f32 v[18:19], v[18:19], v[22:23] neg_lo:[0,1] neg_hi:[0,1]
	v_pk_add_f32 v[94:95], v[112:113], v[110:111] neg_lo:[0,1] neg_hi:[0,1]
	s_waitcnt lgkmcnt(4)
	v_pk_mul_f32 v[22:23], v[18:19], v[100:101] op_sel:[1,1] op_sel_hi:[1,0]
	v_pk_mul_f32 v[96:97], v[100:101], v[94:95] op_sel:[1,1] op_sel_hi:[0,1]
	v_pk_fma_f32 v[122:123], v[100:101], v[94:95], v[96:97] op_sel_hi:[1,0,1] neg_lo:[0,0,1]
	s_ashr_i32 s21, s20, 31
	v_pk_add_f32 v[94:95], v[4:5], v[20:21] neg_lo:[0,1] neg_hi:[0,1]
	v_pk_add_f32 v[4:5], v[4:5], v[20:21]
	s_waitcnt lgkmcnt(3)
	v_pk_mul_f32 v[96:97], v[94:95], v[102:103] op_sel:[1,1] op_sel_hi:[1,0]
	s_lshl_b64 s[0:1], s[20:21], s0
	v_pk_fma_f32 v[124:125], v[94:95], v[102:103], v[96:97] op_sel_hi:[0,1,1] neg_lo:[0,0,1]
	v_pk_add_f32 v[94:95], v[12:13], v[28:29] neg_lo:[0,1] neg_hi:[0,1]
	v_pk_add_f32 v[12:13], v[12:13], v[28:29]
	v_pk_mul_f32 v[96:97], v[94:95], v[102:103] op_sel:[1,0] op_sel_hi:[0,0]
	v_pk_fma_f32 v[126:127], v[94:95], v[102:103], v[96:97] op_sel:[0,1,0] neg_hi:[0,0,1]
	v_pk_add_f32 v[20:21], v[4:5], v[12:13]
	v_pk_add_f32 v[94:95], v[124:125], v[126:127] neg_lo:[0,1] neg_hi:[0,1]
	v_pk_add_f32 v[4:5], v[4:5], v[12:13] neg_lo:[0,1] neg_hi:[0,1]
	v_pk_mul_f32 v[96:97], v[98:99], v[94:95] op_sel:[1,1] op_sel_hi:[0,1]
	v_pk_fma_f32 v[102:103], v[98:99], v[94:95], v[96:97] op_sel_hi:[1,0,1] neg_lo:[0,0,1]
	s_lshl_b64 s[0:1], s[0:1], 3
	v_pk_add_f32 v[94:95], v[8:9], v[24:25] neg_lo:[0,1] neg_hi:[0,1]
	v_pk_add_f32 v[8:9], v[8:9], v[24:25]
	s_waitcnt lgkmcnt(2)
	v_pk_mul_f32 v[96:97], v[94:95], v[104:105] op_sel:[1,1] op_sel_hi:[1,0]
	s_add_u32 s0, s4, s0
	v_pk_fma_f32 v[128:129], v[94:95], v[104:105], v[96:97] op_sel_hi:[0,1,1] neg_lo:[0,0,1]
	v_pk_add_f32 v[94:95], v[16:17], v[32:33] neg_lo:[0,1] neg_hi:[0,1]
	v_pk_add_f32 v[16:17], v[16:17], v[32:33]
	v_pk_mul_f32 v[96:97], v[94:95], v[104:105] op_sel:[1,0] op_sel_hi:[0,0]
	v_pk_fma_f32 v[130:131], v[94:95], v[104:105], v[96:97] op_sel:[0,1,0] neg_hi:[0,0,1]
	v_pk_add_f32 v[24:25], v[8:9], v[16:17]
	v_pk_add_f32 v[94:95], v[128:129], v[130:131] neg_lo:[0,1] neg_hi:[0,1]
	v_pk_add_f32 v[28:29], v[20:21], v[24:25]
	s_waitcnt lgkmcnt(1)
	v_pk_mul_f32 v[96:97], v[106:107], v[94:95] op_sel_hi:[0,1]
	v_pk_fma_f32 v[104:105], v[106:107], v[94:95], v[96:97] op_sel:[1,0,1] op_sel_hi:[1,1,0] neg_hi:[0,0,1]
	v_pk_add_f32 v[30:31], v[26:27], v[28:29]
	v_pk_add_f32 v[94:95], v[102:103], v[104:105] neg_lo:[0,1] neg_hi:[0,1]
	v_pk_add_f32 v[26:27], v[26:27], v[28:29] neg_lo:[0,1] neg_hi:[0,1]
	v_pk_mul_f32 v[96:97], v[100:101], v[94:95] op_sel_hi:[0,1]
	v_pk_fma_f32 v[132:133], v[100:101], v[94:95], v[96:97] op_sel:[1,0,1] op_sel_hi:[1,1,0] neg_hi:[0,0,1]
	s_waitcnt lgkmcnt(0)
; template <int R, class XT, class TWT>
; __device__ __forceinline__ void dif_task(XT X, TWT tw, int s, int task) {
;     const int lgM = 13 - s, lgq = lgM - R, q = 1 << lgq;
;     const int j0 = task & (q - 1), blk = task >> lgq, base = (blk << lgM) + j0;
;     const int pb = PADI(base), qp = (q >= 32) ? q + (q >> 4) : q;
;     f32x2v v[1 << R];
; #pragma unroll
;     for (int k = 0; k < (1 << R); ++k) v[k] = X[pb + k * qp];
; #pragma unroll
;     for (int r = 0; r < R; ++r) {
;         const int pb = R - 1 - r;
; #pragma unroll
;         for (int k = 0; k < (1 << R); ++k) if (!((k >> pb) & 1)) {
;             const int klo = k & ((1 << pb) - 1);
;             const f32x2v w = tw[(j0 + (klo << lgq)) << (s + r)];
;             const f32x2v a = v[k], b = v[k + (1 << pb)], d = a - b;
;             v[k] = a + b; v[k + (1 << pb)] = (f32x2v){d.x * w.x - d.y * w.y, d.x * w.y + d.y * w.x};
;         }
;     }
; #pragma unroll
;     for (int k = 0; k < (1 << R); ++k) X[pb + k * qp] = v[k];
; }
	v_xor_b32_e32 v96, 0x80000000, v108
	v_cndmask_b32_e64 v97, v96, v109, s[38:39]
	v_cndmask_b32_e64 v96, v109, v108, s[38:39]
	v_pk_mul_f32 v[28:29], v[26:27], v[96:97] op_sel:[1,1] op_sel_hi:[1,0]
	s_nop 0
	v_pk_fma_f32 v[32:33], v[26:27], v[96:97], v[28:29] op_sel_hi:[0,1,1] neg_lo:[0,0,1]
	v_pk_fma_f32 v[26:27], v[18:19], v[100:101], v[22:23] op_sel_hi:[0,1,1] neg_lo:[0,0,1]
	v_pk_add_f32 v[18:19], v[20:21], v[24:25] neg_lo:[0,1] neg_hi:[0,1]
	v_pk_add_f32 v[94:95], v[122:123], v[132:133] neg_lo:[0,1] neg_hi:[0,1]
	v_pk_mul_f32 v[20:21], v[18:19], v[100:101] op_sel_hi:[1,0]
	v_mov_b32_e32 v108, s8
	v_pk_fma_f32 v[22:23], v[18:19], v[100:101], v[20:21] op_sel:[0,1,1] op_sel_hi:[1,1,0] neg_hi:[0,0,1]
	s_addc_u32 s1, s5, s1
	v_pk_add_f32 v[20:21], v[26:27], v[22:23] neg_lo:[0,1] neg_hi:[0,1]
	v_pk_add_f32 v[18:19], v[26:27], v[22:23]
	v_pk_mul_f32 v[22:23], v[96:97], v[20:21] op_sel:[1,1] op_sel_hi:[0,1]
	v_pk_fma_f32 v[24:25], v[96:97], v[20:21], v[22:23] op_sel_hi:[1,0,1] neg_lo:[0,0,1]
	s_nop 0
	v_pk_fma_f32 v[20:21], v[2:3], v[34:35], v[10:11] op_sel_hi:[0,1,1] neg_lo:[0,0,1]
	v_pk_add_f32 v[2:3], v[6:7], v[14:15] neg_lo:[0,1] neg_hi:[0,1]
	s_nop 0
	v_pk_mul_f32 v[6:7], v[2:3], v[34:35] op_sel_hi:[1,0]
	s_nop 0
	v_pk_fma_f32 v[10:11], v[2:3], v[34:35], v[6:7] op_sel:[0,1,1] op_sel_hi:[1,1,0] neg_hi:[0,0,1]
	v_pk_mul_f32 v[6:7], v[4:5], v[98:99] op_sel:[1,1] op_sel_hi:[1,0]
	s_nop 0
	v_pk_fma_f32 v[12:13], v[4:5], v[98:99], v[6:7] op_sel_hi:[0,1,1] neg_lo:[0,0,1]
	v_pk_add_f32 v[4:5], v[8:9], v[16:17] neg_lo:[0,1] neg_hi:[0,1]
	v_pk_add_f32 v[2:3], v[20:21], v[10:11]
	v_pk_mul_f32 v[6:7], v[4:5], v[106:107] op_sel_hi:[1,0]
	v_pk_add_f32 v[16:17], v[124:125], v[126:127]
	v_pk_fma_f32 v[8:9], v[4:5], v[106:107], v[6:7] op_sel:[0,1,1] op_sel_hi:[1,1,0] neg_hi:[0,0,1]
	s_nop 0
	v_pk_add_f32 v[4:5], v[12:13], v[8:9]
	s_nop 0
	v_pk_add_f32 v[6:7], v[2:3], v[4:5]
	v_pk_add_f32 v[2:3], v[2:3], v[4:5] neg_lo:[0,1] neg_hi:[0,1]
	s_nop 0
	v_pk_mul_f32 v[4:5], v[96:97], v[2:3] op_sel:[1,1] op_sel_hi:[0,1]
	v_pk_fma_f32 v[14:15], v[96:97], v[2:3], v[4:5] op_sel_hi:[1,0,1] neg_lo:[0,0,1]
	s_nop 0
	v_pk_add_f32 v[2:3], v[20:21], v[10:11] neg_lo:[0,1] neg_hi:[0,1]
	v_pk_add_f32 v[20:21], v[128:129], v[130:131]
	v_pk_mul_f32 v[4:5], v[100:101], v[2:3] op_sel:[1,1] op_sel_hi:[0,1]
	v_pk_fma_f32 v[10:11], v[100:101], v[2:3], v[4:5] op_sel_hi:[1,0,1] neg_lo:[0,0,1]
	v_pk_add_f32 v[22:23], v[16:17], v[20:21]
	v_pk_add_f32 v[2:3], v[12:13], v[8:9] neg_lo:[0,1] neg_hi:[0,1]
	s_nop 0
	v_pk_mul_f32 v[4:5], v[100:101], v[2:3] op_sel_hi:[0,1]
	v_pk_fma_f32 v[8:9], v[100:101], v[2:3], v[4:5] op_sel:[1,0,1] op_sel_hi:[1,1,0] neg_hi:[0,0,1]
	s_nop 0
	v_pk_add_f32 v[4:5], v[10:11], v[8:9] neg_lo:[0,1] neg_hi:[0,1]
	v_pk_add_f32 v[2:3], v[10:11], v[8:9]
	v_pk_mul_f32 v[8:9], v[96:97], v[4:5] op_sel:[1,1] op_sel_hi:[0,1]
	v_pk_fma_f32 v[10:11], v[96:97], v[4:5], v[8:9] op_sel_hi:[1,0,1] neg_lo:[0,0,1]
	v_pk_add_f32 v[8:9], v[118:119], v[120:121]
	v_pk_add_f32 v[4:5], v[114:115], v[116:117]
	s_nop 0
	v_pk_add_f32 v[12:13], v[4:5], v[8:9]
	v_pk_add_f32 v[4:5], v[4:5], v[8:9] neg_lo:[0,1] neg_hi:[0,1]
	v_pk_add_f32 v[26:27], v[12:13], v[22:23]
	v_pk_add_f32 v[12:13], v[12:13], v[22:23] neg_lo:[0,1] neg_hi:[0,1]
	v_pk_mul_f32 v[8:9], v[100:101], v[4:5] op_sel:[1,1] op_sel_hi:[0,1]
	v_pk_mul_f32 v[22:23], v[12:13], v[96:97] op_sel:[1,1] op_sel_hi:[1,0]
	s_nop 0
	v_pk_fma_f32 v[28:29], v[12:13], v[96:97], v[22:23] op_sel_hi:[0,1,1] neg_lo:[0,0,1]
	v_pk_fma_f32 v[12:13], v[100:101], v[4:5], v[8:9] op_sel_hi:[1,0,1] neg_lo:[0,0,1]
	s_nop 0
	v_pk_add_f32 v[4:5], v[16:17], v[20:21] neg_lo:[0,1] neg_hi:[0,1]
	s_nop 0
	v_pk_mul_f32 v[8:9], v[100:101], v[4:5] op_sel_hi:[0,1]
	v_pk_fma_f32 v[16:17], v[100:101], v[4:5], v[8:9] op_sel:[1,0,1] op_sel_hi:[1,1,0] neg_hi:[0,0,1]
	s_nop 0
	v_pk_add_f32 v[8:9], v[12:13], v[16:17] neg_lo:[0,1] neg_hi:[0,1]
	v_pk_add_f32 v[4:5], v[12:13], v[16:17]
	v_pk_mul_f32 v[12:13], v[96:97], v[8:9] op_sel:[1,1] op_sel_hi:[0,1]
	v_pk_fma_f32 v[16:17], v[96:97], v[8:9], v[12:13] op_sel_hi:[1,0,1] neg_lo:[0,0,1]
	v_pk_add_f32 v[12:13], v[102:103], v[104:105]
	v_pk_add_f32 v[8:9], v[112:113], v[110:111]
	s_nop 0
	v_pk_add_f32 v[20:21], v[8:9], v[12:13]
	v_pk_add_f32 v[8:9], v[8:9], v[12:13] neg_lo:[0,1] neg_hi:[0,1]
	s_nop 0
	v_pk_mul_f32 v[12:13], v[96:97], v[8:9] op_sel:[1,1] op_sel_hi:[0,1]
	v_pk_fma_f32 v[22:23], v[96:97], v[8:9], v[12:13] op_sel_hi:[1,0,1] neg_lo:[0,0,1]
	v_pk_mul_f32 v[12:13], v[96:97], v[94:95] op_sel:[1,1] op_sel_hi:[0,1]
	v_pk_fma_f32 v[34:35], v[96:97], v[94:95], v[12:13] op_sel_hi:[1,0,1] neg_lo:[0,0,1]
	v_pk_add_f32 v[8:9], v[122:123], v[132:133]
	ds_write2_b64 v76, v[30:31], v[32:33] offset1:34
	ds_write2_b64 v76, v[18:19], v[24:25] offset0:68 offset1:102
	ds_write2_b64 v76, v[6:7], v[14:15] offset0:136 offset1:170
	ds_write2_b64 v76, v[2:3], v[10:11] offset0:204 offset1:238
	ds_write2_b64 v134, v[26:27], v[28:29] offset0:16 offset1:50
	ds_write2_b64 v134, v[4:5], v[16:17] offset0:84 offset1:118
	ds_write2_b64 v134, v[20:21], v[22:23] offset0:152 offset1:186
	ds_write2_b64 v134, v[8:9], v[34:35] offset0:220 offset1:254
	s_waitcnt lgkmcnt(0)
	s_barrier
; template <int R, class XT, class TWT>
; __device__ __forceinline__ void dif_task(XT X, TWT tw, int s, int task) {
;     const int lgM = 13 - s, lgq = lgM - R, q = 1 << lgq;
;     const int j0 = task & (q - 1), blk = task >> lgq, base = (blk << lgM) + j0;
;     const int pb = PADI(base), qp = (q >= 32) ? q + (q >> 4) : q;
;     f32x2v v[1 << R];
; #pragma unroll
;     for (int k = 0; k < (1 << R); ++k) v[k] = X[pb + k * qp];
; #pragma unroll
;     for (int r = 0; r < R; ++r) {
;         const int pb = R - 1 - r;
; #pragma unroll
;         for (int k = 0; k < (1 << R); ++k) if (!((k >> pb) & 1)) {
;             const int klo = k & ((1 << pb) - 1);
;             const f32x2v w = tw[(j0 + (klo << lgq)) << (s + r)];
;             const f32x2v a = v[k], b = v[k + (1 << pb)], d = a - b;
;             v[k] = a + b; v[k + (1 << pb)] = (f32x2v){d.x * w.x - d.y * w.y, d.x * w.y + d.y * w.x};
;         }
;     }
; #pragma unroll
;     for (int k = 0; k < (1 << R); ++k) X[pb + k * qp] = v[k];
; }
	ds_read2_b64 v[2:5], v77 offset1:2
	ds_read2_b64 v[6:9], v77 offset0:4 offset1:6
	ds_read2_b64 v[10:13], v77 offset0:8 offset1:10
	ds_read2_b64 v[14:17], v77 offset0:12 offset1:14
	ds_read2_b64 v[18:21], v77 offset0:16 offset1:18
	ds_read2_b64 v[22:25], v77 offset0:20 offset1:22
	ds_read2_b64 v[26:29], v77 offset0:24 offset1:26
	ds_read2_b64 v[30:33], v77 offset0:28 offset1:30
	ds_read2st64_b64 v[94:97], v88 offset1:16
	ds_read_b64 v[34:35], v89
	ds_read_b64 v[98:99], v90
	ds_read_b64 v[100:101], v91
	ds_read_b64 v[102:103], v43
	s_waitcnt lgkmcnt(8)
	v_pk_add_f32 v[110:111], v[2:3], v[18:19] neg_lo:[0,1] neg_hi:[0,1]
	ds_read_b64 v[104:105], v92
	ds_read_b64 v[106:107], v93
	ds_read_b64 v[108:109], v108
	s_waitcnt lgkmcnt(7)
	v_pk_mul_f32 v[112:113], v[110:111], v[94:95] op_sel:[1,1] op_sel_hi:[1,0]
	v_pk_add_f32 v[2:3], v[2:3], v[18:19]
	v_pk_fma_f32 v[114:115], v[110:111], v[94:95], v[112:113] op_sel_hi:[0,1,1] neg_lo:[0,0,1]
	v_pk_add_f32 v[110:111], v[10:11], v[26:27] neg_lo:[0,1] neg_hi:[0,1]
	v_pk_add_f32 v[10:11], v[10:11], v[26:27]
	v_pk_mul_f32 v[112:113], v[110:111], v[94:95] op_sel:[1,0] op_sel_hi:[0,0]
	v_pk_fma_f32 v[116:117], v[110:111], v[94:95], v[112:113] op_sel:[0,1,0] neg_hi:[0,0,1]
	v_pk_add_f32 v[18:19], v[2:3], v[10:11]
	v_pk_add_f32 v[94:95], v[114:115], v[116:117] neg_lo:[0,1] neg_hi:[0,1]
	v_pk_add_f32 v[2:3], v[2:3], v[10:11] neg_lo:[0,1] neg_hi:[0,1]
	s_waitcnt lgkmcnt(4)
	v_pk_mul_f32 v[110:111], v[100:101], v[94:95] op_sel:[1,1] op_sel_hi:[0,1]
	v_pk_fma_f32 v[112:113], v[100:101], v[94:95], v[110:111] op_sel_hi:[1,0,1] neg_lo:[0,0,1]
	v_pk_mul_f32 v[10:11], v[2:3], v[100:101] op_sel:[1,1] op_sel_hi:[1,0]
	v_pk_add_f32 v[94:95], v[6:7], v[22:23] neg_lo:[0,1] neg_hi:[0,1]
	v_pk_add_f32 v[6:7], v[6:7], v[22:23]
	v_pk_mul_f32 v[110:111], v[94:95], v[96:97] op_sel:[1,1] op_sel_hi:[1,0]
	s_nop 0
	v_pk_fma_f32 v[118:119], v[94:95], v[96:97], v[110:111] op_sel_hi:[0,1,1] neg_lo:[0,0,1]
	v_pk_add_f32 v[94:95], v[14:15], v[30:31] neg_lo:[0,1] neg_hi:[0,1]
	v_pk_add_f32 v[14:15], v[14:15], v[30:31]
	v_pk_mul_f32 v[110:111], v[94:95], v[96:97] op_sel:[1,0] op_sel_hi:[0,0]
	v_pk_fma_f32 v[120:121], v[94:95], v[96:97], v[110:111] op_sel:[0,1,0] neg_hi:[0,0,1]
	v_pk_add_f32 v[22:23], v[6:7], v[14:15]
	v_pk_add_f32 v[94:95], v[118:119], v[120:121] neg_lo:[0,1] neg_hi:[0,1]
	v_pk_add_f32 v[26:27], v[18:19], v[22:23]
	v_pk_mul_f32 v[96:97], v[100:101], v[94:95] op_sel_hi:[0,1]
	v_pk_fma_f32 v[110:111], v[100:101], v[94:95], v[96:97] op_sel:[1,0,1] op_sel_hi:[1,1,0] neg_hi:[0,0,1]
	v_pk_add_f32 v[18:19], v[18:19], v[22:23] neg_lo:[0,1] neg_hi:[0,1]
	v_pk_add_f32 v[94:95], v[112:113], v[110:111] neg_lo:[0,1] neg_hi:[0,1]
	s_waitcnt lgkmcnt(1)
	v_pk_mul_f32 v[22:23], v[18:19], v[106:107] op_sel:[1,1] op_sel_hi:[1,0]
	v_pk_mul_f32 v[96:97], v[106:107], v[94:95] op_sel:[1,1] op_sel_hi:[0,1]
	v_pk_fma_f32 v[122:123], v[106:107], v[94:95], v[96:97] op_sel_hi:[1,0,1] neg_lo:[0,0,1]
	s_nop 0
	v_pk_add_f32 v[94:95], v[4:5], v[20:21] neg_lo:[0,1] neg_hi:[0,1]
	v_pk_add_f32 v[4:5], v[4:5], v[20:21]
	v_pk_mul_f32 v[96:97], v[94:95], v[34:35] op_sel:[1,1] op_sel_hi:[1,0]
	s_nop 0
	v_pk_fma_f32 v[124:125], v[94:95], v[34:35], v[96:97] op_sel_hi:[0,1,1] neg_lo:[0,0,1]
	v_pk_add_f32 v[94:95], v[12:13], v[28:29] neg_lo:[0,1] neg_hi:[0,1]
	v_pk_add_f32 v[12:13], v[12:13], v[28:29]
	v_pk_mul_f32 v[96:97], v[94:95], v[34:35] op_sel:[1,0] op_sel_hi:[0,0]
	v_pk_fma_f32 v[126:127], v[94:95], v[34:35], v[96:97] op_sel:[0,1,0] neg_hi:[0,0,1]
	v_pk_add_f32 v[20:21], v[4:5], v[12:13]
	v_pk_add_f32 v[34:35], v[124:125], v[126:127] neg_lo:[0,1] neg_hi:[0,1]
	v_pk_add_f32 v[4:5], v[4:5], v[12:13] neg_lo:[0,1] neg_hi:[0,1]
	v_pk_mul_f32 v[94:95], v[104:105], v[34:35] op_sel:[1,1] op_sel_hi:[0,1]
	v_pk_fma_f32 v[96:97], v[104:105], v[34:35], v[94:95] op_sel_hi:[1,0,1] neg_lo:[0,0,1]
	s_nop 0
	v_pk_add_f32 v[34:35], v[8:9], v[24:25] neg_lo:[0,1] neg_hi:[0,1]
	v_pk_add_f32 v[8:9], v[8:9], v[24:25]
	v_pk_mul_f32 v[94:95], v[34:35], v[98:99] op_sel:[1,1] op_sel_hi:[1,0]
	s_nop 0
	v_pk_fma_f32 v[128:129], v[34:35], v[98:99], v[94:95] op_sel_hi:[0,1,1] neg_lo:[0,0,1]
	v_pk_add_f32 v[34:35], v[16:17], v[32:33] neg_lo:[0,1] neg_hi:[0,1]
	v_pk_add_f32 v[16:17], v[16:17], v[32:33]
	v_pk_mul_f32 v[94:95], v[34:35], v[98:99] op_sel:[1,0] op_sel_hi:[0,0]
	v_pk_fma_f32 v[130:131], v[34:35], v[98:99], v[94:95] op_sel:[0,1,0] neg_hi:[0,0,1]
	v_pk_add_f32 v[24:25], v[8:9], v[16:17]
	v_pk_add_f32 v[34:35], v[128:129], v[130:131] neg_lo:[0,1] neg_hi:[0,1]
	v_pk_add_f32 v[28:29], v[20:21], v[24:25]
	v_pk_mul_f32 v[94:95], v[102:103], v[34:35] op_sel_hi:[0,1]
	v_pk_fma_f32 v[98:99], v[102:103], v[34:35], v[94:95] op_sel:[1,0,1] op_sel_hi:[1,1,0] neg_hi:[0,0,1]
	v_pk_add_f32 v[30:31], v[26:27], v[28:29]
	v_pk_add_f32 v[34:35], v[96:97], v[98:99] neg_lo:[0,1] neg_hi:[0,1]
	v_pk_add_f32 v[26:27], v[26:27], v[28:29] neg_lo:[0,1] neg_hi:[0,1]
	v_pk_mul_f32 v[94:95], v[106:107], v[34:35] op_sel_hi:[0,1]
	v_pk_fma_f32 v[132:133], v[106:107], v[34:35], v[94:95] op_sel:[1,0,1] op_sel_hi:[1,1,0] neg_hi:[0,0,1]
	s_waitcnt lgkmcnt(0)
; template <int R, class XT, class TWT>
; __device__ __forceinline__ void dif_task(XT X, TWT tw, int s, int task) {
;     const int lgM = 13 - s, lgq = lgM - R, q = 1 << lgq;
;     const int j0 = task & (q - 1), blk = task >> lgq, base = (blk << lgM) + j0;
;     const int pb = PADI(base), qp = (q >= 32) ? q + (q >> 4) : q;
;     f32x2v v[1 << R];
; #pragma unroll
;     for (int k = 0; k < (1 << R); ++k) v[k] = X[pb + k * qp];
; #pragma unroll
;     for (int r = 0; r < R; ++r) {
;         const int pb = R - 1 - r;
; #pragma unroll
;         for (int k = 0; k < (1 << R); ++k) if (!((k >> pb) & 1)) {
;             const int klo = k & ((1 << pb) - 1);
;             const f32x2v w = tw[(j0 + (klo << lgq)) << (s + r)];
;             const f32x2v a = v[k], b = v[k + (1 << pb)], d = a - b;
;             v[k] = a + b; v[k + (1 << pb)] = (f32x2v){d.x * w.x - d.y * w.y, d.x * w.y + d.y * w.x};
;         }
;     }
; #pragma unroll
;     for (int k = 0; k < (1 << R); ++k) X[pb + k * qp] = v[k];
; }
; __device__ __forceinline__ void phase_spectra(Frame& F0, int l) {
;     ...
;         fft_fwd_upper(X, tw, 13 - lgN, F.tid);
;         f32x2v* SP = (f32x2v*)(F.ws + (lat ? WS_SPEC : WS_SPECC)) + (size_t)col0 * N; const float sc = 1.0f / (float)N;
	v_xor_b32_e32 v94, 0x80000000, v108
	v_cndmask_b32_e64 v95, v94, v109, s[40:41]
	v_cndmask_b32_e64 v94, v109, v108, s[40:41]
	v_pk_mul_f32 v[28:29], v[26:27], v[94:95] op_sel:[1,1] op_sel_hi:[1,0]
	s_nop 0
	v_pk_fma_f32 v[32:33], v[26:27], v[94:95], v[28:29] op_sel_hi:[0,1,1] neg_lo:[0,0,1]
	v_pk_fma_f32 v[26:27], v[18:19], v[106:107], v[22:23] op_sel_hi:[0,1,1] neg_lo:[0,0,1]
	v_pk_add_f32 v[18:19], v[20:21], v[24:25] neg_lo:[0,1] neg_hi:[0,1]
	v_pk_add_f32 v[34:35], v[122:123], v[132:133] neg_lo:[0,1] neg_hi:[0,1]
	v_pk_mul_f32 v[20:21], v[18:19], v[106:107] op_sel_hi:[1,0]
	s_nop 0
	v_pk_fma_f32 v[22:23], v[18:19], v[106:107], v[20:21] op_sel:[0,1,1] op_sel_hi:[1,1,0] neg_hi:[0,0,1]
	s_nop 0
	v_pk_add_f32 v[20:21], v[26:27], v[22:23] neg_lo:[0,1] neg_hi:[0,1]
	v_pk_add_f32 v[18:19], v[26:27], v[22:23]
	v_pk_mul_f32 v[22:23], v[94:95], v[20:21] op_sel:[1,1] op_sel_hi:[0,1]
	v_pk_fma_f32 v[24:25], v[94:95], v[20:21], v[22:23] op_sel_hi:[1,0,1] neg_lo:[0,0,1]
	s_nop 0
	v_pk_fma_f32 v[20:21], v[2:3], v[100:101], v[10:11] op_sel_hi:[0,1,1] neg_lo:[0,0,1]
	v_pk_add_f32 v[2:3], v[6:7], v[14:15] neg_lo:[0,1] neg_hi:[0,1]
	s_nop 0
	v_pk_mul_f32 v[6:7], v[2:3], v[100:101] op_sel_hi:[1,0]
	s_nop 0
	v_pk_fma_f32 v[10:11], v[2:3], v[100:101], v[6:7] op_sel:[0,1,1] op_sel_hi:[1,1,0] neg_hi:[0,0,1]
	v_pk_mul_f32 v[6:7], v[4:5], v[104:105] op_sel:[1,1] op_sel_hi:[1,0]
	s_nop 0
	v_pk_fma_f32 v[12:13], v[4:5], v[104:105], v[6:7] op_sel_hi:[0,1,1] neg_lo:[0,0,1]
	v_pk_add_f32 v[4:5], v[8:9], v[16:17] neg_lo:[0,1] neg_hi:[0,1]
	v_pk_add_f32 v[2:3], v[20:21], v[10:11]
	v_pk_mul_f32 v[6:7], v[4:5], v[102:103] op_sel_hi:[1,0]
	v_pk_add_f32 v[16:17], v[124:125], v[126:127]
	v_pk_fma_f32 v[8:9], v[4:5], v[102:103], v[6:7] op_sel:[0,1,1] op_sel_hi:[1,1,0] neg_hi:[0,0,1]
	s_nop 0
	v_pk_add_f32 v[4:5], v[12:13], v[8:9]
	s_nop 0
	v_pk_add_f32 v[6:7], v[2:3], v[4:5]
	v_pk_add_f32 v[2:3], v[2:3], v[4:5] neg_lo:[0,1] neg_hi:[0,1]
	s_nop 0
	v_pk_mul_f32 v[4:5], v[94:95], v[2:3] op_sel:[1,1] op_sel_hi:[0,1]
	v_pk_fma_f32 v[14:15], v[94:95], v[2:3], v[4:5] op_sel_hi:[1,0,1] neg_lo:[0,0,1]
	s_nop 0
	v_pk_add_f32 v[2:3], v[20:21], v[10:11] neg_lo:[0,1] neg_hi:[0,1]
	v_pk_add_f32 v[20:21], v[128:129], v[130:131]
	v_pk_mul_f32 v[4:5], v[106:107], v[2:3] op_sel:[1,1] op_sel_hi:[0,1]
	v_pk_fma_f32 v[10:11], v[106:107], v[2:3], v[4:5] op_sel_hi:[1,0,1] neg_lo:[0,0,1]
	v_pk_add_f32 v[22:23], v[16:17], v[20:21]
	v_pk_add_f32 v[2:3], v[12:13], v[8:9] neg_lo:[0,1] neg_hi:[0,1]
	s_nop 0
	v_pk_mul_f32 v[4:5], v[106:107], v[2:3] op_sel_hi:[0,1]
	v_pk_fma_f32 v[8:9], v[106:107], v[2:3], v[4:5] op_sel:[1,0,1] op_sel_hi:[1,1,0] neg_hi:[0,0,1]
	s_nop 0
	v_pk_add_f32 v[4:5], v[10:11], v[8:9] neg_lo:[0,1] neg_hi:[0,1]
	v_pk_add_f32 v[2:3], v[10:11], v[8:9]
	v_pk_mul_f32 v[8:9], v[94:95], v[4:5] op_sel:[1,1] op_sel_hi:[0,1]
	v_pk_fma_f32 v[10:11], v[94:95], v[4:5], v[8:9] op_sel_hi:[1,0,1] neg_lo:[0,0,1]
	v_pk_add_f32 v[8:9], v[118:119], v[120:121]
	v_pk_add_f32 v[4:5], v[114:115], v[116:117]
	s_nop 0
	v_pk_add_f32 v[12:13], v[4:5], v[8:9]
	v_pk_add_f32 v[4:5], v[4:5], v[8:9] neg_lo:[0,1] neg_hi:[0,1]
	v_pk_add_f32 v[26:27], v[12:13], v[22:23]
	v_pk_add_f32 v[12:13], v[12:13], v[22:23] neg_lo:[0,1] neg_hi:[0,1]
	v_pk_mul_f32 v[8:9], v[106:107], v[4:5] op_sel:[1,1] op_sel_hi:[0,1]
	v_pk_mul_f32 v[22:23], v[12:13], v[94:95] op_sel:[1,1] op_sel_hi:[1,0]
	s_nop 0
	v_pk_fma_f32 v[28:29], v[12:13], v[94:95], v[22:23] op_sel_hi:[0,1,1] neg_lo:[0,0,1]
	v_pk_fma_f32 v[12:13], v[106:107], v[4:5], v[8:9] op_sel_hi:[1,0,1] neg_lo:[0,0,1]
	s_nop 0
	v_pk_add_f32 v[4:5], v[16:17], v[20:21] neg_lo:[0,1] neg_hi:[0,1]
	s_nop 0
	v_pk_mul_f32 v[8:9], v[106:107], v[4:5] op_sel_hi:[0,1]
	v_pk_fma_f32 v[16:17], v[106:107], v[4:5], v[8:9] op_sel:[1,0,1] op_sel_hi:[1,1,0] neg_hi:[0,0,1]
	s_nop 0
	v_pk_add_f32 v[8:9], v[12:13], v[16:17] neg_lo:[0,1] neg_hi:[0,1]
	v_pk_add_f32 v[4:5], v[12:13], v[16:17]
	v_pk_mul_f32 v[12:13], v[94:95], v[8:9] op_sel:[1,1] op_sel_hi:[0,1]
	v_pk_fma_f32 v[16:17], v[94:95], v[8:9], v[12:13] op_sel_hi:[1,0,1] neg_lo:[0,0,1]
	v_pk_add_f32 v[12:13], v[96:97], v[98:99]
	v_pk_add_f32 v[8:9], v[112:113], v[110:111]
	s_nop 0
	v_pk_add_f32 v[20:21], v[8:9], v[12:13]
	v_pk_add_f32 v[8:9], v[8:9], v[12:13] neg_lo:[0,1] neg_hi:[0,1]
	s_nop 0
	v_pk_mul_f32 v[12:13], v[94:95], v[8:9] op_sel:[1,1] op_sel_hi:[0,1]
	v_pk_fma_f32 v[22:23], v[94:95], v[8:9], v[12:13] op_sel_hi:[1,0,1] neg_lo:[0,0,1]
	v_pk_mul_f32 v[12:13], v[94:95], v[34:35] op_sel:[1,1] op_sel_hi:[0,1]
	v_pk_fma_f32 v[96:97], v[94:95], v[34:35], v[12:13] neg_lo:[0,0,1] neg_hi:[0,0,1]
	v_pk_fma_f32 v[12:13], v[94:95], v[34:35], v[12:13] op_sel_hi:[1,0,1]
	v_pk_add_f32 v[8:9], v[122:123], v[132:133]
	v_mov_b32_e32 v97, v13
	ds_write2_b64 v77, v[30:31], v[32:33] offset1:2
	ds_write2_b64 v77, v[18:19], v[24:25] offset0:4 offset1:6
	ds_write2_b64 v77, v[6:7], v[14:15] offset0:8 offset1:10
	ds_write2_b64 v77, v[2:3], v[10:11] offset0:12 offset1:14
	ds_write2_b64 v77, v[26:27], v[28:29] offset0:16 offset1:18
	ds_write2_b64 v77, v[4:5], v[16:17] offset0:20 offset1:22
	ds_write2_b64 v77, v[20:21], v[22:23] offset0:24 offset1:26
	ds_write2_b64 v77, v[8:9], v[96:97] offset0:28 offset1:30
	v_cvt_f32_u32_e32 v2, s12
	s_waitcnt lgkmcnt(0)
	s_barrier
	v_div_scale_f32 v3, s[2:3], v2, v2, 1.0
	v_rcp_f32_e32 v4, v3
	s_mov_b32 s2, 0
	v_fma_f32 v5, -v3, v4, 1.0
	v_fmac_f32_e32 v4, v5, v4
	v_div_scale_f32 v5, vcc, 1.0, v2, 1.0
	v_mul_f32_e32 v6, v5, v4
	v_fma_f32 v7, -v3, v6, v5
	v_fmac_f32_e32 v6, v7, v4
	v_fma_f32 v3, -v3, v6, v5
	v_div_fmas_f32 v3, v3, v4, v6
	v_div_fixup_f32 v2, v3, v2, 1.0
	v_mov_b32_e32 v4, v2
	v_mov_b32_e32 v5, v2
	v_mov_b32_e32 v6, v78

; template <int R, class XT, class TWT>
; __device__ __forceinline__ void dif_task(XT X, TWT tw, int s, int task) {
;     const int lgM = 13 - s, lgq = lgM - R, q = 1 << lgq;
;     const int j0 = task & (q - 1), blk = task >> lgq, base = (blk << lgM) + j0;
;     const int pb = PADI(base), qp = (q >= 32) ? q + (q >> 4) : q;
;     f32x2v v[1 << R];
; #pragma unroll
;     for (int k = 0; k < (1 << R); ++k) v[k] = X[pb + k * qp];
; #pragma unroll
;     for (int r = 0; r < R; ++r) {
;         const int pb = R - 1 - r;
; #pragma unroll
;         for (int k = 0; k < (1 << R); ++k) if (!((k >> pb) & 1)) {
;             const int klo = k & ((1 << pb) - 1);
;             const f32x2v w = tw[(j0 + (klo << lgq)) << (s + r)];
;             const f32x2v a = v[k], b = v[k + (1 << pb)], d = a - b;
;             v[k] = a + b; v[k + (1 << pb)] = (f32x2v){d.x * w.x - d.y * w.y, d.x * w.y + d.y * w.x};
;         }
;     }
; #pragma unroll
;     for (int k = 0; k < (1 << R); ++k) X[pb + k * qp] = v[k];
; }
; template <bool LAT>
; __device__ __forceinline__ void hyconv_unit(const Frame& F, LAS f32x2v* X, const TwHalf tw, LAS bf16* OUT, const float* skip, bf16* MIX, int u) {
;     ...
;             const f32x2v* SP = SPb + (size_t)ord * 256 * N;
;             f32x4 kq[8];
; #pragma unroll
;             for (int r = 0; r < 8; ++r) kq[r] = *(const f32x4*)(SP + 2 * (F.tid + 512 * r));
;             fft_fwd_upper(X, tw, 13 - lgN, F.tid);
.LBB0_780:
	s_lshl_b32 s90, s0, 21
	s_xor_b64 s[20:21], s[22:23], -1
	s_lshl_b64 s[2:3], s[90:91], 3
	s_add_u32 s2, s29, s2
	s_addc_u32 s3, s52, s3
	v_lshl_add_u64 v[0:1], v[34:35], 3, s[2:3]
	v_lshl_add_u64 v[2:3], v[36:37], 3, s[2:3]
	global_load_dwordx4 v[28:31], v[0:1], off
	global_load_dwordx4 v[24:27], v[2:3], off
	v_lshl_add_u64 v[0:1], v[38:39], 3, s[2:3]
	v_lshl_add_u64 v[2:3], v[40:41], 3, s[2:3]
	global_load_dwordx4 v[20:23], v[0:1], off
	global_load_dwordx4 v[16:19], v[2:3], off
	v_lshl_add_u64 v[0:1], v[42:43], 3, s[2:3]
	v_lshl_add_u64 v[2:3], v[44:45], 3, s[2:3]
	global_load_dwordx4 v[12:15], v[0:1], off
	global_load_dwordx4 v[8:11], v[2:3], off
	v_lshl_add_u64 v[0:1], v[46:47], 3, s[2:3]
	v_lshl_add_u64 v[2:3], v[48:49], 3, s[2:3]
	global_load_dwordx4 v[4:7], v[0:1], off
	s_nop 0
	global_load_dwordx4 v[0:3], v[2:3], off
	ds_read_b64 v[110:111], v75
	ds_read_b64 v[120:121], v75 offset:4352
	ds_read_b64 v[122:123], v75 offset:8704
	ds_read_b64 v[124:125], v75 offset:13056
	ds_read_b64 v[126:127], v75 offset:17408
	ds_read_b64 v[128:129], v75 offset:21760
	ds_read_b64 v[130:131], v75 offset:26112
	ds_read_b64 v[132:133], v75 offset:30464
	ds_read_b64 v[136:137], v75 offset:34816
	ds_read_b64 v[138:139], v75 offset:39168
	ds_read_b64 v[140:141], v75 offset:43520
	ds_read_b64 v[142:143], v75 offset:47872
	ds_read_b64 v[144:145], v75 offset:52224
	ds_read_b64 v[146:147], v75 offset:56576
	ds_read_b64 v[148:149], v75 offset:60928
	ds_read_b64 v[150:151], v75 offset:65280
	ds_read2st64_b64 v[116:119], v76 offset1:16
	ds_read_b64 v[152:153], v91
	ds_read_b64 v[154:155], v92
	ds_read_b64 v[156:157], v93
	ds_read_b64 v[158:159], v77
	ds_read_b64 v[160:161], v78
	ds_read_b64 v[162:163], v79
	ds_read_b64 v[164:165], v80
	s_waitcnt lgkmcnt(14)
	v_pk_add_f32 v[166:167], v[110:111], v[136:137] neg_lo:[0,1] neg_hi:[0,1]
	v_pk_add_f32 v[110:111], v[110:111], v[136:137]
	s_waitcnt lgkmcnt(7)
	v_pk_mul_f32 v[168:169], v[166:167], v[116:117] op_sel:[1,1] op_sel_hi:[1,0]
	s_lshl_b32 s0, s0, 8
	v_pk_fma_f32 v[170:171], v[166:167], v[116:117], v[168:169] op_sel_hi:[0,1,1] neg_lo:[0,0,1]
	v_pk_add_f32 v[166:167], v[126:127], v[144:145] neg_lo:[0,1] neg_hi:[0,1]
	v_pk_add_f32 v[126:127], v[126:127], v[144:145]
	v_pk_mul_f32 v[168:169], v[166:167], v[116:117] op_sel:[1,0] op_sel_hi:[0,0]
	v_pk_fma_f32 v[172:173], v[166:167], v[116:117], v[168:169] op_sel:[0,1,0] neg_hi:[0,0,1]
	v_pk_add_f32 v[136:137], v[110:111], v[126:127]
	v_pk_add_f32 v[116:117], v[170:171], v[172:173] neg_lo:[0,1] neg_hi:[0,1]
	v_pk_add_f32 v[110:111], v[110:111], v[126:127] neg_lo:[0,1] neg_hi:[0,1]
	s_waitcnt lgkmcnt(6)
	v_pk_mul_f32 v[166:167], v[152:153], v[116:117] op_sel:[1,1] op_sel_hi:[0,1]
	v_pk_fma_f32 v[168:169], v[152:153], v[116:117], v[166:167] op_sel_hi:[1,0,1] neg_lo:[0,0,1]
	v_pk_mul_f32 v[126:127], v[110:111], v[152:153] op_sel:[1,1] op_sel_hi:[1,0]
	v_pk_add_f32 v[116:117], v[122:123], v[140:141] neg_lo:[0,1] neg_hi:[0,1]
	v_pk_add_f32 v[122:123], v[122:123], v[140:141]
	v_pk_mul_f32 v[166:167], v[116:117], v[118:119] op_sel:[1,1] op_sel_hi:[1,0]
	s_add_i32 s90, s0, s28
	v_pk_fma_f32 v[174:175], v[116:117], v[118:119], v[166:167] op_sel_hi:[0,1,1] neg_lo:[0,0,1]
	v_pk_add_f32 v[116:117], v[130:131], v[148:149] neg_lo:[0,1] neg_hi:[0,1]
	v_pk_add_f32 v[130:131], v[130:131], v[148:149]
	v_pk_mul_f32 v[166:167], v[116:117], v[118:119] op_sel:[1,0] op_sel_hi:[0,0]
	v_pk_fma_f32 v[176:177], v[116:117], v[118:119], v[166:167] op_sel:[0,1,0] neg_hi:[0,0,1]
	v_pk_add_f32 v[140:141], v[122:123], v[130:131]
	v_pk_add_f32 v[116:117], v[174:175], v[176:177] neg_lo:[0,1] neg_hi:[0,1]
	v_pk_add_f32 v[144:145], v[136:137], v[140:141]
	v_pk_mul_f32 v[118:119], v[152:153], v[116:117] op_sel_hi:[0,1]
	v_pk_fma_f32 v[166:167], v[152:153], v[116:117], v[118:119] op_sel:[1,0,1] op_sel_hi:[1,1,0] neg_hi:[0,0,1]
	v_pk_add_f32 v[136:137], v[136:137], v[140:141] neg_lo:[0,1] neg_hi:[0,1]
	v_pk_add_f32 v[116:117], v[168:169], v[166:167] neg_lo:[0,1] neg_hi:[0,1]
	s_waitcnt lgkmcnt(4)
	v_pk_mul_f32 v[140:141], v[136:137], v[156:157] op_sel:[1,1] op_sel_hi:[1,0]
	v_pk_mul_f32 v[118:119], v[156:157], v[116:117] op_sel:[1,1] op_sel_hi:[0,1]
	v_pk_fma_f32 v[178:179], v[156:157], v[116:117], v[118:119] op_sel_hi:[1,0,1] neg_lo:[0,0,1]
	s_lshl_b64 s[0:1], s[90:91], 2
	v_pk_add_f32 v[116:117], v[120:121], v[138:139] neg_lo:[0,1] neg_hi:[0,1]
	v_pk_add_f32 v[120:121], v[120:121], v[138:139]
	s_waitcnt lgkmcnt(3)
	v_pk_mul_f32 v[118:119], v[116:117], v[158:159] op_sel:[1,1] op_sel_hi:[1,0]
	s_add_u32 s0, s6, s0
	v_pk_fma_f32 v[182:183], v[116:117], v[158:159], v[118:119] op_sel_hi:[0,1,1] neg_lo:[0,0,1]
	v_pk_add_f32 v[116:117], v[128:129], v[146:147] neg_lo:[0,1] neg_hi:[0,1]
	v_pk_add_f32 v[128:129], v[128:129], v[146:147]
	v_pk_mul_f32 v[118:119], v[116:117], v[158:159] op_sel:[1,0] op_sel_hi:[0,0]
	v_pk_fma_f32 v[184:185], v[116:117], v[158:159], v[118:119] op_sel:[0,1,0] neg_hi:[0,0,1]
	v_pk_add_f32 v[138:139], v[120:121], v[128:129]
	v_pk_add_f32 v[116:117], v[182:183], v[184:185] neg_lo:[0,1] neg_hi:[0,1]
	v_pk_add_f32 v[120:121], v[120:121], v[128:129] neg_lo:[0,1] neg_hi:[0,1]
	v_pk_mul_f32 v[118:119], v[154:155], v[116:117] op_sel:[1,1] op_sel_hi:[0,1]
	v_pk_fma_f32 v[158:159], v[154:155], v[116:117], v[118:119] op_sel_hi:[1,0,1] neg_lo:[0,0,1]
	s_addc_u32 s1, s7, s1
	v_pk_add_f32 v[116:117], v[124:125], v[142:143] neg_lo:[0,1] neg_hi:[0,1]
	v_pk_add_f32 v[124:125], v[124:125], v[142:143]
	s_waitcnt lgkmcnt(2)
; template <int R, class XT, class TWT>
; __device__ __forceinline__ void dif_task(XT X, TWT tw, int s, int task) {
;     const int lgM = 13 - s, lgq = lgM - R, q = 1 << lgq;
;     const int j0 = task & (q - 1), blk = task >> lgq, base = (blk << lgM) + j0;
;     const int pb = PADI(base), qp = (q >= 32) ? q + (q >> 4) : q;
;     f32x2v v[1 << R];
; #pragma unroll
;     for (int k = 0; k < (1 << R); ++k) v[k] = X[pb + k * qp];
; #pragma unroll
;     for (int r = 0; r < R; ++r) {
;         const int pb = R - 1 - r;
; #pragma unroll
;         for (int k = 0; k < (1 << R); ++k) if (!((k >> pb) & 1)) {
;             const int klo = k & ((1 << pb) - 1);
;             const f32x2v w = tw[(j0 + (klo << lgq)) << (s + r)];
;             const f32x2v a = v[k], b = v[k + (1 << pb)], d = a - b;
;             v[k] = a + b; v[k + (1 << pb)] = (f32x2v){d.x * w.x - d.y * w.y, d.x * w.y + d.y * w.x};
;         }
;     }
; #pragma unroll
;     for (int k = 0; k < (1 << R); ++k) X[pb + k * qp] = v[k];
; }
	v_pk_mul_f32 v[118:119], v[116:117], v[160:161] op_sel:[1,1] op_sel_hi:[1,0]
	s_lshl_b64 s[2:3], s[90:91], 13
	v_pk_fma_f32 v[186:187], v[116:117], v[160:161], v[118:119] op_sel_hi:[0,1,1] neg_lo:[0,0,1]
	v_pk_add_f32 v[116:117], v[132:133], v[150:151] neg_lo:[0,1] neg_hi:[0,1]
	v_pk_add_f32 v[132:133], v[132:133], v[150:151]
	v_pk_mul_f32 v[118:119], v[116:117], v[160:161] op_sel:[1,0] op_sel_hi:[0,0]
	v_pk_fma_f32 v[188:189], v[116:117], v[160:161], v[118:119] op_sel:[0,1,0] neg_hi:[0,0,1]
	v_pk_add_f32 v[142:143], v[124:125], v[132:133]
	v_pk_add_f32 v[116:117], v[186:187], v[188:189] neg_lo:[0,1] neg_hi:[0,1]
	v_pk_add_f32 v[146:147], v[138:139], v[142:143]
	s_waitcnt lgkmcnt(1)
	v_pk_mul_f32 v[118:119], v[162:163], v[116:117] op_sel_hi:[0,1]
	v_pk_fma_f32 v[160:161], v[162:163], v[116:117], v[118:119] op_sel:[1,0,1] op_sel_hi:[1,1,0] neg_hi:[0,0,1]
	v_pk_add_f32 v[148:149], v[144:145], v[146:147]
	v_pk_add_f32 v[116:117], v[158:159], v[160:161] neg_lo:[0,1] neg_hi:[0,1]
	v_pk_add_f32 v[144:145], v[144:145], v[146:147] neg_lo:[0,1] neg_hi:[0,1]
	v_pk_mul_f32 v[118:119], v[156:157], v[116:117] op_sel_hi:[0,1]
	v_pk_fma_f32 v[190:191], v[156:157], v[116:117], v[118:119] op_sel:[1,0,1] op_sel_hi:[1,1,0] neg_hi:[0,0,1]
	s_waitcnt lgkmcnt(0)
	v_xor_b32_e32 v118, 0x80000000, v164
	v_cndmask_b32_e64 v119, v118, v165, s[38:39]
	v_cndmask_b32_e64 v118, v165, v164, s[38:39]
	v_pk_mul_f32 v[146:147], v[144:145], v[118:119] op_sel:[1,1] op_sel_hi:[1,0]
	s_nop 0
	v_pk_fma_f32 v[150:151], v[144:145], v[118:119], v[146:147] op_sel_hi:[0,1,1] neg_lo:[0,0,1]
	v_pk_fma_f32 v[144:145], v[136:137], v[156:157], v[140:141] op_sel_hi:[0,1,1] neg_lo:[0,0,1]
	v_pk_add_f32 v[136:137], v[138:139], v[142:143] neg_lo:[0,1] neg_hi:[0,1]
	v_pk_add_f32 v[116:117], v[178:179], v[190:191] neg_lo:[0,1] neg_hi:[0,1]
	v_pk_mul_f32 v[138:139], v[136:137], v[156:157] op_sel_hi:[1,0]
	s_nop 0
	v_pk_fma_f32 v[140:141], v[136:137], v[156:157], v[138:139] op_sel:[0,1,1] op_sel_hi:[1,1,0] neg_hi:[0,0,1]
	s_nop 0
	v_pk_add_f32 v[138:139], v[144:145], v[140:141] neg_lo:[0,1] neg_hi:[0,1]
	v_pk_add_f32 v[136:137], v[144:145], v[140:141]
	v_pk_mul_f32 v[140:141], v[118:119], v[138:139] op_sel:[1,1] op_sel_hi:[0,1]
	v_pk_fma_f32 v[142:143], v[118:119], v[138:139], v[140:141] op_sel_hi:[1,0,1] neg_lo:[0,0,1]
	s_nop 0
	v_pk_fma_f32 v[138:139], v[110:111], v[152:153], v[126:127] op_sel_hi:[0,1,1] neg_lo:[0,0,1]
	v_pk_add_f32 v[110:111], v[122:123], v[130:131] neg_lo:[0,1] neg_hi:[0,1]
	s_nop 0
	v_pk_mul_f32 v[122:123], v[110:111], v[152:153] op_sel_hi:[1,0]
	s_nop 0
	v_pk_fma_f32 v[126:127], v[110:111], v[152:153], v[122:123] op_sel:[0,1,1] op_sel_hi:[1,1,0] neg_hi:[0,0,1]
	v_pk_mul_f32 v[122:123], v[120:121], v[154:155] op_sel:[1,1] op_sel_hi:[1,0]
	s_nop 0
	v_pk_fma_f32 v[128:129], v[120:121], v[154:155], v[122:123] op_sel_hi:[0,1,1] neg_lo:[0,0,1]
	v_pk_add_f32 v[120:121], v[124:125], v[132:133] neg_lo:[0,1] neg_hi:[0,1]
	v_pk_add_f32 v[110:111], v[138:139], v[126:127]
	v_pk_mul_f32 v[122:123], v[120:121], v[162:163] op_sel_hi:[1,0]
	v_pk_add_f32 v[132:133], v[182:183], v[184:185]
	v_pk_fma_f32 v[124:125], v[120:121], v[162:163], v[122:123] op_sel:[0,1,1] op_sel_hi:[1,1,0] neg_hi:[0,0,1]
	s_nop 0
	v_pk_add_f32 v[120:121], v[128:129], v[124:125]
	s_nop 0
	v_pk_add_f32 v[122:123], v[110:111], v[120:121]
	v_pk_add_f32 v[110:111], v[110:111], v[120:121] neg_lo:[0,1] neg_hi:[0,1]
	s_nop 0
	v_pk_mul_f32 v[120:121], v[118:119], v[110:111] op_sel:[1,1] op_sel_hi:[0,1]
	v_pk_fma_f32 v[130:131], v[118:119], v[110:111], v[120:121] op_sel_hi:[1,0,1] neg_lo:[0,0,1]
	s_nop 0
	v_pk_add_f32 v[110:111], v[138:139], v[126:127] neg_lo:[0,1] neg_hi:[0,1]
	v_pk_add_f32 v[138:139], v[186:187], v[188:189]
	v_pk_mul_f32 v[120:121], v[156:157], v[110:111] op_sel:[1,1] op_sel_hi:[0,1]
	v_pk_fma_f32 v[126:127], v[156:157], v[110:111], v[120:121] op_sel_hi:[1,0,1] neg_lo:[0,0,1]
	v_pk_add_f32 v[140:141], v[132:133], v[138:139]
	v_pk_add_f32 v[110:111], v[128:129], v[124:125] neg_lo:[0,1] neg_hi:[0,1]
	s_nop 0
	v_pk_mul_f32 v[120:121], v[156:157], v[110:111] op_sel_hi:[0,1]
	v_pk_fma_f32 v[124:125], v[156:157], v[110:111], v[120:121] op_sel:[1,0,1] op_sel_hi:[1,1,0] neg_hi:[0,0,1]
	s_nop 0
	v_pk_add_f32 v[120:121], v[126:127], v[124:125] neg_lo:[0,1] neg_hi:[0,1]
	v_pk_add_f32 v[110:111], v[126:127], v[124:125]
	v_pk_mul_f32 v[124:125], v[118:119], v[120:121] op_sel:[1,1] op_sel_hi:[0,1]
	v_pk_fma_f32 v[126:127], v[118:119], v[120:121], v[124:125] op_sel_hi:[1,0,1] neg_lo:[0,0,1]
	v_pk_add_f32 v[124:125], v[174:175], v[176:177]
	v_pk_add_f32 v[120:121], v[170:171], v[172:173]
	s_nop 0
	v_pk_add_f32 v[128:129], v[120:121], v[124:125]
	v_pk_add_f32 v[120:121], v[120:121], v[124:125] neg_lo:[0,1] neg_hi:[0,1]
	v_pk_add_f32 v[144:145], v[128:129], v[140:141]
	v_pk_add_f32 v[128:129], v[128:129], v[140:141] neg_lo:[0,1] neg_hi:[0,1]
	v_pk_mul_f32 v[124:125], v[156:157], v[120:121] op_sel:[1,1] op_sel_hi:[0,1]
	v_pk_mul_f32 v[140:141], v[128:129], v[118:119] op_sel:[1,1] op_sel_hi:[1,0]
	s_nop 0
	v_pk_fma_f32 v[146:147], v[128:129], v[118:119], v[140:141] op_sel_hi:[0,1,1] neg_lo:[0,0,1]
	v_pk_fma_f32 v[128:129], v[156:157], v[120:121], v[124:125] op_sel_hi:[1,0,1] neg_lo:[0,0,1]
	s_nop 0
	v_pk_add_f32 v[120:121], v[132:133], v[138:139] neg_lo:[0,1] neg_hi:[0,1]
	s_nop 0
	v_pk_mul_f32 v[124:125], v[156:157], v[120:121] op_sel_hi:[0,1]
	v_pk_fma_f32 v[132:133], v[156:157], v[120:121], v[124:125] op_sel:[1,0,1] op_sel_hi:[1,1,0] neg_hi:[0,0,1]
	s_nop 0
	v_pk_add_f32 v[124:125], v[128:129], v[132:133] neg_lo:[0,1] neg_hi:[0,1]
	v_pk_add_f32 v[120:121], v[128:129], v[132:133]
	v_pk_mul_f32 v[128:129], v[118:119], v[124:125] op_sel:[1,1] op_sel_hi:[0,1]
; template <int R, class XT, class TWT>
; __device__ __forceinline__ void dif_task(XT X, TWT tw, int s, int task) {
;     const int lgM = 13 - s, lgq = lgM - R, q = 1 << lgq;
;     const int j0 = task & (q - 1), blk = task >> lgq, base = (blk << lgM) + j0;
;     const int pb = PADI(base), qp = (q >= 32) ? q + (q >> 4) : q;
;     f32x2v v[1 << R];
; #pragma unroll
;     for (int k = 0; k < (1 << R); ++k) v[k] = X[pb + k * qp];
; #pragma unroll
;     for (int r = 0; r < R; ++r) {
;         const int pb = R - 1 - r;
; #pragma unroll
;         for (int k = 0; k < (1 << R); ++k) if (!((k >> pb) & 1)) {
;             const int klo = k & ((1 << pb) - 1);
;             const f32x2v w = tw[(j0 + (klo << lgq)) << (s + r)];
;             const f32x2v a = v[k], b = v[k + (1 << pb)], d = a - b;
;             v[k] = a + b; v[k + (1 << pb)] = (f32x2v){d.x * w.x - d.y * w.y, d.x * w.y + d.y * w.x};
;         }
;     }
; #pragma unroll
;     for (int k = 0; k < (1 << R); ++k) X[pb + k * qp] = v[k];
; }
	v_pk_fma_f32 v[132:133], v[118:119], v[124:125], v[128:129] op_sel_hi:[1,0,1] neg_lo:[0,0,1]
	v_pk_add_f32 v[128:129], v[158:159], v[160:161]
	v_pk_add_f32 v[124:125], v[168:169], v[166:167]
	s_nop 0
	v_pk_add_f32 v[138:139], v[124:125], v[128:129]
	v_pk_add_f32 v[124:125], v[124:125], v[128:129] neg_lo:[0,1] neg_hi:[0,1]
	s_nop 0
	v_pk_mul_f32 v[128:129], v[118:119], v[124:125] op_sel:[1,1] op_sel_hi:[0,1]
	v_pk_fma_f32 v[140:141], v[118:119], v[124:125], v[128:129] op_sel_hi:[1,0,1] neg_lo:[0,0,1]
	v_pk_mul_f32 v[128:129], v[118:119], v[116:117] op_sel:[1,1] op_sel_hi:[0,1]
	v_pk_fma_f32 v[152:153], v[118:119], v[116:117], v[128:129] op_sel_hi:[1,0,1] neg_lo:[0,0,1]
	v_pk_add_f32 v[124:125], v[178:179], v[190:191]
	ds_write_b64 v75, v[148:149]
	ds_write_b64 v75, v[150:151] offset:4352
	ds_write_b64 v75, v[136:137] offset:8704
	ds_write_b64 v75, v[142:143] offset:13056
	ds_write_b64 v75, v[122:123] offset:17408
	ds_write_b64 v75, v[130:131] offset:21760
	ds_write_b64 v75, v[110:111] offset:26112
	ds_write_b64 v75, v[126:127] offset:30464
	ds_write_b64 v75, v[144:145] offset:34816
	ds_write_b64 v75, v[146:147] offset:39168
	ds_write_b64 v75, v[120:121] offset:43520
	ds_write_b64 v75, v[132:133] offset:47872
	ds_write_b64 v75, v[138:139] offset:52224
	ds_write_b64 v75, v[140:141] offset:56576
	ds_write_b64 v75, v[124:125] offset:60928
	ds_write_b64 v75, v[152:153] offset:65280
	s_waitcnt lgkmcnt(0)
	s_barrier
	ds_read2_b64 v[116:119], v81 offset1:34
	ds_read2_b64 v[120:123], v81 offset0:68 offset1:102
	ds_read2_b64 v[124:127], v81 offset0:136 offset1:170
	ds_read2_b64 v[128:131], v81 offset0:204 offset1:238
	v_add_u32_e32 v110, 0x800, v81
	ds_read2_b64 v[136:139], v110 offset0:16 offset1:50
	ds_read2_b64 v[140:143], v110 offset0:84 offset1:118
	ds_read2_b64 v[144:147], v110 offset0:152 offset1:186
	ds_read2_b64 v[148:151], v110 offset0:220 offset1:254
	ds_read2st64_b64 v[152:155], v94 offset1:16
	ds_read_b64 v[132:133], v97
	ds_read_b64 v[156:157], v98
	ds_read_b64 v[158:159], v99
	ds_read_b64 v[160:161], v95
	ds_read_b64 v[162:163], v96
	ds_read_b64 v[164:165], v82
	ds_read_b64 v[166:167], v83
	s_waitcnt lgkmcnt(11)
	v_pk_add_f32 v[168:169], v[116:117], v[136:137] neg_lo:[0,1] neg_hi:[0,1]
	v_pk_add_f32 v[116:117], v[116:117], v[136:137]
	s_waitcnt lgkmcnt(7)
	v_pk_mul_f32 v[170:171], v[168:169], v[152:153] op_sel:[1,1] op_sel_hi:[1,0]
	s_waitcnt lgkmcnt(0)
	v_xor_b32_e32 v111, 0x80000000, v166
	v_pk_fma_f32 v[172:173], v[168:169], v[152:153], v[170:171] op_sel_hi:[0,1,1] neg_lo:[0,0,1]
	v_pk_add_f32 v[168:169], v[124:125], v[144:145] neg_lo:[0,1] neg_hi:[0,1]
	v_pk_add_f32 v[124:125], v[124:125], v[144:145]
	v_pk_mul_f32 v[170:171], v[168:169], v[152:153] op_sel:[1,0] op_sel_hi:[0,0]
	v_pk_fma_f32 v[174:175], v[168:169], v[152:153], v[170:171] op_sel:[0,1,0] neg_hi:[0,0,1]
	v_pk_add_f32 v[136:137], v[116:117], v[124:125]
	v_pk_add_f32 v[152:153], v[172:173], v[174:175] neg_lo:[0,1] neg_hi:[0,1]
	v_pk_add_f32 v[116:117], v[116:117], v[124:125] neg_lo:[0,1] neg_hi:[0,1]
	v_pk_mul_f32 v[168:169], v[132:133], v[152:153] op_sel:[1,1] op_sel_hi:[0,1]
	v_pk_fma_f32 v[170:171], v[132:133], v[152:153], v[168:169] op_sel_hi:[1,0,1] neg_lo:[0,0,1]
	v_pk_mul_f32 v[124:125], v[116:117], v[132:133] op_sel:[1,1] op_sel_hi:[1,0]
	v_pk_add_f32 v[152:153], v[120:121], v[140:141] neg_lo:[0,1] neg_hi:[0,1]
	v_pk_add_f32 v[120:121], v[120:121], v[140:141]
	v_pk_mul_f32 v[168:169], v[152:153], v[154:155] op_sel:[1,1] op_sel_hi:[1,0]
	s_nop 0
	v_pk_fma_f32 v[176:177], v[152:153], v[154:155], v[168:169] op_sel_hi:[0,1,1] neg_lo:[0,0,1]
	v_pk_add_f32 v[152:153], v[128:129], v[148:149] neg_lo:[0,1] neg_hi:[0,1]
	v_pk_add_f32 v[128:129], v[128:129], v[148:149]
	v_pk_mul_f32 v[168:169], v[152:153], v[154:155] op_sel:[1,0] op_sel_hi:[0,0]
	v_pk_fma_f32 v[178:179], v[152:153], v[154:155], v[168:169] op_sel:[0,1,0] neg_hi:[0,0,1]
	v_pk_add_f32 v[140:141], v[120:121], v[128:129]
	v_pk_add_f32 v[152:153], v[176:177], v[178:179] neg_lo:[0,1] neg_hi:[0,1]
	v_pk_add_f32 v[144:145], v[136:137], v[140:141]
	v_pk_mul_f32 v[154:155], v[132:133], v[152:153] op_sel_hi:[0,1]
	v_pk_fma_f32 v[168:169], v[132:133], v[152:153], v[154:155] op_sel:[1,0,1] op_sel_hi:[1,1,0] neg_hi:[0,0,1]
	v_pk_add_f32 v[136:137], v[136:137], v[140:141] neg_lo:[0,1] neg_hi:[0,1]
	v_pk_add_f32 v[152:153], v[170:171], v[168:169] neg_lo:[0,1] neg_hi:[0,1]
	v_pk_mul_f32 v[140:141], v[136:137], v[158:159] op_sel:[1,1] op_sel_hi:[1,0]
	v_pk_mul_f32 v[154:155], v[158:159], v[152:153] op_sel:[1,1] op_sel_hi:[0,1]
	v_pk_fma_f32 v[182:183], v[158:159], v[152:153], v[154:155] op_sel_hi:[1,0,1] neg_lo:[0,0,1]
	s_nop 0
	v_pk_add_f32 v[152:153], v[118:119], v[138:139] neg_lo:[0,1] neg_hi:[0,1]
	v_pk_add_f32 v[118:119], v[118:119], v[138:139]
	v_pk_mul_f32 v[154:155], v[152:153], v[160:161] op_sel:[1,1] op_sel_hi:[1,0]
	s_nop 0
	v_pk_fma_f32 v[184:185], v[152:153], v[160:161], v[154:155] op_sel_hi:[0,1,1] neg_lo:[0,0,1]
	v_pk_add_f32 v[152:153], v[126:127], v[146:147] neg_lo:[0,1] neg_hi:[0,1]
	v_pk_add_f32 v[126:127], v[126:127], v[146:147]
	v_pk_mul_f32 v[154:155], v[152:153], v[160:161] op_sel:[1,0] op_sel_hi:[0,0]
	v_pk_fma_f32 v[186:187], v[152:153], v[160:161], v[154:155] op_sel:[0,1,0] neg_hi:[0,0,1]
	v_pk_add_f32 v[138:139], v[118:119], v[126:127]
	v_pk_add_f32 v[152:153], v[184:185], v[186:187] neg_lo:[0,1] neg_hi:[0,1]
	v_pk_add_f32 v[118:119], v[118:119], v[126:127] neg_lo:[0,1] neg_hi:[0,1]
	v_pk_mul_f32 v[154:155], v[156:157], v[152:153] op_sel:[1,1] op_sel_hi:[0,1]
	v_pk_fma_f32 v[160:161], v[156:157], v[152:153], v[154:155] op_sel_hi:[1,0,1] neg_lo:[0,0,1]
	s_nop 0
; template <int R, class XT, class TWT>
; __device__ __forceinline__ void dif_task(XT X, TWT tw, int s, int task) {
;     const int lgM = 13 - s, lgq = lgM - R, q = 1 << lgq;
;     const int j0 = task & (q - 1), blk = task >> lgq, base = (blk << lgM) + j0;
;     const int pb = PADI(base), qp = (q >= 32) ? q + (q >> 4) : q;
;     f32x2v v[1 << R];
; #pragma unroll
;     for (int k = 0; k < (1 << R); ++k) v[k] = X[pb + k * qp];
; #pragma unroll
;     for (int r = 0; r < R; ++r) {
;         const int pb = R - 1 - r;
; #pragma unroll
;         for (int k = 0; k < (1 << R); ++k) if (!((k >> pb) & 1)) {
;             const int klo = k & ((1 << pb) - 1);
;             const f32x2v w = tw[(j0 + (klo << lgq)) << (s + r)];
;             const f32x2v a = v[k], b = v[k + (1 << pb)], d = a - b;
;             v[k] = a + b; v[k + (1 << pb)] = (f32x2v){d.x * w.x - d.y * w.y, d.x * w.y + d.y * w.x};
;         }
;     }
; #pragma unroll
;     for (int k = 0; k < (1 << R); ++k) X[pb + k * qp] = v[k];
; }
	v_pk_add_f32 v[152:153], v[122:123], v[142:143] neg_lo:[0,1] neg_hi:[0,1]
	v_pk_add_f32 v[122:123], v[122:123], v[142:143]
	v_pk_mul_f32 v[154:155], v[152:153], v[162:163] op_sel:[1,1] op_sel_hi:[1,0]
	s_nop 0
	v_pk_fma_f32 v[188:189], v[152:153], v[162:163], v[154:155] op_sel_hi:[0,1,1] neg_lo:[0,0,1]
	v_pk_add_f32 v[152:153], v[130:131], v[150:151] neg_lo:[0,1] neg_hi:[0,1]
	v_pk_add_f32 v[130:131], v[130:131], v[150:151]
	v_pk_mul_f32 v[154:155], v[152:153], v[162:163] op_sel:[1,0] op_sel_hi:[0,0]
	v_pk_fma_f32 v[190:191], v[152:153], v[162:163], v[154:155] op_sel:[0,1,0] neg_hi:[0,0,1]
	v_pk_add_f32 v[142:143], v[122:123], v[130:131]
	v_pk_add_f32 v[152:153], v[188:189], v[190:191] neg_lo:[0,1] neg_hi:[0,1]
	v_pk_add_f32 v[146:147], v[138:139], v[142:143]
	v_pk_mul_f32 v[154:155], v[164:165], v[152:153] op_sel_hi:[0,1]
	v_pk_fma_f32 v[162:163], v[164:165], v[152:153], v[154:155] op_sel:[1,0,1] op_sel_hi:[1,1,0] neg_hi:[0,0,1]
	v_pk_add_f32 v[148:149], v[144:145], v[146:147]
	v_pk_add_f32 v[152:153], v[160:161], v[162:163] neg_lo:[0,1] neg_hi:[0,1]
	v_pk_add_f32 v[144:145], v[144:145], v[146:147] neg_lo:[0,1] neg_hi:[0,1]
	v_pk_mul_f32 v[154:155], v[158:159], v[152:153] op_sel_hi:[0,1]
	v_pk_fma_f32 v[192:193], v[158:159], v[152:153], v[154:155] op_sel:[1,0,1] op_sel_hi:[1,1,0] neg_hi:[0,0,1]
	v_cndmask_b32_e64 v155, v111, v167, s[40:41]
	v_cndmask_b32_e64 v154, v167, v166, s[40:41]
	v_pk_mul_f32 v[146:147], v[144:145], v[154:155] op_sel:[1,1] op_sel_hi:[1,0]
	s_nop 0
	v_pk_fma_f32 v[150:151], v[144:145], v[154:155], v[146:147] op_sel_hi:[0,1,1] neg_lo:[0,0,1]
	v_pk_fma_f32 v[144:145], v[136:137], v[158:159], v[140:141] op_sel_hi:[0,1,1] neg_lo:[0,0,1]
	v_pk_add_f32 v[136:137], v[138:139], v[142:143] neg_lo:[0,1] neg_hi:[0,1]
	v_pk_add_f32 v[152:153], v[182:183], v[192:193] neg_lo:[0,1] neg_hi:[0,1]
	v_pk_mul_f32 v[138:139], v[136:137], v[158:159] op_sel_hi:[1,0]
	v_mov_b32_e32 v111, s16
	v_pk_fma_f32 v[140:141], v[136:137], v[158:159], v[138:139] op_sel:[0,1,1] op_sel_hi:[1,1,0] neg_hi:[0,0,1]
	s_nop 0
	v_pk_add_f32 v[138:139], v[144:145], v[140:141] neg_lo:[0,1] neg_hi:[0,1]
	v_pk_add_f32 v[136:137], v[144:145], v[140:141]
	v_pk_mul_f32 v[140:141], v[154:155], v[138:139] op_sel:[1,1] op_sel_hi:[0,1]
	v_pk_fma_f32 v[142:143], v[154:155], v[138:139], v[140:141] op_sel_hi:[1,0,1] neg_lo:[0,0,1]
	s_nop 0
	v_pk_fma_f32 v[138:139], v[116:117], v[132:133], v[124:125] op_sel_hi:[0,1,1] neg_lo:[0,0,1]
	v_pk_add_f32 v[116:117], v[120:121], v[128:129] neg_lo:[0,1] neg_hi:[0,1]
	s_nop 0
	v_pk_mul_f32 v[120:121], v[116:117], v[132:133] op_sel_hi:[1,0]
	s_nop 0
	v_pk_fma_f32 v[124:125], v[116:117], v[132:133], v[120:121] op_sel:[0,1,1] op_sel_hi:[1,1,0] neg_hi:[0,0,1]
	v_pk_mul_f32 v[120:121], v[118:119], v[156:157] op_sel:[1,1] op_sel_hi:[1,0]
	s_nop 0
	v_pk_fma_f32 v[126:127], v[118:119], v[156:157], v[120:121] op_sel_hi:[0,1,1] neg_lo:[0,0,1]
	v_pk_add_f32 v[118:119], v[122:123], v[130:131] neg_lo:[0,1] neg_hi:[0,1]
	v_pk_add_f32 v[116:117], v[138:139], v[124:125]
	v_pk_mul_f32 v[120:121], v[118:119], v[164:165] op_sel_hi:[1,0]
	v_pk_add_f32 v[130:131], v[184:185], v[186:187]
	v_pk_fma_f32 v[122:123], v[118:119], v[164:165], v[120:121] op_sel:[0,1,1] op_sel_hi:[1,1,0] neg_hi:[0,0,1]
	v_pk_add_f32 v[132:133], v[188:189], v[190:191]
	v_pk_add_f32 v[118:119], v[126:127], v[122:123]
	s_nop 0
	v_pk_add_f32 v[120:121], v[116:117], v[118:119]
	v_pk_add_f32 v[116:117], v[116:117], v[118:119] neg_lo:[0,1] neg_hi:[0,1]
	s_nop 0
	v_pk_mul_f32 v[118:119], v[154:155], v[116:117] op_sel:[1,1] op_sel_hi:[0,1]
	v_pk_fma_f32 v[128:129], v[154:155], v[116:117], v[118:119] op_sel_hi:[1,0,1] neg_lo:[0,0,1]
	s_nop 0
	v_pk_add_f32 v[116:117], v[138:139], v[124:125] neg_lo:[0,1] neg_hi:[0,1]
	v_pk_add_f32 v[138:139], v[130:131], v[132:133]
	v_pk_mul_f32 v[118:119], v[158:159], v[116:117] op_sel:[1,1] op_sel_hi:[0,1]
	v_pk_fma_f32 v[124:125], v[158:159], v[116:117], v[118:119] op_sel_hi:[1,0,1] neg_lo:[0,0,1]
	s_nop 0
	v_pk_add_f32 v[116:117], v[126:127], v[122:123] neg_lo:[0,1] neg_hi:[0,1]
	s_nop 0
	v_pk_mul_f32 v[118:119], v[158:159], v[116:117] op_sel_hi:[0,1]
	v_pk_fma_f32 v[122:123], v[158:159], v[116:117], v[118:119] op_sel:[1,0,1] op_sel_hi:[1,1,0] neg_hi:[0,0,1]
	s_nop 0
	v_pk_add_f32 v[118:119], v[124:125], v[122:123] neg_lo:[0,1] neg_hi:[0,1]
	v_pk_add_f32 v[116:117], v[124:125], v[122:123]
	v_pk_mul_f32 v[122:123], v[154:155], v[118:119] op_sel:[1,1] op_sel_hi:[0,1]
	v_pk_fma_f32 v[124:125], v[154:155], v[118:119], v[122:123] op_sel_hi:[1,0,1] neg_lo:[0,0,1]
	v_pk_add_f32 v[122:123], v[176:177], v[178:179]
	v_pk_add_f32 v[118:119], v[172:173], v[174:175]
	s_nop 0
	v_pk_add_f32 v[126:127], v[118:119], v[122:123]
	v_pk_add_f32 v[118:119], v[118:119], v[122:123] neg_lo:[0,1] neg_hi:[0,1]
	v_pk_add_f32 v[140:141], v[126:127], v[138:139]
	v_pk_add_f32 v[126:127], v[126:127], v[138:139] neg_lo:[0,1] neg_hi:[0,1]
	v_pk_mul_f32 v[122:123], v[158:159], v[118:119] op_sel:[1,1] op_sel_hi:[0,1]
	v_pk_mul_f32 v[138:139], v[126:127], v[154:155] op_sel:[1,1] op_sel_hi:[1,0]
	s_nop 0
	v_pk_fma_f32 v[144:145], v[126:127], v[154:155], v[138:139] op_sel_hi:[0,1,1] neg_lo:[0,0,1]
	v_pk_fma_f32 v[126:127], v[158:159], v[118:119], v[122:123] op_sel_hi:[1,0,1] neg_lo:[0,0,1]
	s_nop 0
	v_pk_add_f32 v[118:119], v[130:131], v[132:133] neg_lo:[0,1] neg_hi:[0,1]
	s_nop 0
	v_pk_mul_f32 v[122:123], v[158:159], v[118:119] op_sel_hi:[0,1]
	v_pk_fma_f32 v[130:131], v[158:159], v[118:119], v[122:123] op_sel:[1,0,1] op_sel_hi:[1,1,0] neg_hi:[0,0,1]
	s_nop 0
	v_pk_add_f32 v[122:123], v[126:127], v[130:131] neg_lo:[0,1] neg_hi:[0,1]
	v_pk_add_f32 v[118:119], v[126:127], v[130:131]
	v_pk_mul_f32 v[126:127], v[154:155], v[122:123] op_sel:[1,1] op_sel_hi:[0,1]
	v_pk_fma_f32 v[130:131], v[154:155], v[122:123], v[126:127] op_sel_hi:[1,0,1] neg_lo:[0,0,1]
	v_pk_add_f32 v[126:127], v[160:161], v[162:163]
	v_pk_add_f32 v[122:123], v[170:171], v[168:169]
	s_nop 0
	v_pk_add_f32 v[132:133], v[122:123], v[126:127]
	v_pk_add_f32 v[122:123], v[122:123], v[126:127] neg_lo:[0,1] neg_hi:[0,1]
	s_nop 0
	v_pk_mul_f32 v[126:127], v[154:155], v[122:123] op_sel:[1,1] op_sel_hi:[0,1]
	v_pk_fma_f32 v[138:139], v[154:155], v[122:123], v[126:127] op_sel_hi:[1,0,1] neg_lo:[0,0,1]
	v_pk_mul_f32 v[126:127], v[154:155], v[152:153] op_sel:[1,1] op_sel_hi:[0,1]
	v_pk_fma_f32 v[146:147], v[154:155], v[152:153], v[126:127] op_sel_hi:[1,0,1] neg_lo:[0,0,1]
	v_pk_add_f32 v[122:123], v[182:183], v[192:193]
	ds_write2_b64 v81, v[148:149], v[150:151] offset1:34
	ds_write2_b64 v81, v[136:137], v[142:143] offset0:68 offset1:102
	ds_write2_b64 v81, v[120:121], v[128:129] offset0:136 offset1:170
	ds_write2_b64 v81, v[116:117], v[124:125] offset0:204 offset1:238
	ds_write2_b64 v110, v[140:141], v[144:145] offset0:16 offset1:50
	ds_write2_b64 v110, v[118:119], v[130:131] offset0:84 offset1:118
	ds_write2_b64 v110, v[132:133], v[138:139] offset0:152 offset1:186
	ds_write2_b64 v110, v[122:123], v[146:147] offset0:220 offset1:254
	s_waitcnt lgkmcnt(0)
	s_barrier
; template <int R, class XT, class TWT>
; __device__ __forceinline__ void dif_task(XT X, TWT tw, int s, int task) {
;     const int lgM = 13 - s, lgq = lgM - R, q = 1 << lgq;
;     const int j0 = task & (q - 1), blk = task >> lgq, base = (blk << lgM) + j0;
;     const int pb = PADI(base), qp = (q >= 32) ? q + (q >> 4) : q;
;     f32x2v v[1 << R];
; #pragma unroll
;     for (int k = 0; k < (1 << R); ++k) v[k] = X[pb + k * qp];
; #pragma unroll
;     for (int r = 0; r < R; ++r) {
;         const int pb = R - 1 - r;
; #pragma unroll
;         for (int k = 0; k < (1 << R); ++k) if (!((k >> pb) & 1)) {
;             const int klo = k & ((1 << pb) - 1);
;             const f32x2v w = tw[(j0 + (klo << lgq)) << (s + r)];
;             const f32x2v a = v[k], b = v[k + (1 << pb)], d = a - b;
;             v[k] = a + b; v[k + (1 << pb)] = (f32x2v){d.x * w.x - d.y * w.y, d.x * w.y + d.y * w.x};
;         }
;     }
; #pragma unroll
;     for (int k = 0; k < (1 << R); ++k) X[pb + k * qp] = v[k];
; }
	ds_read2_b64 v[116:119], v84 offset1:2
	ds_read2_b64 v[120:123], v84 offset0:4 offset1:6
	ds_read2_b64 v[124:127], v84 offset0:8 offset1:10
	ds_read2_b64 v[128:131], v84 offset0:12 offset1:14
	ds_read2_b64 v[136:139], v84 offset0:16 offset1:18
	ds_read2_b64 v[140:143], v84 offset0:20 offset1:22
	ds_read2_b64 v[144:147], v84 offset0:24 offset1:26
	ds_read2_b64 v[148:151], v84 offset0:28 offset1:30
	ds_read2st64_b64 v[152:155], v100 offset1:16
	ds_read_b64 v[132:133], v101
	ds_read_b64 v[156:157], v102
	ds_read_b64 v[158:159], v103
	ds_read_b64 v[160:161], v85
	s_waitcnt lgkmcnt(8)
	v_pk_add_f32 v[168:169], v[116:117], v[136:137] neg_lo:[0,1] neg_hi:[0,1]
	ds_read_b64 v[162:163], v104
	ds_read_b64 v[164:165], v105
	ds_read_b64 v[166:167], v111
	s_waitcnt lgkmcnt(7)
	v_pk_mul_f32 v[170:171], v[168:169], v[152:153] op_sel:[1,1] op_sel_hi:[1,0]
	v_pk_add_f32 v[116:117], v[116:117], v[136:137]
	v_pk_fma_f32 v[172:173], v[168:169], v[152:153], v[170:171] op_sel_hi:[0,1,1] neg_lo:[0,0,1]
	v_pk_add_f32 v[168:169], v[124:125], v[144:145] neg_lo:[0,1] neg_hi:[0,1]
	v_pk_add_f32 v[124:125], v[124:125], v[144:145]
	v_pk_mul_f32 v[170:171], v[168:169], v[152:153] op_sel:[1,0] op_sel_hi:[0,0]
	v_pk_fma_f32 v[174:175], v[168:169], v[152:153], v[170:171] op_sel:[0,1,0] neg_hi:[0,0,1]
	v_pk_add_f32 v[136:137], v[116:117], v[124:125]
	v_pk_add_f32 v[152:153], v[172:173], v[174:175] neg_lo:[0,1] neg_hi:[0,1]
	s_waitcnt lgkmcnt(0)
	v_xor_b32_e32 v135, 0x80000000, v166
	v_pk_mul_f32 v[168:169], v[158:159], v[152:153] op_sel:[1,1] op_sel_hi:[0,1]
	v_pk_fma_f32 v[170:171], v[158:159], v[152:153], v[168:169] op_sel_hi:[1,0,1] neg_lo:[0,0,1]
	v_pk_add_f32 v[116:117], v[116:117], v[124:125] neg_lo:[0,1] neg_hi:[0,1]
	v_pk_add_f32 v[152:153], v[120:121], v[140:141] neg_lo:[0,1] neg_hi:[0,1]
	v_pk_add_f32 v[120:121], v[120:121], v[140:141]
	v_pk_mul_f32 v[168:169], v[152:153], v[154:155] op_sel:[1,1] op_sel_hi:[1,0]
	v_pk_mul_f32 v[124:125], v[116:117], v[158:159] op_sel:[1,1] op_sel_hi:[1,0]
	v_pk_fma_f32 v[176:177], v[152:153], v[154:155], v[168:169] op_sel_hi:[0,1,1] neg_lo:[0,0,1]
	v_pk_add_f32 v[152:153], v[128:129], v[148:149] neg_lo:[0,1] neg_hi:[0,1]
	v_pk_add_f32 v[128:129], v[128:129], v[148:149]
	v_pk_mul_f32 v[168:169], v[152:153], v[154:155] op_sel:[1,0] op_sel_hi:[0,0]
	v_pk_fma_f32 v[178:179], v[152:153], v[154:155], v[168:169] op_sel:[0,1,0] neg_hi:[0,0,1]
	v_pk_add_f32 v[140:141], v[120:121], v[128:129]
	v_pk_add_f32 v[152:153], v[176:177], v[178:179] neg_lo:[0,1] neg_hi:[0,1]
	v_pk_add_f32 v[144:145], v[136:137], v[140:141]
	v_pk_mul_f32 v[154:155], v[158:159], v[152:153] op_sel_hi:[0,1]
	v_pk_fma_f32 v[168:169], v[158:159], v[152:153], v[154:155] op_sel:[1,0,1] op_sel_hi:[1,1,0] neg_hi:[0,0,1]
	v_pk_add_f32 v[136:137], v[136:137], v[140:141] neg_lo:[0,1] neg_hi:[0,1]
	v_pk_add_f32 v[152:153], v[170:171], v[168:169] neg_lo:[0,1] neg_hi:[0,1]
	v_pk_mul_f32 v[140:141], v[136:137], v[164:165] op_sel:[1,1] op_sel_hi:[1,0]
	v_pk_mul_f32 v[154:155], v[164:165], v[152:153] op_sel:[1,1] op_sel_hi:[0,1]
	v_pk_fma_f32 v[182:183], v[164:165], v[152:153], v[154:155] op_sel_hi:[1,0,1] neg_lo:[0,0,1]
	s_nop 0
	v_pk_add_f32 v[152:153], v[118:119], v[138:139] neg_lo:[0,1] neg_hi:[0,1]
	v_pk_add_f32 v[118:119], v[118:119], v[138:139]
	v_pk_mul_f32 v[154:155], v[152:153], v[132:133] op_sel:[1,1] op_sel_hi:[1,0]
	s_nop 0
	v_pk_fma_f32 v[184:185], v[152:153], v[132:133], v[154:155] op_sel_hi:[0,1,1] neg_lo:[0,0,1]
	v_pk_add_f32 v[152:153], v[126:127], v[146:147] neg_lo:[0,1] neg_hi:[0,1]
	v_pk_add_f32 v[126:127], v[126:127], v[146:147]
	v_pk_mul_f32 v[154:155], v[152:153], v[132:133] op_sel:[1,0] op_sel_hi:[0,0]
	v_pk_fma_f32 v[186:187], v[152:153], v[132:133], v[154:155] op_sel:[0,1,0] neg_hi:[0,0,1]
	v_pk_add_f32 v[138:139], v[118:119], v[126:127]
	v_pk_add_f32 v[132:133], v[184:185], v[186:187] neg_lo:[0,1] neg_hi:[0,1]
	v_pk_add_f32 v[118:119], v[118:119], v[126:127] neg_lo:[0,1] neg_hi:[0,1]
	v_pk_mul_f32 v[152:153], v[162:163], v[132:133] op_sel:[1,1] op_sel_hi:[0,1]
	v_pk_fma_f32 v[154:155], v[162:163], v[132:133], v[152:153] op_sel_hi:[1,0,1] neg_lo:[0,0,1]
	s_nop 0
	v_pk_add_f32 v[132:133], v[122:123], v[142:143] neg_lo:[0,1] neg_hi:[0,1]
	v_pk_add_f32 v[122:123], v[122:123], v[142:143]
	v_pk_mul_f32 v[152:153], v[132:133], v[156:157] op_sel:[1,1] op_sel_hi:[1,0]
	s_nop 0
	v_pk_fma_f32 v[188:189], v[132:133], v[156:157], v[152:153] op_sel_hi:[0,1,1] neg_lo:[0,0,1]
	v_pk_add_f32 v[132:133], v[130:131], v[150:151] neg_lo:[0,1] neg_hi:[0,1]
	v_pk_add_f32 v[130:131], v[130:131], v[150:151]
	v_pk_mul_f32 v[152:153], v[132:133], v[156:157] op_sel:[1,0] op_sel_hi:[0,0]
	v_pk_fma_f32 v[190:191], v[132:133], v[156:157], v[152:153] op_sel:[0,1,0] neg_hi:[0,0,1]
	v_pk_add_f32 v[142:143], v[122:123], v[130:131]
	v_pk_add_f32 v[132:133], v[188:189], v[190:191] neg_lo:[0,1] neg_hi:[0,1]
	v_pk_add_f32 v[146:147], v[138:139], v[142:143]
	v_pk_mul_f32 v[152:153], v[160:161], v[132:133] op_sel_hi:[0,1]
	v_pk_fma_f32 v[156:157], v[160:161], v[132:133], v[152:153] op_sel:[1,0,1] op_sel_hi:[1,1,0] neg_hi:[0,0,1]
	v_pk_add_f32 v[148:149], v[144:145], v[146:147]
	v_pk_add_f32 v[132:133], v[154:155], v[156:157] neg_lo:[0,1] neg_hi:[0,1]
	v_pk_add_f32 v[144:145], v[144:145], v[146:147] neg_lo:[0,1] neg_hi:[0,1]
	v_pk_mul_f32 v[152:153], v[164:165], v[132:133] op_sel_hi:[0,1]
	v_pk_fma_f32 v[192:193], v[164:165], v[132:133], v[152:153] op_sel:[1,0,1] op_sel_hi:[1,1,0] neg_hi:[0,0,1]
	v_cndmask_b32_e64 v153, v135, v167, s[42:43]
	v_cndmask_b32_e64 v152, v167, v166, s[42:43]
	v_pk_mul_f32 v[146:147], v[144:145], v[152:153] op_sel:[1,1] op_sel_hi:[1,0]
	s_nop 0
; template <int R, class XT, class TWT>
; __device__ __forceinline__ void dif_task(XT X, TWT tw, int s, int task) {
;     const int lgM = 13 - s, lgq = lgM - R, q = 1 << lgq;
;     const int j0 = task & (q - 1), blk = task >> lgq, base = (blk << lgM) + j0;
;     const int pb = PADI(base), qp = (q >= 32) ? q + (q >> 4) : q;
;     f32x2v v[1 << R];
; #pragma unroll
;     for (int k = 0; k < (1 << R); ++k) v[k] = X[pb + k * qp];
; #pragma unroll
;     for (int r = 0; r < R; ++r) {
;         const int pb = R - 1 - r;
; #pragma unroll
;         for (int k = 0; k < (1 << R); ++k) if (!((k >> pb) & 1)) {
;             const int klo = k & ((1 << pb) - 1);
;             const f32x2v w = tw[(j0 + (klo << lgq)) << (s + r)];
;             const f32x2v a = v[k], b = v[k + (1 << pb)], d = a - b;
;             v[k] = a + b; v[k + (1 << pb)] = (f32x2v){d.x * w.x - d.y * w.y, d.x * w.y + d.y * w.x};
;         }
;     }
; #pragma unroll
;     for (int k = 0; k < (1 << R); ++k) X[pb + k * qp] = v[k];
; }
	v_pk_fma_f32 v[150:151], v[144:145], v[152:153], v[146:147] op_sel_hi:[0,1,1] neg_lo:[0,0,1]
	v_pk_fma_f32 v[144:145], v[136:137], v[164:165], v[140:141] op_sel_hi:[0,1,1] neg_lo:[0,0,1]
	v_pk_add_f32 v[136:137], v[138:139], v[142:143] neg_lo:[0,1] neg_hi:[0,1]
	v_pk_add_f32 v[132:133], v[182:183], v[192:193] neg_lo:[0,1] neg_hi:[0,1]
	v_pk_mul_f32 v[138:139], v[136:137], v[164:165] op_sel_hi:[1,0]
	s_nop 0
	v_pk_fma_f32 v[140:141], v[136:137], v[164:165], v[138:139] op_sel:[0,1,1] op_sel_hi:[1,1,0] neg_hi:[0,0,1]
	s_nop 0
	v_pk_add_f32 v[138:139], v[144:145], v[140:141] neg_lo:[0,1] neg_hi:[0,1]
	v_pk_add_f32 v[136:137], v[144:145], v[140:141]
	v_pk_mul_f32 v[140:141], v[152:153], v[138:139] op_sel:[1,1] op_sel_hi:[0,1]
	v_pk_fma_f32 v[142:143], v[152:153], v[138:139], v[140:141] op_sel_hi:[1,0,1] neg_lo:[0,0,1]
	s_nop 0
	v_pk_fma_f32 v[138:139], v[116:117], v[158:159], v[124:125] op_sel_hi:[0,1,1] neg_lo:[0,0,1]
	v_pk_add_f32 v[116:117], v[120:121], v[128:129] neg_lo:[0,1] neg_hi:[0,1]
	s_nop 0
	v_pk_mul_f32 v[120:121], v[116:117], v[158:159] op_sel_hi:[1,0]
	s_nop 0
	v_pk_fma_f32 v[124:125], v[116:117], v[158:159], v[120:121] op_sel:[0,1,1] op_sel_hi:[1,1,0] neg_hi:[0,0,1]
	v_pk_mul_f32 v[120:121], v[118:119], v[162:163] op_sel:[1,1] op_sel_hi:[1,0]
	s_nop 0
	v_pk_fma_f32 v[126:127], v[118:119], v[162:163], v[120:121] op_sel_hi:[0,1,1] neg_lo:[0,0,1]
	v_pk_add_f32 v[118:119], v[122:123], v[130:131] neg_lo:[0,1] neg_hi:[0,1]
	v_pk_add_f32 v[116:117], v[138:139], v[124:125]
	v_pk_mul_f32 v[120:121], v[118:119], v[160:161] op_sel_hi:[1,0]
	v_pk_add_f32 v[130:131], v[184:185], v[186:187]
	v_pk_fma_f32 v[122:123], v[118:119], v[160:161], v[120:121] op_sel:[0,1,1] op_sel_hi:[1,1,0] neg_hi:[0,0,1]
	s_nop 0
	v_pk_add_f32 v[118:119], v[126:127], v[122:123]
	s_nop 0
	v_pk_add_f32 v[120:121], v[116:117], v[118:119]
	v_pk_add_f32 v[116:117], v[116:117], v[118:119] neg_lo:[0,1] neg_hi:[0,1]
	s_nop 0
	v_pk_mul_f32 v[118:119], v[152:153], v[116:117] op_sel:[1,1] op_sel_hi:[0,1]
	v_pk_fma_f32 v[128:129], v[152:153], v[116:117], v[118:119] op_sel_hi:[1,0,1] neg_lo:[0,0,1]
	s_nop 0
	v_pk_add_f32 v[116:117], v[138:139], v[124:125] neg_lo:[0,1] neg_hi:[0,1]
	v_pk_add_f32 v[138:139], v[188:189], v[190:191]
	v_pk_mul_f32 v[118:119], v[164:165], v[116:117] op_sel:[1,1] op_sel_hi:[0,1]
	v_pk_fma_f32 v[124:125], v[164:165], v[116:117], v[118:119] op_sel_hi:[1,0,1] neg_lo:[0,0,1]
	v_pk_add_f32 v[140:141], v[130:131], v[138:139]
	v_pk_add_f32 v[116:117], v[126:127], v[122:123] neg_lo:[0,1] neg_hi:[0,1]
	s_nop 0
	v_pk_mul_f32 v[118:119], v[164:165], v[116:117] op_sel_hi:[0,1]
	v_pk_fma_f32 v[122:123], v[164:165], v[116:117], v[118:119] op_sel:[1,0,1] op_sel_hi:[1,1,0] neg_hi:[0,0,1]
	s_nop 0
	v_pk_add_f32 v[118:119], v[124:125], v[122:123] neg_lo:[0,1] neg_hi:[0,1]
	v_pk_add_f32 v[116:117], v[124:125], v[122:123]
	v_pk_mul_f32 v[122:123], v[152:153], v[118:119] op_sel:[1,1] op_sel_hi:[0,1]
	v_pk_fma_f32 v[124:125], v[152:153], v[118:119], v[122:123] op_sel_hi:[1,0,1] neg_lo:[0,0,1]
	v_pk_add_f32 v[122:123], v[176:177], v[178:179]
	v_pk_add_f32 v[118:119], v[172:173], v[174:175]
	s_nop 0
	v_pk_add_f32 v[126:127], v[118:119], v[122:123]
	v_pk_add_f32 v[118:119], v[118:119], v[122:123] neg_lo:[0,1] neg_hi:[0,1]
	v_pk_add_f32 v[144:145], v[126:127], v[140:141]
	v_pk_add_f32 v[126:127], v[126:127], v[140:141] neg_lo:[0,1] neg_hi:[0,1]
	v_pk_mul_f32 v[122:123], v[164:165], v[118:119] op_sel:[1,1] op_sel_hi:[0,1]
	v_pk_mul_f32 v[140:141], v[126:127], v[152:153] op_sel:[1,1] op_sel_hi:[1,0]
	s_nop 0
	v_pk_fma_f32 v[146:147], v[126:127], v[152:153], v[140:141] op_sel_hi:[0,1,1] neg_lo:[0,0,1]
	v_pk_fma_f32 v[126:127], v[164:165], v[118:119], v[122:123] op_sel_hi:[1,0,1] neg_lo:[0,0,1]
	s_nop 0
	v_pk_add_f32 v[118:119], v[130:131], v[138:139] neg_lo:[0,1] neg_hi:[0,1]
	s_nop 0
	v_pk_mul_f32 v[122:123], v[164:165], v[118:119] op_sel_hi:[0,1]
	v_pk_fma_f32 v[130:131], v[164:165], v[118:119], v[122:123] op_sel:[1,0,1] op_sel_hi:[1,1,0] neg_hi:[0,0,1]
	s_nop 0
	v_pk_add_f32 v[122:123], v[126:127], v[130:131] neg_lo:[0,1] neg_hi:[0,1]
	v_pk_add_f32 v[118:119], v[126:127], v[130:131]
	v_pk_mul_f32 v[126:127], v[152:153], v[122:123] op_sel:[1,1] op_sel_hi:[0,1]
	v_pk_fma_f32 v[130:131], v[152:153], v[122:123], v[126:127] op_sel_hi:[1,0,1] neg_lo:[0,0,1]
	v_pk_add_f32 v[126:127], v[154:155], v[156:157]
	v_pk_add_f32 v[122:123], v[170:171], v[168:169]
	s_nop 0
	v_pk_add_f32 v[138:139], v[122:123], v[126:127]
	v_pk_add_f32 v[122:123], v[122:123], v[126:127] neg_lo:[0,1] neg_hi:[0,1]
	s_nop 0
	v_pk_mul_f32 v[126:127], v[152:153], v[122:123] op_sel:[1,1] op_sel_hi:[0,1]
	v_pk_fma_f32 v[140:141], v[152:153], v[122:123], v[126:127] op_sel_hi:[1,0,1] neg_lo:[0,0,1]
	v_pk_mul_f32 v[126:127], v[152:153], v[132:133] op_sel:[1,1] op_sel_hi:[0,1]
	v_pk_fma_f32 v[154:155], v[152:153], v[132:133], v[126:127] op_sel_hi:[1,0,1] neg_lo:[0,0,1]
	v_pk_add_f32 v[122:123], v[182:183], v[192:193]
	ds_write2_b64 v84, v[148:149], v[150:151] offset1:2
	ds_write2_b64 v84, v[136:137], v[142:143] offset0:4 offset1:6
	ds_write2_b64 v84, v[120:121], v[128:129] offset0:8 offset1:10
	ds_write2_b64 v84, v[116:117], v[124:125] offset0:12 offset1:14
	ds_write2_b64 v84, v[144:145], v[146:147] offset0:16 offset1:18
	ds_write2_b64 v84, v[118:119], v[130:131] offset0:20 offset1:22
	ds_write2_b64 v84, v[138:139], v[140:141] offset0:24 offset1:26
	ds_write2_b64 v84, v[122:123], v[154:155] offset0:28 offset1:30
	s_waitcnt lgkmcnt(0)
	s_barrier
; template <bool LAT>
; __device__ __forceinline__ void hyconv_unit(const Frame& F, LAS f32x2v* X, const TwHalf tw, LAS bf16* OUT, const float* skip, bf16* MIX, int u) {
;     ...
;             for (int r = 0; r < 8; ++r) { const int e = 2 * (F.tid + 512 * r);
;                 const f32x2v a = X[PADI(e)], b = X[PADI(e + 1)]; const f32x4 k = kq[r];
;                 const f32x2v p = a + b, q = a - b; const f32x2v pk = (f32x2v){p.x * k.x - p.y * k.y, p.x * k.y + p.y * k.x}, qk = (f32x2v){q.x * k.z - q.y * k.w, q.x * k.w + q.y * k.z};
;                 X[PADI(e)] = pk + qk; X[PADI(e + 1)] = pk - qk; }
	ds_read_b128 v[116:119], v33
	s_waitcnt lgkmcnt(0)
	v_pk_add_f32 v[120:121], v[116:117], v[118:119]
	v_pk_add_f32 v[116:117], v[116:117], v[118:119] neg_lo:[0,1] neg_hi:[0,1]
	s_waitcnt vmcnt(7)
	v_pk_mul_f32 v[118:119], v[28:29], v[120:121] op_sel:[1,1] op_sel_hi:[0,1]
	v_pk_fma_f32 v[122:123], v[28:29], v[120:121], v[118:119] op_sel_hi:[1,0,1] neg_lo:[0,0,1]
	s_nop 0
	v_pk_mul_f32 v[28:29], v[30:31], v[116:117] op_sel:[1,1] op_sel_hi:[0,1]
	v_pk_fma_f32 v[118:119], v[30:31], v[116:117], v[28:29] op_sel_hi:[1,0,1] neg_lo:[0,0,1]
	s_nop 0
	v_pk_add_f32 v[28:29], v[122:123], v[118:119]
	v_pk_add_f32 v[30:31], v[122:123], v[118:119] neg_lo:[0,1] neg_hi:[0,1]
	ds_write_b128 v33, v[28:31]
	ds_read_b128 v[28:31], v68 offset:8192
	s_waitcnt lgkmcnt(0)
	v_pk_add_f32 v[116:117], v[28:29], v[30:31]
	v_pk_add_f32 v[28:29], v[28:29], v[30:31] neg_lo:[0,1] neg_hi:[0,1]
	s_waitcnt vmcnt(6)
	v_pk_mul_f32 v[30:31], v[24:25], v[116:117] op_sel:[1,1] op_sel_hi:[0,1]
	v_pk_fma_f32 v[118:119], v[24:25], v[116:117], v[30:31] op_sel_hi:[1,0,1] neg_lo:[0,0,1]
	s_nop 0
	v_pk_mul_f32 v[24:25], v[26:27], v[28:29] op_sel:[1,1] op_sel_hi:[0,1]
	v_pk_fma_f32 v[30:31], v[26:27], v[28:29], v[24:25] op_sel_hi:[1,0,1] neg_lo:[0,0,1]
	s_nop 0
	v_pk_add_f32 v[24:25], v[118:119], v[30:31]
	v_pk_add_f32 v[26:27], v[118:119], v[30:31] neg_lo:[0,1] neg_hi:[0,1]
	ds_write_b128 v68, v[24:27] offset:8192
	ds_read_b128 v[24:27], v69 offset:16384
	s_waitcnt lgkmcnt(0)
	v_pk_add_f32 v[28:29], v[24:25], v[26:27]
	v_pk_add_f32 v[24:25], v[24:25], v[26:27] neg_lo:[0,1] neg_hi:[0,1]
	s_waitcnt vmcnt(5)
	v_pk_mul_f32 v[26:27], v[20:21], v[28:29] op_sel:[1,1] op_sel_hi:[0,1]
	v_pk_fma_f32 v[30:31], v[20:21], v[28:29], v[26:27] op_sel_hi:[1,0,1] neg_lo:[0,0,1]
	s_nop 0
	v_pk_mul_f32 v[20:21], v[22:23], v[24:25] op_sel:[1,1] op_sel_hi:[0,1]
	v_pk_fma_f32 v[26:27], v[22:23], v[24:25], v[20:21] op_sel_hi:[1,0,1] neg_lo:[0,0,1]
	s_nop 0
	v_pk_add_f32 v[20:21], v[30:31], v[26:27]
	v_pk_add_f32 v[22:23], v[30:31], v[26:27] neg_lo:[0,1] neg_hi:[0,1]
	ds_write_b128 v69, v[20:23] offset:16384
	ds_read_b128 v[20:23], v70 offset:24576
	s_waitcnt lgkmcnt(0)
	v_pk_add_f32 v[24:25], v[20:21], v[22:23]
	v_pk_add_f32 v[20:21], v[20:21], v[22:23] neg_lo:[0,1] neg_hi:[0,1]
	s_waitcnt vmcnt(4)
	v_pk_mul_f32 v[22:23], v[16:17], v[24:25] op_sel:[1,1] op_sel_hi:[0,1]
	v_pk_fma_f32 v[26:27], v[16:17], v[24:25], v[22:23] op_sel_hi:[1,0,1] neg_lo:[0,0,1]
	s_nop 0
	v_pk_mul_f32 v[16:17], v[18:19], v[20:21] op_sel:[1,1] op_sel_hi:[0,1]
	v_pk_fma_f32 v[22:23], v[18:19], v[20:21], v[16:17] op_sel_hi:[1,0,1] neg_lo:[0,0,1]
	s_nop 0
	v_pk_add_f32 v[16:17], v[26:27], v[22:23]
	v_pk_add_f32 v[18:19], v[26:27], v[22:23] neg_lo:[0,1] neg_hi:[0,1]
	ds_write_b128 v70, v[16:19] offset:24576
	ds_read_b128 v[16:19], v71 offset:32768
	s_waitcnt lgkmcnt(0)
	v_pk_add_f32 v[20:21], v[16:17], v[18:19]
	v_pk_add_f32 v[16:17], v[16:17], v[18:19] neg_lo:[0,1] neg_hi:[0,1]
	s_waitcnt vmcnt(3)
	v_pk_mul_f32 v[18:19], v[12:13], v[20:21] op_sel:[1,1] op_sel_hi:[0,1]
	v_pk_fma_f32 v[22:23], v[12:13], v[20:21], v[18:19] op_sel_hi:[1,0,1] neg_lo:[0,0,1]
	s_nop 0
	v_pk_mul_f32 v[12:13], v[14:15], v[16:17] op_sel:[1,1] op_sel_hi:[0,1]
	v_pk_fma_f32 v[18:19], v[14:15], v[16:17], v[12:13] op_sel_hi:[1,0,1] neg_lo:[0,0,1]
	s_nop 0
	v_pk_add_f32 v[12:13], v[22:23], v[18:19]
	v_pk_add_f32 v[14:15], v[22:23], v[18:19] neg_lo:[0,1] neg_hi:[0,1]
	ds_write_b128 v71, v[12:15] offset:32768
	ds_read_b128 v[12:15], v72 offset:40960
	s_waitcnt lgkmcnt(0)
	v_pk_add_f32 v[16:17], v[12:13], v[14:15]
	v_pk_add_f32 v[12:13], v[12:13], v[14:15] neg_lo:[0,1] neg_hi:[0,1]
	s_waitcnt vmcnt(2)
	v_pk_mul_f32 v[14:15], v[8:9], v[16:17] op_sel:[1,1] op_sel_hi:[0,1]
	v_pk_fma_f32 v[18:19], v[8:9], v[16:17], v[14:15] op_sel_hi:[1,0,1] neg_lo:[0,0,1]
	s_nop 0
	v_pk_mul_f32 v[8:9], v[10:11], v[12:13] op_sel:[1,1] op_sel_hi:[0,1]
	v_pk_fma_f32 v[14:15], v[10:11], v[12:13], v[8:9] op_sel_hi:[1,0,1] neg_lo:[0,0,1]
	s_nop 0
	v_pk_add_f32 v[8:9], v[18:19], v[14:15]
	v_pk_add_f32 v[10:11], v[18:19], v[14:15] neg_lo:[0,1] neg_hi:[0,1]
	ds_write_b128 v72, v[8:11] offset:40960
	ds_read_b128 v[8:11], v73 offset:49152
	s_waitcnt lgkmcnt(0)
	v_pk_add_f32 v[12:13], v[8:9], v[10:11]
	v_pk_add_f32 v[8:9], v[8:9], v[10:11] neg_lo:[0,1] neg_hi:[0,1]
	s_waitcnt vmcnt(1)
	v_pk_mul_f32 v[10:11], v[4:5], v[12:13] op_sel:[1,1] op_sel_hi:[0,1]
	v_pk_fma_f32 v[14:15], v[4:5], v[12:13], v[10:11] op_sel_hi:[1,0,1] neg_lo:[0,0,1]
	s_nop 0
	v_pk_mul_f32 v[4:5], v[6:7], v[8:9] op_sel:[1,1] op_sel_hi:[0,1]
	v_pk_fma_f32 v[10:11], v[6:7], v[8:9], v[4:5] op_sel_hi:[1,0,1] neg_lo:[0,0,1]
	s_nop 0
	v_pk_add_f32 v[4:5], v[14:15], v[10:11]
	v_pk_add_f32 v[6:7], v[14:15], v[10:11] neg_lo:[0,1] neg_hi:[0,1]
	ds_write_b128 v73, v[4:7] offset:49152
	ds_read_b128 v[4:7], v74 offset:57344
	s_waitcnt lgkmcnt(0)
	v_pk_add_f32 v[8:9], v[4:5], v[6:7]
	v_pk_add_f32 v[4:5], v[4:5], v[6:7] neg_lo:[0,1] neg_hi:[0,1]
	s_waitcnt vmcnt(0)
	v_pk_mul_f32 v[6:7], v[0:1], v[8:9] op_sel:[1,1] op_sel_hi:[0,1]
	v_pk_fma_f32 v[10:11], v[0:1], v[8:9], v[6:7] op_sel_hi:[1,0,1] neg_lo:[0,0,1]
	s_nop 0
	v_pk_mul_f32 v[0:1], v[2:3], v[4:5] op_sel:[1,1] op_sel_hi:[0,1]
	v_pk_fma_f32 v[6:7], v[2:3], v[4:5], v[0:1] op_sel_hi:[1,0,1] neg_lo:[0,0,1]
	s_nop 0
	v_pk_add_f32 v[0:1], v[10:11], v[6:7]
	v_pk_add_f32 v[2:3], v[10:11], v[6:7] neg_lo:[0,1] neg_hi:[0,1]
	ds_write_b128 v74, v[0:3] offset:57344
	s_waitcnt lgkmcnt(0)
	s_barrier
; template <int R, class XT, class TWT>
; __device__ __forceinline__ void dit_task(XT X, TWT tw, int s, int task) {
;     const int lgM = 13 - s, lgq = lgM - R, q = 1 << lgq;
;     const int j0 = task & (q - 1), blk = task >> lgq, base = (blk << lgM) + j0;
;     const int pb = PADI(base), qp = (q >= 32) ? q + (q >> 4) : q;
;     f32x2v v[1 << R];
; #pragma unroll
;     for (int k = 0; k < (1 << R); ++k) v[k] = X[pb + k * qp];
; #pragma unroll
;     for (int r = R - 1; r >= 0; --r) {
;         const int pb = R - 1 - r;
; #pragma unroll
;         for (int k = 0; k < (1 << R); ++k) if (!((k >> pb) & 1)) {
;             const int klo = k & ((1 << pb) - 1);
;             const f32x2v w = tw[(j0 + (klo << lgq)) << (s + r)];
;             const f32x2v a = v[k], qv = v[k + (1 << pb)]; const f32x2v b = (f32x2v){qv.x * w.x + qv.y * w.y, qv.y * w.x - qv.x * w.y};
;             v[k] = a + b; v[k + (1 << pb)] = a - b;
;         }
;     }
; #pragma unroll
;     for (int k = 0; k < (1 << R); ++k) X[pb + k * qp] = v[k];
; }
; template <bool LAT>
; __device__ __forceinline__ void hyconv_unit(const Frame& F, LAS f32x2v* X, const TwHalf tw, LAS bf16* OUT, const float* skip, bf16* MIX, int u) {
;     ...
;                 const float sk = skip[ord * 256 + c0];
	global_load_dword v4, v181, s[0:1]
	ds_read2_b64 v[0:3], v84 offset1:2
	ds_read2_b64 v[6:9], v84 offset0:4 offset1:6
	ds_read2_b64 v[10:13], v84 offset0:8 offset1:10
	ds_read2_b64 v[14:17], v84 offset0:12 offset1:14
	ds_read2_b64 v[18:21], v84 offset0:16 offset1:18
	ds_read2_b64 v[22:25], v84 offset0:20 offset1:22
	ds_read2_b64 v[26:29], v84 offset0:24 offset1:26
	ds_read2_b64 v[116:119], v84 offset0:28 offset1:30
	ds_read_b64 v[30:31], v111
	ds_read_b64 v[124:125], v105
	ds_read_b64 v[126:127], v104
	ds_read2st64_b64 v[120:123], v100 offset1:16
	ds_read_b64 v[128:129], v103
	ds_read_b64 v[130:131], v85
	ds_read_b64 v[132:133], v101
	ds_read_b64 v[136:137], v102
	s_waitcnt lgkmcnt(7)
	v_xor_b32_e32 v5, 0x80000000, v30
	v_cndmask_b32_e64 v139, v5, v31, s[42:43]
	v_cndmask_b32_e64 v138, v31, v30, s[42:43]
	v_mov_b32_e32 v30, v139
	v_pk_mul_f32 v[140:141], v[2:3], v[30:31] op_sel_hi:[1,0]
	s_add_u32 s0, s24, s2
	v_pk_fma_f32 v[142:143], v[2:3], v[138:139], v[140:141] op_sel:[0,0,1] op_sel_hi:[1,0,0] neg_hi:[0,0,1]
	v_pk_mul_f32 v[140:141], v[8:9], v[30:31] op_sel_hi:[1,0]
	s_nop 0
	v_pk_fma_f32 v[144:145], v[8:9], v[138:139], v[140:141] op_sel:[0,0,1] op_sel_hi:[1,0,0] neg_hi:[0,0,1]
	v_pk_add_f32 v[2:3], v[0:1], v[142:143]
	v_pk_add_f32 v[8:9], v[6:7], v[144:145]
	v_pk_add_f32 v[6:7], v[6:7], v[144:145] neg_lo:[0,1] neg_hi:[0,1]
	s_waitcnt lgkmcnt(6)
	v_pk_mul_f32 v[140:141], v[124:125], v[8:9] op_sel:[1,0]
	v_pk_add_f32 v[0:1], v[0:1], v[142:143] neg_lo:[0,1] neg_hi:[0,1]
	v_pk_fma_f32 v[146:147], v[124:125], v[8:9], v[140:141] op_sel:[0,0,1] op_sel_hi:[0,1,0] neg_hi:[0,0,1]
	v_pk_mul_f32 v[140:141], v[12:13], v[30:31] op_sel_hi:[1,0]
	s_nop 0
	v_pk_fma_f32 v[148:149], v[12:13], v[138:139], v[140:141] op_sel:[0,0,1] op_sel_hi:[1,0,0] neg_hi:[0,0,1]
	v_pk_mul_f32 v[140:141], v[16:17], v[30:31] op_sel_hi:[1,0]
	s_nop 0
	v_pk_fma_f32 v[150:151], v[16:17], v[138:139], v[140:141] op_sel:[0,0,1] op_sel_hi:[1,0,0] neg_hi:[0,0,1]
	v_pk_add_f32 v[12:13], v[10:11], v[148:149]
	v_pk_add_f32 v[16:17], v[14:15], v[150:151]
	v_pk_add_f32 v[14:15], v[14:15], v[150:151] neg_lo:[0,1] neg_hi:[0,1]
	v_pk_mul_f32 v[140:141], v[124:125], v[16:17] op_sel:[1,0]
	v_pk_add_f32 v[10:11], v[10:11], v[148:149] neg_lo:[0,1] neg_hi:[0,1]
	v_pk_fma_f32 v[152:153], v[124:125], v[16:17], v[140:141] op_sel:[0,0,1] op_sel_hi:[0,1,0] neg_hi:[0,0,1]
	s_nop 0
	v_pk_add_f32 v[16:17], v[12:13], v[152:153]
	v_pk_add_f32 v[12:13], v[12:13], v[152:153] neg_lo:[0,1] neg_hi:[0,1]
	s_waitcnt lgkmcnt(3)
	v_pk_mul_f32 v[140:141], v[128:129], v[16:17] op_sel:[1,0]
	v_pk_add_f32 v[8:9], v[2:3], v[146:147]
	v_pk_fma_f32 v[154:155], v[128:129], v[16:17], v[140:141] op_sel:[0,0,1] op_sel_hi:[1,1,0]
	v_pk_fma_f32 v[16:17], v[128:129], v[16:17], v[140:141] op_sel:[0,0,1] op_sel_hi:[0,1,0] neg_lo:[0,0,1] neg_hi:[0,0,1]
	v_pk_mul_f32 v[140:141], v[20:21], v[30:31] op_sel_hi:[1,0]
	v_pk_add_f32 v[2:3], v[2:3], v[146:147] neg_lo:[0,1] neg_hi:[0,1]
	v_pk_fma_f32 v[156:157], v[20:21], v[138:139], v[140:141] op_sel:[0,0,1] op_sel_hi:[1,0,0] neg_hi:[0,0,1]
	v_pk_mul_f32 v[140:141], v[24:25], v[30:31] op_sel_hi:[1,0]
	s_nop 0
	v_pk_fma_f32 v[158:159], v[24:25], v[138:139], v[140:141] op_sel:[0,0,1] op_sel_hi:[1,0,0] neg_hi:[0,0,1]
	v_pk_add_f32 v[20:21], v[18:19], v[156:157]
	v_pk_add_f32 v[24:25], v[22:23], v[158:159]
	v_pk_add_f32 v[22:23], v[22:23], v[158:159] neg_lo:[0,1] neg_hi:[0,1]
	v_pk_mul_f32 v[140:141], v[124:125], v[24:25] op_sel:[1,0]
	v_pk_add_f32 v[18:19], v[18:19], v[156:157] neg_lo:[0,1] neg_hi:[0,1]
	v_pk_fma_f32 v[160:161], v[124:125], v[24:25], v[140:141] op_sel:[0,0,1] op_sel_hi:[0,1,0] neg_hi:[0,0,1]
	v_pk_mul_f32 v[140:141], v[28:29], v[30:31] op_sel_hi:[1,0]
	v_pk_mul_f32 v[30:31], v[118:119], v[30:31] op_sel_hi:[1,0]
	v_pk_fma_f32 v[162:163], v[28:29], v[138:139], v[140:141] op_sel:[0,0,1] op_sel_hi:[1,0,0] neg_hi:[0,0,1]
	v_pk_fma_f32 v[140:141], v[118:119], v[138:139], v[30:31] op_sel:[0,0,1] op_sel_hi:[1,0,0] neg_hi:[0,0,1]
	s_nop 0
	v_pk_add_f32 v[30:31], v[116:117], v[140:141]
	v_pk_add_f32 v[28:29], v[26:27], v[162:163]
	v_pk_mul_f32 v[118:119], v[124:125], v[30:31] op_sel:[1,0]
	s_nop 0
	v_pk_fma_f32 v[138:139], v[124:125], v[30:31], v[118:119] op_sel:[0,0,1] op_sel_hi:[0,1,0] neg_hi:[0,0,1]
	s_nop 0
	v_pk_add_f32 v[30:31], v[28:29], v[138:139]
	v_pk_add_f32 v[24:25], v[20:21], v[160:161]
	v_pk_mul_f32 v[118:119], v[128:129], v[30:31] op_sel:[1,0]
	v_pk_add_f32 v[116:117], v[116:117], v[140:141] neg_lo:[0,1] neg_hi:[0,1]
	v_pk_fma_f32 v[164:165], v[128:129], v[30:31], v[118:119] op_sel:[0,0,1] op_sel_hi:[0,1,0] neg_hi:[0,0,1]
	s_nop 0
	v_pk_add_f32 v[30:31], v[24:25], v[164:165]
	v_pk_add_f32 v[26:27], v[26:27], v[162:163] neg_lo:[0,1] neg_hi:[0,1]
	v_pk_mul_f32 v[118:119], v[120:121], v[30:31] op_sel:[1,0]
	v_pk_add_f32 v[28:29], v[28:29], v[138:139] neg_lo:[0,1] neg_hi:[0,1]
	v_pk_fma_f32 v[166:167], v[120:121], v[30:31], v[118:119] op_sel:[0,0,1] op_sel_hi:[1,1,0]
	v_pk_fma_f32 v[30:31], v[120:121], v[30:31], v[118:119] op_sel:[0,0,1] op_sel_hi:[0,1,0] neg_lo:[0,0,1] neg_hi:[0,0,1]
	v_pk_mul_f32 v[118:119], v[124:125], v[6:7] op_sel_hi:[0,1]
	v_pk_fma_f32 v[142:143], v[124:125], v[6:7], v[118:119] op_sel:[1,0,1] op_sel_hi:[1,1,0] neg_lo:[0,0,1]
	v_pk_mul_f32 v[118:119], v[124:125], v[14:15] op_sel_hi:[0,1]
	v_pk_fma_f32 v[144:145], v[124:125], v[14:15], v[118:119] op_sel:[1,0,1] op_sel_hi:[1,1,0] neg_lo:[0,0,1]
	s_nop 0
	v_pk_add_f32 v[14:15], v[10:11], v[144:145]
	v_pk_add_f32 v[6:7], v[0:1], v[142:143]
	v_pk_mul_f32 v[118:119], v[126:127], v[14:15] op_sel:[1,0]
	v_pk_add_f32 v[20:21], v[20:21], v[160:161] neg_lo:[0,1] neg_hi:[0,1]
	v_pk_fma_f32 v[148:149], v[126:127], v[14:15], v[118:119] op_sel:[0,0,1] op_sel_hi:[0,1,0] neg_hi:[0,0,1]
	v_pk_mul_f32 v[118:119], v[124:125], v[22:23] op_sel_hi:[0,1]
	v_pk_fma_f32 v[150:151], v[124:125], v[22:23], v[118:119] op_sel:[1,0,1] op_sel_hi:[1,1,0] neg_lo:[0,0,1]
	v_pk_mul_f32 v[118:119], v[124:125], v[116:117] op_sel_hi:[0,1]
	v_pk_fma_f32 v[140:141], v[124:125], v[116:117], v[118:119] op_sel:[1,0,1] op_sel_hi:[1,1,0] neg_lo:[0,0,1]
	s_nop 0
	v_pk_add_f32 v[116:117], v[26:27], v[140:141]
	v_pk_add_f32 v[22:23], v[18:19], v[150:151]
	v_pk_mul_f32 v[118:119], v[126:127], v[116:117] op_sel:[1,0]
	s_nop 0
	v_pk_fma_f32 v[124:125], v[126:127], v[116:117], v[118:119] op_sel:[0,0,1] op_sel_hi:[0,1,0] neg_hi:[0,0,1]
	s_nop 0
	v_pk_add_f32 v[116:117], v[22:23], v[124:125]
	v_pk_add_f32 v[14:15], v[6:7], v[148:149]
	s_waitcnt lgkmcnt(1)
; template <int R, class XT, class TWT>
; __device__ __forceinline__ void dit_task(XT X, TWT tw, int s, int task) {
;     const int lgM = 13 - s, lgq = lgM - R, q = 1 << lgq;
;     const int j0 = task & (q - 1), blk = task >> lgq, base = (blk << lgM) + j0;
;     const int pb = PADI(base), qp = (q >= 32) ? q + (q >> 4) : q;
;     f32x2v v[1 << R];
; #pragma unroll
;     for (int k = 0; k < (1 << R); ++k) v[k] = X[pb + k * qp];
; #pragma unroll
;     for (int r = R - 1; r >= 0; --r) {
;         const int pb = R - 1 - r;
; #pragma unroll
;         for (int k = 0; k < (1 << R); ++k) if (!((k >> pb) & 1)) {
;             const int klo = k & ((1 << pb) - 1);
;             const f32x2v w = tw[(j0 + (klo << lgq)) << (s + r)];
;             const f32x2v a = v[k], qv = v[k + (1 << pb)]; const f32x2v b = (f32x2v){qv.x * w.x + qv.y * w.y, qv.y * w.x - qv.x * w.y};
;             v[k] = a + b; v[k + (1 << pb)] = a - b;
;         }
;     }
; #pragma unroll
;     for (int k = 0; k < (1 << R); ++k) X[pb + k * qp] = v[k];
; }
	v_pk_mul_f32 v[118:119], v[132:133], v[116:117] op_sel:[1,0]
	v_pk_add_f32 v[10:11], v[10:11], v[144:145] neg_lo:[0,1] neg_hi:[0,1]
	v_pk_fma_f32 v[126:127], v[132:133], v[116:117], v[118:119] op_sel:[0,0,1] op_sel_hi:[0,1,0] neg_hi:[0,0,1]
	v_pk_mul_f32 v[118:119], v[128:129], v[12:13] op_sel_hi:[0,1]
	v_pk_add_f32 v[116:117], v[14:15], v[126:127]
	v_pk_add_f32 v[14:15], v[14:15], v[126:127] neg_lo:[0,1] neg_hi:[0,1]
	v_pk_fma_f32 v[126:127], v[128:129], v[12:13], v[118:119] op_sel:[1,0,1] op_sel_hi:[1,1,0] neg_lo:[0,0,1]
	v_pk_mul_f32 v[118:119], v[128:129], v[28:29] op_sel_hi:[0,1]
	v_pk_fma_f32 v[138:139], v[128:129], v[28:29], v[118:119] op_sel:[1,0,1] op_sel_hi:[1,1,0] neg_lo:[0,0,1]
	s_nop 0
	v_pk_add_f32 v[28:29], v[20:21], v[138:139]
	v_pk_add_f32 v[12:13], v[2:3], v[126:127]
	v_pk_mul_f32 v[118:119], v[122:123], v[28:29] op_sel:[1,0]
	v_pk_add_f32 v[26:27], v[26:27], v[140:141] neg_lo:[0,1] neg_hi:[0,1]
	v_pk_fma_f32 v[128:129], v[122:123], v[28:29], v[118:119] op_sel:[0,0,1] op_sel_hi:[0,1,0] neg_hi:[0,0,1]
	v_pk_mul_f32 v[118:119], v[130:131], v[10:11] op_sel_hi:[0,1]
	v_pk_add_f32 v[28:29], v[12:13], v[128:129]
	v_pk_add_f32 v[12:13], v[12:13], v[128:129] neg_lo:[0,1] neg_hi:[0,1]
	v_pk_fma_f32 v[128:129], v[130:131], v[10:11], v[118:119] op_sel:[1,0,1] op_sel_hi:[1,1,0] neg_lo:[0,0,1]
	v_pk_mul_f32 v[118:119], v[130:131], v[26:27] op_sel_hi:[0,1]
	v_pk_fma_f32 v[140:141], v[130:131], v[26:27], v[118:119] op_sel:[1,0,1] op_sel_hi:[1,1,0] neg_lo:[0,0,1]
	v_pk_add_f32 v[18:19], v[18:19], v[150:151] neg_lo:[0,1] neg_hi:[0,1]
	s_nop 0
	v_pk_add_f32 v[26:27], v[18:19], v[140:141]
	v_pk_add_f32 v[0:1], v[0:1], v[142:143] neg_lo:[0,1] neg_hi:[0,1]
	s_waitcnt lgkmcnt(0)
	v_pk_mul_f32 v[118:119], v[136:137], v[26:27] op_sel:[1,0]
	s_nop 0
	v_pk_fma_f32 v[130:131], v[136:137], v[26:27], v[118:119] op_sel:[0,0,1] op_sel_hi:[0,1,0] neg_hi:[0,0,1]
	v_pk_add_f32 v[24:25], v[24:25], v[164:165] neg_lo:[0,1] neg_hi:[0,1]
	v_pk_add_f32 v[10:11], v[0:1], v[128:129]
	v_pk_mul_f32 v[118:119], v[120:121], v[24:25] op_sel_hi:[0,1]
	v_pk_add_f32 v[22:23], v[22:23], v[124:125] neg_lo:[0,1] neg_hi:[0,1]
	v_pk_add_f32 v[26:27], v[10:11], v[130:131]
	v_pk_add_f32 v[10:11], v[10:11], v[130:131] neg_lo:[0,1] neg_hi:[0,1]
	v_pk_fma_f32 v[130:131], v[120:121], v[24:25], v[118:119] op_sel:[1,0,1] op_sel_hi:[1,1,0] neg_lo:[0,0,1] neg_hi:[0,0,1]
	v_pk_fma_f32 v[24:25], v[120:121], v[24:25], v[118:119] op_sel:[1,0,1] op_sel_hi:[1,1,0]
	v_pk_mul_f32 v[118:119], v[132:133], v[22:23] op_sel_hi:[0,1]
	v_pk_fma_f32 v[120:121], v[132:133], v[22:23], v[118:119] op_sel:[1,0,1] op_sel_hi:[1,1,0] neg_lo:[0,0,1]
	v_pk_add_f32 v[20:21], v[20:21], v[138:139] neg_lo:[0,1] neg_hi:[0,1]
	v_pk_add_f32 v[6:7], v[6:7], v[148:149] neg_lo:[0,1] neg_hi:[0,1]
	v_pk_mul_f32 v[118:119], v[122:123], v[20:21] op_sel_hi:[0,1]
	v_pk_add_f32 v[22:23], v[6:7], v[120:121]
	v_pk_add_f32 v[6:7], v[6:7], v[120:121] neg_lo:[0,1] neg_hi:[0,1]
	v_pk_fma_f32 v[120:121], v[122:123], v[20:21], v[118:119] op_sel:[1,0,1] op_sel_hi:[1,1,0] neg_lo:[0,0,1]
	v_pk_add_f32 v[18:19], v[18:19], v[140:141] neg_lo:[0,1] neg_hi:[0,1]
	v_mov_b32_e32 v155, v17
	v_pk_add_f32 v[2:3], v[2:3], v[126:127] neg_lo:[0,1] neg_hi:[0,1]
	v_pk_mul_f32 v[118:119], v[136:137], v[18:19] op_sel_hi:[0,1]
	v_pk_add_f32 v[16:17], v[8:9], v[154:155]
	v_mov_b32_e32 v167, v31
	v_pk_add_f32 v[20:21], v[2:3], v[120:121]
	v_pk_add_f32 v[2:3], v[2:3], v[120:121] neg_lo:[0,1] neg_hi:[0,1]
	v_pk_fma_f32 v[120:121], v[136:137], v[18:19], v[118:119] op_sel:[1,0,1] op_sel_hi:[1,1,0] neg_lo:[0,0,1]
	v_pk_add_f32 v[30:31], v[16:17], v[166:167]
	v_pk_add_f32 v[8:9], v[8:9], v[154:155] neg_lo:[0,1] neg_hi:[0,1]
	v_mov_b32_e32 v131, v25
	v_pk_add_f32 v[0:1], v[0:1], v[128:129] neg_lo:[0,1] neg_hi:[0,1]
	v_pk_add_f32 v[16:17], v[16:17], v[166:167] neg_lo:[0,1] neg_hi:[0,1]
	v_pk_add_f32 v[24:25], v[8:9], v[130:131]
	v_pk_add_f32 v[8:9], v[8:9], v[130:131] neg_lo:[0,1] neg_hi:[0,1]
	v_pk_add_f32 v[18:19], v[0:1], v[120:121]
	v_pk_add_f32 v[0:1], v[0:1], v[120:121] neg_lo:[0,1] neg_hi:[0,1]
	ds_write2_b64 v84, v[30:31], v[116:117] offset1:2
	ds_write2_b64 v84, v[28:29], v[26:27] offset0:4 offset1:6
	ds_write2_b64 v84, v[24:25], v[22:23] offset0:8 offset1:10
	ds_write2_b64 v84, v[20:21], v[18:19] offset0:12 offset1:14
	ds_write2_b64 v84, v[16:17], v[14:15] offset0:16 offset1:18
	ds_write2_b64 v84, v[12:13], v[10:11] offset0:20 offset1:22
	ds_write2_b64 v84, v[8:9], v[6:7] offset0:24 offset1:26
	ds_write2_b64 v84, v[2:3], v[0:1] offset0:28 offset1:30
	s_waitcnt lgkmcnt(0)
	s_barrier
; template <int R, class XT, class TWT>
; __device__ __forceinline__ void dit_task(XT X, TWT tw, int s, int task) {
;     const int lgM = 13 - s, lgq = lgM - R, q = 1 << lgq;
;     const int j0 = task & (q - 1), blk = task >> lgq, base = (blk << lgM) + j0;
;     const int pb = PADI(base), qp = (q >= 32) ? q + (q >> 4) : q;
;     f32x2v v[1 << R];
; #pragma unroll
;     for (int k = 0; k < (1 << R); ++k) v[k] = X[pb + k * qp];
; #pragma unroll
;     for (int r = R - 1; r >= 0; --r) {
;         const int pb = R - 1 - r;
; #pragma unroll
;         for (int k = 0; k < (1 << R); ++k) if (!((k >> pb) & 1)) {
;             const int klo = k & ((1 << pb) - 1);
;             const f32x2v w = tw[(j0 + (klo << lgq)) << (s + r)];
;             const f32x2v a = v[k], qv = v[k + (1 << pb)]; const f32x2v b = (f32x2v){qv.x * w.x + qv.y * w.y, qv.y * w.x - qv.x * w.y};
;             v[k] = a + b; v[k + (1 << pb)] = a - b;
;         }
;     }
; #pragma unroll
;     for (int k = 0; k < (1 << R); ++k) X[pb + k * qp] = v[k];
; }
; template <bool LAT>
; __device__ __forceinline__ void hyconv_unit(const Frame& F, LAS f32x2v* X, const TwHalf tw, LAS bf16* OUT, const float* skip, bf16* MIX, int u) {
;     ...
;                 unsigned ga[4], gb[4], za[4], zb[4];
; #pragma unroll
;                 for (int r = 0; r < 4; ++r) { const int pr = F.tid + 512 * r; ga[r] = *(const unsigned*)(g0 + 2 * pr); gb[r] = *(const unsigned*)(g1 + 2 * pr); za[r] = *(const unsigned*)(v0 + 2 * pr); zb[r] = *(const unsigned*)(v1 + 2 * pr); }
	v_lshl_add_u64 v[168:169], s[24:25], 0, v[50:51]
	v_lshl_add_u64 v[168:169], s[2:3], 0, v[168:169]
	global_load_dword v182, v[168:169], off
	global_load_dword v183, v[52:53], off
	v_lshl_add_u64 v[170:171], s[26:27], 0, v[50:51]
	v_lshl_add_u64 v[170:171], s[2:3], 0, v[170:171]
	global_load_dword v184, v[170:171], off
	global_load_dword v185, v[54:55], off
	v_lshl_add_u64 v[172:173], s[24:25], 0, v[56:57]
	v_lshl_add_u64 v[172:173], s[2:3], 0, v[172:173]
	global_load_dword v186, v[172:173], off
	v_lshl_add_u64 v[174:175], s[26:27], 0, v[56:57]
	v_lshl_add_u64 v[174:175], s[2:3], 0, v[174:175]
	global_load_dword v187, v[174:175], off
	v_lshl_add_u64 v[176:177], s[24:25], 0, v[62:63]
	v_lshl_add_u64 v[176:177], s[2:3], 0, v[176:177]
	global_load_dword v188, v[176:177], off
	v_lshl_add_u64 v[178:179], s[26:27], 0, v[62:63]
	v_lshl_add_u64 v[178:179], s[2:3], 0, v[178:179]
	global_load_dword v189, v[178:179], off
	global_load_dword v190, v[170:171], off offset:2048
	global_load_dword v191, v[168:169], off offset:2048
	global_load_dword v192, v[58:59], off
	global_load_dword v193, v[60:61], off
	global_load_dword v194, v[64:65], off
	global_load_dword v195, v[66:67], off
	global_load_dword v196, v[54:55], off offset:2048
	global_load_dword v197, v[52:53], off offset:2048
	ds_read2_b64 v[0:3], v81 offset1:34
	ds_read2_b64 v[6:9], v81 offset0:68 offset1:102
	ds_read2_b64 v[10:13], v81 offset0:136 offset1:170
	ds_read2_b64 v[14:17], v81 offset0:204 offset1:238
	ds_read2_b64 v[18:21], v110 offset0:16 offset1:50
	ds_read2_b64 v[22:25], v110 offset0:84 offset1:118
	ds_read2_b64 v[26:29], v110 offset0:152 offset1:186
	ds_read2_b64 v[116:119], v110 offset0:220 offset1:254
	ds_read_b64 v[30:31], v99
	ds_read_b64 v[124:125], v97
	ds_read_b64 v[126:127], v98
	ds_read_b64 v[128:129], v83
	ds_read_b64 v[130:131], v95
	ds_read_b64 v[132:133], v96
	ds_read_b64 v[136:137], v82
	ds_read2st64_b64 v[120:123], v94 offset1:16
	s_waitcnt lgkmcnt(4)
	v_xor_b32_e32 v5, 0x80000000, v128
	v_cndmask_b32_e64 v139, v5, v129, s[40:41]
	v_cndmask_b32_e64 v138, v129, v128, s[40:41]
	v_mov_b32_e32 v128, v139
	v_pk_mul_f32 v[140:141], v[2:3], v[128:129] op_sel_hi:[1,0]
	s_addc_u32 s1, s25, s3
	v_pk_fma_f32 v[142:143], v[2:3], v[138:139], v[140:141] op_sel:[0,0,1] op_sel_hi:[1,0,0] neg_hi:[0,0,1]
	v_pk_mul_f32 v[140:141], v[8:9], v[128:129] op_sel_hi:[1,0]
	s_nop 0
	v_pk_fma_f32 v[144:145], v[8:9], v[138:139], v[140:141] op_sel:[0,0,1] op_sel_hi:[1,0,0] neg_hi:[0,0,1]
	v_pk_add_f32 v[2:3], v[0:1], v[142:143]
	v_pk_add_f32 v[8:9], v[6:7], v[144:145]
	v_pk_add_f32 v[6:7], v[6:7], v[144:145] neg_lo:[0,1] neg_hi:[0,1]
	v_pk_mul_f32 v[140:141], v[30:31], v[8:9] op_sel:[1,0]
	v_pk_add_f32 v[0:1], v[0:1], v[142:143] neg_lo:[0,1] neg_hi:[0,1]
	v_pk_fma_f32 v[146:147], v[30:31], v[8:9], v[140:141] op_sel:[0,0,1] op_sel_hi:[0,1,0] neg_hi:[0,0,1]
	v_pk_mul_f32 v[140:141], v[12:13], v[128:129] op_sel_hi:[1,0]
	s_nop 0
	v_pk_fma_f32 v[148:149], v[12:13], v[138:139], v[140:141] op_sel:[0,0,1] op_sel_hi:[1,0,0] neg_hi:[0,0,1]
	v_pk_mul_f32 v[140:141], v[16:17], v[128:129] op_sel_hi:[1,0]
	s_nop 0
	v_pk_fma_f32 v[150:151], v[16:17], v[138:139], v[140:141] op_sel:[0,0,1] op_sel_hi:[1,0,0] neg_hi:[0,0,1]
	v_pk_add_f32 v[12:13], v[10:11], v[148:149]
	v_pk_add_f32 v[16:17], v[14:15], v[150:151]
	v_pk_add_f32 v[14:15], v[14:15], v[150:151] neg_lo:[0,1] neg_hi:[0,1]
	v_pk_mul_f32 v[140:141], v[30:31], v[16:17] op_sel:[1,0]
	v_pk_add_f32 v[10:11], v[10:11], v[148:149] neg_lo:[0,1] neg_hi:[0,1]
	v_pk_fma_f32 v[152:153], v[30:31], v[16:17], v[140:141] op_sel:[0,0,1] op_sel_hi:[0,1,0] neg_hi:[0,0,1]
	s_nop 0
	v_pk_add_f32 v[16:17], v[12:13], v[152:153]
	v_pk_add_f32 v[12:13], v[12:13], v[152:153] neg_lo:[0,1] neg_hi:[0,1]
	v_pk_mul_f32 v[140:141], v[124:125], v[16:17] op_sel:[1,0]
	v_pk_add_f32 v[8:9], v[2:3], v[146:147]
	v_pk_fma_f32 v[154:155], v[124:125], v[16:17], v[140:141] op_sel:[0,0,1] op_sel_hi:[1,1,0]
	v_pk_fma_f32 v[16:17], v[124:125], v[16:17], v[140:141] op_sel:[0,0,1] op_sel_hi:[0,1,0] neg_lo:[0,0,1] neg_hi:[0,0,1]
	v_pk_mul_f32 v[140:141], v[20:21], v[128:129] op_sel_hi:[1,0]
	v_pk_add_f32 v[2:3], v[2:3], v[146:147] neg_lo:[0,1] neg_hi:[0,1]
	v_pk_fma_f32 v[156:157], v[20:21], v[138:139], v[140:141] op_sel:[0,0,1] op_sel_hi:[1,0,0] neg_hi:[0,0,1]
	v_pk_mul_f32 v[140:141], v[24:25], v[128:129] op_sel_hi:[1,0]
	s_nop 0
	v_pk_fma_f32 v[158:159], v[24:25], v[138:139], v[140:141] op_sel:[0,0,1] op_sel_hi:[1,0,0] neg_hi:[0,0,1]
	v_pk_add_f32 v[20:21], v[18:19], v[156:157]
	v_pk_add_f32 v[24:25], v[22:23], v[158:159]
	v_pk_add_f32 v[22:23], v[22:23], v[158:159] neg_lo:[0,1] neg_hi:[0,1]
	v_pk_mul_f32 v[140:141], v[30:31], v[24:25] op_sel:[1,0]
	v_pk_add_f32 v[18:19], v[18:19], v[156:157] neg_lo:[0,1] neg_hi:[0,1]
	v_pk_fma_f32 v[160:161], v[30:31], v[24:25], v[140:141] op_sel:[0,0,1] op_sel_hi:[0,1,0] neg_hi:[0,0,1]
	v_pk_mul_f32 v[140:141], v[28:29], v[128:129] op_sel_hi:[1,0]
	v_pk_mul_f32 v[128:129], v[118:119], v[128:129] op_sel_hi:[1,0]
	v_pk_fma_f32 v[162:163], v[28:29], v[138:139], v[140:141] op_sel:[0,0,1] op_sel_hi:[1,0,0] neg_hi:[0,0,1]
	v_pk_fma_f32 v[140:141], v[118:119], v[138:139], v[128:129] op_sel:[0,0,1] op_sel_hi:[1,0,0] neg_hi:[0,0,1]
	s_nop 0
	v_pk_add_f32 v[118:119], v[116:117], v[140:141]
	v_pk_add_f32 v[28:29], v[26:27], v[162:163]
	v_pk_mul_f32 v[128:129], v[30:31], v[118:119] op_sel:[1,0]
	s_nop 0
	v_pk_fma_f32 v[138:139], v[30:31], v[118:119], v[128:129] op_sel:[0,0,1] op_sel_hi:[0,1,0] neg_hi:[0,0,1]
	s_nop 0
	v_pk_add_f32 v[118:119], v[28:29], v[138:139]
	v_pk_add_f32 v[24:25], v[20:21], v[160:161]
	v_pk_mul_f32 v[128:129], v[124:125], v[118:119] op_sel:[1,0]
	v_pk_add_f32 v[116:117], v[116:117], v[140:141] neg_lo:[0,1] neg_hi:[0,1]
	v_pk_fma_f32 v[164:165], v[124:125], v[118:119], v[128:129] op_sel:[0,0,1] op_sel_hi:[0,1,0] neg_hi:[0,0,1]
	s_nop 0
	v_pk_add_f32 v[118:119], v[24:25], v[164:165]
	v_pk_add_f32 v[26:27], v[26:27], v[162:163] neg_lo:[0,1] neg_hi:[0,1]
	s_waitcnt lgkmcnt(0)
; template <int R, class XT, class TWT>
; __device__ __forceinline__ void dit_task(XT X, TWT tw, int s, int task) {
;     const int lgM = 13 - s, lgq = lgM - R, q = 1 << lgq;
;     const int j0 = task & (q - 1), blk = task >> lgq, base = (blk << lgM) + j0;
;     const int pb = PADI(base), qp = (q >= 32) ? q + (q >> 4) : q;
;     f32x2v v[1 << R];
; #pragma unroll
;     for (int k = 0; k < (1 << R); ++k) v[k] = X[pb + k * qp];
; #pragma unroll
;     for (int r = R - 1; r >= 0; --r) {
;         const int pb = R - 1 - r;
; #pragma unroll
;         for (int k = 0; k < (1 << R); ++k) if (!((k >> pb) & 1)) {
;             const int klo = k & ((1 << pb) - 1);
;             const f32x2v w = tw[(j0 + (klo << lgq)) << (s + r)];
;             const f32x2v a = v[k], qv = v[k + (1 << pb)]; const f32x2v b = (f32x2v){qv.x * w.x + qv.y * w.y, qv.y * w.x - qv.x * w.y};
;             v[k] = a + b; v[k + (1 << pb)] = a - b;
;         }
;     }
; #pragma unroll
;     for (int k = 0; k < (1 << R); ++k) X[pb + k * qp] = v[k];
; }
	v_pk_mul_f32 v[128:129], v[120:121], v[118:119] op_sel:[1,0]
	v_pk_add_f32 v[28:29], v[28:29], v[138:139] neg_lo:[0,1] neg_hi:[0,1]
	v_pk_fma_f32 v[166:167], v[120:121], v[118:119], v[128:129] op_sel:[0,0,1] op_sel_hi:[1,1,0]
	v_pk_fma_f32 v[118:119], v[120:121], v[118:119], v[128:129] op_sel:[0,0,1] op_sel_hi:[0,1,0] neg_lo:[0,0,1] neg_hi:[0,0,1]
	v_pk_mul_f32 v[128:129], v[30:31], v[6:7] op_sel_hi:[0,1]
	v_pk_fma_f32 v[142:143], v[30:31], v[6:7], v[128:129] op_sel:[1,0,1] op_sel_hi:[1,1,0] neg_lo:[0,0,1]
	v_pk_mul_f32 v[128:129], v[30:31], v[14:15] op_sel_hi:[0,1]
	v_pk_fma_f32 v[144:145], v[30:31], v[14:15], v[128:129] op_sel:[1,0,1] op_sel_hi:[1,1,0] neg_lo:[0,0,1]
	s_nop 0
	v_pk_add_f32 v[14:15], v[10:11], v[144:145]
	v_pk_add_f32 v[6:7], v[0:1], v[142:143]
	v_pk_mul_f32 v[128:129], v[126:127], v[14:15] op_sel:[1,0]
	v_pk_add_f32 v[20:21], v[20:21], v[160:161] neg_lo:[0,1] neg_hi:[0,1]
	v_pk_fma_f32 v[148:149], v[126:127], v[14:15], v[128:129] op_sel:[0,0,1] op_sel_hi:[0,1,0] neg_hi:[0,0,1]
	v_pk_mul_f32 v[128:129], v[30:31], v[22:23] op_sel_hi:[0,1]
	v_pk_fma_f32 v[150:151], v[30:31], v[22:23], v[128:129] op_sel:[1,0,1] op_sel_hi:[1,1,0] neg_lo:[0,0,1]
	v_pk_mul_f32 v[128:129], v[30:31], v[116:117] op_sel_hi:[0,1]
	v_pk_fma_f32 v[140:141], v[30:31], v[116:117], v[128:129] op_sel:[1,0,1] op_sel_hi:[1,1,0] neg_lo:[0,0,1]
	s_nop 0
	v_pk_add_f32 v[30:31], v[26:27], v[140:141]
	v_pk_add_f32 v[22:23], v[18:19], v[150:151]
	v_pk_mul_f32 v[116:117], v[126:127], v[30:31] op_sel:[1,0]
	s_nop 0
	v_pk_fma_f32 v[128:129], v[126:127], v[30:31], v[116:117] op_sel:[0,0,1] op_sel_hi:[0,1,0] neg_hi:[0,0,1]
	s_nop 0
	v_pk_add_f32 v[30:31], v[22:23], v[128:129]
	v_pk_add_f32 v[14:15], v[6:7], v[148:149]
	v_pk_mul_f32 v[116:117], v[130:131], v[30:31] op_sel:[1,0]
	v_pk_add_f32 v[10:11], v[10:11], v[144:145] neg_lo:[0,1] neg_hi:[0,1]
	v_pk_fma_f32 v[126:127], v[130:131], v[30:31], v[116:117] op_sel:[0,0,1] op_sel_hi:[0,1,0] neg_hi:[0,0,1]
	v_pk_mul_f32 v[116:117], v[124:125], v[12:13] op_sel_hi:[0,1]
	v_pk_add_f32 v[30:31], v[14:15], v[126:127]
	v_pk_add_f32 v[14:15], v[14:15], v[126:127] neg_lo:[0,1] neg_hi:[0,1]
	v_pk_fma_f32 v[126:127], v[124:125], v[12:13], v[116:117] op_sel:[1,0,1] op_sel_hi:[1,1,0] neg_lo:[0,0,1]
	v_pk_mul_f32 v[116:117], v[124:125], v[28:29] op_sel_hi:[0,1]
	v_pk_fma_f32 v[138:139], v[124:125], v[28:29], v[116:117] op_sel:[1,0,1] op_sel_hi:[1,1,0] neg_lo:[0,0,1]
	s_nop 0
	v_pk_add_f32 v[28:29], v[20:21], v[138:139]
	v_pk_add_f32 v[12:13], v[2:3], v[126:127]
	v_pk_mul_f32 v[116:117], v[122:123], v[28:29] op_sel:[1,0]
	v_pk_add_f32 v[26:27], v[26:27], v[140:141] neg_lo:[0,1] neg_hi:[0,1]
	v_pk_fma_f32 v[124:125], v[122:123], v[28:29], v[116:117] op_sel:[0,0,1] op_sel_hi:[0,1,0] neg_hi:[0,0,1]
	v_pk_mul_f32 v[116:117], v[136:137], v[10:11] op_sel_hi:[0,1]
	v_pk_add_f32 v[28:29], v[12:13], v[124:125]
	v_pk_add_f32 v[12:13], v[12:13], v[124:125] neg_lo:[0,1] neg_hi:[0,1]
	v_pk_fma_f32 v[124:125], v[136:137], v[10:11], v[116:117] op_sel:[1,0,1] op_sel_hi:[1,1,0] neg_lo:[0,0,1]
	v_pk_mul_f32 v[116:117], v[136:137], v[26:27] op_sel_hi:[0,1]
	v_pk_fma_f32 v[140:141], v[136:137], v[26:27], v[116:117] op_sel:[1,0,1] op_sel_hi:[1,1,0] neg_lo:[0,0,1]
	v_pk_add_f32 v[18:19], v[18:19], v[150:151] neg_lo:[0,1] neg_hi:[0,1]
	s_nop 0
	v_pk_add_f32 v[26:27], v[18:19], v[140:141]
	v_pk_add_f32 v[0:1], v[0:1], v[142:143] neg_lo:[0,1] neg_hi:[0,1]
	v_pk_mul_f32 v[116:117], v[132:133], v[26:27] op_sel:[1,0]
	s_nop 0
	v_pk_fma_f32 v[136:137], v[132:133], v[26:27], v[116:117] op_sel:[0,0,1] op_sel_hi:[0,1,0] neg_hi:[0,0,1]
	v_pk_add_f32 v[24:25], v[24:25], v[164:165] neg_lo:[0,1] neg_hi:[0,1]
	v_pk_add_f32 v[10:11], v[0:1], v[124:125]
	v_pk_mul_f32 v[116:117], v[120:121], v[24:25] op_sel_hi:[0,1]
	v_pk_add_f32 v[22:23], v[22:23], v[128:129] neg_lo:[0,1] neg_hi:[0,1]
	v_pk_add_f32 v[26:27], v[10:11], v[136:137]
	v_pk_add_f32 v[10:11], v[10:11], v[136:137] neg_lo:[0,1] neg_hi:[0,1]
	v_pk_fma_f32 v[136:137], v[120:121], v[24:25], v[116:117] op_sel:[1,0,1] op_sel_hi:[1,1,0] neg_lo:[0,0,1] neg_hi:[0,0,1]
	v_pk_fma_f32 v[24:25], v[120:121], v[24:25], v[116:117] op_sel:[1,0,1] op_sel_hi:[1,1,0]
	v_pk_mul_f32 v[116:117], v[130:131], v[22:23] op_sel_hi:[0,1]
	v_pk_fma_f32 v[120:121], v[130:131], v[22:23], v[116:117] op_sel:[1,0,1] op_sel_hi:[1,1,0] neg_lo:[0,0,1]
	v_pk_add_f32 v[20:21], v[20:21], v[138:139] neg_lo:[0,1] neg_hi:[0,1]
	v_pk_add_f32 v[6:7], v[6:7], v[148:149] neg_lo:[0,1] neg_hi:[0,1]
	v_pk_mul_f32 v[116:117], v[122:123], v[20:21] op_sel_hi:[0,1]
	v_pk_add_f32 v[22:23], v[6:7], v[120:121]
	v_pk_add_f32 v[6:7], v[6:7], v[120:121] neg_lo:[0,1] neg_hi:[0,1]
	v_pk_fma_f32 v[120:121], v[122:123], v[20:21], v[116:117] op_sel:[1,0,1] op_sel_hi:[1,1,0] neg_lo:[0,0,1]
	v_pk_add_f32 v[18:19], v[18:19], v[140:141] neg_lo:[0,1] neg_hi:[0,1]
	v_mov_b32_e32 v155, v17
	v_pk_add_f32 v[2:3], v[2:3], v[126:127] neg_lo:[0,1] neg_hi:[0,1]
	v_pk_mul_f32 v[116:117], v[132:133], v[18:19] op_sel_hi:[0,1]
	v_pk_add_f32 v[16:17], v[8:9], v[154:155]
	v_mov_b32_e32 v167, v119
	v_pk_add_f32 v[20:21], v[2:3], v[120:121]
	v_pk_add_f32 v[2:3], v[2:3], v[120:121] neg_lo:[0,1] neg_hi:[0,1]
	v_pk_fma_f32 v[120:121], v[132:133], v[18:19], v[116:117] op_sel:[1,0,1] op_sel_hi:[1,1,0] neg_lo:[0,0,1]
	v_pk_add_f32 v[118:119], v[16:17], v[166:167]
	v_pk_add_f32 v[8:9], v[8:9], v[154:155] neg_lo:[0,1] neg_hi:[0,1]
	v_mov_b32_e32 v137, v25
	v_pk_add_f32 v[0:1], v[0:1], v[124:125] neg_lo:[0,1] neg_hi:[0,1]
	v_pk_add_f32 v[16:17], v[16:17], v[166:167] neg_lo:[0,1] neg_hi:[0,1]
	v_pk_add_f32 v[24:25], v[8:9], v[136:137]
	v_pk_add_f32 v[8:9], v[8:9], v[136:137] neg_lo:[0,1] neg_hi:[0,1]
	v_pk_add_f32 v[18:19], v[0:1], v[120:121]
	v_pk_add_f32 v[0:1], v[0:1], v[120:121] neg_lo:[0,1] neg_hi:[0,1]
	ds_write2_b64 v81, v[118:119], v[30:31] offset1:34
	ds_write2_b64 v81, v[28:29], v[26:27] offset0:68 offset1:102
	ds_write2_b64 v81, v[24:25], v[22:23] offset0:136 offset1:170
	ds_write2_b64 v81, v[20:21], v[18:19] offset0:204 offset1:238
	ds_write2_b64 v110, v[16:17], v[14:15] offset0:16 offset1:50
	ds_write2_b64 v110, v[12:13], v[10:11] offset0:84 offset1:118
	ds_write2_b64 v110, v[8:9], v[6:7] offset0:152 offset1:186
	ds_write2_b64 v110, v[2:3], v[0:1] offset0:220 offset1:254
	s_waitcnt lgkmcnt(0)
	s_barrier
; template <int R, class XT, class TWT>
; __device__ __forceinline__ void dit_task(XT X, TWT tw, int s, int task) {
;     const int lgM = 13 - s, lgq = lgM - R, q = 1 << lgq;
;     const int j0 = task & (q - 1), blk = task >> lgq, base = (blk << lgM) + j0;
;     const int pb = PADI(base), qp = (q >= 32) ? q + (q >> 4) : q;
;     f32x2v v[1 << R];
; #pragma unroll
;     for (int k = 0; k < (1 << R); ++k) v[k] = X[pb + k * qp];
; #pragma unroll
;     for (int r = R - 1; r >= 0; --r) {
;         const int pb = R - 1 - r;
; #pragma unroll
;         for (int k = 0; k < (1 << R); ++k) if (!((k >> pb) & 1)) {
;             const int klo = k & ((1 << pb) - 1);
;             const f32x2v w = tw[(j0 + (klo << lgq)) << (s + r)];
;             const f32x2v a = v[k], qv = v[k + (1 << pb)]; const f32x2v b = (f32x2v){qv.x * w.x + qv.y * w.y, qv.y * w.x - qv.x * w.y};
;             v[k] = a + b; v[k + (1 << pb)] = a - b;
;         }
;     }
; #pragma unroll
;     for (int k = 0; k < (1 << R); ++k) X[pb + k * qp] = v[k];
; }
	ds_read_b64 v[6:7], v75
	ds_read_b64 v[8:9], v75 offset:4352
	ds_read_b64 v[10:11], v75 offset:8704
	ds_read_b64 v[12:13], v75 offset:13056
	ds_read_b64 v[14:15], v75 offset:17408
	ds_read_b64 v[16:17], v75 offset:21760
	ds_read_b64 v[18:19], v75 offset:26112
	ds_read_b64 v[20:21], v75 offset:30464
	ds_read_b64 v[22:23], v75 offset:34816
	ds_read_b64 v[24:25], v75 offset:39168
	ds_read_b64 v[26:27], v75 offset:43520
	ds_read_b64 v[28:29], v75 offset:47872
	ds_read_b64 v[30:31], v75 offset:52224
	ds_read_b64 v[110:111], v75 offset:56576
	ds_read_b64 v[116:117], v75 offset:60928
	ds_read_b64 v[118:119], v75 offset:65280
	ds_read_b64 v[120:121], v80
	ds_read_b64 v[122:123], v93
	ds_read_b64 v[124:125], v91
	ds_read_b64 v[126:127], v92
	ds_read2st64_b64 v[0:3], v76 offset1:16
	ds_read_b64 v[128:129], v79
	ds_read_b64 v[130:131], v77
	ds_read_b64 v[132:133], v78
	s_waitcnt lgkmcnt(7)
	v_xor_b32_e32 v5, 0x80000000, v120
	v_cndmask_b32_e64 v137, v5, v121, s[38:39]
	v_cndmask_b32_e64 v136, v121, v120, s[38:39]
	v_mov_b32_e32 v120, v137
	v_pk_mul_f32 v[138:139], v[8:9], v[120:121] op_sel_hi:[1,0]
	s_add_u32 s2, s26, s2
	v_pk_fma_f32 v[140:141], v[8:9], v[136:137], v[138:139] op_sel:[0,0,1] op_sel_hi:[1,0,0] neg_hi:[0,0,1]
	v_pk_mul_f32 v[138:139], v[12:13], v[120:121] op_sel_hi:[1,0]
	s_nop 0
	v_pk_fma_f32 v[142:143], v[12:13], v[136:137], v[138:139] op_sel:[0,0,1] op_sel_hi:[1,0,0] neg_hi:[0,0,1]
	v_pk_add_f32 v[8:9], v[6:7], v[140:141]
	v_pk_add_f32 v[12:13], v[10:11], v[142:143]
	v_pk_add_f32 v[10:11], v[10:11], v[142:143] neg_lo:[0,1] neg_hi:[0,1]
	s_waitcnt lgkmcnt(6)
	v_pk_mul_f32 v[138:139], v[122:123], v[12:13] op_sel:[1,0]
	v_pk_add_f32 v[6:7], v[6:7], v[140:141] neg_lo:[0,1] neg_hi:[0,1]
	v_pk_fma_f32 v[144:145], v[122:123], v[12:13], v[138:139] op_sel:[0,0,1] op_sel_hi:[0,1,0] neg_hi:[0,0,1]
	v_pk_mul_f32 v[138:139], v[16:17], v[120:121] op_sel_hi:[1,0]
	s_nop 0
	v_pk_fma_f32 v[146:147], v[16:17], v[136:137], v[138:139] op_sel:[0,0,1] op_sel_hi:[1,0,0] neg_hi:[0,0,1]
	v_pk_mul_f32 v[138:139], v[20:21], v[120:121] op_sel_hi:[1,0]
	s_nop 0
	v_pk_fma_f32 v[148:149], v[20:21], v[136:137], v[138:139] op_sel:[0,0,1] op_sel_hi:[1,0,0] neg_hi:[0,0,1]
	v_pk_add_f32 v[16:17], v[14:15], v[146:147]
	v_pk_add_f32 v[20:21], v[18:19], v[148:149]
	v_pk_add_f32 v[18:19], v[18:19], v[148:149] neg_lo:[0,1] neg_hi:[0,1]
	v_pk_mul_f32 v[138:139], v[122:123], v[20:21] op_sel:[1,0]
	v_pk_add_f32 v[14:15], v[14:15], v[146:147] neg_lo:[0,1] neg_hi:[0,1]
	v_pk_fma_f32 v[150:151], v[122:123], v[20:21], v[138:139] op_sel:[0,0,1] op_sel_hi:[0,1,0] neg_hi:[0,0,1]
	s_nop 0
	v_pk_add_f32 v[20:21], v[16:17], v[150:151]
	v_pk_add_f32 v[16:17], v[16:17], v[150:151] neg_lo:[0,1] neg_hi:[0,1]
	s_waitcnt lgkmcnt(5)
	v_pk_mul_f32 v[138:139], v[124:125], v[20:21] op_sel:[1,0]
	v_pk_add_f32 v[12:13], v[8:9], v[144:145]
	v_pk_fma_f32 v[152:153], v[124:125], v[20:21], v[138:139] op_sel:[0,0,1] op_sel_hi:[1,1,0]
	v_pk_fma_f32 v[20:21], v[124:125], v[20:21], v[138:139] op_sel:[0,0,1] op_sel_hi:[0,1,0] neg_lo:[0,0,1] neg_hi:[0,0,1]
	v_pk_mul_f32 v[138:139], v[24:25], v[120:121] op_sel_hi:[1,0]
	v_pk_add_f32 v[8:9], v[8:9], v[144:145] neg_lo:[0,1] neg_hi:[0,1]
	v_pk_fma_f32 v[154:155], v[24:25], v[136:137], v[138:139] op_sel:[0,0,1] op_sel_hi:[1,0,0] neg_hi:[0,0,1]
	v_pk_mul_f32 v[138:139], v[28:29], v[120:121] op_sel_hi:[1,0]
	s_nop 0
	v_pk_fma_f32 v[156:157], v[28:29], v[136:137], v[138:139] op_sel:[0,0,1] op_sel_hi:[1,0,0] neg_hi:[0,0,1]
	v_pk_add_f32 v[24:25], v[22:23], v[154:155]
	v_pk_add_f32 v[28:29], v[26:27], v[156:157]
	v_pk_add_f32 v[26:27], v[26:27], v[156:157] neg_lo:[0,1] neg_hi:[0,1]
	v_pk_mul_f32 v[138:139], v[122:123], v[28:29] op_sel:[1,0]
	v_pk_add_f32 v[22:23], v[22:23], v[154:155] neg_lo:[0,1] neg_hi:[0,1]
	v_pk_fma_f32 v[158:159], v[122:123], v[28:29], v[138:139] op_sel:[0,0,1] op_sel_hi:[0,1,0] neg_hi:[0,0,1]
	v_pk_mul_f32 v[138:139], v[110:111], v[120:121] op_sel_hi:[1,0]
	v_pk_mul_f32 v[120:121], v[118:119], v[120:121] op_sel_hi:[1,0]
	v_pk_fma_f32 v[160:161], v[110:111], v[136:137], v[138:139] op_sel:[0,0,1] op_sel_hi:[1,0,0] neg_hi:[0,0,1]
	v_pk_fma_f32 v[138:139], v[118:119], v[136:137], v[120:121] op_sel:[0,0,1] op_sel_hi:[1,0,0] neg_hi:[0,0,1]
	s_nop 0
	v_pk_add_f32 v[118:119], v[116:117], v[138:139]
	v_pk_add_f32 v[110:111], v[30:31], v[160:161]
	v_pk_mul_f32 v[120:121], v[122:123], v[118:119] op_sel:[1,0]
	s_nop 0
	v_pk_fma_f32 v[136:137], v[122:123], v[118:119], v[120:121] op_sel:[0,0,1] op_sel_hi:[0,1,0] neg_hi:[0,0,1]
	s_nop 0
	v_pk_add_f32 v[118:119], v[110:111], v[136:137]
	v_pk_add_f32 v[28:29], v[24:25], v[158:159]
	v_pk_mul_f32 v[120:121], v[124:125], v[118:119] op_sel:[1,0]
	v_pk_add_f32 v[116:117], v[116:117], v[138:139] neg_lo:[0,1] neg_hi:[0,1]
	v_pk_fma_f32 v[162:163], v[124:125], v[118:119], v[120:121] op_sel:[0,0,1] op_sel_hi:[0,1,0] neg_hi:[0,0,1]
	s_nop 0
	v_pk_add_f32 v[118:119], v[28:29], v[162:163]
	v_pk_add_f32 v[30:31], v[30:31], v[160:161] neg_lo:[0,1] neg_hi:[0,1]
	s_waitcnt lgkmcnt(3)
; template <int R, class XT, class TWT>
; __device__ __forceinline__ void dit_task(XT X, TWT tw, int s, int task) {
;     const int lgM = 13 - s, lgq = lgM - R, q = 1 << lgq;
;     const int j0 = task & (q - 1), blk = task >> lgq, base = (blk << lgM) + j0;
;     const int pb = PADI(base), qp = (q >= 32) ? q + (q >> 4) : q;
;     f32x2v v[1 << R];
; #pragma unroll
;     for (int k = 0; k < (1 << R); ++k) v[k] = X[pb + k * qp];
; #pragma unroll
;     for (int r = R - 1; r >= 0; --r) {
;         const int pb = R - 1 - r;
; #pragma unroll
;         for (int k = 0; k < (1 << R); ++k) if (!((k >> pb) & 1)) {
;             const int klo = k & ((1 << pb) - 1);
;             const f32x2v w = tw[(j0 + (klo << lgq)) << (s + r)];
;             const f32x2v a = v[k], qv = v[k + (1 << pb)]; const f32x2v b = (f32x2v){qv.x * w.x + qv.y * w.y, qv.y * w.x - qv.x * w.y};
;             v[k] = a + b; v[k + (1 << pb)] = a - b;
;         }
;     }
; #pragma unroll
;     for (int k = 0; k < (1 << R); ++k) X[pb + k * qp] = v[k];
; }
	v_pk_mul_f32 v[120:121], v[0:1], v[118:119] op_sel:[1,0]
	v_pk_add_f32 v[110:111], v[110:111], v[136:137] neg_lo:[0,1] neg_hi:[0,1]
	v_pk_fma_f32 v[164:165], v[0:1], v[118:119], v[120:121] op_sel:[0,0,1] op_sel_hi:[1,1,0]
	v_pk_fma_f32 v[118:119], v[0:1], v[118:119], v[120:121] op_sel:[0,0,1] op_sel_hi:[0,1,0] neg_lo:[0,0,1] neg_hi:[0,0,1]
	v_pk_mul_f32 v[120:121], v[122:123], v[10:11] op_sel_hi:[0,1]
	v_pk_fma_f32 v[140:141], v[122:123], v[10:11], v[120:121] op_sel:[1,0,1] op_sel_hi:[1,1,0] neg_lo:[0,0,1]
	v_pk_mul_f32 v[120:121], v[122:123], v[18:19] op_sel_hi:[0,1]
	v_pk_fma_f32 v[142:143], v[122:123], v[18:19], v[120:121] op_sel:[1,0,1] op_sel_hi:[1,1,0] neg_lo:[0,0,1]
	s_nop 0
	v_pk_add_f32 v[18:19], v[14:15], v[142:143]
	v_pk_add_f32 v[10:11], v[6:7], v[140:141]
	v_pk_mul_f32 v[120:121], v[126:127], v[18:19] op_sel:[1,0]
	v_pk_add_f32 v[24:25], v[24:25], v[158:159] neg_lo:[0,1] neg_hi:[0,1]
	v_pk_fma_f32 v[146:147], v[126:127], v[18:19], v[120:121] op_sel:[0,0,1] op_sel_hi:[0,1,0] neg_hi:[0,0,1]
	v_pk_mul_f32 v[120:121], v[122:123], v[26:27] op_sel_hi:[0,1]
	v_pk_fma_f32 v[148:149], v[122:123], v[26:27], v[120:121] op_sel:[1,0,1] op_sel_hi:[1,1,0] neg_lo:[0,0,1]
	v_pk_mul_f32 v[120:121], v[122:123], v[116:117] op_sel_hi:[0,1]
	v_pk_fma_f32 v[138:139], v[122:123], v[116:117], v[120:121] op_sel:[1,0,1] op_sel_hi:[1,1,0] neg_lo:[0,0,1]
	s_nop 0
	v_pk_add_f32 v[116:117], v[30:31], v[138:139]
	v_pk_add_f32 v[26:27], v[22:23], v[148:149]
	v_pk_mul_f32 v[120:121], v[126:127], v[116:117] op_sel:[1,0]
	s_nop 0
	v_pk_fma_f32 v[122:123], v[126:127], v[116:117], v[120:121] op_sel:[0,0,1] op_sel_hi:[0,1,0] neg_hi:[0,0,1]
	s_nop 0
	v_pk_add_f32 v[116:117], v[26:27], v[122:123]
	v_pk_add_f32 v[18:19], v[10:11], v[146:147]
	s_waitcnt lgkmcnt(1)
	v_pk_mul_f32 v[120:121], v[130:131], v[116:117] op_sel:[1,0]
	v_pk_add_f32 v[14:15], v[14:15], v[142:143] neg_lo:[0,1] neg_hi:[0,1]
	v_pk_fma_f32 v[126:127], v[130:131], v[116:117], v[120:121] op_sel:[0,0,1] op_sel_hi:[0,1,0] neg_hi:[0,0,1]
	v_pk_mul_f32 v[120:121], v[124:125], v[16:17] op_sel_hi:[0,1]
	v_pk_add_f32 v[116:117], v[18:19], v[126:127]
	v_pk_add_f32 v[18:19], v[18:19], v[126:127] neg_lo:[0,1] neg_hi:[0,1]
	v_pk_fma_f32 v[126:127], v[124:125], v[16:17], v[120:121] op_sel:[1,0,1] op_sel_hi:[1,1,0] neg_lo:[0,0,1]
	v_pk_mul_f32 v[120:121], v[124:125], v[110:111] op_sel_hi:[0,1]
	v_pk_fma_f32 v[136:137], v[124:125], v[110:111], v[120:121] op_sel:[1,0,1] op_sel_hi:[1,1,0] neg_lo:[0,0,1]
	s_nop 0
	v_pk_add_f32 v[110:111], v[24:25], v[136:137]
	v_pk_add_f32 v[16:17], v[8:9], v[126:127]
	v_pk_mul_f32 v[120:121], v[2:3], v[110:111] op_sel:[1,0]
	v_pk_add_f32 v[30:31], v[30:31], v[138:139] neg_lo:[0,1] neg_hi:[0,1]
	v_pk_fma_f32 v[124:125], v[2:3], v[110:111], v[120:121] op_sel:[0,0,1] op_sel_hi:[0,1,0] neg_hi:[0,0,1]
	v_pk_mul_f32 v[120:121], v[128:129], v[14:15] op_sel_hi:[0,1]
	v_pk_add_f32 v[110:111], v[16:17], v[124:125]
	v_pk_add_f32 v[16:17], v[16:17], v[124:125] neg_lo:[0,1] neg_hi:[0,1]
	v_pk_fma_f32 v[124:125], v[128:129], v[14:15], v[120:121] op_sel:[1,0,1] op_sel_hi:[1,1,0] neg_lo:[0,0,1]
	v_pk_mul_f32 v[120:121], v[128:129], v[30:31] op_sel_hi:[0,1]
	v_pk_fma_f32 v[138:139], v[128:129], v[30:31], v[120:121] op_sel:[1,0,1] op_sel_hi:[1,1,0] neg_lo:[0,0,1]
	v_pk_add_f32 v[22:23], v[22:23], v[148:149] neg_lo:[0,1] neg_hi:[0,1]
	s_nop 0
	v_pk_add_f32 v[30:31], v[22:23], v[138:139]
	v_pk_add_f32 v[6:7], v[6:7], v[140:141] neg_lo:[0,1] neg_hi:[0,1]
	s_waitcnt lgkmcnt(0)
	v_pk_mul_f32 v[120:121], v[132:133], v[30:31] op_sel:[1,0]
	s_nop 0
	v_pk_fma_f32 v[128:129], v[132:133], v[30:31], v[120:121] op_sel:[0,0,1] op_sel_hi:[0,1,0] neg_hi:[0,0,1]
	v_pk_add_f32 v[28:29], v[28:29], v[162:163] neg_lo:[0,1] neg_hi:[0,1]
	v_pk_add_f32 v[14:15], v[6:7], v[124:125]
	v_pk_mul_f32 v[120:121], v[0:1], v[28:29] op_sel_hi:[0,1]
	v_pk_add_f32 v[26:27], v[26:27], v[122:123] neg_lo:[0,1] neg_hi:[0,1]
	v_pk_add_f32 v[30:31], v[14:15], v[128:129]
	v_pk_add_f32 v[14:15], v[14:15], v[128:129] neg_lo:[0,1] neg_hi:[0,1]
	v_pk_fma_f32 v[128:129], v[0:1], v[28:29], v[120:121] op_sel:[1,0,1] op_sel_hi:[1,1,0] neg_lo:[0,0,1] neg_hi:[0,0,1]
	v_pk_fma_f32 v[0:1], v[0:1], v[28:29], v[120:121] op_sel:[1,0,1] op_sel_hi:[1,1,0]
	v_pk_mul_f32 v[28:29], v[130:131], v[26:27] op_sel_hi:[0,1]
	v_pk_fma_f32 v[120:121], v[130:131], v[26:27], v[28:29] op_sel:[1,0,1] op_sel_hi:[1,1,0] neg_lo:[0,0,1]
	v_pk_add_f32 v[24:25], v[24:25], v[136:137] neg_lo:[0,1] neg_hi:[0,1]
	v_pk_add_f32 v[10:11], v[10:11], v[146:147] neg_lo:[0,1] neg_hi:[0,1]
	v_pk_mul_f32 v[28:29], v[2:3], v[24:25] op_sel_hi:[0,1]
	v_pk_add_f32 v[22:23], v[22:23], v[138:139] neg_lo:[0,1] neg_hi:[0,1]
	v_mov_b32_e32 v153, v21
	v_pk_add_f32 v[26:27], v[10:11], v[120:121]
	v_pk_add_f32 v[10:11], v[10:11], v[120:121] neg_lo:[0,1] neg_hi:[0,1]
	v_pk_fma_f32 v[120:121], v[2:3], v[24:25], v[28:29] op_sel:[1,0,1] op_sel_hi:[1,1,0] neg_lo:[0,0,1] neg_hi:[0,0,1]
	v_pk_fma_f32 v[2:3], v[2:3], v[24:25], v[28:29] op_sel:[1,0,1] op_sel_hi:[1,1,0]
	v_pk_mul_f32 v[24:25], v[132:133], v[22:23] op_sel_hi:[0,1]
	v_pk_add_f32 v[20:21], v[12:13], v[152:153]
	v_mov_b32_e32 v165, v119
	v_pk_fma_f32 v[28:29], v[132:133], v[22:23], v[24:25] op_sel:[1,0,1] op_sel_hi:[1,1,0] neg_lo:[0,0,1]
	v_pk_add_f32 v[118:119], v[20:21], v[164:165]
	v_pk_add_f32 v[12:13], v[12:13], v[152:153] neg_lo:[0,1] neg_hi:[0,1]
	v_mov_b32_e32 v129, v1
	v_pk_add_f32 v[8:9], v[8:9], v[126:127] neg_lo:[0,1] neg_hi:[0,1]
	v_mov_b32_e32 v121, v3
	v_pk_add_f32 v[6:7], v[6:7], v[124:125] neg_lo:[0,1] neg_hi:[0,1]
	s_addc_u32 s3, s27, s3
	v_pk_add_f32 v[20:21], v[20:21], v[164:165] neg_lo:[0,1] neg_hi:[0,1]
	v_pk_add_f32 v[0:1], v[12:13], v[128:129]
	v_pk_add_f32 v[12:13], v[12:13], v[128:129] neg_lo:[0,1] neg_hi:[0,1]
	v_pk_add_f32 v[2:3], v[8:9], v[120:121]
	v_pk_add_f32 v[8:9], v[8:9], v[120:121] neg_lo:[0,1] neg_hi:[0,1]
	v_pk_add_f32 v[22:23], v[6:7], v[28:29]
	v_pk_add_f32 v[6:7], v[6:7], v[28:29] neg_lo:[0,1] neg_hi:[0,1]
	ds_write_b64 v75, v[118:119]
	ds_write_b64 v75, v[116:117] offset:4352
	ds_write_b64 v75, v[110:111] offset:8704
	ds_write_b64 v75, v[30:31] offset:13056
	ds_write_b64 v75, v[0:1] offset:17408
	ds_write_b64 v75, v[26:27] offset:21760
	ds_write_b64 v75, v[2:3] offset:26112
	ds_write_b64 v75, v[22:23] offset:30464
	ds_write_b64 v75, v[20:21] offset:34816
	ds_write_b64 v75, v[18:19] offset:39168
	ds_write_b64 v75, v[16:17] offset:43520
	ds_write_b64 v75, v[14:15] offset:47872
	ds_write_b64 v75, v[12:13] offset:52224
	ds_write_b64 v75, v[10:11] offset:56576
	ds_write_b64 v75, v[8:9] offset:60928
	ds_write_b64 v75, v[6:7] offset:65280
	s_waitcnt lgkmcnt(0)
	s_barrier
; #define LAS __attribute__((address_space(3)))
; template <bool LAT>
; __device__ __forceinline__ void hyconv_unit(const Frame& F, LAS f32x2v* X, const TwHalf tw, LAS bf16* OUT, const float* skip, bf16* MIX, int u) {
;     ...
;                 for (int r = 0; r < 4; ++r) { const int pr = F.tid + 512 * r; ga[r] = *(const unsigned*)(g0 + 2 * pr); gb[r] = *(const unsigned*)(g1 + 2 * pr); za[r] = *(const unsigned*)(v0 + 2 * pr); zb[r] = *(const unsigned*)(v1 + 2 * pr); }
; #pragma unroll
;                 for (int r = 0; r < 8; ++r) { const int e = 2 * (F.tid + 512 * r); f32x4 zz = (f32x4){0.f, 0.f, 0.f, 0.f};
;                     if (r < 4) { const f32x4 xx = *(const LAS f32x4*)(X + PADI(e));
;                         zz.x = bflo(ga[r]) * (xx.x + bflo(za[r]) * sk); zz.y = bflo(gb[r]) * (xx.y + bflo(zb[r]) * sk); zz.z = bfhi(ga[r]) * (xx.z + bfhi(za[r]) * sk); zz.w = bfhi(gb[r]) * (xx.w + bfhi(zb[r]) * sk);
	s_waitcnt vmcnt(0)
	v_mov_b32_e32 v5, v182
	v_mov_b32_e32 v21, v183
	v_mov_b32_e32 v23, v184
	v_mov_b32_e32 v25, v185
	v_mov_b32_e32 v13, v186
	v_mov_b32_e32 v12, v187
	v_mov_b32_e32 v9, v188
	v_mov_b32_e32 v8, v189
	v_mov_b32_e32 v16, v190
	v_mov_b32_e32 v18, v191
	v_mov_b32_e32 v15, v192
	v_mov_b32_e32 v14, v193
	v_mov_b32_e32 v11, v194
	v_mov_b32_e32 v10, v195
	v_mov_b32_e32 v17, v196
	v_mov_b32_e32 v19, v197
	ds_read_b128 v[0:3], v33
	s_and_b64 vcc, exec, s[20:21]
	s_mov_b64 s[0:1], -1
	s_waitcnt lgkmcnt(0)
	v_mov_b32_e32 v26, v0
	v_mov_b32_e32 v27, v2
	v_mov_b32_e32 v2, v1
	s_waitcnt vmcnt(15)
	v_lshlrev_b32_e32 v6, 16, v5
	s_waitcnt vmcnt(14)
	v_lshlrev_b32_e32 v20, 16, v21
	v_and_b32_e32 v21, 0xffff0000, v21
	s_waitcnt vmcnt(12)
	v_lshlrev_b32_e32 v24, 16, v25
	v_and_b32_e32 v25, 0xffff0000, v25
	v_lshlrev_b32_e32 v22, 16, v23
	v_and_b32_e32 v7, 0xffff0000, v5
	v_pk_fma_f32 v[20:21], v[4:5], v[20:21], v[26:27] op_sel_hi:[0,1,1]
	v_and_b32_e32 v23, 0xffff0000, v23
	v_pk_fma_f32 v[0:1], v[4:5], v[24:25], v[2:3] op_sel_hi:[0,1,1]
	v_pk_mul_f32 v[6:7], v[20:21], v[6:7]
	v_pk_mul_f32 v[2:3], v[0:1], v[22:23]
	s_cbranch_vccnz .LBB0_795
	s_andn2_b64 vcc, exec, s[0:1]
	s_cbranch_vccz .LBB0_796

; #define LAS __attribute__((address_space(3)))
; __device__ __forceinline__ void lds_barrier() { asm volatile("s_waitcnt lgkmcnt(0)" ::: "memory"); __builtin_amdgcn_s_barrier(); asm volatile("" ::: "memory"); }
; template <int R, class XT, class TWT>
; __device__ __forceinline__ void dif_task(XT X, TWT tw, int s, int task) {
;     const int lgM = 13 - s, lgq = lgM - R, q = 1 << lgq;
;     const int j0 = task & (q - 1), blk = task >> lgq, base = (blk << lgM) + j0;
;     const int pb = PADI(base), qp = (q >= 32) ? q + (q >> 4) : q;
;     f32x2v v[1 << R];
; #pragma unroll
;     for (int k = 0; k < (1 << R); ++k) v[k] = X[pb + k * qp];
; #pragma unroll
;     for (int r = 0; r < R; ++r) {
;         const int pb = R - 1 - r;
; #pragma unroll
;         for (int k = 0; k < (1 << R); ++k) if (!((k >> pb) & 1)) {
;             const int klo = k & ((1 << pb) - 1);
;             const f32x2v w = tw[(j0 + (klo << lgq)) << (s + r)];
;             const f32x2v a = v[k], b = v[k + (1 << pb)], d = a - b;
;             v[k] = a + b; v[k + (1 << pb)] = (f32x2v){d.x * w.x - d.y * w.y, d.x * w.y + d.y * w.x};
;         }
;     }
; #pragma unroll
;     for (int k = 0; k < (1 << R); ++k) X[pb + k * qp] = v[k];
; }
; template <bool LAT>
; __device__ __forceinline__ void hyconv_unit(const Frame& F, LAS f32x2v* X, const TwHalf tw, LAS bf16* OUT, const float* skip, bf16* MIX, int u) {
;     ...
;                 if (r < 4) xx = (f32x4){bflo(w0[r]), bflo(w1[r]), bfhi(w0[r]), bfhi(w1[r])};
;                 *(LAS f32x4*)(X + PADI(e)) = xx; }
;         } else {
;             f32x2v v[16];
;             { const bf16* p0 = H0 + (size_t)(512 + c0) * L + n; const bf16* p1 = H1 + (size_t)(512 + c0) * L + n;
; #pragma unroll
;               for (int r = 0; r < 16; ++r) { v[r] = (f32x2v){0.f, 0.f}; if (act) v[r] = (f32x2v){bf2f(p0[r * L]), bf2f(p1[r * L])}; } }
; #pragma unroll
;             for (int r = 0; r < 16; ++r) X[PADI(F.tid + 512 * r)] = v[r];
;         }
;         lds_barrier();
; #pragma unroll 1
;         for (int ord = 0; ord < 2; ++ord) {
;             const f32x2v* SP = SPb + (size_t)ord * 256 * N;
;             f32x4 kq[8];
; #pragma unroll
;             for (int r = 0; r < 8; ++r) kq[r] = *(const f32x4*)(SP + 2 * (F.tid + 512 * r));
;             fft_fwd_upper(X, tw, 13 - lgN, F.tid);
.LBB0_847:
	s_lshl_b32 s90, s2, 17
	s_lshl_b64 s[0:1], s[90:91], 3
	s_add_u32 s0, s4, s0
	s_addc_u32 s1, s5, s1
	v_lshl_add_u64 v[0:1], v[34:35], 3, s[0:1]
	v_lshl_add_u64 v[2:3], v[36:37], 3, s[0:1]
	global_load_dwordx4 v[28:31], v[0:1], off
	global_load_dwordx4 v[24:27], v[2:3], off
	v_lshl_add_u64 v[0:1], v[38:39], 3, s[0:1]
	v_lshl_add_u64 v[2:3], v[40:41], 3, s[0:1]
	global_load_dwordx4 v[20:23], v[0:1], off
	global_load_dwordx4 v[16:19], v[2:3], off
	v_lshl_add_u64 v[0:1], v[42:43], 3, s[0:1]
	v_lshl_add_u64 v[2:3], v[44:45], 3, s[0:1]
	global_load_dwordx4 v[12:15], v[0:1], off
	global_load_dwordx4 v[8:11], v[2:3], off
	v_lshl_add_u64 v[0:1], v[46:47], 3, s[0:1]
	v_lshl_add_u64 v[2:3], v[48:49], 3, s[0:1]
	global_load_dwordx4 v[4:7], v[0:1], off
	s_nop 0
	global_load_dwordx4 v[0:3], v[2:3], off
	ds_read2_b64 v[100:103], v135 offset1:34
	ds_read2_b64 v[104:107], v135 offset0:68 offset1:102
	ds_read2_b64 v[108:111], v135 offset0:136 offset1:170
	ds_read2_b64 v[112:115], v135 offset0:204 offset1:238
	v_add_u32_e32 v98, 0x800, v135
	ds_read2_b64 v[116:119], v98 offset0:16 offset1:50
	ds_read2_b64 v[120:123], v98 offset0:84 offset1:118
	ds_read2_b64 v[124:127], v98 offset0:152 offset1:186
	ds_read2_b64 v[128:131], v98 offset0:220 offset1:254
	ds_read2st64_b64 v[176:179], v33 offset1:16
	ds_read_b64 v[132:133], v165
	ds_read_b64 v[182:183], v166
	ds_read_b64 v[184:185], v167
	ds_read_b64 v[186:187], v168
	ds_read_b64 v[188:189], v169
	ds_read_b64 v[190:191], v139
	ds_read_b64 v[192:193], v136
	s_waitcnt lgkmcnt(11)
	v_pk_add_f32 v[194:195], v[100:101], v[116:117] neg_lo:[0,1] neg_hi:[0,1]
	v_pk_add_f32 v[100:101], v[100:101], v[116:117]
	s_waitcnt lgkmcnt(7)
	v_pk_mul_f32 v[196:197], v[194:195], v[176:177] op_sel:[1,1] op_sel_hi:[1,0]
	s_lshl_b32 s0, s2, 8
	v_pk_fma_f32 v[198:199], v[194:195], v[176:177], v[196:197] op_sel_hi:[0,1,1] neg_lo:[0,0,1]
	v_pk_add_f32 v[194:195], v[108:109], v[124:125] neg_lo:[0,1] neg_hi:[0,1]
	v_pk_add_f32 v[108:109], v[108:109], v[124:125]
	v_pk_mul_f32 v[196:197], v[194:195], v[176:177] op_sel:[1,0] op_sel_hi:[0,0]
	v_pk_fma_f32 v[202:203], v[194:195], v[176:177], v[196:197] op_sel:[0,1,0] neg_hi:[0,0,1]
	v_pk_add_f32 v[116:117], v[100:101], v[108:109]
	v_pk_add_f32 v[176:177], v[198:199], v[202:203] neg_lo:[0,1] neg_hi:[0,1]
	s_waitcnt lgkmcnt(0)
	v_xor_b32_e32 v99, 0x80000000, v192
	v_pk_mul_f32 v[194:195], v[184:185], v[176:177] op_sel:[1,1] op_sel_hi:[0,1]
	v_pk_fma_f32 v[196:197], v[184:185], v[176:177], v[194:195] op_sel_hi:[1,0,1] neg_lo:[0,0,1]
	v_pk_add_f32 v[100:101], v[100:101], v[108:109] neg_lo:[0,1] neg_hi:[0,1]
	v_pk_add_f32 v[176:177], v[104:105], v[120:121] neg_lo:[0,1] neg_hi:[0,1]
	v_pk_add_f32 v[104:105], v[104:105], v[120:121]
	v_pk_mul_f32 v[194:195], v[176:177], v[178:179] op_sel:[1,1] op_sel_hi:[1,0]
	v_pk_mul_f32 v[108:109], v[100:101], v[184:185] op_sel:[1,1] op_sel_hi:[1,0]
	v_pk_fma_f32 v[204:205], v[176:177], v[178:179], v[194:195] op_sel_hi:[0,1,1] neg_lo:[0,0,1]
	v_pk_add_f32 v[176:177], v[112:113], v[128:129] neg_lo:[0,1] neg_hi:[0,1]
	v_pk_add_f32 v[112:113], v[112:113], v[128:129]
	v_pk_mul_f32 v[194:195], v[176:177], v[178:179] op_sel:[1,0] op_sel_hi:[0,0]
	v_pk_fma_f32 v[206:207], v[176:177], v[178:179], v[194:195] op_sel:[0,1,0] neg_hi:[0,0,1]
	v_pk_add_f32 v[120:121], v[104:105], v[112:113]
	v_pk_add_f32 v[176:177], v[204:205], v[206:207] neg_lo:[0,1] neg_hi:[0,1]
	v_pk_add_f32 v[124:125], v[116:117], v[120:121]
	v_pk_mul_f32 v[178:179], v[184:185], v[176:177] op_sel_hi:[0,1]
	v_pk_fma_f32 v[194:195], v[184:185], v[176:177], v[178:179] op_sel:[1,0,1] op_sel_hi:[1,1,0] neg_hi:[0,0,1]
	v_pk_add_f32 v[116:117], v[116:117], v[120:121] neg_lo:[0,1] neg_hi:[0,1]
	v_pk_add_f32 v[176:177], v[196:197], v[194:195] neg_lo:[0,1] neg_hi:[0,1]
	v_pk_mul_f32 v[120:121], v[116:117], v[188:189] op_sel:[1,1] op_sel_hi:[1,0]
	v_pk_mul_f32 v[178:179], v[188:189], v[176:177] op_sel:[1,1] op_sel_hi:[0,1]
	v_pk_fma_f32 v[208:209], v[188:189], v[176:177], v[178:179] op_sel_hi:[1,0,1] neg_lo:[0,0,1]
	s_or_b32 s14, s0, s24
	v_pk_add_f32 v[176:177], v[102:103], v[118:119] neg_lo:[0,1] neg_hi:[0,1]
	v_pk_add_f32 v[102:103], v[102:103], v[118:119]
	v_pk_mul_f32 v[178:179], v[176:177], v[132:133] op_sel:[1,1] op_sel_hi:[1,0]
	s_nop 0
	s_lshl_b32 s90, s14, 9
	v_pk_fma_f32 v[220:221], v[176:177], v[132:133], v[178:179] op_sel_hi:[0,1,1] neg_lo:[0,0,1]
	v_pk_add_f32 v[176:177], v[110:111], v[126:127] neg_lo:[0,1] neg_hi:[0,1]
	v_pk_add_f32 v[110:111], v[110:111], v[126:127]
	v_pk_mul_f32 v[178:179], v[176:177], v[132:133] op_sel:[1,0] op_sel_hi:[0,0]
	v_pk_fma_f32 v[222:223], v[176:177], v[132:133], v[178:179] op_sel:[0,1,0] neg_hi:[0,0,1]
	v_pk_add_f32 v[118:119], v[102:103], v[110:111]
	v_pk_add_f32 v[132:133], v[220:221], v[222:223] neg_lo:[0,1] neg_hi:[0,1]
	v_pk_add_f32 v[102:103], v[102:103], v[110:111] neg_lo:[0,1] neg_hi:[0,1]
	v_pk_mul_f32 v[176:177], v[186:187], v[132:133] op_sel:[1,1] op_sel_hi:[0,1]
	v_pk_fma_f32 v[178:179], v[186:187], v[132:133], v[176:177] op_sel_hi:[1,0,1] neg_lo:[0,0,1]
	s_nop 0
	v_pk_add_f32 v[132:133], v[106:107], v[122:123] neg_lo:[0,1] neg_hi:[0,1]
	v_pk_add_f32 v[106:107], v[106:107], v[122:123]
	v_pk_mul_f32 v[176:177], v[132:133], v[182:183] op_sel:[1,1] op_sel_hi:[1,0]
	s_nop 0
	v_pk_fma_f32 v[224:225], v[132:133], v[182:183], v[176:177] op_sel_hi:[0,1,1] neg_lo:[0,0,1]
	v_pk_add_f32 v[132:133], v[114:115], v[130:131] neg_lo:[0,1] neg_hi:[0,1]
	v_pk_add_f32 v[114:115], v[114:115], v[130:131]
	v_pk_mul_f32 v[176:177], v[132:133], v[182:183] op_sel:[1,0] op_sel_hi:[0,0]
	v_pk_fma_f32 v[226:227], v[132:133], v[182:183], v[176:177] op_sel:[0,1,0] neg_hi:[0,0,1]
; template <int R, class XT, class TWT>
; __device__ __forceinline__ void dif_task(XT X, TWT tw, int s, int task) {
;     const int lgM = 13 - s, lgq = lgM - R, q = 1 << lgq;
;     const int j0 = task & (q - 1), blk = task >> lgq, base = (blk << lgM) + j0;
;     const int pb = PADI(base), qp = (q >= 32) ? q + (q >> 4) : q;
;     f32x2v v[1 << R];
; #pragma unroll
;     for (int k = 0; k < (1 << R); ++k) v[k] = X[pb + k * qp];
; #pragma unroll
;     for (int r = 0; r < R; ++r) {
;         const int pb = R - 1 - r;
; #pragma unroll
;         for (int k = 0; k < (1 << R); ++k) if (!((k >> pb) & 1)) {
;             const int klo = k & ((1 << pb) - 1);
;             const f32x2v w = tw[(j0 + (klo << lgq)) << (s + r)];
;             const f32x2v a = v[k], b = v[k + (1 << pb)], d = a - b;
;             v[k] = a + b; v[k + (1 << pb)] = (f32x2v){d.x * w.x - d.y * w.y, d.x * w.y + d.y * w.x};
;         }
;     }
; #pragma unroll
;     for (int k = 0; k < (1 << R); ++k) X[pb + k * qp] = v[k];
; }
	v_pk_add_f32 v[122:123], v[106:107], v[114:115]
	v_pk_add_f32 v[132:133], v[224:225], v[226:227] neg_lo:[0,1] neg_hi:[0,1]
	v_pk_add_f32 v[126:127], v[118:119], v[122:123]
	v_pk_mul_f32 v[176:177], v[190:191], v[132:133] op_sel_hi:[0,1]
	v_pk_fma_f32 v[182:183], v[190:191], v[132:133], v[176:177] op_sel:[1,0,1] op_sel_hi:[1,1,0] neg_hi:[0,0,1]
	v_pk_add_f32 v[128:129], v[124:125], v[126:127]
	v_pk_add_f32 v[132:133], v[178:179], v[182:183] neg_lo:[0,1] neg_hi:[0,1]
	v_pk_add_f32 v[124:125], v[124:125], v[126:127] neg_lo:[0,1] neg_hi:[0,1]
	v_pk_mul_f32 v[176:177], v[188:189], v[132:133] op_sel_hi:[0,1]
	v_pk_fma_f32 v[228:229], v[188:189], v[132:133], v[176:177] op_sel:[1,0,1] op_sel_hi:[1,1,0] neg_hi:[0,0,1]
	v_cndmask_b32_e64 v177, v99, v193, s[44:45]
	v_cndmask_b32_e64 v176, v193, v192, s[44:45]
	v_pk_mul_f32 v[126:127], v[124:125], v[176:177] op_sel:[1,1] op_sel_hi:[1,0]
	s_nop 0
	v_pk_fma_f32 v[130:131], v[124:125], v[176:177], v[126:127] op_sel_hi:[0,1,1] neg_lo:[0,0,1]
	v_pk_fma_f32 v[124:125], v[116:117], v[188:189], v[120:121] op_sel_hi:[0,1,1] neg_lo:[0,0,1]
	v_pk_add_f32 v[116:117], v[118:119], v[122:123] neg_lo:[0,1] neg_hi:[0,1]
	v_pk_add_f32 v[132:133], v[208:209], v[228:229] neg_lo:[0,1] neg_hi:[0,1]
	v_pk_mul_f32 v[118:119], v[116:117], v[188:189] op_sel_hi:[1,0]
	v_mov_b32_e32 v99, s18
	v_pk_fma_f32 v[120:121], v[116:117], v[188:189], v[118:119] op_sel:[0,1,1] op_sel_hi:[1,1,0] neg_hi:[0,0,1]
	s_nop 0
	v_pk_add_f32 v[118:119], v[124:125], v[120:121] neg_lo:[0,1] neg_hi:[0,1]
	v_pk_add_f32 v[116:117], v[124:125], v[120:121]
	v_pk_mul_f32 v[120:121], v[176:177], v[118:119] op_sel:[1,1] op_sel_hi:[0,1]
	v_pk_fma_f32 v[122:123], v[176:177], v[118:119], v[120:121] op_sel_hi:[1,0,1] neg_lo:[0,0,1]
	s_nop 0
	v_pk_fma_f32 v[118:119], v[100:101], v[184:185], v[108:109] op_sel_hi:[0,1,1] neg_lo:[0,0,1]
	v_pk_add_f32 v[100:101], v[104:105], v[112:113] neg_lo:[0,1] neg_hi:[0,1]
	s_nop 0
	v_pk_mul_f32 v[104:105], v[100:101], v[184:185] op_sel_hi:[1,0]
	s_nop 0
	v_pk_fma_f32 v[108:109], v[100:101], v[184:185], v[104:105] op_sel:[0,1,1] op_sel_hi:[1,1,0] neg_hi:[0,0,1]
	v_pk_mul_f32 v[104:105], v[102:103], v[186:187] op_sel:[1,1] op_sel_hi:[1,0]
	s_nop 0
	v_pk_fma_f32 v[110:111], v[102:103], v[186:187], v[104:105] op_sel_hi:[0,1,1] neg_lo:[0,0,1]
	v_pk_add_f32 v[102:103], v[106:107], v[114:115] neg_lo:[0,1] neg_hi:[0,1]
	v_pk_add_f32 v[100:101], v[118:119], v[108:109]
	v_pk_mul_f32 v[104:105], v[102:103], v[190:191] op_sel_hi:[1,0]
	v_pk_add_f32 v[114:115], v[220:221], v[222:223]
	v_pk_fma_f32 v[106:107], v[102:103], v[190:191], v[104:105] op_sel:[0,1,1] op_sel_hi:[1,1,0] neg_hi:[0,0,1]
	s_nop 0
	v_pk_add_f32 v[102:103], v[110:111], v[106:107]
	s_nop 0
	v_pk_add_f32 v[104:105], v[100:101], v[102:103]
	v_pk_add_f32 v[100:101], v[100:101], v[102:103] neg_lo:[0,1] neg_hi:[0,1]
	s_nop 0
	v_pk_mul_f32 v[102:103], v[176:177], v[100:101] op_sel:[1,1] op_sel_hi:[0,1]
	v_pk_fma_f32 v[112:113], v[176:177], v[100:101], v[102:103] op_sel_hi:[1,0,1] neg_lo:[0,0,1]
	s_nop 0
	v_pk_add_f32 v[100:101], v[118:119], v[108:109] neg_lo:[0,1] neg_hi:[0,1]
	v_pk_add_f32 v[118:119], v[224:225], v[226:227]
	v_pk_mul_f32 v[102:103], v[188:189], v[100:101] op_sel:[1,1] op_sel_hi:[0,1]
	v_pk_fma_f32 v[108:109], v[188:189], v[100:101], v[102:103] op_sel_hi:[1,0,1] neg_lo:[0,0,1]
	v_pk_add_f32 v[120:121], v[114:115], v[118:119]
	v_pk_add_f32 v[100:101], v[110:111], v[106:107] neg_lo:[0,1] neg_hi:[0,1]
	s_nop 0
	v_pk_mul_f32 v[102:103], v[188:189], v[100:101] op_sel_hi:[0,1]
	v_pk_fma_f32 v[106:107], v[188:189], v[100:101], v[102:103] op_sel:[1,0,1] op_sel_hi:[1,1,0] neg_hi:[0,0,1]
	s_nop 0
	v_pk_add_f32 v[102:103], v[108:109], v[106:107] neg_lo:[0,1] neg_hi:[0,1]
	v_pk_add_f32 v[100:101], v[108:109], v[106:107]
	v_pk_mul_f32 v[106:107], v[176:177], v[102:103] op_sel:[1,1] op_sel_hi:[0,1]
	v_pk_fma_f32 v[108:109], v[176:177], v[102:103], v[106:107] op_sel_hi:[1,0,1] neg_lo:[0,0,1]
	v_pk_add_f32 v[106:107], v[204:205], v[206:207]
	v_pk_add_f32 v[102:103], v[198:199], v[202:203]
	s_nop 0
	v_pk_add_f32 v[110:111], v[102:103], v[106:107]
	v_pk_add_f32 v[102:103], v[102:103], v[106:107] neg_lo:[0,1] neg_hi:[0,1]
	v_pk_add_f32 v[124:125], v[110:111], v[120:121]
	v_pk_add_f32 v[110:111], v[110:111], v[120:121] neg_lo:[0,1] neg_hi:[0,1]
	v_pk_mul_f32 v[106:107], v[188:189], v[102:103] op_sel:[1,1] op_sel_hi:[0,1]
	v_pk_mul_f32 v[120:121], v[110:111], v[176:177] op_sel:[1,1] op_sel_hi:[1,0]
	s_nop 0
	v_pk_fma_f32 v[126:127], v[110:111], v[176:177], v[120:121] op_sel_hi:[0,1,1] neg_lo:[0,0,1]
	v_pk_fma_f32 v[110:111], v[188:189], v[102:103], v[106:107] op_sel_hi:[1,0,1] neg_lo:[0,0,1]
	s_nop 0
	v_pk_add_f32 v[102:103], v[114:115], v[118:119] neg_lo:[0,1] neg_hi:[0,1]
	s_nop 0
	v_pk_mul_f32 v[106:107], v[188:189], v[102:103] op_sel_hi:[0,1]
	v_pk_fma_f32 v[114:115], v[188:189], v[102:103], v[106:107] op_sel:[1,0,1] op_sel_hi:[1,1,0] neg_hi:[0,0,1]
	s_nop 0
	v_pk_add_f32 v[106:107], v[110:111], v[114:115] neg_lo:[0,1] neg_hi:[0,1]
	v_pk_add_f32 v[102:103], v[110:111], v[114:115]
	v_pk_mul_f32 v[110:111], v[176:177], v[106:107] op_sel:[1,1] op_sel_hi:[0,1]
	v_pk_fma_f32 v[114:115], v[176:177], v[106:107], v[110:111] op_sel_hi:[1,0,1] neg_lo:[0,0,1]
	v_pk_add_f32 v[110:111], v[178:179], v[182:183]
	v_pk_add_f32 v[106:107], v[196:197], v[194:195]
	s_nop 0
	v_pk_add_f32 v[118:119], v[106:107], v[110:111]
	v_pk_add_f32 v[106:107], v[106:107], v[110:111] neg_lo:[0,1] neg_hi:[0,1]
	s_nop 0
	v_pk_mul_f32 v[110:111], v[176:177], v[106:107] op_sel:[1,1] op_sel_hi:[0,1]
	v_pk_fma_f32 v[120:121], v[176:177], v[106:107], v[110:111] op_sel_hi:[1,0,1] neg_lo:[0,0,1]
	v_pk_mul_f32 v[110:111], v[176:177], v[132:133] op_sel:[1,1] op_sel_hi:[0,1]
	v_pk_fma_f32 v[178:179], v[176:177], v[132:133], v[110:111] op_sel_hi:[1,0,1] neg_lo:[0,0,1]
	v_pk_add_f32 v[106:107], v[208:209], v[228:229]
	ds_write2_b64 v135, v[128:129], v[130:131] offset1:34
	ds_write2_b64 v135, v[116:117], v[122:123] offset0:68 offset1:102
	ds_write2_b64 v135, v[104:105], v[112:113] offset0:136 offset1:170
	ds_write2_b64 v135, v[100:101], v[108:109] offset0:204 offset1:238
	ds_write2_b64 v98, v[124:125], v[126:127] offset0:16 offset1:50
	ds_write2_b64 v98, v[102:103], v[114:115] offset0:84 offset1:118
	ds_write2_b64 v98, v[118:119], v[120:121] offset0:152 offset1:186
	ds_write2_b64 v98, v[106:107], v[178:179] offset0:220 offset1:254
	s_waitcnt lgkmcnt(0)
	s_barrier
; template <int R, class XT, class TWT>
; __device__ __forceinline__ void dif_task(XT X, TWT tw, int s, int task) {
;     const int lgM = 13 - s, lgq = lgM - R, q = 1 << lgq;
;     const int j0 = task & (q - 1), blk = task >> lgq, base = (blk << lgM) + j0;
;     const int pb = PADI(base), qp = (q >= 32) ? q + (q >> 4) : q;
;     f32x2v v[1 << R];
; #pragma unroll
;     for (int k = 0; k < (1 << R); ++k) v[k] = X[pb + k * qp];
; #pragma unroll
;     for (int r = 0; r < R; ++r) {
;         const int pb = R - 1 - r;
; #pragma unroll
;         for (int k = 0; k < (1 << R); ++k) if (!((k >> pb) & 1)) {
;             const int klo = k & ((1 << pb) - 1);
;             const f32x2v w = tw[(j0 + (klo << lgq)) << (s + r)];
;             const f32x2v a = v[k], b = v[k + (1 << pb)], d = a - b;
;             v[k] = a + b; v[k + (1 << pb)] = (f32x2v){d.x * w.x - d.y * w.y, d.x * w.y + d.y * w.x};
;         }
;     }
; #pragma unroll
;     for (int k = 0; k < (1 << R); ++k) X[pb + k * qp] = v[k];
; }
	ds_read2_b64 v[100:103], v137 offset1:2
	ds_read2_b64 v[104:107], v137 offset0:4 offset1:6
	ds_read2_b64 v[108:111], v137 offset0:8 offset1:10
	ds_read2_b64 v[112:115], v137 offset0:12 offset1:14
	ds_read2_b64 v[116:119], v137 offset0:16 offset1:18
	ds_read2_b64 v[120:123], v137 offset0:20 offset1:22
	ds_read2_b64 v[124:127], v137 offset0:24 offset1:26
	ds_read2_b64 v[128:131], v137 offset0:28 offset1:30
	ds_read2st64_b64 v[176:179], v170 offset1:16
	ds_read_b64 v[132:133], v171
	ds_read_b64 v[182:183], v172
	ds_read_b64 v[184:185], v173
	ds_read_b64 v[186:187], v156
	s_waitcnt lgkmcnt(8)
	v_pk_add_f32 v[194:195], v[100:101], v[116:117] neg_lo:[0,1] neg_hi:[0,1]
	ds_read_b64 v[188:189], v174
	ds_read_b64 v[190:191], v175
	ds_read_b64 v[192:193], v99
	s_waitcnt lgkmcnt(7)
	v_pk_mul_f32 v[196:197], v[194:195], v[176:177] op_sel:[1,1] op_sel_hi:[1,0]
	v_pk_add_f32 v[100:101], v[100:101], v[116:117]
	v_pk_fma_f32 v[198:199], v[194:195], v[176:177], v[196:197] op_sel_hi:[0,1,1] neg_lo:[0,0,1]
	v_pk_add_f32 v[194:195], v[108:109], v[124:125] neg_lo:[0,1] neg_hi:[0,1]
	v_pk_add_f32 v[108:109], v[108:109], v[124:125]
	v_pk_mul_f32 v[196:197], v[194:195], v[176:177] op_sel:[1,0] op_sel_hi:[0,0]
	v_pk_fma_f32 v[202:203], v[194:195], v[176:177], v[196:197] op_sel:[0,1,0] neg_hi:[0,0,1]
	v_pk_add_f32 v[116:117], v[100:101], v[108:109]
	v_pk_add_f32 v[176:177], v[198:199], v[202:203] neg_lo:[0,1] neg_hi:[0,1]
	v_pk_add_f32 v[100:101], v[100:101], v[108:109] neg_lo:[0,1] neg_hi:[0,1]
	s_waitcnt lgkmcnt(4)
	v_pk_mul_f32 v[194:195], v[184:185], v[176:177] op_sel:[1,1] op_sel_hi:[0,1]
	v_pk_fma_f32 v[196:197], v[184:185], v[176:177], v[194:195] op_sel_hi:[1,0,1] neg_lo:[0,0,1]
	v_pk_mul_f32 v[108:109], v[100:101], v[184:185] op_sel:[1,1] op_sel_hi:[1,0]
	v_pk_add_f32 v[176:177], v[104:105], v[120:121] neg_lo:[0,1] neg_hi:[0,1]
	v_pk_add_f32 v[104:105], v[104:105], v[120:121]
	v_pk_mul_f32 v[194:195], v[176:177], v[178:179] op_sel:[1,1] op_sel_hi:[1,0]
	s_nop 0
	v_pk_fma_f32 v[204:205], v[176:177], v[178:179], v[194:195] op_sel_hi:[0,1,1] neg_lo:[0,0,1]
	v_pk_add_f32 v[176:177], v[112:113], v[128:129] neg_lo:[0,1] neg_hi:[0,1]
	v_pk_add_f32 v[112:113], v[112:113], v[128:129]
	v_pk_mul_f32 v[194:195], v[176:177], v[178:179] op_sel:[1,0] op_sel_hi:[0,0]
	v_pk_fma_f32 v[206:207], v[176:177], v[178:179], v[194:195] op_sel:[0,1,0] neg_hi:[0,0,1]
	v_pk_add_f32 v[120:121], v[104:105], v[112:113]
	v_pk_add_f32 v[176:177], v[204:205], v[206:207] neg_lo:[0,1] neg_hi:[0,1]
	v_pk_add_f32 v[124:125], v[116:117], v[120:121]
	v_pk_mul_f32 v[178:179], v[184:185], v[176:177] op_sel_hi:[0,1]
	v_pk_fma_f32 v[194:195], v[184:185], v[176:177], v[178:179] op_sel:[1,0,1] op_sel_hi:[1,1,0] neg_hi:[0,0,1]
	v_pk_add_f32 v[116:117], v[116:117], v[120:121] neg_lo:[0,1] neg_hi:[0,1]
	v_pk_add_f32 v[176:177], v[196:197], v[194:195] neg_lo:[0,1] neg_hi:[0,1]
	s_waitcnt lgkmcnt(1)
	v_pk_mul_f32 v[120:121], v[116:117], v[190:191] op_sel:[1,1] op_sel_hi:[1,0]
	v_pk_mul_f32 v[178:179], v[190:191], v[176:177] op_sel:[1,1] op_sel_hi:[0,1]
	v_pk_fma_f32 v[208:209], v[190:191], v[176:177], v[178:179] op_sel_hi:[1,0,1] neg_lo:[0,0,1]
	s_nop 0
	v_pk_add_f32 v[176:177], v[102:103], v[118:119] neg_lo:[0,1] neg_hi:[0,1]
	v_pk_add_f32 v[102:103], v[102:103], v[118:119]
	v_pk_mul_f32 v[178:179], v[176:177], v[132:133] op_sel:[1,1] op_sel_hi:[1,0]
	s_nop 0
	v_pk_fma_f32 v[220:221], v[176:177], v[132:133], v[178:179] op_sel_hi:[0,1,1] neg_lo:[0,0,1]
	v_pk_add_f32 v[176:177], v[110:111], v[126:127] neg_lo:[0,1] neg_hi:[0,1]
	v_pk_add_f32 v[110:111], v[110:111], v[126:127]
	v_pk_mul_f32 v[178:179], v[176:177], v[132:133] op_sel:[1,0] op_sel_hi:[0,0]
	v_pk_fma_f32 v[222:223], v[176:177], v[132:133], v[178:179] op_sel:[0,1,0] neg_hi:[0,0,1]
	v_pk_add_f32 v[118:119], v[102:103], v[110:111]
	v_pk_add_f32 v[132:133], v[220:221], v[222:223] neg_lo:[0,1] neg_hi:[0,1]
	v_pk_add_f32 v[102:103], v[102:103], v[110:111] neg_lo:[0,1] neg_hi:[0,1]
	v_pk_mul_f32 v[176:177], v[188:189], v[132:133] op_sel:[1,1] op_sel_hi:[0,1]
	v_pk_fma_f32 v[178:179], v[188:189], v[132:133], v[176:177] op_sel_hi:[1,0,1] neg_lo:[0,0,1]
	s_nop 0
	v_pk_add_f32 v[132:133], v[106:107], v[122:123] neg_lo:[0,1] neg_hi:[0,1]
	v_pk_add_f32 v[106:107], v[106:107], v[122:123]
	v_pk_mul_f32 v[176:177], v[132:133], v[182:183] op_sel:[1,1] op_sel_hi:[1,0]
	s_nop 0
	v_pk_fma_f32 v[224:225], v[132:133], v[182:183], v[176:177] op_sel_hi:[0,1,1] neg_lo:[0,0,1]
	v_pk_add_f32 v[132:133], v[114:115], v[130:131] neg_lo:[0,1] neg_hi:[0,1]
	v_pk_add_f32 v[114:115], v[114:115], v[130:131]
	v_pk_mul_f32 v[176:177], v[132:133], v[182:183] op_sel:[1,0] op_sel_hi:[0,0]
	v_pk_fma_f32 v[226:227], v[132:133], v[182:183], v[176:177] op_sel:[0,1,0] neg_hi:[0,0,1]
	v_pk_add_f32 v[122:123], v[106:107], v[114:115]
	v_pk_add_f32 v[132:133], v[224:225], v[226:227] neg_lo:[0,1] neg_hi:[0,1]
	v_pk_add_f32 v[126:127], v[118:119], v[122:123]
	v_pk_mul_f32 v[176:177], v[186:187], v[132:133] op_sel_hi:[0,1]
	v_pk_fma_f32 v[182:183], v[186:187], v[132:133], v[176:177] op_sel:[1,0,1] op_sel_hi:[1,1,0] neg_hi:[0,0,1]
	v_pk_add_f32 v[128:129], v[124:125], v[126:127]
	v_pk_add_f32 v[132:133], v[178:179], v[182:183] neg_lo:[0,1] neg_hi:[0,1]
	v_pk_add_f32 v[124:125], v[124:125], v[126:127] neg_lo:[0,1] neg_hi:[0,1]
	v_pk_mul_f32 v[176:177], v[190:191], v[132:133] op_sel_hi:[0,1]
	v_pk_fma_f32 v[228:229], v[190:191], v[132:133], v[176:177] op_sel:[1,0,1] op_sel_hi:[1,1,0] neg_hi:[0,0,1]
	s_waitcnt lgkmcnt(0)
; template <int R, class XT, class TWT>
; __device__ __forceinline__ void dif_task(XT X, TWT tw, int s, int task) {
;     const int lgM = 13 - s, lgq = lgM - R, q = 1 << lgq;
;     const int j0 = task & (q - 1), blk = task >> lgq, base = (blk << lgM) + j0;
;     const int pb = PADI(base), qp = (q >= 32) ? q + (q >> 4) : q;
;     f32x2v v[1 << R];
; #pragma unroll
;     for (int k = 0; k < (1 << R); ++k) v[k] = X[pb + k * qp];
; #pragma unroll
;     for (int r = 0; r < R; ++r) {
;         const int pb = R - 1 - r;
; #pragma unroll
;         for (int k = 0; k < (1 << R); ++k) if (!((k >> pb) & 1)) {
;             const int klo = k & ((1 << pb) - 1);
;             const f32x2v w = tw[(j0 + (klo << lgq)) << (s + r)];
;             const f32x2v a = v[k], b = v[k + (1 << pb)], d = a - b;
;             v[k] = a + b; v[k + (1 << pb)] = (f32x2v){d.x * w.x - d.y * w.y, d.x * w.y + d.y * w.x};
;         }
;     }
; #pragma unroll
;     for (int k = 0; k < (1 << R); ++k) X[pb + k * qp] = v[k];
; }
	v_xor_b32_e32 v176, 0x80000000, v192
	v_cndmask_b32_e64 v177, v176, v193, s[42:43]
	v_cndmask_b32_e64 v176, v193, v192, s[42:43]
	v_pk_mul_f32 v[126:127], v[124:125], v[176:177] op_sel:[1,1] op_sel_hi:[1,0]
	s_nop 0
	v_pk_fma_f32 v[130:131], v[124:125], v[176:177], v[126:127] op_sel_hi:[0,1,1] neg_lo:[0,0,1]
	v_pk_fma_f32 v[124:125], v[116:117], v[190:191], v[120:121] op_sel_hi:[0,1,1] neg_lo:[0,0,1]
	v_pk_add_f32 v[116:117], v[118:119], v[122:123] neg_lo:[0,1] neg_hi:[0,1]
	v_pk_add_f32 v[132:133], v[208:209], v[228:229] neg_lo:[0,1] neg_hi:[0,1]
	v_pk_mul_f32 v[118:119], v[116:117], v[190:191] op_sel_hi:[1,0]
	s_nop 0
	v_pk_fma_f32 v[120:121], v[116:117], v[190:191], v[118:119] op_sel:[0,1,1] op_sel_hi:[1,1,0] neg_hi:[0,0,1]
	s_nop 0
	v_pk_add_f32 v[118:119], v[124:125], v[120:121] neg_lo:[0,1] neg_hi:[0,1]
	v_pk_add_f32 v[116:117], v[124:125], v[120:121]
	v_pk_mul_f32 v[120:121], v[176:177], v[118:119] op_sel:[1,1] op_sel_hi:[0,1]
	v_pk_fma_f32 v[122:123], v[176:177], v[118:119], v[120:121] op_sel_hi:[1,0,1] neg_lo:[0,0,1]
	s_nop 0
	v_pk_fma_f32 v[118:119], v[100:101], v[184:185], v[108:109] op_sel_hi:[0,1,1] neg_lo:[0,0,1]
	v_pk_add_f32 v[100:101], v[104:105], v[112:113] neg_lo:[0,1] neg_hi:[0,1]
	s_nop 0
	v_pk_mul_f32 v[104:105], v[100:101], v[184:185] op_sel_hi:[1,0]
	s_nop 0
	v_pk_fma_f32 v[108:109], v[100:101], v[184:185], v[104:105] op_sel:[0,1,1] op_sel_hi:[1,1,0] neg_hi:[0,0,1]
	v_pk_mul_f32 v[104:105], v[102:103], v[188:189] op_sel:[1,1] op_sel_hi:[1,0]
	s_nop 0
	v_pk_fma_f32 v[110:111], v[102:103], v[188:189], v[104:105] op_sel_hi:[0,1,1] neg_lo:[0,0,1]
	v_pk_add_f32 v[102:103], v[106:107], v[114:115] neg_lo:[0,1] neg_hi:[0,1]
	v_pk_add_f32 v[100:101], v[118:119], v[108:109]
	v_pk_mul_f32 v[104:105], v[102:103], v[186:187] op_sel_hi:[1,0]
	v_pk_add_f32 v[114:115], v[220:221], v[222:223]
	v_pk_fma_f32 v[106:107], v[102:103], v[186:187], v[104:105] op_sel:[0,1,1] op_sel_hi:[1,1,0] neg_hi:[0,0,1]
	s_nop 0
	v_pk_add_f32 v[102:103], v[110:111], v[106:107]
	s_nop 0
	v_pk_add_f32 v[104:105], v[100:101], v[102:103]
	v_pk_add_f32 v[100:101], v[100:101], v[102:103] neg_lo:[0,1] neg_hi:[0,1]
	s_nop 0
	v_pk_mul_f32 v[102:103], v[176:177], v[100:101] op_sel:[1,1] op_sel_hi:[0,1]
	v_pk_fma_f32 v[112:113], v[176:177], v[100:101], v[102:103] op_sel_hi:[1,0,1] neg_lo:[0,0,1]
	s_nop 0
	v_pk_add_f32 v[100:101], v[118:119], v[108:109] neg_lo:[0,1] neg_hi:[0,1]
	v_pk_add_f32 v[118:119], v[224:225], v[226:227]
	v_pk_mul_f32 v[102:103], v[190:191], v[100:101] op_sel:[1,1] op_sel_hi:[0,1]
	v_pk_fma_f32 v[108:109], v[190:191], v[100:101], v[102:103] op_sel_hi:[1,0,1] neg_lo:[0,0,1]
	v_pk_add_f32 v[120:121], v[114:115], v[118:119]
	v_pk_add_f32 v[100:101], v[110:111], v[106:107] neg_lo:[0,1] neg_hi:[0,1]
	s_nop 0
	v_pk_mul_f32 v[102:103], v[190:191], v[100:101] op_sel_hi:[0,1]
	v_pk_fma_f32 v[106:107], v[190:191], v[100:101], v[102:103] op_sel:[1,0,1] op_sel_hi:[1,1,0] neg_hi:[0,0,1]
	s_nop 0
	v_pk_add_f32 v[102:103], v[108:109], v[106:107] neg_lo:[0,1] neg_hi:[0,1]
	v_pk_add_f32 v[100:101], v[108:109], v[106:107]
	v_pk_mul_f32 v[106:107], v[176:177], v[102:103] op_sel:[1,1] op_sel_hi:[0,1]
	v_pk_fma_f32 v[108:109], v[176:177], v[102:103], v[106:107] op_sel_hi:[1,0,1] neg_lo:[0,0,1]
	v_pk_add_f32 v[106:107], v[204:205], v[206:207]
	v_pk_add_f32 v[102:103], v[198:199], v[202:203]
	s_nop 0
	v_pk_add_f32 v[110:111], v[102:103], v[106:107]
	v_pk_add_f32 v[102:103], v[102:103], v[106:107] neg_lo:[0,1] neg_hi:[0,1]
	v_pk_add_f32 v[124:125], v[110:111], v[120:121]
	v_pk_add_f32 v[110:111], v[110:111], v[120:121] neg_lo:[0,1] neg_hi:[0,1]
	v_pk_mul_f32 v[106:107], v[190:191], v[102:103] op_sel:[1,1] op_sel_hi:[0,1]
	v_pk_mul_f32 v[120:121], v[110:111], v[176:177] op_sel:[1,1] op_sel_hi:[1,0]
	s_nop 0
	v_pk_fma_f32 v[126:127], v[110:111], v[176:177], v[120:121] op_sel_hi:[0,1,1] neg_lo:[0,0,1]
	v_pk_fma_f32 v[110:111], v[190:191], v[102:103], v[106:107] op_sel_hi:[1,0,1] neg_lo:[0,0,1]
	s_nop 0
	v_pk_add_f32 v[102:103], v[114:115], v[118:119] neg_lo:[0,1] neg_hi:[0,1]
	s_nop 0
	v_pk_mul_f32 v[106:107], v[190:191], v[102:103] op_sel_hi:[0,1]
	v_pk_fma_f32 v[114:115], v[190:191], v[102:103], v[106:107] op_sel:[1,0,1] op_sel_hi:[1,1,0] neg_hi:[0,0,1]
	s_nop 0
	v_pk_add_f32 v[106:107], v[110:111], v[114:115] neg_lo:[0,1] neg_hi:[0,1]
	v_pk_add_f32 v[102:103], v[110:111], v[114:115]
	v_pk_mul_f32 v[110:111], v[176:177], v[106:107] op_sel:[1,1] op_sel_hi:[0,1]
	v_pk_fma_f32 v[114:115], v[176:177], v[106:107], v[110:111] op_sel_hi:[1,0,1] neg_lo:[0,0,1]
	v_pk_add_f32 v[110:111], v[178:179], v[182:183]
	v_pk_add_f32 v[106:107], v[196:197], v[194:195]
	s_nop 0
	v_pk_add_f32 v[118:119], v[106:107], v[110:111]
	v_pk_add_f32 v[106:107], v[106:107], v[110:111] neg_lo:[0,1] neg_hi:[0,1]
	s_nop 0
	v_pk_mul_f32 v[110:111], v[176:177], v[106:107] op_sel:[1,1] op_sel_hi:[0,1]
	v_pk_fma_f32 v[120:121], v[176:177], v[106:107], v[110:111] op_sel_hi:[1,0,1] neg_lo:[0,0,1]
	v_pk_mul_f32 v[110:111], v[176:177], v[132:133] op_sel:[1,1] op_sel_hi:[0,1]
	v_pk_fma_f32 v[178:179], v[176:177], v[132:133], v[110:111] op_sel_hi:[1,0,1] neg_lo:[0,0,1]
	v_pk_add_f32 v[106:107], v[208:209], v[228:229]
	ds_write2_b64 v137, v[128:129], v[130:131] offset1:2
	ds_write2_b64 v137, v[116:117], v[122:123] offset0:4 offset1:6
	ds_write2_b64 v137, v[104:105], v[112:113] offset0:8 offset1:10
	ds_write2_b64 v137, v[100:101], v[108:109] offset0:12 offset1:14
	ds_write2_b64 v137, v[124:125], v[126:127] offset0:16 offset1:18
	ds_write2_b64 v137, v[102:103], v[114:115] offset0:20 offset1:22
	ds_write2_b64 v137, v[118:119], v[120:121] offset0:24 offset1:26
	ds_write2_b64 v137, v[106:107], v[178:179] offset0:28 offset1:30
	s_waitcnt lgkmcnt(0)
	s_barrier
; template <bool LAT>
; __device__ __forceinline__ void hyconv_unit(const Frame& F, LAS f32x2v* X, const TwHalf tw, LAS bf16* OUT, const float* skip, bf16* MIX, int u) {
;     ...
;             const f32x2v* SP = SPb + (size_t)ord * 256 * N;
;             f32x4 kq[8];
; #pragma unroll
;             for (int r = 0; r < 8; ++r) kq[r] = *(const f32x4*)(SP + 2 * (F.tid + 512 * r));
;             fft_fwd_upper(X, tw, 13 - lgN, F.tid);
; #pragma unroll
;             for (int r = 0; r < 8; ++r) { const int e = 2 * (F.tid + 512 * r);
;                 const f32x2v a = X[PADI(e)], b = X[PADI(e + 1)]; const f32x4 k = kq[r];
;                 const f32x2v p = a + b, q = a - b; const f32x2v pk = (f32x2v){p.x * k.x - p.y * k.y, p.x * k.y + p.y * k.x}, qk = (f32x2v){q.x * k.z - q.y * k.w, q.x * k.w + q.y * k.z};
;                 X[PADI(e)] = pk + qk; X[PADI(e + 1)] = pk - qk; }
	ds_read_b128 v[100:103], v157
	s_waitcnt lgkmcnt(0)
	v_pk_add_f32 v[104:105], v[100:101], v[102:103]
	v_pk_add_f32 v[100:101], v[100:101], v[102:103] neg_lo:[0,1] neg_hi:[0,1]
	s_waitcnt vmcnt(7)
	v_pk_mul_f32 v[102:103], v[28:29], v[104:105] op_sel:[1,1] op_sel_hi:[0,1]
	v_pk_fma_f32 v[106:107], v[28:29], v[104:105], v[102:103] op_sel_hi:[1,0,1] neg_lo:[0,0,1]
	s_nop 0
	v_pk_mul_f32 v[28:29], v[30:31], v[100:101] op_sel:[1,1] op_sel_hi:[0,1]
	v_pk_fma_f32 v[102:103], v[30:31], v[100:101], v[28:29] op_sel_hi:[1,0,1] neg_lo:[0,0,1]
	s_nop 0
	v_pk_add_f32 v[28:29], v[106:107], v[102:103]
	v_pk_add_f32 v[30:31], v[106:107], v[102:103] neg_lo:[0,1] neg_hi:[0,1]
	ds_write_b128 v157, v[28:31]
	ds_read_b128 v[28:31], v158 offset:8192
	s_waitcnt lgkmcnt(0)
	v_pk_add_f32 v[100:101], v[28:29], v[30:31]
	v_pk_add_f32 v[28:29], v[28:29], v[30:31] neg_lo:[0,1] neg_hi:[0,1]
	s_waitcnt vmcnt(6)
	v_pk_mul_f32 v[30:31], v[24:25], v[100:101] op_sel:[1,1] op_sel_hi:[0,1]
	v_pk_fma_f32 v[102:103], v[24:25], v[100:101], v[30:31] op_sel_hi:[1,0,1] neg_lo:[0,0,1]
	s_nop 0
	v_pk_mul_f32 v[24:25], v[26:27], v[28:29] op_sel:[1,1] op_sel_hi:[0,1]
	v_pk_fma_f32 v[30:31], v[26:27], v[28:29], v[24:25] op_sel_hi:[1,0,1] neg_lo:[0,0,1]
	s_nop 0
	v_pk_add_f32 v[24:25], v[102:103], v[30:31]
	v_pk_add_f32 v[26:27], v[102:103], v[30:31] neg_lo:[0,1] neg_hi:[0,1]
	ds_write_b128 v158, v[24:27] offset:8192
	ds_read_b128 v[24:27], v159 offset:16384
	s_waitcnt lgkmcnt(0)
	v_pk_add_f32 v[28:29], v[24:25], v[26:27]
	v_pk_add_f32 v[24:25], v[24:25], v[26:27] neg_lo:[0,1] neg_hi:[0,1]
	s_waitcnt vmcnt(5)
	v_pk_mul_f32 v[26:27], v[20:21], v[28:29] op_sel:[1,1] op_sel_hi:[0,1]
	v_pk_fma_f32 v[30:31], v[20:21], v[28:29], v[26:27] op_sel_hi:[1,0,1] neg_lo:[0,0,1]
	s_nop 0
	v_pk_mul_f32 v[20:21], v[22:23], v[24:25] op_sel:[1,1] op_sel_hi:[0,1]
	v_pk_fma_f32 v[26:27], v[22:23], v[24:25], v[20:21] op_sel_hi:[1,0,1] neg_lo:[0,0,1]
	s_nop 0
	v_pk_add_f32 v[20:21], v[30:31], v[26:27]
	v_pk_add_f32 v[22:23], v[30:31], v[26:27] neg_lo:[0,1] neg_hi:[0,1]
	ds_write_b128 v159, v[20:23] offset:16384
	ds_read_b128 v[20:23], v160 offset:24576
	s_waitcnt lgkmcnt(0)
	v_pk_add_f32 v[24:25], v[20:21], v[22:23]
	v_pk_add_f32 v[20:21], v[20:21], v[22:23] neg_lo:[0,1] neg_hi:[0,1]
	s_waitcnt vmcnt(4)
	v_pk_mul_f32 v[22:23], v[16:17], v[24:25] op_sel:[1,1] op_sel_hi:[0,1]
	v_pk_fma_f32 v[26:27], v[16:17], v[24:25], v[22:23] op_sel_hi:[1,0,1] neg_lo:[0,0,1]
	s_nop 0
	v_pk_mul_f32 v[16:17], v[18:19], v[20:21] op_sel:[1,1] op_sel_hi:[0,1]
	v_pk_fma_f32 v[22:23], v[18:19], v[20:21], v[16:17] op_sel_hi:[1,0,1] neg_lo:[0,0,1]
	s_nop 0
	v_pk_add_f32 v[16:17], v[26:27], v[22:23]
	v_pk_add_f32 v[18:19], v[26:27], v[22:23] neg_lo:[0,1] neg_hi:[0,1]
	ds_write_b128 v160, v[16:19] offset:24576
	ds_read_b128 v[16:19], v161 offset:32768
	s_waitcnt lgkmcnt(0)
	v_pk_add_f32 v[20:21], v[16:17], v[18:19]
	v_pk_add_f32 v[16:17], v[16:17], v[18:19] neg_lo:[0,1] neg_hi:[0,1]
	s_waitcnt vmcnt(3)
	v_pk_mul_f32 v[18:19], v[12:13], v[20:21] op_sel:[1,1] op_sel_hi:[0,1]
	v_pk_fma_f32 v[22:23], v[12:13], v[20:21], v[18:19] op_sel_hi:[1,0,1] neg_lo:[0,0,1]
	s_nop 0
	v_pk_mul_f32 v[12:13], v[14:15], v[16:17] op_sel:[1,1] op_sel_hi:[0,1]
	v_pk_fma_f32 v[18:19], v[14:15], v[16:17], v[12:13] op_sel_hi:[1,0,1] neg_lo:[0,0,1]
	s_nop 0
	v_pk_add_f32 v[12:13], v[22:23], v[18:19]
	v_pk_add_f32 v[14:15], v[22:23], v[18:19] neg_lo:[0,1] neg_hi:[0,1]
	ds_write_b128 v161, v[12:15] offset:32768
	ds_read_b128 v[12:15], v162 offset:40960
	s_waitcnt lgkmcnt(0)
	v_pk_add_f32 v[16:17], v[12:13], v[14:15]
	v_pk_add_f32 v[12:13], v[12:13], v[14:15] neg_lo:[0,1] neg_hi:[0,1]
	s_waitcnt vmcnt(2)
	v_pk_mul_f32 v[14:15], v[8:9], v[16:17] op_sel:[1,1] op_sel_hi:[0,1]
	v_pk_fma_f32 v[18:19], v[8:9], v[16:17], v[14:15] op_sel_hi:[1,0,1] neg_lo:[0,0,1]
	s_nop 0
	v_pk_mul_f32 v[8:9], v[10:11], v[12:13] op_sel:[1,1] op_sel_hi:[0,1]
	v_pk_fma_f32 v[14:15], v[10:11], v[12:13], v[8:9] op_sel_hi:[1,0,1] neg_lo:[0,0,1]
	s_nop 0
	v_pk_add_f32 v[8:9], v[18:19], v[14:15]
	v_pk_add_f32 v[10:11], v[18:19], v[14:15] neg_lo:[0,1] neg_hi:[0,1]
	ds_write_b128 v162, v[8:11] offset:40960
	ds_read_b128 v[8:11], v163 offset:49152
	s_waitcnt lgkmcnt(0)
	v_pk_add_f32 v[12:13], v[8:9], v[10:11]
	v_pk_add_f32 v[8:9], v[8:9], v[10:11] neg_lo:[0,1] neg_hi:[0,1]
	s_waitcnt vmcnt(1)
	v_pk_mul_f32 v[10:11], v[4:5], v[12:13] op_sel:[1,1] op_sel_hi:[0,1]
	v_pk_fma_f32 v[14:15], v[4:5], v[12:13], v[10:11] op_sel_hi:[1,0,1] neg_lo:[0,0,1]
	s_nop 0
	v_pk_mul_f32 v[4:5], v[6:7], v[8:9] op_sel:[1,1] op_sel_hi:[0,1]
	v_pk_fma_f32 v[10:11], v[6:7], v[8:9], v[4:5] op_sel_hi:[1,0,1] neg_lo:[0,0,1]
	s_nop 0
	v_pk_add_f32 v[4:5], v[14:15], v[10:11]
	v_pk_add_f32 v[6:7], v[14:15], v[10:11] neg_lo:[0,1] neg_hi:[0,1]
	ds_write_b128 v163, v[4:7] offset:49152
	ds_read_b128 v[4:7], v164 offset:57344
	s_waitcnt lgkmcnt(0)
	v_pk_add_f32 v[8:9], v[4:5], v[6:7]
	v_pk_add_f32 v[4:5], v[4:5], v[6:7] neg_lo:[0,1] neg_hi:[0,1]
	s_waitcnt vmcnt(0)
	v_pk_mul_f32 v[6:7], v[0:1], v[8:9] op_sel:[1,1] op_sel_hi:[0,1]
	v_pk_fma_f32 v[10:11], v[0:1], v[8:9], v[6:7] op_sel_hi:[1,0,1] neg_lo:[0,0,1]
	s_nop 0
	v_pk_mul_f32 v[0:1], v[2:3], v[4:5] op_sel:[1,1] op_sel_hi:[0,1]
	v_pk_fma_f32 v[6:7], v[2:3], v[4:5], v[0:1] op_sel_hi:[1,0,1] neg_lo:[0,0,1]
	s_nop 0
	v_pk_add_f32 v[0:1], v[10:11], v[6:7]
	v_pk_add_f32 v[2:3], v[10:11], v[6:7] neg_lo:[0,1] neg_hi:[0,1]
	ds_write_b128 v164, v[0:3] offset:57344
	s_waitcnt lgkmcnt(0)
	s_barrier
; template <int R, class XT, class TWT>
; __device__ __forceinline__ void dit_task(XT X, TWT tw, int s, int task) {
;     const int lgM = 13 - s, lgq = lgM - R, q = 1 << lgq;
;     const int j0 = task & (q - 1), blk = task >> lgq, base = (blk << lgM) + j0;
;     const int pb = PADI(base), qp = (q >= 32) ? q + (q >> 4) : q;
;     f32x2v v[1 << R];
; #pragma unroll
;     for (int k = 0; k < (1 << R); ++k) v[k] = X[pb + k * qp];
; #pragma unroll
;     for (int r = R - 1; r >= 0; --r) {
;         const int pb = R - 1 - r;
; #pragma unroll
;         for (int k = 0; k < (1 << R); ++k) if (!((k >> pb) & 1)) {
;             const int klo = k & ((1 << pb) - 1);
;             const f32x2v w = tw[(j0 + (klo << lgq)) << (s + r)];
;             const f32x2v a = v[k], qv = v[k + (1 << pb)]; const f32x2v b = (f32x2v){qv.x * w.x + qv.y * w.y, qv.y * w.x - qv.x * w.y};
;             v[k] = a + b; v[k + (1 << pb)] = a - b;
;         }
;     }
; #pragma unroll
;     for (int k = 0; k < (1 << R); ++k) X[pb + k * qp] = v[k];
	ds_read2_b64 v[0:3], v137 offset1:2
	ds_read2_b64 v[4:7], v137 offset0:4 offset1:6
	ds_read2_b64 v[8:11], v137 offset0:8 offset1:10
	ds_read2_b64 v[12:15], v137 offset0:12 offset1:14
	ds_read2_b64 v[16:19], v137 offset0:16 offset1:18
	ds_read2_b64 v[20:23], v137 offset0:20 offset1:22
	ds_read2_b64 v[24:27], v137 offset0:24 offset1:26
	ds_read2_b64 v[28:31], v137 offset0:28 offset1:30
	ds_read_b64 v[104:105], v99
	ds_read_b64 v[106:107], v175
	ds_read_b64 v[108:109], v174
	ds_read2st64_b64 v[100:103], v170 offset1:16
	ds_read_b64 v[110:111], v173
	ds_read_b64 v[112:113], v156
	ds_read_b64 v[114:115], v171
	ds_read_b64 v[116:117], v172
	s_waitcnt lgkmcnt(7)
	v_xor_b32_e32 v99, 0x80000000, v104
	v_cndmask_b32_e64 v119, v99, v105, s[42:43]
	v_cndmask_b32_e64 v118, v105, v104, s[42:43]
	v_mov_b32_e32 v104, v119
	v_pk_mul_f32 v[120:121], v[2:3], v[104:105] op_sel_hi:[1,0]
	s_nop 0
	v_pk_fma_f32 v[122:123], v[2:3], v[118:119], v[120:121] op_sel:[0,0,1] op_sel_hi:[1,0,0] neg_hi:[0,0,1]
	v_pk_mul_f32 v[120:121], v[6:7], v[104:105] op_sel_hi:[1,0]
	s_nop 0
	v_pk_fma_f32 v[124:125], v[6:7], v[118:119], v[120:121] op_sel:[0,0,1] op_sel_hi:[1,0,0] neg_hi:[0,0,1]
	v_pk_add_f32 v[2:3], v[0:1], v[122:123]
	v_pk_add_f32 v[6:7], v[4:5], v[124:125]
	v_pk_add_f32 v[4:5], v[4:5], v[124:125] neg_lo:[0,1] neg_hi:[0,1]
	s_waitcnt lgkmcnt(6)
	v_pk_mul_f32 v[120:121], v[106:107], v[6:7] op_sel:[1,0]
	v_pk_add_f32 v[0:1], v[0:1], v[122:123] neg_lo:[0,1] neg_hi:[0,1]
	v_pk_fma_f32 v[126:127], v[106:107], v[6:7], v[120:121] op_sel:[0,0,1] op_sel_hi:[0,1,0] neg_hi:[0,0,1]
	v_pk_mul_f32 v[120:121], v[10:11], v[104:105] op_sel_hi:[1,0]
	s_nop 0
	v_pk_fma_f32 v[128:129], v[10:11], v[118:119], v[120:121] op_sel:[0,0,1] op_sel_hi:[1,0,0] neg_hi:[0,0,1]
	v_pk_mul_f32 v[120:121], v[14:15], v[104:105] op_sel_hi:[1,0]
	s_nop 0
	v_pk_fma_f32 v[130:131], v[14:15], v[118:119], v[120:121] op_sel:[0,0,1] op_sel_hi:[1,0,0] neg_hi:[0,0,1]
	v_pk_add_f32 v[10:11], v[8:9], v[128:129]
	v_pk_add_f32 v[14:15], v[12:13], v[130:131]
	v_pk_add_f32 v[12:13], v[12:13], v[130:131] neg_lo:[0,1] neg_hi:[0,1]
	v_pk_mul_f32 v[120:121], v[106:107], v[14:15] op_sel:[1,0]
	v_pk_add_f32 v[8:9], v[8:9], v[128:129] neg_lo:[0,1] neg_hi:[0,1]
	v_pk_fma_f32 v[132:133], v[106:107], v[14:15], v[120:121] op_sel:[0,0,1] op_sel_hi:[0,1,0] neg_hi:[0,0,1]
	s_nop 0
	v_pk_add_f32 v[14:15], v[10:11], v[132:133]
	v_pk_add_f32 v[10:11], v[10:11], v[132:133] neg_lo:[0,1] neg_hi:[0,1]
	s_waitcnt lgkmcnt(3)
	v_pk_mul_f32 v[120:121], v[110:111], v[14:15] op_sel:[1,0]
	v_pk_add_f32 v[6:7], v[2:3], v[126:127]
	v_pk_fma_f32 v[176:177], v[110:111], v[14:15], v[120:121] op_sel:[0,0,1] op_sel_hi:[1,1,0]
	v_pk_fma_f32 v[14:15], v[110:111], v[14:15], v[120:121] op_sel:[0,0,1] op_sel_hi:[0,1,0] neg_lo:[0,0,1] neg_hi:[0,0,1]
	v_pk_mul_f32 v[120:121], v[18:19], v[104:105] op_sel_hi:[1,0]
	v_pk_add_f32 v[2:3], v[2:3], v[126:127] neg_lo:[0,1] neg_hi:[0,1]
	v_pk_fma_f32 v[178:179], v[18:19], v[118:119], v[120:121] op_sel:[0,0,1] op_sel_hi:[1,0,0] neg_hi:[0,0,1]
	v_pk_mul_f32 v[120:121], v[22:23], v[104:105] op_sel_hi:[1,0]
	s_nop 0
	v_pk_fma_f32 v[182:183], v[22:23], v[118:119], v[120:121] op_sel:[0,0,1] op_sel_hi:[1,0,0] neg_hi:[0,0,1]
	v_pk_add_f32 v[18:19], v[16:17], v[178:179]
	v_pk_add_f32 v[22:23], v[20:21], v[182:183]
	v_pk_add_f32 v[20:21], v[20:21], v[182:183] neg_lo:[0,1] neg_hi:[0,1]
	v_pk_mul_f32 v[120:121], v[106:107], v[22:23] op_sel:[1,0]
	v_pk_add_f32 v[16:17], v[16:17], v[178:179] neg_lo:[0,1] neg_hi:[0,1]
	v_pk_fma_f32 v[184:185], v[106:107], v[22:23], v[120:121] op_sel:[0,0,1] op_sel_hi:[0,1,0] neg_hi:[0,0,1]
	v_pk_mul_f32 v[120:121], v[26:27], v[104:105] op_sel_hi:[1,0]
	v_pk_mul_f32 v[104:105], v[30:31], v[104:105] op_sel_hi:[1,0]
	v_pk_fma_f32 v[186:187], v[26:27], v[118:119], v[120:121] op_sel:[0,0,1] op_sel_hi:[1,0,0] neg_hi:[0,0,1]
	v_pk_fma_f32 v[120:121], v[30:31], v[118:119], v[104:105] op_sel:[0,0,1] op_sel_hi:[1,0,0] neg_hi:[0,0,1]
	s_nop 0
	v_pk_add_f32 v[30:31], v[28:29], v[120:121]
	v_pk_add_f32 v[26:27], v[24:25], v[186:187]
	v_pk_mul_f32 v[104:105], v[106:107], v[30:31] op_sel:[1,0]
	s_nop 0
	v_pk_fma_f32 v[118:119], v[106:107], v[30:31], v[104:105] op_sel:[0,0,1] op_sel_hi:[0,1,0] neg_hi:[0,0,1]
	s_nop 0
	v_pk_add_f32 v[30:31], v[26:27], v[118:119]
	v_pk_add_f32 v[22:23], v[18:19], v[184:185]
	v_pk_mul_f32 v[104:105], v[110:111], v[30:31] op_sel:[1,0]
	v_pk_add_f32 v[28:29], v[28:29], v[120:121] neg_lo:[0,1] neg_hi:[0,1]
	v_pk_fma_f32 v[188:189], v[110:111], v[30:31], v[104:105] op_sel:[0,0,1] op_sel_hi:[0,1,0] neg_hi:[0,0,1]
	s_nop 0
	v_pk_add_f32 v[30:31], v[22:23], v[188:189]
	v_pk_add_f32 v[24:25], v[24:25], v[186:187] neg_lo:[0,1] neg_hi:[0,1]
	v_pk_mul_f32 v[104:105], v[100:101], v[30:31] op_sel:[1,0]
	v_pk_add_f32 v[26:27], v[26:27], v[118:119] neg_lo:[0,1] neg_hi:[0,1]
	v_pk_fma_f32 v[190:191], v[100:101], v[30:31], v[104:105] op_sel:[0,0,1] op_sel_hi:[1,1,0]
	v_pk_fma_f32 v[30:31], v[100:101], v[30:31], v[104:105] op_sel:[0,0,1] op_sel_hi:[0,1,0] neg_lo:[0,0,1] neg_hi:[0,0,1]
	v_pk_mul_f32 v[104:105], v[106:107], v[4:5] op_sel_hi:[0,1]
	v_pk_fma_f32 v[122:123], v[106:107], v[4:5], v[104:105] op_sel:[1,0,1] op_sel_hi:[1,1,0] neg_lo:[0,0,1]
	v_pk_mul_f32 v[104:105], v[106:107], v[12:13] op_sel_hi:[0,1]
	v_pk_fma_f32 v[124:125], v[106:107], v[12:13], v[104:105] op_sel:[1,0,1] op_sel_hi:[1,1,0] neg_lo:[0,0,1]
	s_nop 0
	v_pk_add_f32 v[12:13], v[8:9], v[124:125]
	v_pk_add_f32 v[4:5], v[0:1], v[122:123]
	v_pk_mul_f32 v[104:105], v[108:109], v[12:13] op_sel:[1,0]
	v_pk_add_f32 v[18:19], v[18:19], v[184:185] neg_lo:[0,1] neg_hi:[0,1]
	v_pk_fma_f32 v[128:129], v[108:109], v[12:13], v[104:105] op_sel:[0,0,1] op_sel_hi:[0,1,0] neg_hi:[0,0,1]
	v_pk_mul_f32 v[104:105], v[106:107], v[20:21] op_sel_hi:[0,1]
	v_pk_fma_f32 v[130:131], v[106:107], v[20:21], v[104:105] op_sel:[1,0,1] op_sel_hi:[1,1,0] neg_lo:[0,0,1]
	v_pk_mul_f32 v[104:105], v[106:107], v[28:29] op_sel_hi:[0,1]
	v_pk_fma_f32 v[120:121], v[106:107], v[28:29], v[104:105] op_sel:[1,0,1] op_sel_hi:[1,1,0] neg_lo:[0,0,1]
	s_nop 0
	v_pk_add_f32 v[28:29], v[24:25], v[120:121]
	v_pk_add_f32 v[20:21], v[16:17], v[130:131]
	v_pk_mul_f32 v[104:105], v[108:109], v[28:29] op_sel:[1,0]
	s_nop 0
	v_pk_fma_f32 v[106:107], v[108:109], v[28:29], v[104:105] op_sel:[0,0,1] op_sel_hi:[0,1,0] neg_hi:[0,0,1]
	s_nop 0
	v_pk_add_f32 v[28:29], v[20:21], v[106:107]
	v_pk_add_f32 v[12:13], v[4:5], v[128:129]
	s_waitcnt lgkmcnt(1)
; template <int R, class XT, class TWT>
; __device__ __forceinline__ void dit_task(XT X, TWT tw, int s, int task) {
;     const int lgM = 13 - s, lgq = lgM - R, q = 1 << lgq;
;     const int j0 = task & (q - 1), blk = task >> lgq, base = (blk << lgM) + j0;
;     const int pb = PADI(base), qp = (q >= 32) ? q + (q >> 4) : q;
;     f32x2v v[1 << R];
; #pragma unroll
;     for (int k = 0; k < (1 << R); ++k) v[k] = X[pb + k * qp];
; #pragma unroll
;     for (int r = R - 1; r >= 0; --r) {
;         const int pb = R - 1 - r;
; #pragma unroll
;         for (int k = 0; k < (1 << R); ++k) if (!((k >> pb) & 1)) {
;             const int klo = k & ((1 << pb) - 1);
;             const f32x2v w = tw[(j0 + (klo << lgq)) << (s + r)];
;             const f32x2v a = v[k], qv = v[k + (1 << pb)]; const f32x2v b = (f32x2v){qv.x * w.x + qv.y * w.y, qv.y * w.x - qv.x * w.y};
;             v[k] = a + b; v[k + (1 << pb)] = a - b;
;         }
;     }
; #pragma unroll
;     for (int k = 0; k < (1 << R); ++k) X[pb + k * qp] = v[k];
	v_pk_mul_f32 v[104:105], v[114:115], v[28:29] op_sel:[1,0]
	v_pk_add_f32 v[8:9], v[8:9], v[124:125] neg_lo:[0,1] neg_hi:[0,1]
	v_pk_fma_f32 v[108:109], v[114:115], v[28:29], v[104:105] op_sel:[0,0,1] op_sel_hi:[0,1,0] neg_hi:[0,0,1]
	v_pk_mul_f32 v[104:105], v[110:111], v[10:11] op_sel_hi:[0,1]
	v_pk_add_f32 v[28:29], v[12:13], v[108:109]
	v_pk_add_f32 v[12:13], v[12:13], v[108:109] neg_lo:[0,1] neg_hi:[0,1]
	v_pk_fma_f32 v[108:109], v[110:111], v[10:11], v[104:105] op_sel:[1,0,1] op_sel_hi:[1,1,0] neg_lo:[0,0,1]
	v_pk_mul_f32 v[104:105], v[110:111], v[26:27] op_sel_hi:[0,1]
	v_pk_fma_f32 v[118:119], v[110:111], v[26:27], v[104:105] op_sel:[1,0,1] op_sel_hi:[1,1,0] neg_lo:[0,0,1]
	s_nop 0
	v_pk_add_f32 v[26:27], v[18:19], v[118:119]
	v_pk_add_f32 v[10:11], v[2:3], v[108:109]
	v_pk_mul_f32 v[104:105], v[102:103], v[26:27] op_sel:[1,0]
	v_pk_add_f32 v[24:25], v[24:25], v[120:121] neg_lo:[0,1] neg_hi:[0,1]
	v_pk_fma_f32 v[110:111], v[102:103], v[26:27], v[104:105] op_sel:[0,0,1] op_sel_hi:[0,1,0] neg_hi:[0,0,1]
	v_pk_mul_f32 v[104:105], v[112:113], v[8:9] op_sel_hi:[0,1]
	v_pk_add_f32 v[26:27], v[10:11], v[110:111]
	v_pk_add_f32 v[10:11], v[10:11], v[110:111] neg_lo:[0,1] neg_hi:[0,1]
	v_pk_fma_f32 v[110:111], v[112:113], v[8:9], v[104:105] op_sel:[1,0,1] op_sel_hi:[1,1,0] neg_lo:[0,0,1]
	v_pk_mul_f32 v[104:105], v[112:113], v[24:25] op_sel_hi:[0,1]
	v_pk_fma_f32 v[120:121], v[112:113], v[24:25], v[104:105] op_sel:[1,0,1] op_sel_hi:[1,1,0] neg_lo:[0,0,1]
	v_pk_add_f32 v[16:17], v[16:17], v[130:131] neg_lo:[0,1] neg_hi:[0,1]
	s_nop 0
	v_pk_add_f32 v[24:25], v[16:17], v[120:121]
	v_pk_add_f32 v[0:1], v[0:1], v[122:123] neg_lo:[0,1] neg_hi:[0,1]
	s_waitcnt lgkmcnt(0)
	v_pk_mul_f32 v[104:105], v[116:117], v[24:25] op_sel:[1,0]
	s_nop 0
	v_pk_fma_f32 v[112:113], v[116:117], v[24:25], v[104:105] op_sel:[0,0,1] op_sel_hi:[0,1,0] neg_hi:[0,0,1]
	v_pk_add_f32 v[22:23], v[22:23], v[188:189] neg_lo:[0,1] neg_hi:[0,1]
	v_pk_add_f32 v[8:9], v[0:1], v[110:111]
	v_pk_mul_f32 v[104:105], v[100:101], v[22:23] op_sel_hi:[0,1]
	v_pk_add_f32 v[20:21], v[20:21], v[106:107] neg_lo:[0,1] neg_hi:[0,1]
	v_pk_add_f32 v[24:25], v[8:9], v[112:113]
	v_pk_add_f32 v[8:9], v[8:9], v[112:113] neg_lo:[0,1] neg_hi:[0,1]
	v_pk_fma_f32 v[112:113], v[100:101], v[22:23], v[104:105] op_sel:[1,0,1] op_sel_hi:[1,1,0] neg_lo:[0,0,1] neg_hi:[0,0,1]
	v_pk_fma_f32 v[22:23], v[100:101], v[22:23], v[104:105] op_sel:[1,0,1] op_sel_hi:[1,1,0]
	v_pk_mul_f32 v[100:101], v[114:115], v[20:21] op_sel_hi:[0,1]
	v_pk_fma_f32 v[104:105], v[114:115], v[20:21], v[100:101] op_sel:[1,0,1] op_sel_hi:[1,1,0] neg_lo:[0,0,1]
	v_pk_add_f32 v[18:19], v[18:19], v[118:119] neg_lo:[0,1] neg_hi:[0,1]
	v_pk_add_f32 v[4:5], v[4:5], v[128:129] neg_lo:[0,1] neg_hi:[0,1]
	v_pk_mul_f32 v[100:101], v[102:103], v[18:19] op_sel_hi:[0,1]
	v_pk_add_f32 v[16:17], v[16:17], v[120:121] neg_lo:[0,1] neg_hi:[0,1]
	v_mov_b32_e32 v177, v15
	v_pk_add_f32 v[20:21], v[4:5], v[104:105]
	v_pk_add_f32 v[4:5], v[4:5], v[104:105] neg_lo:[0,1] neg_hi:[0,1]
	v_pk_fma_f32 v[104:105], v[102:103], v[18:19], v[100:101] op_sel:[1,0,1] op_sel_hi:[1,1,0] neg_lo:[0,0,1] neg_hi:[0,0,1]
	v_pk_fma_f32 v[18:19], v[102:103], v[18:19], v[100:101] op_sel:[1,0,1] op_sel_hi:[1,1,0]
	v_pk_mul_f32 v[100:101], v[116:117], v[16:17] op_sel_hi:[0,1]
	v_pk_add_f32 v[14:15], v[6:7], v[176:177]
	v_mov_b32_e32 v191, v31
	v_pk_fma_f32 v[102:103], v[116:117], v[16:17], v[100:101] op_sel:[1,0,1] op_sel_hi:[1,1,0] neg_lo:[0,0,1]
	v_pk_add_f32 v[30:31], v[14:15], v[190:191]
	v_pk_add_f32 v[6:7], v[6:7], v[176:177] neg_lo:[0,1] neg_hi:[0,1]
	v_mov_b32_e32 v113, v23
	v_pk_add_f32 v[2:3], v[2:3], v[108:109] neg_lo:[0,1] neg_hi:[0,1]
	v_mov_b32_e32 v105, v19
	v_pk_add_f32 v[0:1], v[0:1], v[110:111] neg_lo:[0,1] neg_hi:[0,1]
	v_pk_add_f32 v[14:15], v[14:15], v[190:191] neg_lo:[0,1] neg_hi:[0,1]
	v_pk_add_f32 v[22:23], v[6:7], v[112:113]
	v_pk_add_f32 v[6:7], v[6:7], v[112:113] neg_lo:[0,1] neg_hi:[0,1]
	v_pk_add_f32 v[18:19], v[2:3], v[104:105]
	v_pk_add_f32 v[2:3], v[2:3], v[104:105] neg_lo:[0,1] neg_hi:[0,1]
	v_pk_add_f32 v[16:17], v[0:1], v[102:103]
	v_pk_add_f32 v[0:1], v[0:1], v[102:103] neg_lo:[0,1] neg_hi:[0,1]
	ds_write2_b64 v137, v[30:31], v[28:29] offset1:2
	ds_write2_b64 v137, v[26:27], v[24:25] offset0:4 offset1:6
	ds_write2_b64 v137, v[22:23], v[20:21] offset0:8 offset1:10
	ds_write2_b64 v137, v[18:19], v[16:17] offset0:12 offset1:14
	ds_write2_b64 v137, v[14:15], v[12:13] offset0:16 offset1:18
	ds_write2_b64 v137, v[10:11], v[8:9] offset0:20 offset1:22
	ds_write2_b64 v137, v[6:7], v[4:5] offset0:24 offset1:26
	ds_write2_b64 v137, v[2:3], v[0:1] offset0:28 offset1:30
	s_waitcnt lgkmcnt(0)
	s_barrier
; template <int R, class XT, class TWT>
; __device__ __forceinline__ void dit_task(XT X, TWT tw, int s, int task) {
;     const int lgM = 13 - s, lgq = lgM - R, q = 1 << lgq;
;     const int j0 = task & (q - 1), blk = task >> lgq, base = (blk << lgM) + j0;
;     const int pb = PADI(base), qp = (q >= 32) ? q + (q >> 4) : q;
;     f32x2v v[1 << R];
; #pragma unroll
;     for (int k = 0; k < (1 << R); ++k) v[k] = X[pb + k * qp];
; #pragma unroll
;     for (int r = R - 1; r >= 0; --r) {
;         const int pb = R - 1 - r;
; #pragma unroll
;         for (int k = 0; k < (1 << R); ++k) if (!((k >> pb) & 1)) {
;             const int klo = k & ((1 << pb) - 1);
;             const f32x2v w = tw[(j0 + (klo << lgq)) << (s + r)];
;             const f32x2v a = v[k], qv = v[k + (1 << pb)]; const f32x2v b = (f32x2v){qv.x * w.x + qv.y * w.y, qv.y * w.x - qv.x * w.y};
;             v[k] = a + b; v[k + (1 << pb)] = a - b;
;         }
;     }
; #pragma unroll
;     for (int k = 0; k < (1 << R); ++k) X[pb + k * qp] = v[k];
	ds_read2_b64 v[0:3], v135 offset1:34
	ds_read2_b64 v[4:7], v135 offset0:68 offset1:102
	ds_read2_b64 v[8:11], v135 offset0:136 offset1:170
	ds_read2_b64 v[12:15], v135 offset0:204 offset1:238
	ds_read2_b64 v[16:19], v98 offset0:16 offset1:50
	ds_read2_b64 v[20:23], v98 offset0:84 offset1:118
	ds_read2_b64 v[24:27], v98 offset0:152 offset1:186
	ds_read2_b64 v[28:31], v98 offset0:220 offset1:254
	ds_read_b64 v[104:105], v136
	ds_read_b64 v[106:107], v169
	ds_read_b64 v[108:109], v167
	ds_read_b64 v[110:111], v168
	ds_read2st64_b64 v[100:103], v33 offset1:16
	ds_read_b64 v[112:113], v139
	ds_read_b64 v[114:115], v165
	ds_read_b64 v[116:117], v166
	s_waitcnt lgkmcnt(7)
	v_xor_b32_e32 v99, 0x80000000, v104
	v_cndmask_b32_e64 v119, v99, v105, s[44:45]
	v_cndmask_b32_e64 v118, v105, v104, s[44:45]
	v_mov_b32_e32 v104, v119
	v_pk_mul_f32 v[120:121], v[2:3], v[104:105] op_sel_hi:[1,0]
	s_nop 0
	v_pk_fma_f32 v[122:123], v[2:3], v[118:119], v[120:121] op_sel:[0,0,1] op_sel_hi:[1,0,0] neg_hi:[0,0,1]
	v_pk_mul_f32 v[120:121], v[6:7], v[104:105] op_sel_hi:[1,0]
	s_nop 0
	v_pk_fma_f32 v[124:125], v[6:7], v[118:119], v[120:121] op_sel:[0,0,1] op_sel_hi:[1,0,0] neg_hi:[0,0,1]
	v_pk_add_f32 v[2:3], v[0:1], v[122:123]
	v_pk_add_f32 v[6:7], v[4:5], v[124:125]
	v_pk_add_f32 v[4:5], v[4:5], v[124:125] neg_lo:[0,1] neg_hi:[0,1]
	s_waitcnt lgkmcnt(6)
	v_pk_mul_f32 v[120:121], v[106:107], v[6:7] op_sel:[1,0]
	v_pk_add_f32 v[0:1], v[0:1], v[122:123] neg_lo:[0,1] neg_hi:[0,1]
	v_pk_fma_f32 v[126:127], v[106:107], v[6:7], v[120:121] op_sel:[0,0,1] op_sel_hi:[0,1,0] neg_hi:[0,0,1]
	v_pk_mul_f32 v[120:121], v[10:11], v[104:105] op_sel_hi:[1,0]
	s_nop 0
	v_pk_fma_f32 v[128:129], v[10:11], v[118:119], v[120:121] op_sel:[0,0,1] op_sel_hi:[1,0,0] neg_hi:[0,0,1]
	v_pk_mul_f32 v[120:121], v[14:15], v[104:105] op_sel_hi:[1,0]
	s_nop 0
	v_pk_fma_f32 v[130:131], v[14:15], v[118:119], v[120:121] op_sel:[0,0,1] op_sel_hi:[1,0,0] neg_hi:[0,0,1]
	v_pk_add_f32 v[10:11], v[8:9], v[128:129]
	v_pk_add_f32 v[14:15], v[12:13], v[130:131]
	v_pk_add_f32 v[12:13], v[12:13], v[130:131] neg_lo:[0,1] neg_hi:[0,1]
	v_pk_mul_f32 v[120:121], v[106:107], v[14:15] op_sel:[1,0]
	v_pk_add_f32 v[8:9], v[8:9], v[128:129] neg_lo:[0,1] neg_hi:[0,1]
	v_pk_fma_f32 v[132:133], v[106:107], v[14:15], v[120:121] op_sel:[0,0,1] op_sel_hi:[0,1,0] neg_hi:[0,0,1]
	s_nop 0
	v_pk_add_f32 v[14:15], v[10:11], v[132:133]
	v_pk_add_f32 v[10:11], v[10:11], v[132:133] neg_lo:[0,1] neg_hi:[0,1]
	s_waitcnt lgkmcnt(5)
	v_pk_mul_f32 v[120:121], v[108:109], v[14:15] op_sel:[1,0]
	v_pk_add_f32 v[6:7], v[2:3], v[126:127]
	v_pk_fma_f32 v[176:177], v[108:109], v[14:15], v[120:121] op_sel:[0,0,1] op_sel_hi:[1,1,0]
	v_pk_fma_f32 v[14:15], v[108:109], v[14:15], v[120:121] op_sel:[0,0,1] op_sel_hi:[0,1,0] neg_lo:[0,0,1] neg_hi:[0,0,1]
	v_pk_mul_f32 v[120:121], v[18:19], v[104:105] op_sel_hi:[1,0]
	v_pk_add_f32 v[2:3], v[2:3], v[126:127] neg_lo:[0,1] neg_hi:[0,1]
	v_pk_fma_f32 v[178:179], v[18:19], v[118:119], v[120:121] op_sel:[0,0,1] op_sel_hi:[1,0,0] neg_hi:[0,0,1]
	v_pk_mul_f32 v[120:121], v[22:23], v[104:105] op_sel_hi:[1,0]
	s_nop 0
	v_pk_fma_f32 v[182:183], v[22:23], v[118:119], v[120:121] op_sel:[0,0,1] op_sel_hi:[1,0,0] neg_hi:[0,0,1]
	v_pk_add_f32 v[18:19], v[16:17], v[178:179]
	v_pk_add_f32 v[22:23], v[20:21], v[182:183]
	v_pk_add_f32 v[20:21], v[20:21], v[182:183] neg_lo:[0,1] neg_hi:[0,1]
	v_pk_mul_f32 v[120:121], v[106:107], v[22:23] op_sel:[1,0]
	v_pk_add_f32 v[16:17], v[16:17], v[178:179] neg_lo:[0,1] neg_hi:[0,1]
	v_pk_fma_f32 v[184:185], v[106:107], v[22:23], v[120:121] op_sel:[0,0,1] op_sel_hi:[0,1,0] neg_hi:[0,0,1]
	v_pk_mul_f32 v[120:121], v[26:27], v[104:105] op_sel_hi:[1,0]
	v_pk_mul_f32 v[104:105], v[30:31], v[104:105] op_sel_hi:[1,0]
	v_pk_fma_f32 v[186:187], v[26:27], v[118:119], v[120:121] op_sel:[0,0,1] op_sel_hi:[1,0,0] neg_hi:[0,0,1]
	v_pk_fma_f32 v[120:121], v[30:31], v[118:119], v[104:105] op_sel:[0,0,1] op_sel_hi:[1,0,0] neg_hi:[0,0,1]
	s_nop 0
	v_pk_add_f32 v[30:31], v[28:29], v[120:121]
	v_pk_add_f32 v[26:27], v[24:25], v[186:187]
	v_pk_mul_f32 v[104:105], v[106:107], v[30:31] op_sel:[1,0]
	s_nop 0
	v_pk_fma_f32 v[118:119], v[106:107], v[30:31], v[104:105] op_sel:[0,0,1] op_sel_hi:[0,1,0] neg_hi:[0,0,1]
	s_nop 0
	v_pk_add_f32 v[30:31], v[26:27], v[118:119]
	v_pk_add_f32 v[22:23], v[18:19], v[184:185]
	v_pk_mul_f32 v[104:105], v[108:109], v[30:31] op_sel:[1,0]
	v_pk_add_f32 v[28:29], v[28:29], v[120:121] neg_lo:[0,1] neg_hi:[0,1]
	v_pk_fma_f32 v[188:189], v[108:109], v[30:31], v[104:105] op_sel:[0,0,1] op_sel_hi:[0,1,0] neg_hi:[0,0,1]
	s_nop 0
	v_pk_add_f32 v[30:31], v[22:23], v[188:189]
	v_pk_add_f32 v[24:25], v[24:25], v[186:187] neg_lo:[0,1] neg_hi:[0,1]
	s_waitcnt lgkmcnt(3)
	v_pk_mul_f32 v[104:105], v[100:101], v[30:31] op_sel:[1,0]
	v_pk_add_f32 v[26:27], v[26:27], v[118:119] neg_lo:[0,1] neg_hi:[0,1]
	v_pk_fma_f32 v[190:191], v[100:101], v[30:31], v[104:105] op_sel:[0,0,1] op_sel_hi:[1,1,0]
	v_pk_fma_f32 v[30:31], v[100:101], v[30:31], v[104:105] op_sel:[0,0,1] op_sel_hi:[0,1,0] neg_lo:[0,0,1] neg_hi:[0,0,1]
	v_pk_mul_f32 v[104:105], v[106:107], v[4:5] op_sel_hi:[0,1]
	v_pk_fma_f32 v[122:123], v[106:107], v[4:5], v[104:105] op_sel:[1,0,1] op_sel_hi:[1,1,0] neg_lo:[0,0,1]
	v_pk_mul_f32 v[104:105], v[106:107], v[12:13] op_sel_hi:[0,1]
	v_pk_fma_f32 v[124:125], v[106:107], v[12:13], v[104:105] op_sel:[1,0,1] op_sel_hi:[1,1,0] neg_lo:[0,0,1]
	s_nop 0
	v_pk_add_f32 v[12:13], v[8:9], v[124:125]
	v_pk_add_f32 v[4:5], v[0:1], v[122:123]
	v_pk_mul_f32 v[104:105], v[110:111], v[12:13] op_sel:[1,0]
	v_pk_add_f32 v[18:19], v[18:19], v[184:185] neg_lo:[0,1] neg_hi:[0,1]
	v_pk_fma_f32 v[128:129], v[110:111], v[12:13], v[104:105] op_sel:[0,0,1] op_sel_hi:[0,1,0] neg_hi:[0,0,1]
	v_pk_mul_f32 v[104:105], v[106:107], v[20:21] op_sel_hi:[0,1]
	v_pk_fma_f32 v[130:131], v[106:107], v[20:21], v[104:105] op_sel:[1,0,1] op_sel_hi:[1,1,0] neg_lo:[0,0,1]
	v_pk_mul_f32 v[104:105], v[106:107], v[28:29] op_sel_hi:[0,1]
	v_pk_fma_f32 v[120:121], v[106:107], v[28:29], v[104:105] op_sel:[1,0,1] op_sel_hi:[1,1,0] neg_lo:[0,0,1]
	s_nop 0
	v_pk_add_f32 v[28:29], v[24:25], v[120:121]
	v_pk_add_f32 v[20:21], v[16:17], v[130:131]
	v_pk_mul_f32 v[104:105], v[110:111], v[28:29] op_sel:[1,0]
	s_nop 0
	v_pk_fma_f32 v[106:107], v[110:111], v[28:29], v[104:105] op_sel:[0,0,1] op_sel_hi:[0,1,0] neg_hi:[0,0,1]
	s_nop 0
	v_pk_add_f32 v[28:29], v[20:21], v[106:107]
	v_pk_add_f32 v[12:13], v[4:5], v[128:129]
	s_waitcnt lgkmcnt(1)
; template <int R, class XT, class TWT>
; __device__ __forceinline__ void dit_task(XT X, TWT tw, int s, int task) {
;     const int lgM = 13 - s, lgq = lgM - R, q = 1 << lgq;
;     const int j0 = task & (q - 1), blk = task >> lgq, base = (blk << lgM) + j0;
;     const int pb = PADI(base), qp = (q >= 32) ? q + (q >> 4) : q;
;     f32x2v v[1 << R];
; #pragma unroll
;     for (int k = 0; k < (1 << R); ++k) v[k] = X[pb + k * qp];
; #pragma unroll
;     for (int r = R - 1; r >= 0; --r) {
;         const int pb = R - 1 - r;
; #pragma unroll
;         for (int k = 0; k < (1 << R); ++k) if (!((k >> pb) & 1)) {
;             const int klo = k & ((1 << pb) - 1);
;             const f32x2v w = tw[(j0 + (klo << lgq)) << (s + r)];
;             const f32x2v a = v[k], qv = v[k + (1 << pb)]; const f32x2v b = (f32x2v){qv.x * w.x + qv.y * w.y, qv.y * w.x - qv.x * w.y};
;             v[k] = a + b; v[k + (1 << pb)] = a - b;
;         }
;     }
; #pragma unroll
;     for (int k = 0; k < (1 << R); ++k) X[pb + k * qp] = v[k];
	v_pk_mul_f32 v[104:105], v[114:115], v[28:29] op_sel:[1,0]
	v_pk_add_f32 v[8:9], v[8:9], v[124:125] neg_lo:[0,1] neg_hi:[0,1]
	v_pk_fma_f32 v[110:111], v[114:115], v[28:29], v[104:105] op_sel:[0,0,1] op_sel_hi:[0,1,0] neg_hi:[0,0,1]
	v_pk_mul_f32 v[104:105], v[108:109], v[10:11] op_sel_hi:[0,1]
	v_pk_add_f32 v[28:29], v[12:13], v[110:111]
	v_pk_add_f32 v[12:13], v[12:13], v[110:111] neg_lo:[0,1] neg_hi:[0,1]
	v_pk_fma_f32 v[110:111], v[108:109], v[10:11], v[104:105] op_sel:[1,0,1] op_sel_hi:[1,1,0] neg_lo:[0,0,1]
	v_pk_mul_f32 v[104:105], v[108:109], v[26:27] op_sel_hi:[0,1]
	v_pk_fma_f32 v[118:119], v[108:109], v[26:27], v[104:105] op_sel:[1,0,1] op_sel_hi:[1,1,0] neg_lo:[0,0,1]
	s_nop 0
	v_pk_add_f32 v[26:27], v[18:19], v[118:119]
	v_pk_add_f32 v[10:11], v[2:3], v[110:111]
	v_pk_mul_f32 v[104:105], v[102:103], v[26:27] op_sel:[1,0]
	v_pk_add_f32 v[24:25], v[24:25], v[120:121] neg_lo:[0,1] neg_hi:[0,1]
	v_pk_fma_f32 v[108:109], v[102:103], v[26:27], v[104:105] op_sel:[0,0,1] op_sel_hi:[0,1,0] neg_hi:[0,0,1]
	v_pk_mul_f32 v[104:105], v[112:113], v[8:9] op_sel_hi:[0,1]
	v_pk_add_f32 v[26:27], v[10:11], v[108:109]
	v_pk_add_f32 v[10:11], v[10:11], v[108:109] neg_lo:[0,1] neg_hi:[0,1]
	v_pk_fma_f32 v[108:109], v[112:113], v[8:9], v[104:105] op_sel:[1,0,1] op_sel_hi:[1,1,0] neg_lo:[0,0,1]
	v_pk_mul_f32 v[104:105], v[112:113], v[24:25] op_sel_hi:[0,1]
	v_pk_fma_f32 v[120:121], v[112:113], v[24:25], v[104:105] op_sel:[1,0,1] op_sel_hi:[1,1,0] neg_lo:[0,0,1]
	v_pk_add_f32 v[16:17], v[16:17], v[130:131] neg_lo:[0,1] neg_hi:[0,1]
	s_nop 0
	v_pk_add_f32 v[24:25], v[16:17], v[120:121]
	v_pk_add_f32 v[0:1], v[0:1], v[122:123] neg_lo:[0,1] neg_hi:[0,1]
	s_waitcnt lgkmcnt(0)
	v_pk_mul_f32 v[104:105], v[116:117], v[24:25] op_sel:[1,0]
	s_nop 0
	v_pk_fma_f32 v[112:113], v[116:117], v[24:25], v[104:105] op_sel:[0,0,1] op_sel_hi:[0,1,0] neg_hi:[0,0,1]
	v_pk_add_f32 v[22:23], v[22:23], v[188:189] neg_lo:[0,1] neg_hi:[0,1]
	v_pk_add_f32 v[8:9], v[0:1], v[108:109]
	v_pk_mul_f32 v[104:105], v[100:101], v[22:23] op_sel_hi:[0,1]
	v_pk_add_f32 v[20:21], v[20:21], v[106:107] neg_lo:[0,1] neg_hi:[0,1]
	v_pk_add_f32 v[24:25], v[8:9], v[112:113]
	v_pk_add_f32 v[8:9], v[8:9], v[112:113] neg_lo:[0,1] neg_hi:[0,1]
	v_pk_fma_f32 v[112:113], v[100:101], v[22:23], v[104:105] op_sel:[1,0,1] op_sel_hi:[1,1,0] neg_lo:[0,0,1] neg_hi:[0,0,1]
	v_pk_fma_f32 v[22:23], v[100:101], v[22:23], v[104:105] op_sel:[1,0,1] op_sel_hi:[1,1,0]
	v_pk_mul_f32 v[100:101], v[114:115], v[20:21] op_sel_hi:[0,1]
	v_pk_fma_f32 v[104:105], v[114:115], v[20:21], v[100:101] op_sel:[1,0,1] op_sel_hi:[1,1,0] neg_lo:[0,0,1]
	v_pk_add_f32 v[18:19], v[18:19], v[118:119] neg_lo:[0,1] neg_hi:[0,1]
	v_pk_add_f32 v[4:5], v[4:5], v[128:129] neg_lo:[0,1] neg_hi:[0,1]
	v_pk_mul_f32 v[100:101], v[102:103], v[18:19] op_sel_hi:[0,1]
	v_pk_add_f32 v[16:17], v[16:17], v[120:121] neg_lo:[0,1] neg_hi:[0,1]
	v_mov_b32_e32 v177, v15
	v_pk_add_f32 v[20:21], v[4:5], v[104:105]
	v_pk_add_f32 v[4:5], v[4:5], v[104:105] neg_lo:[0,1] neg_hi:[0,1]
	v_pk_fma_f32 v[104:105], v[102:103], v[18:19], v[100:101] op_sel:[1,0,1] op_sel_hi:[1,1,0] neg_lo:[0,0,1] neg_hi:[0,0,1]
	v_pk_fma_f32 v[18:19], v[102:103], v[18:19], v[100:101] op_sel:[1,0,1] op_sel_hi:[1,1,0]
	v_pk_mul_f32 v[100:101], v[116:117], v[16:17] op_sel_hi:[0,1]
	v_pk_add_f32 v[14:15], v[6:7], v[176:177]
	v_mov_b32_e32 v191, v31
	v_pk_fma_f32 v[102:103], v[116:117], v[16:17], v[100:101] op_sel:[1,0,1] op_sel_hi:[1,1,0] neg_lo:[0,0,1]
	v_pk_add_f32 v[30:31], v[14:15], v[190:191]
	v_pk_add_f32 v[6:7], v[6:7], v[176:177] neg_lo:[0,1] neg_hi:[0,1]
	v_mov_b32_e32 v113, v23
	v_pk_add_f32 v[2:3], v[2:3], v[110:111] neg_lo:[0,1] neg_hi:[0,1]
	v_mov_b32_e32 v105, v19
	v_pk_add_f32 v[0:1], v[0:1], v[108:109] neg_lo:[0,1] neg_hi:[0,1]
	v_pk_add_f32 v[14:15], v[14:15], v[190:191] neg_lo:[0,1] neg_hi:[0,1]
	v_pk_add_f32 v[22:23], v[6:7], v[112:113]
	v_pk_add_f32 v[6:7], v[6:7], v[112:113] neg_lo:[0,1] neg_hi:[0,1]
	v_pk_add_f32 v[18:19], v[2:3], v[104:105]
	v_pk_add_f32 v[2:3], v[2:3], v[104:105] neg_lo:[0,1] neg_hi:[0,1]
	v_pk_add_f32 v[16:17], v[0:1], v[102:103]
	v_pk_add_f32 v[0:1], v[0:1], v[102:103] neg_lo:[0,1] neg_hi:[0,1]
	ds_write2_b64 v135, v[30:31], v[28:29] offset1:34
	ds_write2_b64 v135, v[26:27], v[24:25] offset0:68 offset1:102
	ds_write2_b64 v135, v[22:23], v[20:21] offset0:136 offset1:170
	ds_write2_b64 v135, v[18:19], v[16:17] offset0:204 offset1:238
	ds_write2_b64 v98, v[14:15], v[12:13] offset0:16 offset1:50
	ds_write2_b64 v98, v[10:11], v[8:9] offset0:84 offset1:118
	ds_write2_b64 v98, v[6:7], v[4:5] offset0:152 offset1:186
	ds_write2_b64 v98, v[2:3], v[0:1] offset0:220 offset1:254
	s_waitcnt lgkmcnt(0)
	s_barrier
; template <bool LAT>
; __device__ __forceinline__ void hyconv_unit(const Frame& F, LAS f32x2v* X, const TwHalf tw, LAS bf16* OUT, const float* skip, bf16* MIX, int u) {
;     ...
;                 f32x2v g[16], zp[16];
;                 { const bf16* g0 = H0 + (size_t)(ord * 256 + c0) * L + n; const bf16* g1 = H1 + (size_t)(ord * 256 + c0) * L + n; const bf16* v0 = H0 + (size_t)(512 + c0) * L + n; const bf16* v1 = H1 + (size_t)(512 + c0) * L + n;
; #pragma unroll
;                   for (int r = 0; r < 16; ++r) { g[r] = (f32x2v){0.f, 0.f}; zp[r] = g[r]; if (act) { g[r] = (f32x2v){bf2f(g0[r * L]), bf2f(g1[r * L])}; zp[r] = (f32x2v){bf2f(v0[r * L]), bf2f(v1[r * L])}; } } }
	v_lshl_add_u64 v[104:105], v[56:57], 0, s[90:91]
	v_lshl_add_u64 v[102:103], v[62:63], 0, s[90:91]
	v_mov_b32_e32 v2, 0
	v_mov_b32_e32 v3, 0
	v_mov_b32_e32 v4, 0
	v_mov_b32_e32 v5, 0
	v_mov_b32_e32 v0, 0
	v_mov_b32_e32 v1, 0
	v_mov_b32_e32 v6, 0
	v_mov_b32_e32 v7, 0
	v_mov_b32_e32 v10, 0
	v_mov_b32_e32 v11, 0
	v_mov_b32_e32 v12, 0
	v_mov_b32_e32 v13, 0
	v_mov_b32_e32 v8, 0
	v_mov_b32_e32 v9, 0
	v_mov_b32_e32 v14, 0
	v_mov_b32_e32 v15, 0
	v_mov_b32_e32 v18, 0
	v_mov_b32_e32 v19, 0
	v_mov_b32_e32 v20, 0
	v_mov_b32_e32 v21, 0
	v_mov_b32_e32 v16, 0
	v_mov_b32_e32 v17, 0
	v_mov_b32_e32 v22, 0
	v_mov_b32_e32 v23, 0
	v_mov_b32_e32 v26, 0
	v_mov_b32_e32 v27, 0
	v_mov_b32_e32 v28, 0
	v_mov_b32_e32 v29, 0
	v_mov_b32_e32 v24, 0
	v_mov_b32_e32 v25, 0
	v_mov_b32_e32 v98, 0
	v_mov_b32_e32 v99, 0
	v_mov_b32_e32 v100, 0
	v_mov_b32_e32 v101, 0
	v_mov_b32_e32 v106, 0
	v_mov_b32_e32 v107, 0
	v_mov_b32_e32 v30, 0
	v_mov_b32_e32 v31, 0
	v_mov_b32_e32 v108, 0
	v_mov_b32_e32 v109, 0
	v_mov_b32_e32 v112, 0
	v_mov_b32_e32 v113, 0
	v_mov_b32_e32 v114, 0
	v_mov_b32_e32 v115, 0
	v_mov_b32_e32 v110, 0
	v_mov_b32_e32 v111, 0
	v_mov_b32_e32 v116, 0
	v_mov_b32_e32 v117, 0
	v_mov_b32_e32 v120, 0
	v_mov_b32_e32 v121, 0
	v_mov_b32_e32 v122, 0
	v_mov_b32_e32 v123, 0
	v_mov_b32_e32 v118, 0
	v_mov_b32_e32 v119, 0
	v_mov_b32_e32 v124, 0
	v_mov_b32_e32 v125, 0
	v_mov_b32_e32 v128, 0
	v_mov_b32_e32 v129, 0
	v_mov_b32_e32 v130, 0
	v_mov_b32_e32 v131, 0
	v_mov_b32_e32 v126, 0
	v_mov_b32_e32 v127, 0
	v_mov_b32_e32 v132, 0
	v_mov_b32_e32 v133, 0
	s_and_saveexec_b64 s[0:1], s[38:39]
	s_mov_b64 s[2:3], 0x1000
	v_lshl_add_u64 v[192:193], v[104:105], 0, s[2:3]
	v_lshl_add_u64 v[194:195], v[102:103], 0, s[2:3]
	global_load_ushort v2, v[104:105], off
	global_load_ushort v3, v[102:103], off
	global_load_ushort v4, v[52:53], off
	global_load_ushort v5, v[54:55], off
	global_load_ushort v0, v[104:105], off offset:512
	global_load_ushort v1, v[102:103], off offset:512
	global_load_ushort v6, v[52:53], off offset:512
	global_load_ushort v7, v[54:55], off offset:512
	global_load_ushort v10, v[104:105], off offset:1024
	global_load_ushort v11, v[102:103], off offset:1024
	global_load_ushort v12, v[52:53], off offset:1024
	global_load_ushort v13, v[54:55], off offset:1024
	global_load_ushort v8, v[104:105], off offset:1536
	global_load_ushort v9, v[102:103], off offset:1536
	global_load_ushort v14, v[52:53], off offset:1536
	global_load_ushort v15, v[54:55], off offset:1536
	global_load_ushort v18, v[104:105], off offset:2048
	global_load_ushort v19, v[102:103], off offset:2048
	global_load_ushort v20, v[52:53], off offset:2048
	global_load_ushort v21, v[54:55], off offset:2048
	global_load_ushort v16, v[104:105], off offset:2560
	global_load_ushort v17, v[102:103], off offset:2560
	global_load_ushort v22, v[52:53], off offset:2560
	global_load_ushort v23, v[54:55], off offset:2560
	global_load_ushort v26, v[104:105], off offset:3072
	global_load_ushort v27, v[102:103], off offset:3072
	global_load_ushort v28, v[52:53], off offset:3072
	global_load_ushort v29, v[54:55], off offset:3072
	global_load_ushort v24, v[104:105], off offset:3584
	global_load_ushort v25, v[102:103], off offset:3584
	global_load_ushort v98, v[52:53], off offset:3584
	global_load_ushort v99, v[54:55], off offset:3584
	global_load_ushort v100, v[192:193], off
	global_load_ushort v101, v[194:195], off
	global_load_ushort v106, v[66:67], off
	global_load_ushort v107, v[68:69], off
	global_load_ushort v30, v[192:193], off offset:512
	global_load_ushort v31, v[194:195], off offset:512
	global_load_ushort v108, v[70:71], off
	global_load_ushort v109, v[72:73], off
	global_load_ushort v112, v[192:193], off offset:1024
	global_load_ushort v113, v[194:195], off offset:1024
	global_load_ushort v114, v[74:75], off
	global_load_ushort v115, v[76:77], off
	global_load_ushort v110, v[192:193], off offset:1536
	global_load_ushort v111, v[194:195], off offset:1536
	global_load_ushort v116, v[78:79], off
	global_load_ushort v117, v[80:81], off
	s_waitcnt vmcnt(24)
	global_load_ushort v120, v[192:193], off offset:2048
	global_load_ushort v121, v[194:195], off offset:2048
	global_load_ushort v122, v[82:83], off
	global_load_ushort v123, v[84:85], off
	global_load_ushort v118, v[192:193], off offset:2560
	global_load_ushort v119, v[194:195], off offset:2560
	global_load_ushort v124, v[86:87], off
	global_load_ushort v125, v[88:89], off
	global_load_ushort v128, v[192:193], off offset:3072
	global_load_ushort v129, v[194:195], off offset:3072
	global_load_ushort v130, v[90:91], off
	global_load_ushort v131, v[92:93], off
	global_load_ushort v126, v[192:193], off offset:3584
	global_load_ushort v127, v[194:195], off offset:3584
	global_load_ushort v132, v[94:95], off
	global_load_ushort v133, v[96:97], off
	s_waitcnt vmcnt(0)
; __device__ __forceinline__ unsigned pk2(float lo, float hi) { const f32x2cv v = {lo, hi}; return __builtin_bit_cast(unsigned, __builtin_convertvector(v, bf16x2cv)); }
; __device__ __forceinline__ unsigned f2bf(float f) { return pk2(f, 0.f); }
; template <bool LAT>
; __device__ __forceinline__ void hyconv_unit(const Frame& F, LAS f32x2v* X, const TwHalf tw, LAS bf16* OUT, const float* skip, bf16* MIX, int u) {
;     ...
;                   for (int r = 0; r < 16; ++r) { g[r] = (f32x2v){0.f, 0.f}; zp[r] = g[r]; if (act) { g[r] = (f32x2v){bf2f(g0[r * L]), bf2f(g1[r * L])}; zp[r] = (f32x2v){bf2f(v0[r * L]), bf2f(v1[r * L])}; } } }
;                 f32x2v z[16];
; #pragma unroll
;                 for (int r = 0; r < 16; ++r) { z[r] = g[r] * (X[PADI(F.tid + 512 * r)] + zp[r] * skip[ord * 256 + c0 + r]); }
;                 if (ord == 0) { bf16* v0 = H0 + (size_t)(512 + c0) * L + n; bf16* v1 = H1 + (size_t)(512 + c0) * L + n;
; #pragma unroll
;                     for (int r = 0; r < 16; ++r) { if (act) { v0[r * L] = (bf16)f2bf(z[r].x); v1[r * L] = (bf16)f2bf(z[r].y); } X[PADI(F.tid + 512 * r)] = z[r]; } }
;                 else if (act) {
;                     v4u oa, ob, oc, od;
;                     oa.x = pk2(z[0].x, z[1].x); oa.y = pk2(z[2].x, z[3].x); oa.z = pk2(z[4].x, z[5].x); oa.w = pk2(z[6].x, z[7].x); ob.x = pk2(z[8].x, z[9].x); ob.y = pk2(z[10].x, z[11].x); ob.z = pk2(z[12].x, z[13].x); ob.w = pk2(z[14].x, z[15].x);
;                     oc.x = pk2(z[0].y, z[1].y); oc.y = pk2(z[2].y, z[3].y); oc.z = pk2(z[4].y, z[5].y); oc.w = pk2(z[6].y, z[7].y); od.x = pk2(z[8].y, z[9].y); od.y = pk2(z[10].y, z[11].y); od.z = pk2(z[12].y, z[13].y); od.w = pk2(z[14].y, z[15].y);
;                     bf16* m0 = MIX + (size_t)(rowb + n) * 1024 + c0; bf16* m1 = m0 + (size_t)L * 1024;
;                     *(v4u*)m0 = oa; *(v4u*)(m0 + 8) = ob; *(v4u*)m1 = oc; *(v4u*)(m1 + 8) = od; }
	v_lshlrev_b32_e32 v2, 16, v2
	v_lshlrev_b32_e32 v3, 16, v3
	v_lshlrev_b32_e32 v4, 16, v4
	v_lshlrev_b32_e32 v5, 16, v5
	v_lshlrev_b32_e32 v0, 16, v0
	v_lshlrev_b32_e32 v1, 16, v1
	v_lshlrev_b32_e32 v6, 16, v6
	v_lshlrev_b32_e32 v7, 16, v7
	v_lshlrev_b32_e32 v10, 16, v10
	v_lshlrev_b32_e32 v11, 16, v11
	v_lshlrev_b32_e32 v12, 16, v12
	v_lshlrev_b32_e32 v13, 16, v13
	v_lshlrev_b32_e32 v8, 16, v8
	v_lshlrev_b32_e32 v9, 16, v9
	v_lshlrev_b32_e32 v14, 16, v14
	v_lshlrev_b32_e32 v15, 16, v15
	v_lshlrev_b32_e32 v18, 16, v18
	v_lshlrev_b32_e32 v19, 16, v19
	v_lshlrev_b32_e32 v20, 16, v20
	v_lshlrev_b32_e32 v21, 16, v21
	v_lshlrev_b32_e32 v16, 16, v16
	v_lshlrev_b32_e32 v17, 16, v17
	v_lshlrev_b32_e32 v22, 16, v22
	v_lshlrev_b32_e32 v23, 16, v23
	v_lshlrev_b32_e32 v26, 16, v26
	v_lshlrev_b32_e32 v27, 16, v27
	v_lshlrev_b32_e32 v28, 16, v28
	v_lshlrev_b32_e32 v29, 16, v29
	v_lshlrev_b32_e32 v24, 16, v24
	v_lshlrev_b32_e32 v25, 16, v25
	v_lshlrev_b32_e32 v98, 16, v98
	v_lshlrev_b32_e32 v99, 16, v99
	v_lshlrev_b32_e32 v100, 16, v100
	v_lshlrev_b32_e32 v101, 16, v101
	v_lshlrev_b32_e32 v106, 16, v106
	v_lshlrev_b32_e32 v107, 16, v107
	v_lshlrev_b32_e32 v30, 16, v30
	v_lshlrev_b32_e32 v31, 16, v31
	v_lshlrev_b32_e32 v108, 16, v108
	v_lshlrev_b32_e32 v109, 16, v109
	v_lshlrev_b32_e32 v112, 16, v112
	v_lshlrev_b32_e32 v113, 16, v113
	v_lshlrev_b32_e32 v114, 16, v114
	v_lshlrev_b32_e32 v115, 16, v115
	v_lshlrev_b32_e32 v110, 16, v110
	v_lshlrev_b32_e32 v111, 16, v111
	v_lshlrev_b32_e32 v116, 16, v116
	v_lshlrev_b32_e32 v117, 16, v117
	v_lshlrev_b32_e32 v120, 16, v120
	v_lshlrev_b32_e32 v121, 16, v121
	v_lshlrev_b32_e32 v122, 16, v122
	v_lshlrev_b32_e32 v123, 16, v123
	v_lshlrev_b32_e32 v118, 16, v118
	v_lshlrev_b32_e32 v119, 16, v119
	v_lshlrev_b32_e32 v124, 16, v124
	v_lshlrev_b32_e32 v125, 16, v125
	v_lshlrev_b32_e32 v128, 16, v128
	v_lshlrev_b32_e32 v129, 16, v129
	v_lshlrev_b32_e32 v130, 16, v130
	v_lshlrev_b32_e32 v131, 16, v131
	v_lshlrev_b32_e32 v126, 16, v126
	v_lshlrev_b32_e32 v127, 16, v127
	v_lshlrev_b32_e32 v132, 16, v132
	v_lshlrev_b32_e32 v133, 16, v133
	s_or_b64 exec, exec, s[0:1]
	s_mov_b32 s15, s91
	s_xor_b64 s[0:1], s[20:21], -1
	s_lshl_b64 s[2:3], s[14:15], 2
	s_add_u32 s2, s6, s2
	s_addc_u32 s3, s7, s3
	ds_read_b64 v[190:191], v140
	global_load_dwordx4 v[176:179], v181, s[2:3] offset:48
	global_load_dwordx4 v[182:185], v181, s[2:3] offset:32
	global_load_dwordx4 v[186:189], v181, s[2:3] offset:16
	global_load_dwordx4 v[102:105], v181, s[2:3]
	s_mov_b64 s[2:3], -1
	s_and_b64 vcc, exec, s[0:1]
	s_waitcnt vmcnt(0) lgkmcnt(0)
	v_pk_fma_f32 v[4:5], v[4:5], v[102:103], v[190:191] op_sel_hi:[1,0,1]
	s_nop 0
	v_pk_mul_f32 v[2:3], v[2:3], v[4:5]
	ds_read_b64 v[4:5], v141 offset:4096
	s_waitcnt lgkmcnt(0)
	v_pk_fma_f32 v[4:5], v[6:7], v[102:103], v[4:5] op_sel:[0,1,0]
	s_nop 0
	v_pk_mul_f32 v[102:103], v[0:1], v[4:5]
	ds_read_b64 v[0:1], v142 offset:8192
	v_mov_b32_e32 v6, v105
	s_waitcnt lgkmcnt(0)
	v_pk_fma_f32 v[0:1], v[12:13], v[104:105], v[0:1] op_sel_hi:[1,0,1]
	s_nop 0
	v_pk_mul_f32 v[4:5], v[10:11], v[0:1]
	ds_read_b64 v[0:1], v143 offset:12288
	v_mov_b32_e32 v10, v189
	s_waitcnt lgkmcnt(0)
	v_pk_fma_f32 v[0:1], v[14:15], v[6:7], v[0:1] op_sel_hi:[1,0,1]
	s_nop 0
	v_pk_mul_f32 v[104:105], v[8:9], v[0:1]
	ds_read_b64 v[0:1], v144 offset:16384
	ds_read_b64 v[6:7], v145 offset:20480
	s_waitcnt lgkmcnt(1)
	v_pk_fma_f32 v[0:1], v[20:21], v[186:187], v[0:1] op_sel_hi:[1,0,1]
	s_waitcnt lgkmcnt(0)
	v_pk_fma_f32 v[6:7], v[22:23], v[186:187], v[6:7] op_sel:[0,1,0]
	v_pk_mul_f32 v[0:1], v[18:19], v[0:1]
	v_pk_mul_f32 v[12:13], v[16:17], v[6:7]
	ds_read_b64 v[6:7], v146 offset:24576
	v_mov_b32_e32 v18, v185
	s_waitcnt lgkmcnt(0)
	v_pk_fma_f32 v[6:7], v[28:29], v[188:189], v[6:7] op_sel_hi:[1,0,1]
	s_nop 0
	v_pk_mul_f32 v[8:9], v[26:27], v[6:7]
	ds_read_b64 v[6:7], v147 offset:28672
	ds_read_b64 v[26:27], v155 offset:61440
	v_mov_b32_e32 v28, v179
	s_waitcnt lgkmcnt(1)
	v_pk_fma_f32 v[6:7], v[98:99], v[10:11], v[6:7] op_sel_hi:[1,0,1]
	s_nop 0
	v_pk_mul_f32 v[22:23], v[24:25], v[6:7]
	ds_read_b64 v[6:7], v148 offset:32768
	ds_read_b64 v[10:11], v149 offset:36864
	s_waitcnt lgkmcnt(2)
	v_pk_fma_f32 v[26:27], v[132:133], v[28:29], v[26:27] op_sel_hi:[1,0,1]
	s_waitcnt lgkmcnt(1)
	v_pk_fma_f32 v[6:7], v[106:107], v[182:183], v[6:7] op_sel_hi:[1,0,1]
	s_waitcnt lgkmcnt(0)
	v_pk_fma_f32 v[10:11], v[108:109], v[182:183], v[10:11] op_sel:[0,1,0]
	v_pk_mul_f32 v[6:7], v[100:101], v[6:7]
	v_pk_mul_f32 v[16:17], v[30:31], v[10:11]
	ds_read_b64 v[10:11], v150 offset:40960
	v_pk_mul_f32 v[26:27], v[126:127], v[26:27]
	s_waitcnt lgkmcnt(0)
	v_pk_fma_f32 v[10:11], v[114:115], v[184:185], v[10:11] op_sel_hi:[1,0,1]
	s_nop 0
	v_pk_mul_f32 v[14:15], v[112:113], v[10:11]
	ds_read_b64 v[10:11], v151 offset:45056
	s_waitcnt lgkmcnt(0)
	v_pk_fma_f32 v[10:11], v[116:117], v[18:19], v[10:11] op_sel_hi:[1,0,1]
	s_nop 0
	v_pk_mul_f32 v[24:25], v[110:111], v[10:11]
	ds_read_b64 v[10:11], v152 offset:49152
	ds_read_b64 v[18:19], v153 offset:53248
	s_waitcnt lgkmcnt(1)
	v_pk_fma_f32 v[10:11], v[122:123], v[176:177], v[10:11] op_sel_hi:[1,0,1]
	s_waitcnt lgkmcnt(0)
	v_pk_fma_f32 v[18:19], v[124:125], v[176:177], v[18:19] op_sel:[0,1,0]
	v_pk_mul_f32 v[10:11], v[120:121], v[10:11]
	v_pk_mul_f32 v[20:21], v[118:119], v[18:19]
	ds_read_b64 v[18:19], v154 offset:57344
	s_waitcnt lgkmcnt(0)
	v_pk_fma_f32 v[18:19], v[130:131], v[178:179], v[18:19] op_sel_hi:[1,0,1]
	s_nop 0
	v_pk_mul_f32 v[18:19], v[128:129], v[18:19]
	s_cbranch_vccz .LBB0_883
	s_and_saveexec_b64 s[2:3], s[38:39]
	s_cbranch_execz .LBB0_882
	v_cvt_pk_bf16_f32 v28, v2, v102
	v_cvt_pk_bf16_f32 v29, v4, v104
	v_cvt_pk_bf16_f32 v30, v0, v12
	v_cvt_pk_bf16_f32 v31, v8, v22
	v_cvt_pk_bf16_f32 v98, v6, v16
	v_cvt_pk_bf16_f32 v99, v14, v24
	v_cvt_pk_bf16_f32 v100, v10, v20
	v_cvt_pk_bf16_f32 v101, v18, v26
	v_cvt_pk_bf16_f32 v106, v3, v103
	v_cvt_pk_bf16_f32 v107, v5, v105
	v_cvt_pk_bf16_f32 v108, v1, v13
	v_cvt_pk_bf16_f32 v109, v9, v23
	v_cvt_pk_bf16_f32 v110, v7, v17
	v_cvt_pk_bf16_f32 v111, v15, v25
	v_cvt_pk_bf16_f32 v112, v11, v21
	v_cvt_pk_bf16_f32 v113, v19, v27
	global_store_dwordx4 v[58:59], v[28:31], off
	global_store_dwordx4 v[58:59], v[98:101], off offset:16
	global_store_dwordx4 v[60:61], v[106:109], off
	global_store_dwordx4 v[64:65], v[110:113], off

; template <int R, class XT, class TWT>
; __device__ __forceinline__ void dif_task(XT X, TWT tw, int s, int task) {
;     const int lgM = 13 - s, lgq = lgM - R, q = 1 << lgq;
;     const int j0 = task & (q - 1), blk = task >> lgq, base = (blk << lgM) + j0;
;     const int pb = PADI(base), qp = (q >= 32) ? q + (q >> 4) : q;
;     f32x2v v[1 << R];
; #pragma unroll
;     for (int k = 0; k < (1 << R); ++k) v[k] = X[pb + k * qp];
; #pragma unroll
;     for (int r = 0; r < R; ++r) {
;         const int pb = R - 1 - r;
; #pragma unroll
;         for (int k = 0; k < (1 << R); ++k) if (!((k >> pb) & 1)) {
;             const int klo = k & ((1 << pb) - 1);
;             const f32x2v w = tw[(j0 + (klo << lgq)) << (s + r)];
;             const f32x2v a = v[k], b = v[k + (1 << pb)], d = a - b;
;             v[k] = a + b; v[k + (1 << pb)] = (f32x2v){d.x * w.x - d.y * w.y, d.x * w.y + d.y * w.x};
;         }
;     }
; #pragma unroll
;     for (int k = 0; k < (1 << R); ++k) X[pb + k * qp] = v[k];
; template <bool LAT>
; __device__ __forceinline__ void hyconv_unit(const Frame& F, LAS f32x2v* X, const TwHalf tw, LAS bf16* OUT, const float* skip, bf16* MIX, int u) {
;     ...
;             const f32x2v* SP = SPb + (size_t)ord * 256 * N;
;             f32x4 kq[8];
; #pragma unroll
;             for (int r = 0; r < 8; ++r) kq[r] = *(const f32x4*)(SP + 2 * (F.tid + 512 * r));
.LBB0_937:
	s_lshl_b32 s90, s2, 17
	s_lshl_b64 s[0:1], s[90:91], 3
	s_add_u32 s0, s5, s0
	s_addc_u32 s1, s8, s1
	v_lshl_add_u64 v[0:1], v[44:45], 3, s[0:1]
	v_lshl_add_u64 v[2:3], v[50:51], 3, s[0:1]
	global_load_dwordx4 v[28:31], v[0:1], off
	global_load_dwordx4 v[24:27], v[2:3], off
	v_lshl_add_u64 v[0:1], v[52:53], 3, s[0:1]
	v_lshl_add_u64 v[2:3], v[54:55], 3, s[0:1]
	global_load_dwordx4 v[20:23], v[0:1], off
	global_load_dwordx4 v[16:19], v[2:3], off
	v_lshl_add_u64 v[0:1], v[56:57], 3, s[0:1]
	v_lshl_add_u64 v[2:3], v[58:59], 3, s[0:1]
	global_load_dwordx4 v[12:15], v[0:1], off
	global_load_dwordx4 v[8:11], v[2:3], off
	v_lshl_add_u64 v[0:1], v[60:61], 3, s[0:1]
	v_lshl_add_u64 v[2:3], v[62:63], 3, s[0:1]
	global_load_dwordx4 v[4:7], v[0:1], off
	s_nop 0
	global_load_dwordx4 v[0:3], v[2:3], off
	ds_read2_b64 v[96:99], v130 offset1:34
	ds_read2_b64 v[100:103], v130 offset0:68 offset1:102
	ds_read2_b64 v[104:107], v130 offset0:136 offset1:170
	ds_read2_b64 v[108:111], v130 offset0:204 offset1:238
	v_add_u32_e32 v94, 0x800, v130
	ds_read2_b64 v[112:115], v94 offset0:16 offset1:50
	ds_read2_b64 v[116:119], v94 offset0:84 offset1:118
	ds_read2_b64 v[120:123], v94 offset0:152 offset1:186
	ds_read2_b64 v[124:127], v94 offset0:220 offset1:254
	ds_read2st64_b64 v[172:175], v159 offset1:16
	ds_read_b64 v[128:129], v160
	ds_read_b64 v[176:177], v161
	ds_read_b64 v[178:179], v162
	ds_read_b64 v[182:183], v163
	ds_read_b64 v[184:185], v164
	ds_read_b64 v[186:187], v133
	ds_read_b64 v[188:189], v131
	s_waitcnt lgkmcnt(11)
	v_pk_add_f32 v[190:191], v[96:97], v[112:113] neg_lo:[0,1] neg_hi:[0,1]
	v_pk_add_f32 v[96:97], v[96:97], v[112:113]
	s_waitcnt lgkmcnt(7)
	v_pk_mul_f32 v[192:193], v[190:191], v[172:173] op_sel:[1,1] op_sel_hi:[1,0]
	s_lshl_b32 s0, s2, 8
	v_pk_fma_f32 v[194:195], v[190:191], v[172:173], v[192:193] op_sel_hi:[0,1,1] neg_lo:[0,0,1]
	v_pk_add_f32 v[190:191], v[104:105], v[120:121] neg_lo:[0,1] neg_hi:[0,1]
	v_pk_add_f32 v[104:105], v[104:105], v[120:121]
	v_pk_mul_f32 v[192:193], v[190:191], v[172:173] op_sel:[1,0] op_sel_hi:[0,0]
	v_pk_fma_f32 v[196:197], v[190:191], v[172:173], v[192:193] op_sel:[0,1,0] neg_hi:[0,0,1]
	v_pk_add_f32 v[112:113], v[96:97], v[104:105]
	v_pk_add_f32 v[172:173], v[194:195], v[196:197] neg_lo:[0,1] neg_hi:[0,1]
	s_waitcnt lgkmcnt(0)
	v_xor_b32_e32 v95, 0x80000000, v188
	v_pk_mul_f32 v[190:191], v[178:179], v[172:173] op_sel:[1,1] op_sel_hi:[0,1]
	v_pk_fma_f32 v[192:193], v[178:179], v[172:173], v[190:191] op_sel_hi:[1,0,1] neg_lo:[0,0,1]
	v_pk_add_f32 v[96:97], v[96:97], v[104:105] neg_lo:[0,1] neg_hi:[0,1]
	v_pk_add_f32 v[172:173], v[100:101], v[116:117] neg_lo:[0,1] neg_hi:[0,1]
	v_pk_add_f32 v[100:101], v[100:101], v[116:117]
	v_pk_mul_f32 v[190:191], v[172:173], v[174:175] op_sel:[1,1] op_sel_hi:[1,0]
	v_pk_mul_f32 v[104:105], v[96:97], v[178:179] op_sel:[1,1] op_sel_hi:[1,0]
	v_pk_fma_f32 v[198:199], v[172:173], v[174:175], v[190:191] op_sel_hi:[0,1,1] neg_lo:[0,0,1]
	v_pk_add_f32 v[172:173], v[108:109], v[124:125] neg_lo:[0,1] neg_hi:[0,1]
	v_pk_add_f32 v[108:109], v[108:109], v[124:125]
	v_pk_mul_f32 v[190:191], v[172:173], v[174:175] op_sel:[1,0] op_sel_hi:[0,0]
	v_pk_fma_f32 v[202:203], v[172:173], v[174:175], v[190:191] op_sel:[0,1,0] neg_hi:[0,0,1]
	v_pk_add_f32 v[116:117], v[100:101], v[108:109]
	v_pk_add_f32 v[172:173], v[198:199], v[202:203] neg_lo:[0,1] neg_hi:[0,1]
	v_pk_add_f32 v[120:121], v[112:113], v[116:117]
	v_pk_mul_f32 v[174:175], v[178:179], v[172:173] op_sel_hi:[0,1]
	v_pk_fma_f32 v[190:191], v[178:179], v[172:173], v[174:175] op_sel:[1,0,1] op_sel_hi:[1,1,0] neg_hi:[0,0,1]
	v_pk_add_f32 v[112:113], v[112:113], v[116:117] neg_lo:[0,1] neg_hi:[0,1]
	v_pk_add_f32 v[172:173], v[192:193], v[190:191] neg_lo:[0,1] neg_hi:[0,1]
	v_pk_mul_f32 v[116:117], v[112:113], v[184:185] op_sel:[1,1] op_sel_hi:[1,0]
	v_pk_mul_f32 v[174:175], v[184:185], v[172:173] op_sel:[1,1] op_sel_hi:[0,1]
	v_pk_fma_f32 v[204:205], v[184:185], v[172:173], v[174:175] op_sel_hi:[1,0,1] neg_lo:[0,0,1]
	s_or_b32 s14, s0, s16
	v_pk_add_f32 v[172:173], v[98:99], v[114:115] neg_lo:[0,1] neg_hi:[0,1]
	v_pk_add_f32 v[98:99], v[98:99], v[114:115]
	v_pk_mul_f32 v[174:175], v[172:173], v[128:129] op_sel:[1,1] op_sel_hi:[1,0]
	s_nop 0
	s_lshl_b32 s90, s14, 9
	v_pk_fma_f32 v[206:207], v[172:173], v[128:129], v[174:175] op_sel_hi:[0,1,1] neg_lo:[0,0,1]
	v_pk_add_f32 v[172:173], v[106:107], v[122:123] neg_lo:[0,1] neg_hi:[0,1]
	v_pk_add_f32 v[106:107], v[106:107], v[122:123]
	v_pk_mul_f32 v[174:175], v[172:173], v[128:129] op_sel:[1,0] op_sel_hi:[0,0]
	v_pk_fma_f32 v[208:209], v[172:173], v[128:129], v[174:175] op_sel:[0,1,0] neg_hi:[0,0,1]
	v_pk_add_f32 v[114:115], v[98:99], v[106:107]
	v_pk_add_f32 v[128:129], v[206:207], v[208:209] neg_lo:[0,1] neg_hi:[0,1]
	v_pk_add_f32 v[98:99], v[98:99], v[106:107] neg_lo:[0,1] neg_hi:[0,1]
	v_pk_mul_f32 v[172:173], v[182:183], v[128:129] op_sel:[1,1] op_sel_hi:[0,1]
	v_pk_fma_f32 v[174:175], v[182:183], v[128:129], v[172:173] op_sel_hi:[1,0,1] neg_lo:[0,0,1]
	s_nop 0
	v_pk_add_f32 v[128:129], v[102:103], v[118:119] neg_lo:[0,1] neg_hi:[0,1]
	v_pk_add_f32 v[102:103], v[102:103], v[118:119]
	v_pk_mul_f32 v[172:173], v[128:129], v[176:177] op_sel:[1,1] op_sel_hi:[1,0]
	s_nop 0
	v_pk_fma_f32 v[220:221], v[128:129], v[176:177], v[172:173] op_sel_hi:[0,1,1] neg_lo:[0,0,1]
	v_pk_add_f32 v[128:129], v[110:111], v[126:127] neg_lo:[0,1] neg_hi:[0,1]
	v_pk_add_f32 v[110:111], v[110:111], v[126:127]
	v_pk_mul_f32 v[172:173], v[128:129], v[176:177] op_sel:[1,0] op_sel_hi:[0,0]
	v_pk_fma_f32 v[222:223], v[128:129], v[176:177], v[172:173] op_sel:[0,1,0] neg_hi:[0,0,1]
	v_pk_add_f32 v[118:119], v[102:103], v[110:111]
; template <int R, class XT, class TWT>
; __device__ __forceinline__ void dif_task(XT X, TWT tw, int s, int task) {
;     const int lgM = 13 - s, lgq = lgM - R, q = 1 << lgq;
;     const int j0 = task & (q - 1), blk = task >> lgq, base = (blk << lgM) + j0;
;     const int pb = PADI(base), qp = (q >= 32) ? q + (q >> 4) : q;
;     f32x2v v[1 << R];
; #pragma unroll
;     for (int k = 0; k < (1 << R); ++k) v[k] = X[pb + k * qp];
; #pragma unroll
;     for (int r = 0; r < R; ++r) {
;         const int pb = R - 1 - r;
; #pragma unroll
;         for (int k = 0; k < (1 << R); ++k) if (!((k >> pb) & 1)) {
;             const int klo = k & ((1 << pb) - 1);
;             const f32x2v w = tw[(j0 + (klo << lgq)) << (s + r)];
;             const f32x2v a = v[k], b = v[k + (1 << pb)], d = a - b;
;             v[k] = a + b; v[k + (1 << pb)] = (f32x2v){d.x * w.x - d.y * w.y, d.x * w.y + d.y * w.x};
;         }
;     }
; #pragma unroll
;     for (int k = 0; k < (1 << R); ++k) X[pb + k * qp] = v[k];
	v_pk_add_f32 v[128:129], v[220:221], v[222:223] neg_lo:[0,1] neg_hi:[0,1]
	v_pk_add_f32 v[122:123], v[114:115], v[118:119]
	v_pk_mul_f32 v[172:173], v[186:187], v[128:129] op_sel_hi:[0,1]
	v_pk_fma_f32 v[176:177], v[186:187], v[128:129], v[172:173] op_sel:[1,0,1] op_sel_hi:[1,1,0] neg_hi:[0,0,1]
	v_pk_add_f32 v[124:125], v[120:121], v[122:123]
	v_pk_add_f32 v[128:129], v[174:175], v[176:177] neg_lo:[0,1] neg_hi:[0,1]
	v_pk_add_f32 v[120:121], v[120:121], v[122:123] neg_lo:[0,1] neg_hi:[0,1]
	v_pk_mul_f32 v[172:173], v[184:185], v[128:129] op_sel_hi:[0,1]
	v_pk_fma_f32 v[224:225], v[184:185], v[128:129], v[172:173] op_sel:[1,0,1] op_sel_hi:[1,1,0] neg_hi:[0,0,1]
	v_cndmask_b32_e64 v173, v95, v189, s[44:45]
	v_cndmask_b32_e64 v172, v189, v188, s[44:45]
	v_pk_mul_f32 v[122:123], v[120:121], v[172:173] op_sel:[1,1] op_sel_hi:[1,0]
	s_nop 0
	v_pk_fma_f32 v[126:127], v[120:121], v[172:173], v[122:123] op_sel_hi:[0,1,1] neg_lo:[0,0,1]
	v_pk_fma_f32 v[120:121], v[112:113], v[184:185], v[116:117] op_sel_hi:[0,1,1] neg_lo:[0,0,1]
	v_pk_add_f32 v[112:113], v[114:115], v[118:119] neg_lo:[0,1] neg_hi:[0,1]
	v_pk_add_f32 v[128:129], v[204:205], v[224:225] neg_lo:[0,1] neg_hi:[0,1]
	v_pk_mul_f32 v[114:115], v[112:113], v[184:185] op_sel_hi:[1,0]
	v_mov_b32_e32 v95, s4
	v_pk_fma_f32 v[116:117], v[112:113], v[184:185], v[114:115] op_sel:[0,1,1] op_sel_hi:[1,1,0] neg_hi:[0,0,1]
	s_nop 0
	v_pk_add_f32 v[114:115], v[120:121], v[116:117] neg_lo:[0,1] neg_hi:[0,1]
	v_pk_add_f32 v[112:113], v[120:121], v[116:117]
	v_pk_mul_f32 v[116:117], v[172:173], v[114:115] op_sel:[1,1] op_sel_hi:[0,1]
	v_pk_fma_f32 v[118:119], v[172:173], v[114:115], v[116:117] op_sel_hi:[1,0,1] neg_lo:[0,0,1]
	s_nop 0
	v_pk_fma_f32 v[114:115], v[96:97], v[178:179], v[104:105] op_sel_hi:[0,1,1] neg_lo:[0,0,1]
	v_pk_add_f32 v[96:97], v[100:101], v[108:109] neg_lo:[0,1] neg_hi:[0,1]
	s_nop 0
	v_pk_mul_f32 v[100:101], v[96:97], v[178:179] op_sel_hi:[1,0]
	s_nop 0
	v_pk_fma_f32 v[104:105], v[96:97], v[178:179], v[100:101] op_sel:[0,1,1] op_sel_hi:[1,1,0] neg_hi:[0,0,1]
	v_pk_mul_f32 v[100:101], v[98:99], v[182:183] op_sel:[1,1] op_sel_hi:[1,0]
	s_nop 0
	v_pk_fma_f32 v[106:107], v[98:99], v[182:183], v[100:101] op_sel_hi:[0,1,1] neg_lo:[0,0,1]
	v_pk_add_f32 v[98:99], v[102:103], v[110:111] neg_lo:[0,1] neg_hi:[0,1]
	v_pk_add_f32 v[96:97], v[114:115], v[104:105]
	v_pk_mul_f32 v[100:101], v[98:99], v[186:187] op_sel_hi:[1,0]
	v_pk_add_f32 v[110:111], v[206:207], v[208:209]
	v_pk_fma_f32 v[102:103], v[98:99], v[186:187], v[100:101] op_sel:[0,1,1] op_sel_hi:[1,1,0] neg_hi:[0,0,1]
	s_nop 0
	v_pk_add_f32 v[98:99], v[106:107], v[102:103]
	s_nop 0
	v_pk_add_f32 v[100:101], v[96:97], v[98:99]
	v_pk_add_f32 v[96:97], v[96:97], v[98:99] neg_lo:[0,1] neg_hi:[0,1]
	s_nop 0
	v_pk_mul_f32 v[98:99], v[172:173], v[96:97] op_sel:[1,1] op_sel_hi:[0,1]
	v_pk_fma_f32 v[108:109], v[172:173], v[96:97], v[98:99] op_sel_hi:[1,0,1] neg_lo:[0,0,1]
	s_nop 0
	v_pk_add_f32 v[96:97], v[114:115], v[104:105] neg_lo:[0,1] neg_hi:[0,1]
	v_pk_add_f32 v[114:115], v[220:221], v[222:223]
	v_pk_mul_f32 v[98:99], v[184:185], v[96:97] op_sel:[1,1] op_sel_hi:[0,1]
	v_pk_fma_f32 v[104:105], v[184:185], v[96:97], v[98:99] op_sel_hi:[1,0,1] neg_lo:[0,0,1]
	v_pk_add_f32 v[116:117], v[110:111], v[114:115]
	v_pk_add_f32 v[96:97], v[106:107], v[102:103] neg_lo:[0,1] neg_hi:[0,1]
	s_nop 0
	v_pk_mul_f32 v[98:99], v[184:185], v[96:97] op_sel_hi:[0,1]
	v_pk_fma_f32 v[102:103], v[184:185], v[96:97], v[98:99] op_sel:[1,0,1] op_sel_hi:[1,1,0] neg_hi:[0,0,1]
	s_nop 0
	v_pk_add_f32 v[98:99], v[104:105], v[102:103] neg_lo:[0,1] neg_hi:[0,1]
	v_pk_add_f32 v[96:97], v[104:105], v[102:103]
	v_pk_mul_f32 v[102:103], v[172:173], v[98:99] op_sel:[1,1] op_sel_hi:[0,1]
	v_pk_fma_f32 v[104:105], v[172:173], v[98:99], v[102:103] op_sel_hi:[1,0,1] neg_lo:[0,0,1]
	v_pk_add_f32 v[102:103], v[198:199], v[202:203]
	v_pk_add_f32 v[98:99], v[194:195], v[196:197]
	s_nop 0
	v_pk_add_f32 v[106:107], v[98:99], v[102:103]
	v_pk_add_f32 v[98:99], v[98:99], v[102:103] neg_lo:[0,1] neg_hi:[0,1]
	v_pk_add_f32 v[120:121], v[106:107], v[116:117]
	v_pk_add_f32 v[106:107], v[106:107], v[116:117] neg_lo:[0,1] neg_hi:[0,1]
	v_pk_mul_f32 v[102:103], v[184:185], v[98:99] op_sel:[1,1] op_sel_hi:[0,1]
	v_pk_mul_f32 v[116:117], v[106:107], v[172:173] op_sel:[1,1] op_sel_hi:[1,0]
	s_nop 0
	v_pk_fma_f32 v[122:123], v[106:107], v[172:173], v[116:117] op_sel_hi:[0,1,1] neg_lo:[0,0,1]
	v_pk_fma_f32 v[106:107], v[184:185], v[98:99], v[102:103] op_sel_hi:[1,0,1] neg_lo:[0,0,1]
	s_nop 0
	v_pk_add_f32 v[98:99], v[110:111], v[114:115] neg_lo:[0,1] neg_hi:[0,1]
	s_nop 0
	v_pk_mul_f32 v[102:103], v[184:185], v[98:99] op_sel_hi:[0,1]
	v_pk_fma_f32 v[110:111], v[184:185], v[98:99], v[102:103] op_sel:[1,0,1] op_sel_hi:[1,1,0] neg_hi:[0,0,1]
	s_nop 0
	v_pk_add_f32 v[102:103], v[106:107], v[110:111] neg_lo:[0,1] neg_hi:[0,1]
	v_pk_add_f32 v[98:99], v[106:107], v[110:111]
	v_pk_mul_f32 v[106:107], v[172:173], v[102:103] op_sel:[1,1] op_sel_hi:[0,1]
	v_pk_fma_f32 v[110:111], v[172:173], v[102:103], v[106:107] op_sel_hi:[1,0,1] neg_lo:[0,0,1]
	v_pk_add_f32 v[106:107], v[174:175], v[176:177]
	v_pk_add_f32 v[102:103], v[192:193], v[190:191]
	s_nop 0
	v_pk_add_f32 v[114:115], v[102:103], v[106:107]
	v_pk_add_f32 v[102:103], v[102:103], v[106:107] neg_lo:[0,1] neg_hi:[0,1]
	s_nop 0
	v_pk_mul_f32 v[106:107], v[172:173], v[102:103] op_sel:[1,1] op_sel_hi:[0,1]
	v_pk_fma_f32 v[116:117], v[172:173], v[102:103], v[106:107] op_sel_hi:[1,0,1] neg_lo:[0,0,1]
	v_pk_mul_f32 v[106:107], v[172:173], v[128:129] op_sel:[1,1] op_sel_hi:[0,1]
	v_pk_fma_f32 v[174:175], v[172:173], v[128:129], v[106:107] op_sel_hi:[1,0,1] neg_lo:[0,0,1]
	v_pk_add_f32 v[102:103], v[204:205], v[224:225]
	ds_write2_b64 v130, v[124:125], v[126:127] offset1:34
	ds_write2_b64 v130, v[112:113], v[118:119] offset0:68 offset1:102
	ds_write2_b64 v130, v[100:101], v[108:109] offset0:136 offset1:170
	ds_write2_b64 v130, v[96:97], v[104:105] offset0:204 offset1:238
	ds_write2_b64 v94, v[120:121], v[122:123] offset0:16 offset1:50
	ds_write2_b64 v94, v[98:99], v[110:111] offset0:84 offset1:118
	ds_write2_b64 v94, v[114:115], v[116:117] offset0:152 offset1:186
	ds_write2_b64 v94, v[102:103], v[174:175] offset0:220 offset1:254
	s_waitcnt lgkmcnt(0)
	s_barrier
; template <int R, class XT, class TWT>
; __device__ __forceinline__ void dif_task(XT X, TWT tw, int s, int task) {
;     const int lgM = 13 - s, lgq = lgM - R, q = 1 << lgq;
;     const int j0 = task & (q - 1), blk = task >> lgq, base = (blk << lgM) + j0;
;     const int pb = PADI(base), qp = (q >= 32) ? q + (q >> 4) : q;
;     f32x2v v[1 << R];
; #pragma unroll
;     for (int k = 0; k < (1 << R); ++k) v[k] = X[pb + k * qp];
; #pragma unroll
;     for (int r = 0; r < R; ++r) {
;         const int pb = R - 1 - r;
; #pragma unroll
;         for (int k = 0; k < (1 << R); ++k) if (!((k >> pb) & 1)) {
;             const int klo = k & ((1 << pb) - 1);
;             const f32x2v w = tw[(j0 + (klo << lgq)) << (s + r)];
;             const f32x2v a = v[k], b = v[k + (1 << pb)], d = a - b;
;             v[k] = a + b; v[k + (1 << pb)] = (f32x2v){d.x * w.x - d.y * w.y, d.x * w.y + d.y * w.x};
;         }
;     }
; #pragma unroll
;     for (int k = 0; k < (1 << R); ++k) X[pb + k * qp] = v[k];
	ds_read2_b64 v[96:99], v132 offset1:2
	ds_read2_b64 v[100:103], v132 offset0:4 offset1:6
	ds_read2_b64 v[104:107], v132 offset0:8 offset1:10
	ds_read2_b64 v[108:111], v132 offset0:12 offset1:14
	ds_read2_b64 v[112:115], v132 offset0:16 offset1:18
	ds_read2_b64 v[116:119], v132 offset0:20 offset1:22
	ds_read2_b64 v[120:123], v132 offset0:24 offset1:26
	ds_read2_b64 v[124:127], v132 offset0:28 offset1:30
	ds_read2st64_b64 v[172:175], v165 offset1:16
	ds_read_b64 v[128:129], v166
	ds_read_b64 v[176:177], v167
	ds_read_b64 v[178:179], v168
	ds_read_b64 v[182:183], v150
	s_waitcnt lgkmcnt(8)
	v_pk_add_f32 v[190:191], v[96:97], v[112:113] neg_lo:[0,1] neg_hi:[0,1]
	ds_read_b64 v[184:185], v169
	ds_read_b64 v[186:187], v170
	ds_read_b64 v[188:189], v95
	s_waitcnt lgkmcnt(7)
	v_pk_mul_f32 v[192:193], v[190:191], v[172:173] op_sel:[1,1] op_sel_hi:[1,0]
	v_pk_add_f32 v[96:97], v[96:97], v[112:113]
	v_pk_fma_f32 v[194:195], v[190:191], v[172:173], v[192:193] op_sel_hi:[0,1,1] neg_lo:[0,0,1]
	v_pk_add_f32 v[190:191], v[104:105], v[120:121] neg_lo:[0,1] neg_hi:[0,1]
	v_pk_add_f32 v[104:105], v[104:105], v[120:121]
	v_pk_mul_f32 v[192:193], v[190:191], v[172:173] op_sel:[1,0] op_sel_hi:[0,0]
	v_pk_fma_f32 v[196:197], v[190:191], v[172:173], v[192:193] op_sel:[0,1,0] neg_hi:[0,0,1]
	v_pk_add_f32 v[112:113], v[96:97], v[104:105]
	v_pk_add_f32 v[172:173], v[194:195], v[196:197] neg_lo:[0,1] neg_hi:[0,1]
	s_waitcnt lgkmcnt(0)
	v_xor_b32_e32 v171, 0x80000000, v188
	v_pk_mul_f32 v[190:191], v[178:179], v[172:173] op_sel:[1,1] op_sel_hi:[0,1]
	v_pk_fma_f32 v[192:193], v[178:179], v[172:173], v[190:191] op_sel_hi:[1,0,1] neg_lo:[0,0,1]
	v_pk_add_f32 v[96:97], v[96:97], v[104:105] neg_lo:[0,1] neg_hi:[0,1]
	v_pk_add_f32 v[172:173], v[100:101], v[116:117] neg_lo:[0,1] neg_hi:[0,1]
	v_pk_add_f32 v[100:101], v[100:101], v[116:117]
	v_pk_mul_f32 v[190:191], v[172:173], v[174:175] op_sel:[1,1] op_sel_hi:[1,0]
	v_pk_mul_f32 v[104:105], v[96:97], v[178:179] op_sel:[1,1] op_sel_hi:[1,0]
	v_pk_fma_f32 v[198:199], v[172:173], v[174:175], v[190:191] op_sel_hi:[0,1,1] neg_lo:[0,0,1]
	v_pk_add_f32 v[172:173], v[108:109], v[124:125] neg_lo:[0,1] neg_hi:[0,1]
	v_pk_add_f32 v[108:109], v[108:109], v[124:125]
	v_pk_mul_f32 v[190:191], v[172:173], v[174:175] op_sel:[1,0] op_sel_hi:[0,0]
	v_pk_fma_f32 v[202:203], v[172:173], v[174:175], v[190:191] op_sel:[0,1,0] neg_hi:[0,0,1]
	v_pk_add_f32 v[116:117], v[100:101], v[108:109]
	v_pk_add_f32 v[172:173], v[198:199], v[202:203] neg_lo:[0,1] neg_hi:[0,1]
	v_pk_add_f32 v[120:121], v[112:113], v[116:117]
	v_pk_mul_f32 v[174:175], v[178:179], v[172:173] op_sel_hi:[0,1]
	v_pk_fma_f32 v[190:191], v[178:179], v[172:173], v[174:175] op_sel:[1,0,1] op_sel_hi:[1,1,0] neg_hi:[0,0,1]
	v_pk_add_f32 v[112:113], v[112:113], v[116:117] neg_lo:[0,1] neg_hi:[0,1]
	v_pk_add_f32 v[172:173], v[192:193], v[190:191] neg_lo:[0,1] neg_hi:[0,1]
	v_pk_mul_f32 v[116:117], v[112:113], v[186:187] op_sel:[1,1] op_sel_hi:[1,0]
	v_pk_mul_f32 v[174:175], v[186:187], v[172:173] op_sel:[1,1] op_sel_hi:[0,1]
	v_pk_fma_f32 v[204:205], v[186:187], v[172:173], v[174:175] op_sel_hi:[1,0,1] neg_lo:[0,0,1]
	s_nop 0
	v_pk_add_f32 v[172:173], v[98:99], v[114:115] neg_lo:[0,1] neg_hi:[0,1]
	v_pk_add_f32 v[98:99], v[98:99], v[114:115]
	v_pk_mul_f32 v[174:175], v[172:173], v[128:129] op_sel:[1,1] op_sel_hi:[1,0]
	s_nop 0
	v_pk_fma_f32 v[206:207], v[172:173], v[128:129], v[174:175] op_sel_hi:[0,1,1] neg_lo:[0,0,1]
	v_pk_add_f32 v[172:173], v[106:107], v[122:123] neg_lo:[0,1] neg_hi:[0,1]
	v_pk_add_f32 v[106:107], v[106:107], v[122:123]
	v_pk_mul_f32 v[174:175], v[172:173], v[128:129] op_sel:[1,0] op_sel_hi:[0,0]
	v_pk_fma_f32 v[208:209], v[172:173], v[128:129], v[174:175] op_sel:[0,1,0] neg_hi:[0,0,1]
	v_pk_add_f32 v[114:115], v[98:99], v[106:107]
	v_pk_add_f32 v[128:129], v[206:207], v[208:209] neg_lo:[0,1] neg_hi:[0,1]
	v_pk_add_f32 v[98:99], v[98:99], v[106:107] neg_lo:[0,1] neg_hi:[0,1]
	v_pk_mul_f32 v[172:173], v[184:185], v[128:129] op_sel:[1,1] op_sel_hi:[0,1]
	v_pk_fma_f32 v[174:175], v[184:185], v[128:129], v[172:173] op_sel_hi:[1,0,1] neg_lo:[0,0,1]
	s_nop 0
	v_pk_add_f32 v[128:129], v[102:103], v[118:119] neg_lo:[0,1] neg_hi:[0,1]
	v_pk_add_f32 v[102:103], v[102:103], v[118:119]
	v_pk_mul_f32 v[172:173], v[128:129], v[176:177] op_sel:[1,1] op_sel_hi:[1,0]
	s_nop 0
	v_pk_fma_f32 v[220:221], v[128:129], v[176:177], v[172:173] op_sel_hi:[0,1,1] neg_lo:[0,0,1]
	v_pk_add_f32 v[128:129], v[110:111], v[126:127] neg_lo:[0,1] neg_hi:[0,1]
	v_pk_add_f32 v[110:111], v[110:111], v[126:127]
	v_pk_mul_f32 v[172:173], v[128:129], v[176:177] op_sel:[1,0] op_sel_hi:[0,0]
	v_pk_fma_f32 v[222:223], v[128:129], v[176:177], v[172:173] op_sel:[0,1,0] neg_hi:[0,0,1]
	v_pk_add_f32 v[118:119], v[102:103], v[110:111]
	v_pk_add_f32 v[128:129], v[220:221], v[222:223] neg_lo:[0,1] neg_hi:[0,1]
	v_pk_add_f32 v[122:123], v[114:115], v[118:119]
	v_pk_mul_f32 v[172:173], v[182:183], v[128:129] op_sel_hi:[0,1]
	v_pk_fma_f32 v[176:177], v[182:183], v[128:129], v[172:173] op_sel:[1,0,1] op_sel_hi:[1,1,0] neg_hi:[0,0,1]
	v_pk_add_f32 v[124:125], v[120:121], v[122:123]
	v_pk_add_f32 v[128:129], v[174:175], v[176:177] neg_lo:[0,1] neg_hi:[0,1]
	v_pk_add_f32 v[120:121], v[120:121], v[122:123] neg_lo:[0,1] neg_hi:[0,1]
	v_pk_mul_f32 v[172:173], v[186:187], v[128:129] op_sel_hi:[0,1]
	v_pk_fma_f32 v[224:225], v[186:187], v[128:129], v[172:173] op_sel:[1,0,1] op_sel_hi:[1,1,0] neg_hi:[0,0,1]
	v_cndmask_b32_e64 v173, v171, v189, s[42:43]
	v_cndmask_b32_e64 v172, v189, v188, s[42:43]
	v_pk_mul_f32 v[122:123], v[120:121], v[172:173] op_sel:[1,1] op_sel_hi:[1,0]
	s_nop 0
; template <int R, class XT, class TWT>
; __device__ __forceinline__ void dif_task(XT X, TWT tw, int s, int task) {
;     const int lgM = 13 - s, lgq = lgM - R, q = 1 << lgq;
;     const int j0 = task & (q - 1), blk = task >> lgq, base = (blk << lgM) + j0;
;     const int pb = PADI(base), qp = (q >= 32) ? q + (q >> 4) : q;
;     f32x2v v[1 << R];
; #pragma unroll
;     for (int k = 0; k < (1 << R); ++k) v[k] = X[pb + k * qp];
; #pragma unroll
;     for (int r = 0; r < R; ++r) {
;         const int pb = R - 1 - r;
; #pragma unroll
;         for (int k = 0; k < (1 << R); ++k) if (!((k >> pb) & 1)) {
;             const int klo = k & ((1 << pb) - 1);
;             const f32x2v w = tw[(j0 + (klo << lgq)) << (s + r)];
;             const f32x2v a = v[k], b = v[k + (1 << pb)], d = a - b;
;             v[k] = a + b; v[k + (1 << pb)] = (f32x2v){d.x * w.x - d.y * w.y, d.x * w.y + d.y * w.x};
;         }
;     }
; #pragma unroll
;     for (int k = 0; k < (1 << R); ++k) X[pb + k * qp] = v[k];
	v_pk_fma_f32 v[126:127], v[120:121], v[172:173], v[122:123] op_sel_hi:[0,1,1] neg_lo:[0,0,1]
	v_pk_fma_f32 v[120:121], v[112:113], v[186:187], v[116:117] op_sel_hi:[0,1,1] neg_lo:[0,0,1]
	v_pk_add_f32 v[112:113], v[114:115], v[118:119] neg_lo:[0,1] neg_hi:[0,1]
	v_pk_add_f32 v[128:129], v[204:205], v[224:225] neg_lo:[0,1] neg_hi:[0,1]
	v_pk_mul_f32 v[114:115], v[112:113], v[186:187] op_sel_hi:[1,0]
	s_nop 0
	v_pk_fma_f32 v[116:117], v[112:113], v[186:187], v[114:115] op_sel:[0,1,1] op_sel_hi:[1,1,0] neg_hi:[0,0,1]
	s_nop 0
	v_pk_add_f32 v[114:115], v[120:121], v[116:117] neg_lo:[0,1] neg_hi:[0,1]
	v_pk_add_f32 v[112:113], v[120:121], v[116:117]
	v_pk_mul_f32 v[116:117], v[172:173], v[114:115] op_sel:[1,1] op_sel_hi:[0,1]
	v_pk_fma_f32 v[118:119], v[172:173], v[114:115], v[116:117] op_sel_hi:[1,0,1] neg_lo:[0,0,1]
	s_nop 0
	v_pk_fma_f32 v[114:115], v[96:97], v[178:179], v[104:105] op_sel_hi:[0,1,1] neg_lo:[0,0,1]
	v_pk_add_f32 v[96:97], v[100:101], v[108:109] neg_lo:[0,1] neg_hi:[0,1]
	s_nop 0
	v_pk_mul_f32 v[100:101], v[96:97], v[178:179] op_sel_hi:[1,0]
	s_nop 0
	v_pk_fma_f32 v[104:105], v[96:97], v[178:179], v[100:101] op_sel:[0,1,1] op_sel_hi:[1,1,0] neg_hi:[0,0,1]
	v_pk_mul_f32 v[100:101], v[98:99], v[184:185] op_sel:[1,1] op_sel_hi:[1,0]
	s_nop 0
	v_pk_fma_f32 v[106:107], v[98:99], v[184:185], v[100:101] op_sel_hi:[0,1,1] neg_lo:[0,0,1]
	v_pk_add_f32 v[98:99], v[102:103], v[110:111] neg_lo:[0,1] neg_hi:[0,1]
	v_pk_add_f32 v[96:97], v[114:115], v[104:105]
	v_pk_mul_f32 v[100:101], v[98:99], v[182:183] op_sel_hi:[1,0]
	v_pk_add_f32 v[110:111], v[206:207], v[208:209]
	v_pk_fma_f32 v[102:103], v[98:99], v[182:183], v[100:101] op_sel:[0,1,1] op_sel_hi:[1,1,0] neg_hi:[0,0,1]
	s_nop 0
	v_pk_add_f32 v[98:99], v[106:107], v[102:103]
	s_nop 0
	v_pk_add_f32 v[100:101], v[96:97], v[98:99]
	v_pk_add_f32 v[96:97], v[96:97], v[98:99] neg_lo:[0,1] neg_hi:[0,1]
	s_nop 0
	v_pk_mul_f32 v[98:99], v[172:173], v[96:97] op_sel:[1,1] op_sel_hi:[0,1]
	v_pk_fma_f32 v[108:109], v[172:173], v[96:97], v[98:99] op_sel_hi:[1,0,1] neg_lo:[0,0,1]
	s_nop 0
	v_pk_add_f32 v[96:97], v[114:115], v[104:105] neg_lo:[0,1] neg_hi:[0,1]
	v_pk_add_f32 v[114:115], v[220:221], v[222:223]
	v_pk_mul_f32 v[98:99], v[186:187], v[96:97] op_sel:[1,1] op_sel_hi:[0,1]
	v_pk_fma_f32 v[104:105], v[186:187], v[96:97], v[98:99] op_sel_hi:[1,0,1] neg_lo:[0,0,1]
	v_pk_add_f32 v[116:117], v[110:111], v[114:115]
	v_pk_add_f32 v[96:97], v[106:107], v[102:103] neg_lo:[0,1] neg_hi:[0,1]
	s_nop 0
	v_pk_mul_f32 v[98:99], v[186:187], v[96:97] op_sel_hi:[0,1]
	v_pk_fma_f32 v[102:103], v[186:187], v[96:97], v[98:99] op_sel:[1,0,1] op_sel_hi:[1,1,0] neg_hi:[0,0,1]
	s_nop 0
	v_pk_add_f32 v[98:99], v[104:105], v[102:103] neg_lo:[0,1] neg_hi:[0,1]
	v_pk_add_f32 v[96:97], v[104:105], v[102:103]
	v_pk_mul_f32 v[102:103], v[172:173], v[98:99] op_sel:[1,1] op_sel_hi:[0,1]
	v_pk_fma_f32 v[104:105], v[172:173], v[98:99], v[102:103] op_sel_hi:[1,0,1] neg_lo:[0,0,1]
	v_pk_add_f32 v[102:103], v[198:199], v[202:203]
	v_pk_add_f32 v[98:99], v[194:195], v[196:197]
	s_nop 0
	v_pk_add_f32 v[106:107], v[98:99], v[102:103]
	v_pk_add_f32 v[98:99], v[98:99], v[102:103] neg_lo:[0,1] neg_hi:[0,1]
	v_pk_add_f32 v[120:121], v[106:107], v[116:117]
	v_pk_add_f32 v[106:107], v[106:107], v[116:117] neg_lo:[0,1] neg_hi:[0,1]
	v_pk_mul_f32 v[102:103], v[186:187], v[98:99] op_sel:[1,1] op_sel_hi:[0,1]
	v_pk_mul_f32 v[116:117], v[106:107], v[172:173] op_sel:[1,1] op_sel_hi:[1,0]
	s_nop 0
	v_pk_fma_f32 v[122:123], v[106:107], v[172:173], v[116:117] op_sel_hi:[0,1,1] neg_lo:[0,0,1]
	v_pk_fma_f32 v[106:107], v[186:187], v[98:99], v[102:103] op_sel_hi:[1,0,1] neg_lo:[0,0,1]
	s_nop 0
	v_pk_add_f32 v[98:99], v[110:111], v[114:115] neg_lo:[0,1] neg_hi:[0,1]
	s_nop 0
	v_pk_mul_f32 v[102:103], v[186:187], v[98:99] op_sel_hi:[0,1]
	v_pk_fma_f32 v[110:111], v[186:187], v[98:99], v[102:103] op_sel:[1,0,1] op_sel_hi:[1,1,0] neg_hi:[0,0,1]
	s_nop 0
	v_pk_add_f32 v[102:103], v[106:107], v[110:111] neg_lo:[0,1] neg_hi:[0,1]
	v_pk_add_f32 v[98:99], v[106:107], v[110:111]
	v_pk_mul_f32 v[106:107], v[172:173], v[102:103] op_sel:[1,1] op_sel_hi:[0,1]
	v_pk_fma_f32 v[110:111], v[172:173], v[102:103], v[106:107] op_sel_hi:[1,0,1] neg_lo:[0,0,1]
	v_pk_add_f32 v[106:107], v[174:175], v[176:177]
	v_pk_add_f32 v[102:103], v[192:193], v[190:191]
	s_nop 0
	v_pk_add_f32 v[114:115], v[102:103], v[106:107]
	v_pk_add_f32 v[102:103], v[102:103], v[106:107] neg_lo:[0,1] neg_hi:[0,1]
	s_nop 0
	v_pk_mul_f32 v[106:107], v[172:173], v[102:103] op_sel:[1,1] op_sel_hi:[0,1]
	v_pk_fma_f32 v[116:117], v[172:173], v[102:103], v[106:107] op_sel_hi:[1,0,1] neg_lo:[0,0,1]
	v_pk_mul_f32 v[106:107], v[172:173], v[128:129] op_sel:[1,1] op_sel_hi:[0,1]
	v_pk_fma_f32 v[174:175], v[172:173], v[128:129], v[106:107] op_sel_hi:[1,0,1] neg_lo:[0,0,1]
	v_pk_add_f32 v[102:103], v[204:205], v[224:225]
	ds_write2_b64 v132, v[124:125], v[126:127] offset1:2
	ds_write2_b64 v132, v[112:113], v[118:119] offset0:4 offset1:6
	ds_write2_b64 v132, v[100:101], v[108:109] offset0:8 offset1:10
	ds_write2_b64 v132, v[96:97], v[104:105] offset0:12 offset1:14
	ds_write2_b64 v132, v[120:121], v[122:123] offset0:16 offset1:18
	ds_write2_b64 v132, v[98:99], v[110:111] offset0:20 offset1:22
	ds_write2_b64 v132, v[114:115], v[116:117] offset0:24 offset1:26
	ds_write2_b64 v132, v[102:103], v[174:175] offset0:28 offset1:30
	s_waitcnt lgkmcnt(0)
	s_barrier
; template <bool LAT>
; __device__ __forceinline__ void hyconv_unit(const Frame& F, LAS f32x2v* X, const TwHalf tw, LAS bf16* OUT, const float* skip, bf16* MIX, int u) {
;     ...
;             for (int r = 0; r < 8; ++r) { const int e = 2 * (F.tid + 512 * r);
;                 const f32x2v a = X[PADI(e)], b = X[PADI(e + 1)]; const f32x4 k = kq[r];
;                 const f32x2v p = a + b, q = a - b; const f32x2v pk = (f32x2v){p.x * k.x - p.y * k.y, p.x * k.y + p.y * k.x}, qk = (f32x2v){q.x * k.z - q.y * k.w, q.x * k.w + q.y * k.z};
;                 X[PADI(e)] = pk + qk; X[PADI(e + 1)] = pk - qk; }
	ds_read_b128 v[96:99], v151
	s_waitcnt lgkmcnt(0)
	v_pk_add_f32 v[100:101], v[96:97], v[98:99]
	v_pk_add_f32 v[96:97], v[96:97], v[98:99] neg_lo:[0,1] neg_hi:[0,1]
	s_waitcnt vmcnt(7)
	v_pk_mul_f32 v[98:99], v[28:29], v[100:101] op_sel:[1,1] op_sel_hi:[0,1]
	v_pk_fma_f32 v[102:103], v[28:29], v[100:101], v[98:99] op_sel_hi:[1,0,1] neg_lo:[0,0,1]
	s_nop 0
	v_pk_mul_f32 v[28:29], v[30:31], v[96:97] op_sel:[1,1] op_sel_hi:[0,1]
	v_pk_fma_f32 v[98:99], v[30:31], v[96:97], v[28:29] op_sel_hi:[1,0,1] neg_lo:[0,0,1]
	s_nop 0
	v_pk_add_f32 v[28:29], v[102:103], v[98:99]
	v_pk_add_f32 v[30:31], v[102:103], v[98:99] neg_lo:[0,1] neg_hi:[0,1]
	ds_write_b128 v151, v[28:31]
	ds_read_b128 v[28:31], v152 offset:8192
	s_waitcnt lgkmcnt(0)
	v_pk_add_f32 v[96:97], v[28:29], v[30:31]
	v_pk_add_f32 v[28:29], v[28:29], v[30:31] neg_lo:[0,1] neg_hi:[0,1]
	s_waitcnt vmcnt(6)
	v_pk_mul_f32 v[30:31], v[24:25], v[96:97] op_sel:[1,1] op_sel_hi:[0,1]
	v_pk_fma_f32 v[98:99], v[24:25], v[96:97], v[30:31] op_sel_hi:[1,0,1] neg_lo:[0,0,1]
	s_nop 0
	v_pk_mul_f32 v[24:25], v[26:27], v[28:29] op_sel:[1,1] op_sel_hi:[0,1]
	v_pk_fma_f32 v[30:31], v[26:27], v[28:29], v[24:25] op_sel_hi:[1,0,1] neg_lo:[0,0,1]
	s_nop 0
	v_pk_add_f32 v[24:25], v[98:99], v[30:31]
	v_pk_add_f32 v[26:27], v[98:99], v[30:31] neg_lo:[0,1] neg_hi:[0,1]
	ds_write_b128 v152, v[24:27] offset:8192
	ds_read_b128 v[24:27], v153 offset:16384
	s_waitcnt lgkmcnt(0)
	v_pk_add_f32 v[28:29], v[24:25], v[26:27]
	v_pk_add_f32 v[24:25], v[24:25], v[26:27] neg_lo:[0,1] neg_hi:[0,1]
	s_waitcnt vmcnt(5)
	v_pk_mul_f32 v[26:27], v[20:21], v[28:29] op_sel:[1,1] op_sel_hi:[0,1]
	v_pk_fma_f32 v[30:31], v[20:21], v[28:29], v[26:27] op_sel_hi:[1,0,1] neg_lo:[0,0,1]
	s_nop 0
	v_pk_mul_f32 v[20:21], v[22:23], v[24:25] op_sel:[1,1] op_sel_hi:[0,1]
	v_pk_fma_f32 v[26:27], v[22:23], v[24:25], v[20:21] op_sel_hi:[1,0,1] neg_lo:[0,0,1]
	s_nop 0
	v_pk_add_f32 v[20:21], v[30:31], v[26:27]
	v_pk_add_f32 v[22:23], v[30:31], v[26:27] neg_lo:[0,1] neg_hi:[0,1]
	ds_write_b128 v153, v[20:23] offset:16384
	ds_read_b128 v[20:23], v154 offset:24576
	s_waitcnt lgkmcnt(0)
	v_pk_add_f32 v[24:25], v[20:21], v[22:23]
	v_pk_add_f32 v[20:21], v[20:21], v[22:23] neg_lo:[0,1] neg_hi:[0,1]
	s_waitcnt vmcnt(4)
	v_pk_mul_f32 v[22:23], v[16:17], v[24:25] op_sel:[1,1] op_sel_hi:[0,1]
	v_pk_fma_f32 v[26:27], v[16:17], v[24:25], v[22:23] op_sel_hi:[1,0,1] neg_lo:[0,0,1]
	s_nop 0
	v_pk_mul_f32 v[16:17], v[18:19], v[20:21] op_sel:[1,1] op_sel_hi:[0,1]
	v_pk_fma_f32 v[22:23], v[18:19], v[20:21], v[16:17] op_sel_hi:[1,0,1] neg_lo:[0,0,1]
	s_nop 0
	v_pk_add_f32 v[16:17], v[26:27], v[22:23]
	v_pk_add_f32 v[18:19], v[26:27], v[22:23] neg_lo:[0,1] neg_hi:[0,1]
	ds_write_b128 v154, v[16:19] offset:24576
	ds_read_b128 v[16:19], v155 offset:32768
	s_waitcnt lgkmcnt(0)
	v_pk_add_f32 v[20:21], v[16:17], v[18:19]
	v_pk_add_f32 v[16:17], v[16:17], v[18:19] neg_lo:[0,1] neg_hi:[0,1]
	s_waitcnt vmcnt(3)
	v_pk_mul_f32 v[18:19], v[12:13], v[20:21] op_sel:[1,1] op_sel_hi:[0,1]
	v_pk_fma_f32 v[22:23], v[12:13], v[20:21], v[18:19] op_sel_hi:[1,0,1] neg_lo:[0,0,1]
	s_nop 0
	v_pk_mul_f32 v[12:13], v[14:15], v[16:17] op_sel:[1,1] op_sel_hi:[0,1]
	v_pk_fma_f32 v[18:19], v[14:15], v[16:17], v[12:13] op_sel_hi:[1,0,1] neg_lo:[0,0,1]
	s_nop 0
	v_pk_add_f32 v[12:13], v[22:23], v[18:19]
	v_pk_add_f32 v[14:15], v[22:23], v[18:19] neg_lo:[0,1] neg_hi:[0,1]
	ds_write_b128 v155, v[12:15] offset:32768
	ds_read_b128 v[12:15], v156 offset:40960
	s_waitcnt lgkmcnt(0)
	v_pk_add_f32 v[16:17], v[12:13], v[14:15]
	v_pk_add_f32 v[12:13], v[12:13], v[14:15] neg_lo:[0,1] neg_hi:[0,1]
	s_waitcnt vmcnt(2)
	v_pk_mul_f32 v[14:15], v[8:9], v[16:17] op_sel:[1,1] op_sel_hi:[0,1]
	v_pk_fma_f32 v[18:19], v[8:9], v[16:17], v[14:15] op_sel_hi:[1,0,1] neg_lo:[0,0,1]
	s_nop 0
	v_pk_mul_f32 v[8:9], v[10:11], v[12:13] op_sel:[1,1] op_sel_hi:[0,1]
	v_pk_fma_f32 v[14:15], v[10:11], v[12:13], v[8:9] op_sel_hi:[1,0,1] neg_lo:[0,0,1]
	s_nop 0
	v_pk_add_f32 v[8:9], v[18:19], v[14:15]
	v_pk_add_f32 v[10:11], v[18:19], v[14:15] neg_lo:[0,1] neg_hi:[0,1]
	ds_write_b128 v156, v[8:11] offset:40960
	ds_read_b128 v[8:11], v157 offset:49152
	s_waitcnt lgkmcnt(0)
	v_pk_add_f32 v[12:13], v[8:9], v[10:11]
	v_pk_add_f32 v[8:9], v[8:9], v[10:11] neg_lo:[0,1] neg_hi:[0,1]
	s_waitcnt vmcnt(1)
	v_pk_mul_f32 v[10:11], v[4:5], v[12:13] op_sel:[1,1] op_sel_hi:[0,1]
	v_pk_fma_f32 v[14:15], v[4:5], v[12:13], v[10:11] op_sel_hi:[1,0,1] neg_lo:[0,0,1]
	s_nop 0
	v_pk_mul_f32 v[4:5], v[6:7], v[8:9] op_sel:[1,1] op_sel_hi:[0,1]
	v_pk_fma_f32 v[10:11], v[6:7], v[8:9], v[4:5] op_sel_hi:[1,0,1] neg_lo:[0,0,1]
	s_nop 0
	v_pk_add_f32 v[4:5], v[14:15], v[10:11]
	v_pk_add_f32 v[6:7], v[14:15], v[10:11] neg_lo:[0,1] neg_hi:[0,1]
	ds_write_b128 v157, v[4:7] offset:49152
	ds_read_b128 v[4:7], v158 offset:57344
	s_waitcnt lgkmcnt(0)
	v_pk_add_f32 v[8:9], v[4:5], v[6:7]
	v_pk_add_f32 v[4:5], v[4:5], v[6:7] neg_lo:[0,1] neg_hi:[0,1]
	s_waitcnt vmcnt(0)
	v_pk_mul_f32 v[6:7], v[0:1], v[8:9] op_sel:[1,1] op_sel_hi:[0,1]
	v_pk_fma_f32 v[10:11], v[0:1], v[8:9], v[6:7] op_sel_hi:[1,0,1] neg_lo:[0,0,1]
	s_nop 0
	v_pk_mul_f32 v[0:1], v[2:3], v[4:5] op_sel:[1,1] op_sel_hi:[0,1]
	v_pk_fma_f32 v[6:7], v[2:3], v[4:5], v[0:1] op_sel_hi:[1,0,1] neg_lo:[0,0,1]
	s_nop 0
	v_pk_add_f32 v[0:1], v[10:11], v[6:7]
	v_pk_add_f32 v[2:3], v[10:11], v[6:7] neg_lo:[0,1] neg_hi:[0,1]
	ds_write_b128 v158, v[0:3] offset:57344
	s_waitcnt lgkmcnt(0)
	s_barrier
; template <int R, class XT, class TWT>
; __device__ __forceinline__ void dit_task(XT X, TWT tw, int s, int task) {
;     const int lgM = 13 - s, lgq = lgM - R, q = 1 << lgq;
;     const int j0 = task & (q - 1), blk = task >> lgq, base = (blk << lgM) + j0;
;     const int pb = PADI(base), qp = (q >= 32) ? q + (q >> 4) : q;
;     f32x2v v[1 << R];
; #pragma unroll
;     for (int k = 0; k < (1 << R); ++k) v[k] = X[pb + k * qp];
; #pragma unroll
;     for (int r = R - 1; r >= 0; --r) {
;         const int pb = R - 1 - r;
; #pragma unroll
;         for (int k = 0; k < (1 << R); ++k) if (!((k >> pb) & 1)) {
;             const int klo = k & ((1 << pb) - 1);
;             const f32x2v w = tw[(j0 + (klo << lgq)) << (s + r)];
;             const f32x2v a = v[k], qv = v[k + (1 << pb)]; const f32x2v b = (f32x2v){qv.x * w.x + qv.y * w.y, qv.y * w.x - qv.x * w.y};
;             v[k] = a + b; v[k + (1 << pb)] = a - b;
;         }
;     }
; #pragma unroll
;     for (int k = 0; k < (1 << R); ++k) X[pb + k * qp] = v[k];
	ds_read2_b64 v[0:3], v132 offset1:2
	ds_read2_b64 v[4:7], v132 offset0:4 offset1:6
	ds_read2_b64 v[8:11], v132 offset0:8 offset1:10
	ds_read2_b64 v[12:15], v132 offset0:12 offset1:14
	ds_read2_b64 v[16:19], v132 offset0:16 offset1:18
	ds_read2_b64 v[20:23], v132 offset0:20 offset1:22
	ds_read2_b64 v[24:27], v132 offset0:24 offset1:26
	ds_read2_b64 v[28:31], v132 offset0:28 offset1:30
	ds_read_b64 v[100:101], v95
	ds_read_b64 v[102:103], v170
	ds_read_b64 v[104:105], v169
	ds_read2st64_b64 v[96:99], v165 offset1:16
	ds_read_b64 v[106:107], v168
	ds_read_b64 v[108:109], v150
	ds_read_b64 v[110:111], v166
	ds_read_b64 v[112:113], v167
	s_waitcnt lgkmcnt(7)
	v_xor_b32_e32 v95, 0x80000000, v100
	v_cndmask_b32_e64 v115, v95, v101, s[42:43]
	v_cndmask_b32_e64 v114, v101, v100, s[42:43]
	v_mov_b32_e32 v100, v115
	v_pk_mul_f32 v[116:117], v[2:3], v[100:101] op_sel_hi:[1,0]
	s_nop 0
	v_pk_fma_f32 v[118:119], v[2:3], v[114:115], v[116:117] op_sel:[0,0,1] op_sel_hi:[1,0,0] neg_hi:[0,0,1]
	v_pk_mul_f32 v[116:117], v[6:7], v[100:101] op_sel_hi:[1,0]
	s_nop 0
	v_pk_fma_f32 v[120:121], v[6:7], v[114:115], v[116:117] op_sel:[0,0,1] op_sel_hi:[1,0,0] neg_hi:[0,0,1]
	v_pk_add_f32 v[2:3], v[0:1], v[118:119]
	v_pk_add_f32 v[6:7], v[4:5], v[120:121]
	v_pk_add_f32 v[4:5], v[4:5], v[120:121] neg_lo:[0,1] neg_hi:[0,1]
	s_waitcnt lgkmcnt(6)
	v_pk_mul_f32 v[116:117], v[102:103], v[6:7] op_sel:[1,0]
	v_pk_add_f32 v[0:1], v[0:1], v[118:119] neg_lo:[0,1] neg_hi:[0,1]
	v_pk_fma_f32 v[122:123], v[102:103], v[6:7], v[116:117] op_sel:[0,0,1] op_sel_hi:[0,1,0] neg_hi:[0,0,1]
	v_pk_mul_f32 v[116:117], v[10:11], v[100:101] op_sel_hi:[1,0]
	s_nop 0
	v_pk_fma_f32 v[124:125], v[10:11], v[114:115], v[116:117] op_sel:[0,0,1] op_sel_hi:[1,0,0] neg_hi:[0,0,1]
	v_pk_mul_f32 v[116:117], v[14:15], v[100:101] op_sel_hi:[1,0]
	s_nop 0
	v_pk_fma_f32 v[126:127], v[14:15], v[114:115], v[116:117] op_sel:[0,0,1] op_sel_hi:[1,0,0] neg_hi:[0,0,1]
	v_pk_add_f32 v[10:11], v[8:9], v[124:125]
	v_pk_add_f32 v[14:15], v[12:13], v[126:127]
	v_pk_add_f32 v[12:13], v[12:13], v[126:127] neg_lo:[0,1] neg_hi:[0,1]
	v_pk_mul_f32 v[116:117], v[102:103], v[14:15] op_sel:[1,0]
	v_pk_add_f32 v[8:9], v[8:9], v[124:125] neg_lo:[0,1] neg_hi:[0,1]
	v_pk_fma_f32 v[128:129], v[102:103], v[14:15], v[116:117] op_sel:[0,0,1] op_sel_hi:[0,1,0] neg_hi:[0,0,1]
	s_nop 0
	v_pk_add_f32 v[14:15], v[10:11], v[128:129]
	v_pk_add_f32 v[10:11], v[10:11], v[128:129] neg_lo:[0,1] neg_hi:[0,1]
	s_waitcnt lgkmcnt(3)
	v_pk_mul_f32 v[116:117], v[106:107], v[14:15] op_sel:[1,0]
	v_pk_add_f32 v[6:7], v[2:3], v[122:123]
	v_pk_fma_f32 v[172:173], v[106:107], v[14:15], v[116:117] op_sel:[0,0,1] op_sel_hi:[1,1,0]
	v_pk_fma_f32 v[14:15], v[106:107], v[14:15], v[116:117] op_sel:[0,0,1] op_sel_hi:[0,1,0] neg_lo:[0,0,1] neg_hi:[0,0,1]
	v_pk_mul_f32 v[116:117], v[18:19], v[100:101] op_sel_hi:[1,0]
	v_pk_add_f32 v[2:3], v[2:3], v[122:123] neg_lo:[0,1] neg_hi:[0,1]
	v_pk_fma_f32 v[174:175], v[18:19], v[114:115], v[116:117] op_sel:[0,0,1] op_sel_hi:[1,0,0] neg_hi:[0,0,1]
	v_pk_mul_f32 v[116:117], v[22:23], v[100:101] op_sel_hi:[1,0]
	s_nop 0
	v_pk_fma_f32 v[176:177], v[22:23], v[114:115], v[116:117] op_sel:[0,0,1] op_sel_hi:[1,0,0] neg_hi:[0,0,1]
	v_pk_add_f32 v[18:19], v[16:17], v[174:175]
	v_pk_add_f32 v[22:23], v[20:21], v[176:177]
	v_pk_add_f32 v[20:21], v[20:21], v[176:177] neg_lo:[0,1] neg_hi:[0,1]
	v_pk_mul_f32 v[116:117], v[102:103], v[22:23] op_sel:[1,0]
	v_pk_add_f32 v[16:17], v[16:17], v[174:175] neg_lo:[0,1] neg_hi:[0,1]
	v_pk_fma_f32 v[178:179], v[102:103], v[22:23], v[116:117] op_sel:[0,0,1] op_sel_hi:[0,1,0] neg_hi:[0,0,1]
	v_pk_mul_f32 v[116:117], v[26:27], v[100:101] op_sel_hi:[1,0]
	v_pk_mul_f32 v[100:101], v[30:31], v[100:101] op_sel_hi:[1,0]
	v_pk_fma_f32 v[182:183], v[26:27], v[114:115], v[116:117] op_sel:[0,0,1] op_sel_hi:[1,0,0] neg_hi:[0,0,1]
	v_pk_fma_f32 v[116:117], v[30:31], v[114:115], v[100:101] op_sel:[0,0,1] op_sel_hi:[1,0,0] neg_hi:[0,0,1]
	s_nop 0
	v_pk_add_f32 v[30:31], v[28:29], v[116:117]
	v_pk_add_f32 v[26:27], v[24:25], v[182:183]
	v_pk_mul_f32 v[100:101], v[102:103], v[30:31] op_sel:[1,0]
	s_nop 0
	v_pk_fma_f32 v[114:115], v[102:103], v[30:31], v[100:101] op_sel:[0,0,1] op_sel_hi:[0,1,0] neg_hi:[0,0,1]
	s_nop 0
	v_pk_add_f32 v[30:31], v[26:27], v[114:115]
	v_pk_add_f32 v[22:23], v[18:19], v[178:179]
	v_pk_mul_f32 v[100:101], v[106:107], v[30:31] op_sel:[1,0]
	v_pk_add_f32 v[28:29], v[28:29], v[116:117] neg_lo:[0,1] neg_hi:[0,1]
	v_pk_fma_f32 v[184:185], v[106:107], v[30:31], v[100:101] op_sel:[0,0,1] op_sel_hi:[0,1,0] neg_hi:[0,0,1]
	s_nop 0
	v_pk_add_f32 v[30:31], v[22:23], v[184:185]
	v_pk_add_f32 v[24:25], v[24:25], v[182:183] neg_lo:[0,1] neg_hi:[0,1]
	v_pk_mul_f32 v[100:101], v[96:97], v[30:31] op_sel:[1,0]
	v_pk_add_f32 v[26:27], v[26:27], v[114:115] neg_lo:[0,1] neg_hi:[0,1]
	v_pk_fma_f32 v[186:187], v[96:97], v[30:31], v[100:101] op_sel:[0,0,1] op_sel_hi:[1,1,0]
	v_pk_fma_f32 v[30:31], v[96:97], v[30:31], v[100:101] op_sel:[0,0,1] op_sel_hi:[0,1,0] neg_lo:[0,0,1] neg_hi:[0,0,1]
	v_pk_mul_f32 v[100:101], v[102:103], v[4:5] op_sel_hi:[0,1]
	v_pk_fma_f32 v[118:119], v[102:103], v[4:5], v[100:101] op_sel:[1,0,1] op_sel_hi:[1,1,0] neg_lo:[0,0,1]
	v_pk_mul_f32 v[100:101], v[102:103], v[12:13] op_sel_hi:[0,1]
	v_pk_fma_f32 v[120:121], v[102:103], v[12:13], v[100:101] op_sel:[1,0,1] op_sel_hi:[1,1,0] neg_lo:[0,0,1]
	s_nop 0
	v_pk_add_f32 v[12:13], v[8:9], v[120:121]
	v_pk_add_f32 v[4:5], v[0:1], v[118:119]
	v_pk_mul_f32 v[100:101], v[104:105], v[12:13] op_sel:[1,0]
	v_pk_add_f32 v[18:19], v[18:19], v[178:179] neg_lo:[0,1] neg_hi:[0,1]
	v_pk_fma_f32 v[124:125], v[104:105], v[12:13], v[100:101] op_sel:[0,0,1] op_sel_hi:[0,1,0] neg_hi:[0,0,1]
	v_pk_mul_f32 v[100:101], v[102:103], v[20:21] op_sel_hi:[0,1]
	v_pk_fma_f32 v[126:127], v[102:103], v[20:21], v[100:101] op_sel:[1,0,1] op_sel_hi:[1,1,0] neg_lo:[0,0,1]
	v_pk_mul_f32 v[100:101], v[102:103], v[28:29] op_sel_hi:[0,1]
	v_pk_fma_f32 v[116:117], v[102:103], v[28:29], v[100:101] op_sel:[1,0,1] op_sel_hi:[1,1,0] neg_lo:[0,0,1]
	s_nop 0
	v_pk_add_f32 v[28:29], v[24:25], v[116:117]
	v_pk_add_f32 v[20:21], v[16:17], v[126:127]
	v_pk_mul_f32 v[100:101], v[104:105], v[28:29] op_sel:[1,0]
	s_nop 0
	v_pk_fma_f32 v[102:103], v[104:105], v[28:29], v[100:101] op_sel:[0,0,1] op_sel_hi:[0,1,0] neg_hi:[0,0,1]
	s_nop 0
	v_pk_add_f32 v[28:29], v[20:21], v[102:103]
	v_pk_add_f32 v[12:13], v[4:5], v[124:125]
	s_waitcnt lgkmcnt(1)
; template <int R, class XT, class TWT>
; __device__ __forceinline__ void dit_task(XT X, TWT tw, int s, int task) {
;     const int lgM = 13 - s, lgq = lgM - R, q = 1 << lgq;
;     const int j0 = task & (q - 1), blk = task >> lgq, base = (blk << lgM) + j0;
;     const int pb = PADI(base), qp = (q >= 32) ? q + (q >> 4) : q;
;     f32x2v v[1 << R];
; #pragma unroll
;     for (int k = 0; k < (1 << R); ++k) v[k] = X[pb + k * qp];
; #pragma unroll
;     for (int r = R - 1; r >= 0; --r) {
;         const int pb = R - 1 - r;
; #pragma unroll
;         for (int k = 0; k < (1 << R); ++k) if (!((k >> pb) & 1)) {
;             const int klo = k & ((1 << pb) - 1);
;             const f32x2v w = tw[(j0 + (klo << lgq)) << (s + r)];
;             const f32x2v a = v[k], qv = v[k + (1 << pb)]; const f32x2v b = (f32x2v){qv.x * w.x + qv.y * w.y, qv.y * w.x - qv.x * w.y};
;             v[k] = a + b; v[k + (1 << pb)] = a - b;
;         }
;     }
; #pragma unroll
;     for (int k = 0; k < (1 << R); ++k) X[pb + k * qp] = v[k];
	v_pk_mul_f32 v[100:101], v[110:111], v[28:29] op_sel:[1,0]
	v_pk_add_f32 v[8:9], v[8:9], v[120:121] neg_lo:[0,1] neg_hi:[0,1]
	v_pk_fma_f32 v[104:105], v[110:111], v[28:29], v[100:101] op_sel:[0,0,1] op_sel_hi:[0,1,0] neg_hi:[0,0,1]
	v_pk_mul_f32 v[100:101], v[106:107], v[10:11] op_sel_hi:[0,1]
	v_pk_add_f32 v[28:29], v[12:13], v[104:105]
	v_pk_add_f32 v[12:13], v[12:13], v[104:105] neg_lo:[0,1] neg_hi:[0,1]
	v_pk_fma_f32 v[104:105], v[106:107], v[10:11], v[100:101] op_sel:[1,0,1] op_sel_hi:[1,1,0] neg_lo:[0,0,1]
	v_pk_mul_f32 v[100:101], v[106:107], v[26:27] op_sel_hi:[0,1]
	v_pk_fma_f32 v[114:115], v[106:107], v[26:27], v[100:101] op_sel:[1,0,1] op_sel_hi:[1,1,0] neg_lo:[0,0,1]
	s_nop 0
	v_pk_add_f32 v[26:27], v[18:19], v[114:115]
	v_pk_add_f32 v[10:11], v[2:3], v[104:105]
	v_pk_mul_f32 v[100:101], v[98:99], v[26:27] op_sel:[1,0]
	v_pk_add_f32 v[24:25], v[24:25], v[116:117] neg_lo:[0,1] neg_hi:[0,1]
	v_pk_fma_f32 v[106:107], v[98:99], v[26:27], v[100:101] op_sel:[0,0,1] op_sel_hi:[0,1,0] neg_hi:[0,0,1]
	v_pk_mul_f32 v[100:101], v[108:109], v[8:9] op_sel_hi:[0,1]
	v_pk_add_f32 v[26:27], v[10:11], v[106:107]
	v_pk_add_f32 v[10:11], v[10:11], v[106:107] neg_lo:[0,1] neg_hi:[0,1]
	v_pk_fma_f32 v[106:107], v[108:109], v[8:9], v[100:101] op_sel:[1,0,1] op_sel_hi:[1,1,0] neg_lo:[0,0,1]
	v_pk_mul_f32 v[100:101], v[108:109], v[24:25] op_sel_hi:[0,1]
	v_pk_fma_f32 v[116:117], v[108:109], v[24:25], v[100:101] op_sel:[1,0,1] op_sel_hi:[1,1,0] neg_lo:[0,0,1]
	v_pk_add_f32 v[16:17], v[16:17], v[126:127] neg_lo:[0,1] neg_hi:[0,1]
	s_nop 0
	v_pk_add_f32 v[24:25], v[16:17], v[116:117]
	v_pk_add_f32 v[0:1], v[0:1], v[118:119] neg_lo:[0,1] neg_hi:[0,1]
	s_waitcnt lgkmcnt(0)
	v_pk_mul_f32 v[100:101], v[112:113], v[24:25] op_sel:[1,0]
	s_nop 0
	v_pk_fma_f32 v[108:109], v[112:113], v[24:25], v[100:101] op_sel:[0,0,1] op_sel_hi:[0,1,0] neg_hi:[0,0,1]
	v_pk_add_f32 v[22:23], v[22:23], v[184:185] neg_lo:[0,1] neg_hi:[0,1]
	v_pk_add_f32 v[8:9], v[0:1], v[106:107]
	v_pk_mul_f32 v[100:101], v[96:97], v[22:23] op_sel_hi:[0,1]
	v_pk_add_f32 v[20:21], v[20:21], v[102:103] neg_lo:[0,1] neg_hi:[0,1]
	v_pk_add_f32 v[24:25], v[8:9], v[108:109]
	v_pk_add_f32 v[8:9], v[8:9], v[108:109] neg_lo:[0,1] neg_hi:[0,1]
	v_pk_fma_f32 v[108:109], v[96:97], v[22:23], v[100:101] op_sel:[1,0,1] op_sel_hi:[1,1,0] neg_lo:[0,0,1] neg_hi:[0,0,1]
	v_pk_fma_f32 v[22:23], v[96:97], v[22:23], v[100:101] op_sel:[1,0,1] op_sel_hi:[1,1,0]
	v_pk_mul_f32 v[96:97], v[110:111], v[20:21] op_sel_hi:[0,1]
	v_pk_fma_f32 v[100:101], v[110:111], v[20:21], v[96:97] op_sel:[1,0,1] op_sel_hi:[1,1,0] neg_lo:[0,0,1]
	v_pk_add_f32 v[18:19], v[18:19], v[114:115] neg_lo:[0,1] neg_hi:[0,1]
	v_pk_add_f32 v[4:5], v[4:5], v[124:125] neg_lo:[0,1] neg_hi:[0,1]
	v_pk_mul_f32 v[96:97], v[98:99], v[18:19] op_sel_hi:[0,1]
	v_pk_add_f32 v[16:17], v[16:17], v[116:117] neg_lo:[0,1] neg_hi:[0,1]
	v_mov_b32_e32 v173, v15
	v_pk_add_f32 v[20:21], v[4:5], v[100:101]
	v_pk_add_f32 v[4:5], v[4:5], v[100:101] neg_lo:[0,1] neg_hi:[0,1]
	v_pk_fma_f32 v[100:101], v[98:99], v[18:19], v[96:97] op_sel:[1,0,1] op_sel_hi:[1,1,0] neg_lo:[0,0,1] neg_hi:[0,0,1]
	v_pk_fma_f32 v[18:19], v[98:99], v[18:19], v[96:97] op_sel:[1,0,1] op_sel_hi:[1,1,0]
	v_pk_mul_f32 v[96:97], v[112:113], v[16:17] op_sel_hi:[0,1]
	v_pk_add_f32 v[14:15], v[6:7], v[172:173]
	v_mov_b32_e32 v187, v31
	v_pk_fma_f32 v[98:99], v[112:113], v[16:17], v[96:97] op_sel:[1,0,1] op_sel_hi:[1,1,0] neg_lo:[0,0,1]
	v_pk_add_f32 v[30:31], v[14:15], v[186:187]
	v_pk_add_f32 v[6:7], v[6:7], v[172:173] neg_lo:[0,1] neg_hi:[0,1]
	v_mov_b32_e32 v109, v23
	v_pk_add_f32 v[2:3], v[2:3], v[104:105] neg_lo:[0,1] neg_hi:[0,1]
	v_mov_b32_e32 v101, v19
	v_pk_add_f32 v[0:1], v[0:1], v[106:107] neg_lo:[0,1] neg_hi:[0,1]
	v_pk_add_f32 v[14:15], v[14:15], v[186:187] neg_lo:[0,1] neg_hi:[0,1]
	v_pk_add_f32 v[22:23], v[6:7], v[108:109]
	v_pk_add_f32 v[6:7], v[6:7], v[108:109] neg_lo:[0,1] neg_hi:[0,1]
	v_pk_add_f32 v[18:19], v[2:3], v[100:101]
	v_pk_add_f32 v[2:3], v[2:3], v[100:101] neg_lo:[0,1] neg_hi:[0,1]
	v_pk_add_f32 v[16:17], v[0:1], v[98:99]
	v_pk_add_f32 v[0:1], v[0:1], v[98:99] neg_lo:[0,1] neg_hi:[0,1]
	ds_write2_b64 v132, v[30:31], v[28:29] offset1:2
	ds_write2_b64 v132, v[26:27], v[24:25] offset0:4 offset1:6
	ds_write2_b64 v132, v[22:23], v[20:21] offset0:8 offset1:10
	ds_write2_b64 v132, v[18:19], v[16:17] offset0:12 offset1:14
	ds_write2_b64 v132, v[14:15], v[12:13] offset0:16 offset1:18
	ds_write2_b64 v132, v[10:11], v[8:9] offset0:20 offset1:22
	ds_write2_b64 v132, v[6:7], v[4:5] offset0:24 offset1:26
	ds_write2_b64 v132, v[2:3], v[0:1] offset0:28 offset1:30
	s_waitcnt lgkmcnt(0)
	s_barrier
; template <int R, class XT, class TWT>
; __device__ __forceinline__ void dit_task(XT X, TWT tw, int s, int task) {
;     const int lgM = 13 - s, lgq = lgM - R, q = 1 << lgq;
;     const int j0 = task & (q - 1), blk = task >> lgq, base = (blk << lgM) + j0;
;     const int pb = PADI(base), qp = (q >= 32) ? q + (q >> 4) : q;
;     f32x2v v[1 << R];
; #pragma unroll
;     for (int k = 0; k < (1 << R); ++k) v[k] = X[pb + k * qp];
; #pragma unroll
;     for (int r = R - 1; r >= 0; --r) {
;         const int pb = R - 1 - r;
; #pragma unroll
;         for (int k = 0; k < (1 << R); ++k) if (!((k >> pb) & 1)) {
;             const int klo = k & ((1 << pb) - 1);
;             const f32x2v w = tw[(j0 + (klo << lgq)) << (s + r)];
;             const f32x2v a = v[k], qv = v[k + (1 << pb)]; const f32x2v b = (f32x2v){qv.x * w.x + qv.y * w.y, qv.y * w.x - qv.x * w.y};
;             v[k] = a + b; v[k + (1 << pb)] = a - b;
;         }
;     }
; #pragma unroll
;     for (int k = 0; k < (1 << R); ++k) X[pb + k * qp] = v[k];
	ds_read2_b64 v[0:3], v130 offset1:34
	ds_read2_b64 v[4:7], v130 offset0:68 offset1:102
	ds_read2_b64 v[8:11], v130 offset0:136 offset1:170
	ds_read2_b64 v[12:15], v130 offset0:204 offset1:238
	ds_read2_b64 v[16:19], v94 offset0:16 offset1:50
	ds_read2_b64 v[20:23], v94 offset0:84 offset1:118
	ds_read2_b64 v[24:27], v94 offset0:152 offset1:186
	ds_read2_b64 v[28:31], v94 offset0:220 offset1:254
	ds_read_b64 v[100:101], v131
	ds_read_b64 v[102:103], v164
	ds_read_b64 v[104:105], v162
	ds_read_b64 v[106:107], v163
	ds_read2st64_b64 v[96:99], v159 offset1:16
	ds_read_b64 v[108:109], v133
	ds_read_b64 v[110:111], v160
	ds_read_b64 v[112:113], v161
	s_waitcnt lgkmcnt(7)
	v_xor_b32_e32 v95, 0x80000000, v100
	v_cndmask_b32_e64 v115, v95, v101, s[44:45]
	v_cndmask_b32_e64 v114, v101, v100, s[44:45]
	v_mov_b32_e32 v100, v115
	v_pk_mul_f32 v[116:117], v[2:3], v[100:101] op_sel_hi:[1,0]
	s_nop 0
	v_pk_fma_f32 v[118:119], v[2:3], v[114:115], v[116:117] op_sel:[0,0,1] op_sel_hi:[1,0,0] neg_hi:[0,0,1]
	v_pk_mul_f32 v[116:117], v[6:7], v[100:101] op_sel_hi:[1,0]
	s_nop 0
	v_pk_fma_f32 v[120:121], v[6:7], v[114:115], v[116:117] op_sel:[0,0,1] op_sel_hi:[1,0,0] neg_hi:[0,0,1]
	v_pk_add_f32 v[2:3], v[0:1], v[118:119]
	v_pk_add_f32 v[6:7], v[4:5], v[120:121]
	v_pk_add_f32 v[4:5], v[4:5], v[120:121] neg_lo:[0,1] neg_hi:[0,1]
	s_waitcnt lgkmcnt(6)
	v_pk_mul_f32 v[116:117], v[102:103], v[6:7] op_sel:[1,0]
	v_pk_add_f32 v[0:1], v[0:1], v[118:119] neg_lo:[0,1] neg_hi:[0,1]
	v_pk_fma_f32 v[122:123], v[102:103], v[6:7], v[116:117] op_sel:[0,0,1] op_sel_hi:[0,1,0] neg_hi:[0,0,1]
	v_pk_mul_f32 v[116:117], v[10:11], v[100:101] op_sel_hi:[1,0]
	s_nop 0
	v_pk_fma_f32 v[124:125], v[10:11], v[114:115], v[116:117] op_sel:[0,0,1] op_sel_hi:[1,0,0] neg_hi:[0,0,1]
	v_pk_mul_f32 v[116:117], v[14:15], v[100:101] op_sel_hi:[1,0]
	s_nop 0
	v_pk_fma_f32 v[126:127], v[14:15], v[114:115], v[116:117] op_sel:[0,0,1] op_sel_hi:[1,0,0] neg_hi:[0,0,1]
	v_pk_add_f32 v[10:11], v[8:9], v[124:125]
	v_pk_add_f32 v[14:15], v[12:13], v[126:127]
	v_pk_add_f32 v[12:13], v[12:13], v[126:127] neg_lo:[0,1] neg_hi:[0,1]
	v_pk_mul_f32 v[116:117], v[102:103], v[14:15] op_sel:[1,0]
	v_pk_add_f32 v[8:9], v[8:9], v[124:125] neg_lo:[0,1] neg_hi:[0,1]
	v_pk_fma_f32 v[128:129], v[102:103], v[14:15], v[116:117] op_sel:[0,0,1] op_sel_hi:[0,1,0] neg_hi:[0,0,1]
	s_nop 0
	v_pk_add_f32 v[14:15], v[10:11], v[128:129]
	v_pk_add_f32 v[10:11], v[10:11], v[128:129] neg_lo:[0,1] neg_hi:[0,1]
	s_waitcnt lgkmcnt(5)
	v_pk_mul_f32 v[116:117], v[104:105], v[14:15] op_sel:[1,0]
	v_pk_add_f32 v[6:7], v[2:3], v[122:123]
	v_pk_fma_f32 v[172:173], v[104:105], v[14:15], v[116:117] op_sel:[0,0,1] op_sel_hi:[1,1,0]
	v_pk_fma_f32 v[14:15], v[104:105], v[14:15], v[116:117] op_sel:[0,0,1] op_sel_hi:[0,1,0] neg_lo:[0,0,1] neg_hi:[0,0,1]
	v_pk_mul_f32 v[116:117], v[18:19], v[100:101] op_sel_hi:[1,0]
	v_pk_add_f32 v[2:3], v[2:3], v[122:123] neg_lo:[0,1] neg_hi:[0,1]
	v_pk_fma_f32 v[174:175], v[18:19], v[114:115], v[116:117] op_sel:[0,0,1] op_sel_hi:[1,0,0] neg_hi:[0,0,1]
	v_pk_mul_f32 v[116:117], v[22:23], v[100:101] op_sel_hi:[1,0]
	s_nop 0
	v_pk_fma_f32 v[176:177], v[22:23], v[114:115], v[116:117] op_sel:[0,0,1] op_sel_hi:[1,0,0] neg_hi:[0,0,1]
	v_pk_add_f32 v[18:19], v[16:17], v[174:175]
	v_pk_add_f32 v[22:23], v[20:21], v[176:177]
	v_pk_add_f32 v[20:21], v[20:21], v[176:177] neg_lo:[0,1] neg_hi:[0,1]
	v_pk_mul_f32 v[116:117], v[102:103], v[22:23] op_sel:[1,0]
	v_pk_add_f32 v[16:17], v[16:17], v[174:175] neg_lo:[0,1] neg_hi:[0,1]
	v_pk_fma_f32 v[178:179], v[102:103], v[22:23], v[116:117] op_sel:[0,0,1] op_sel_hi:[0,1,0] neg_hi:[0,0,1]
	v_pk_mul_f32 v[116:117], v[26:27], v[100:101] op_sel_hi:[1,0]
	v_pk_mul_f32 v[100:101], v[30:31], v[100:101] op_sel_hi:[1,0]
	v_pk_fma_f32 v[182:183], v[26:27], v[114:115], v[116:117] op_sel:[0,0,1] op_sel_hi:[1,0,0] neg_hi:[0,0,1]
	v_pk_fma_f32 v[116:117], v[30:31], v[114:115], v[100:101] op_sel:[0,0,1] op_sel_hi:[1,0,0] neg_hi:[0,0,1]
	s_nop 0
	v_pk_add_f32 v[30:31], v[28:29], v[116:117]
	v_pk_add_f32 v[26:27], v[24:25], v[182:183]
	v_pk_mul_f32 v[100:101], v[102:103], v[30:31] op_sel:[1,0]
	s_nop 0
	v_pk_fma_f32 v[114:115], v[102:103], v[30:31], v[100:101] op_sel:[0,0,1] op_sel_hi:[0,1,0] neg_hi:[0,0,1]
	s_nop 0
	v_pk_add_f32 v[30:31], v[26:27], v[114:115]
	v_pk_add_f32 v[22:23], v[18:19], v[178:179]
	v_pk_mul_f32 v[100:101], v[104:105], v[30:31] op_sel:[1,0]
	v_pk_add_f32 v[28:29], v[28:29], v[116:117] neg_lo:[0,1] neg_hi:[0,1]
	v_pk_fma_f32 v[184:185], v[104:105], v[30:31], v[100:101] op_sel:[0,0,1] op_sel_hi:[0,1,0] neg_hi:[0,0,1]
	s_nop 0
	v_pk_add_f32 v[30:31], v[22:23], v[184:185]
	v_pk_add_f32 v[24:25], v[24:25], v[182:183] neg_lo:[0,1] neg_hi:[0,1]
	s_waitcnt lgkmcnt(3)
	v_pk_mul_f32 v[100:101], v[96:97], v[30:31] op_sel:[1,0]
	v_pk_add_f32 v[26:27], v[26:27], v[114:115] neg_lo:[0,1] neg_hi:[0,1]
	v_pk_fma_f32 v[186:187], v[96:97], v[30:31], v[100:101] op_sel:[0,0,1] op_sel_hi:[1,1,0]
	v_pk_fma_f32 v[30:31], v[96:97], v[30:31], v[100:101] op_sel:[0,0,1] op_sel_hi:[0,1,0] neg_lo:[0,0,1] neg_hi:[0,0,1]
	v_pk_mul_f32 v[100:101], v[102:103], v[4:5] op_sel_hi:[0,1]
	v_pk_fma_f32 v[118:119], v[102:103], v[4:5], v[100:101] op_sel:[1,0,1] op_sel_hi:[1,1,0] neg_lo:[0,0,1]
	v_pk_mul_f32 v[100:101], v[102:103], v[12:13] op_sel_hi:[0,1]
	v_pk_fma_f32 v[120:121], v[102:103], v[12:13], v[100:101] op_sel:[1,0,1] op_sel_hi:[1,1,0] neg_lo:[0,0,1]
	s_nop 0
	v_pk_add_f32 v[12:13], v[8:9], v[120:121]
	v_pk_add_f32 v[4:5], v[0:1], v[118:119]
	v_pk_mul_f32 v[100:101], v[106:107], v[12:13] op_sel:[1,0]
	v_pk_add_f32 v[18:19], v[18:19], v[178:179] neg_lo:[0,1] neg_hi:[0,1]
	v_pk_fma_f32 v[124:125], v[106:107], v[12:13], v[100:101] op_sel:[0,0,1] op_sel_hi:[0,1,0] neg_hi:[0,0,1]
	v_pk_mul_f32 v[100:101], v[102:103], v[20:21] op_sel_hi:[0,1]
	v_pk_fma_f32 v[126:127], v[102:103], v[20:21], v[100:101] op_sel:[1,0,1] op_sel_hi:[1,1,0] neg_lo:[0,0,1]
	v_pk_mul_f32 v[100:101], v[102:103], v[28:29] op_sel_hi:[0,1]
	v_pk_fma_f32 v[116:117], v[102:103], v[28:29], v[100:101] op_sel:[1,0,1] op_sel_hi:[1,1,0] neg_lo:[0,0,1]
	s_nop 0
	v_pk_add_f32 v[28:29], v[24:25], v[116:117]
	v_pk_add_f32 v[20:21], v[16:17], v[126:127]
	v_pk_mul_f32 v[100:101], v[106:107], v[28:29] op_sel:[1,0]
	s_nop 0
	v_pk_fma_f32 v[102:103], v[106:107], v[28:29], v[100:101] op_sel:[0,0,1] op_sel_hi:[0,1,0] neg_hi:[0,0,1]
	s_nop 0
	v_pk_add_f32 v[28:29], v[20:21], v[102:103]
	v_pk_add_f32 v[12:13], v[4:5], v[124:125]
	s_waitcnt lgkmcnt(1)
; template <int R, class XT, class TWT>
; __device__ __forceinline__ void dit_task(XT X, TWT tw, int s, int task) {
;     const int lgM = 13 - s, lgq = lgM - R, q = 1 << lgq;
;     const int j0 = task & (q - 1), blk = task >> lgq, base = (blk << lgM) + j0;
;     const int pb = PADI(base), qp = (q >= 32) ? q + (q >> 4) : q;
;     f32x2v v[1 << R];
; #pragma unroll
;     for (int k = 0; k < (1 << R); ++k) v[k] = X[pb + k * qp];
; #pragma unroll
;     for (int r = R - 1; r >= 0; --r) {
;         const int pb = R - 1 - r;
; #pragma unroll
;         for (int k = 0; k < (1 << R); ++k) if (!((k >> pb) & 1)) {
;             const int klo = k & ((1 << pb) - 1);
;             const f32x2v w = tw[(j0 + (klo << lgq)) << (s + r)];
;             const f32x2v a = v[k], qv = v[k + (1 << pb)]; const f32x2v b = (f32x2v){qv.x * w.x + qv.y * w.y, qv.y * w.x - qv.x * w.y};
;             v[k] = a + b; v[k + (1 << pb)] = a - b;
;         }
;     }
; #pragma unroll
;     for (int k = 0; k < (1 << R); ++k) X[pb + k * qp] = v[k];
; template <bool LAT>
; __device__ __forceinline__ void hyconv_unit(const Frame& F, LAS f32x2v* X, const TwHalf tw, LAS bf16* OUT, const float* skip, bf16* MIX, int u) {
;     ...
;                 f32x2v g[16], zp[16];
;                 { const bf16* g0 = H0 + (size_t)(ord * 256 + c0) * L + n; const bf16* g1 = H1 + (size_t)(ord * 256 + c0) * L + n; const bf16* v0 = H0 + (size_t)(512 + c0) * L + n; const bf16* v1 = H1 + (size_t)(512 + c0) * L + n;
; #pragma unroll
;                   for (int r = 0; r < 16; ++r) { g[r] = (f32x2v){0.f, 0.f}; zp[r] = g[r]; if (act) { g[r] = (f32x2v){bf2f(g0[r * L]), bf2f(g1[r * L])}; zp[r] = (f32x2v){bf2f(v0[r * L]), bf2f(v1[r * L])}; } } }
	v_pk_mul_f32 v[100:101], v[110:111], v[28:29] op_sel:[1,0]
	v_pk_add_f32 v[8:9], v[8:9], v[120:121] neg_lo:[0,1] neg_hi:[0,1]
	v_pk_fma_f32 v[106:107], v[110:111], v[28:29], v[100:101] op_sel:[0,0,1] op_sel_hi:[0,1,0] neg_hi:[0,0,1]
	v_pk_mul_f32 v[100:101], v[104:105], v[10:11] op_sel_hi:[0,1]
	v_pk_add_f32 v[28:29], v[12:13], v[106:107]
	v_pk_add_f32 v[12:13], v[12:13], v[106:107] neg_lo:[0,1] neg_hi:[0,1]
	v_pk_fma_f32 v[106:107], v[104:105], v[10:11], v[100:101] op_sel:[1,0,1] op_sel_hi:[1,1,0] neg_lo:[0,0,1]
	v_pk_mul_f32 v[100:101], v[104:105], v[26:27] op_sel_hi:[0,1]
	v_pk_fma_f32 v[114:115], v[104:105], v[26:27], v[100:101] op_sel:[1,0,1] op_sel_hi:[1,1,0] neg_lo:[0,0,1]
	s_nop 0
	v_pk_add_f32 v[26:27], v[18:19], v[114:115]
	v_pk_add_f32 v[10:11], v[2:3], v[106:107]
	v_pk_mul_f32 v[100:101], v[98:99], v[26:27] op_sel:[1,0]
	v_pk_add_f32 v[24:25], v[24:25], v[116:117] neg_lo:[0,1] neg_hi:[0,1]
	v_pk_fma_f32 v[104:105], v[98:99], v[26:27], v[100:101] op_sel:[0,0,1] op_sel_hi:[0,1,0] neg_hi:[0,0,1]
	v_pk_mul_f32 v[100:101], v[108:109], v[8:9] op_sel_hi:[0,1]
	v_pk_add_f32 v[26:27], v[10:11], v[104:105]
	v_pk_add_f32 v[10:11], v[10:11], v[104:105] neg_lo:[0,1] neg_hi:[0,1]
	v_pk_fma_f32 v[104:105], v[108:109], v[8:9], v[100:101] op_sel:[1,0,1] op_sel_hi:[1,1,0] neg_lo:[0,0,1]
	v_pk_mul_f32 v[100:101], v[108:109], v[24:25] op_sel_hi:[0,1]
	v_pk_fma_f32 v[116:117], v[108:109], v[24:25], v[100:101] op_sel:[1,0,1] op_sel_hi:[1,1,0] neg_lo:[0,0,1]
	v_pk_add_f32 v[16:17], v[16:17], v[126:127] neg_lo:[0,1] neg_hi:[0,1]
	s_nop 0
	v_pk_add_f32 v[24:25], v[16:17], v[116:117]
	v_pk_add_f32 v[0:1], v[0:1], v[118:119] neg_lo:[0,1] neg_hi:[0,1]
	s_waitcnt lgkmcnt(0)
	v_pk_mul_f32 v[100:101], v[112:113], v[24:25] op_sel:[1,0]
	s_nop 0
	v_pk_fma_f32 v[108:109], v[112:113], v[24:25], v[100:101] op_sel:[0,0,1] op_sel_hi:[0,1,0] neg_hi:[0,0,1]
	v_pk_add_f32 v[22:23], v[22:23], v[184:185] neg_lo:[0,1] neg_hi:[0,1]
	v_pk_add_f32 v[8:9], v[0:1], v[104:105]
	v_pk_mul_f32 v[100:101], v[96:97], v[22:23] op_sel_hi:[0,1]
	v_pk_add_f32 v[20:21], v[20:21], v[102:103] neg_lo:[0,1] neg_hi:[0,1]
	v_pk_add_f32 v[24:25], v[8:9], v[108:109]
	v_pk_add_f32 v[8:9], v[8:9], v[108:109] neg_lo:[0,1] neg_hi:[0,1]
	v_pk_fma_f32 v[108:109], v[96:97], v[22:23], v[100:101] op_sel:[1,0,1] op_sel_hi:[1,1,0] neg_lo:[0,0,1] neg_hi:[0,0,1]
	v_pk_fma_f32 v[22:23], v[96:97], v[22:23], v[100:101] op_sel:[1,0,1] op_sel_hi:[1,1,0]
	v_pk_mul_f32 v[96:97], v[110:111], v[20:21] op_sel_hi:[0,1]
	v_pk_fma_f32 v[100:101], v[110:111], v[20:21], v[96:97] op_sel:[1,0,1] op_sel_hi:[1,1,0] neg_lo:[0,0,1]
	v_pk_add_f32 v[18:19], v[18:19], v[114:115] neg_lo:[0,1] neg_hi:[0,1]
	v_pk_add_f32 v[4:5], v[4:5], v[124:125] neg_lo:[0,1] neg_hi:[0,1]
	v_pk_mul_f32 v[96:97], v[98:99], v[18:19] op_sel_hi:[0,1]
	v_pk_add_f32 v[16:17], v[16:17], v[116:117] neg_lo:[0,1] neg_hi:[0,1]
	v_mov_b32_e32 v173, v15
	v_pk_add_f32 v[20:21], v[4:5], v[100:101]
	v_pk_add_f32 v[4:5], v[4:5], v[100:101] neg_lo:[0,1] neg_hi:[0,1]
	v_pk_fma_f32 v[100:101], v[98:99], v[18:19], v[96:97] op_sel:[1,0,1] op_sel_hi:[1,1,0] neg_lo:[0,0,1] neg_hi:[0,0,1]
	v_pk_fma_f32 v[18:19], v[98:99], v[18:19], v[96:97] op_sel:[1,0,1] op_sel_hi:[1,1,0]
	v_pk_mul_f32 v[96:97], v[112:113], v[16:17] op_sel_hi:[0,1]
	v_pk_add_f32 v[14:15], v[6:7], v[172:173]
	v_mov_b32_e32 v187, v31
	v_pk_fma_f32 v[98:99], v[112:113], v[16:17], v[96:97] op_sel:[1,0,1] op_sel_hi:[1,1,0] neg_lo:[0,0,1]
	v_pk_add_f32 v[30:31], v[14:15], v[186:187]
	v_pk_add_f32 v[6:7], v[6:7], v[172:173] neg_lo:[0,1] neg_hi:[0,1]
	v_mov_b32_e32 v109, v23
	v_pk_add_f32 v[2:3], v[2:3], v[106:107] neg_lo:[0,1] neg_hi:[0,1]
	v_mov_b32_e32 v101, v19
	v_pk_add_f32 v[0:1], v[0:1], v[104:105] neg_lo:[0,1] neg_hi:[0,1]
	v_pk_add_f32 v[14:15], v[14:15], v[186:187] neg_lo:[0,1] neg_hi:[0,1]
	v_pk_add_f32 v[22:23], v[6:7], v[108:109]
	v_pk_add_f32 v[6:7], v[6:7], v[108:109] neg_lo:[0,1] neg_hi:[0,1]
	v_pk_add_f32 v[18:19], v[2:3], v[100:101]
	v_pk_add_f32 v[2:3], v[2:3], v[100:101] neg_lo:[0,1] neg_hi:[0,1]
	v_pk_add_f32 v[16:17], v[0:1], v[98:99]
	v_pk_add_f32 v[0:1], v[0:1], v[98:99] neg_lo:[0,1] neg_hi:[0,1]
	ds_write2_b64 v130, v[30:31], v[28:29] offset1:34
	ds_write2_b64 v130, v[26:27], v[24:25] offset0:68 offset1:102
	ds_write2_b64 v130, v[22:23], v[20:21] offset0:136 offset1:170
	ds_write2_b64 v130, v[18:19], v[16:17] offset0:204 offset1:238
	ds_write2_b64 v94, v[14:15], v[12:13] offset0:16 offset1:50
	ds_write2_b64 v94, v[10:11], v[8:9] offset0:84 offset1:118
	ds_write2_b64 v94, v[6:7], v[4:5] offset0:152 offset1:186
	ds_write2_b64 v94, v[2:3], v[0:1] offset0:220 offset1:254
	s_waitcnt lgkmcnt(0)
	s_barrier
	v_lshl_add_u64 v[100:101], v[38:39], 0, s[90:91]
	v_lshl_add_u64 v[98:99], v[46:47], 0, s[90:91]
	v_mov_b32_e32 v0, 0
	v_mov_b32_e32 v2, 0
	v_mov_b32_e32 v3, 0
	v_mov_b32_e32 v4, 0
	v_mov_b32_e32 v5, 0
	s_and_saveexec_b64 s[0:1], s[40:41]
	s_cbranch_execz .LBB0_939
	global_load_ushort v1, v[100:101], off
	global_load_ushort v3, v[98:99], off
	global_load_ushort v4, v[34:35], off
	global_load_ushort v5, v[36:37], off
	s_waitcnt vmcnt(3)
	v_lshlrev_b32_e32 v2, 16, v1
	s_waitcnt vmcnt(2)
	v_lshlrev_b32_e32 v3, 16, v3
	s_waitcnt vmcnt(1)
	v_lshlrev_b32_e32 v4, 16, v4
	s_waitcnt vmcnt(0)
	v_lshlrev_b32_e32 v5, 16, v5
